# GEMM K-loops: per-segment s_setprio toggling around the MFMA blocks removed
# baseline (speedup 1.0000x reference)
; #define PG8_STAGE_B(bufoff, gbase) do { _Pragma("unroll") for (int _i = 0; _i < 2; ++_i) \
;         __builtin_amdgcn_global_load_lds((const unsigned*)((const char*)(gbase) + voffB[_i]), (LAS unsigned*)(lds + (bufoff) + ldsw + _i * 8192), 16, 0, 0); } while (0)
; #define PG8_STAGE_A(bufoff, V0, V1, kb) do { \
;         __builtin_amdgcn_global_load_lds((const unsigned*)((Abase + (kb)) + (V0)), (LAS unsigned*)(lds + (bufoff) + ldsw), 16, 0, 0); \
;         __builtin_amdgcn_global_load_lds((const unsigned*)((Abase + (kb)) + (V1)), (LAS unsigned*)(lds + (bufoff) + ldsw + 8192), 16, 0, 0); } while (0)
; #define PG8_LDA(dst, b, h) do { _Pragma("unroll") for (int m = 0; m < 4; ++m) _Pragma("unroll") for (int k = 0; k < 2; ++k) dst[m][k] = *(const LAS bf16x8*)(lds + PG8_SA(b, h) + aoff + m * 2048 + k * 1024); } while (0)
; #define PG8_LDB(dst, b, h) do { _Pragma("unroll") for (int n = 0; n < 2; ++n) _Pragma("unroll") for (int k = 0; k < 2; ++k) dst[n][k] = *(const LAS bf16x8*)(lds + PG8_SB(b, h) + boff + n * 2048 + k * 1024); } while (0)
; #define PG8_MMA(ai, bj, At, Bt) do { __builtin_amdgcn_s_setprio(1); _Pragma("unroll") for (int m = 0; m < 4; ++m) _Pragma("unroll") for (int n = 0; n < 2; ++n) _Pragma("unroll") for (int k = 0; k < 2; ++k) \
;         acc[ai][bj][m][n] = __builtin_amdgcn_mfma_f32_16x16x32_bf16(Bt[n][k], At[m][k], acc[ai][bj][m][n], 0, 0, 0); __builtin_amdgcn_s_setprio(0); } while (0)
; #define PG8_WAIT_V(n) asm volatile("s_waitcnt vmcnt(" #n ")" ::: "memory")
; #define PG8_WAIT_L(n) asm volatile("s_waitcnt lgkmcnt(" #n ")" ::: "memory")
; #define PG8_BAR __builtin_amdgcn_s_barrier()
; #define PG8_SCHED __builtin_amdgcn_sched_barrier(0)
; template <class Epi, class Sched, bool ALIGN_EPI>
; __device__ __forceinline__ void gemm_phase(LAS unsigned char* lds, const Gemm g, const Sched& S, const Epi& E) {
;     ...
;             PG8_LDB(B0, 0, 0); PG8_LDB(B1, 0, 1); PG8_SCHED; PG8_LDA(At, 0, 0); PG8_STAGE_A(PG8_SA(1, 1), vc10, vc11, kb1);
;             PG8_WAIT_V(8); PG8_WAIT_L(0); PG8_BAR; PG8_MMA(0, 0, At, B0); PG8_MMA(0, 1, At, B1); PG8_BAR; PG8_SCHED;
;             PG8_LDA(At, 0, 1); PG8_STAGE_B(PG8_SB(0, 0), b2); PG8_STAGE_B(PG8_SB(0, 1), b2 + hstepB); PG8_STAGE_A(PG8_SA(0, 0), s00, s01, kb2);
;             PG8_WAIT_V(8); PG8_WAIT_L(0); PG8_BAR; if (half1) { PG8_MMA(1, 0, At, B0); PG8_MMA(1, 1, At, B1); } PG8_BAR; PG8_SCHED;
.LBB0_158:
	v_add_u32_e32 v5, s54, v223
	ds_read_b128 v[150:153], v5
	ds_read_b128 v[154:157], v5 offset:1024
	ds_read_b128 v[158:161], v5 offset:2048
	ds_read_b128 v[162:165], v5 offset:3072
	v_add_u32_e32 v5, s55, v223
	ds_read_b128 v[134:137], v5
	ds_read_b128 v[138:141], v5 offset:1024
	ds_read_b128 v[142:145], v5 offset:2048
	ds_read_b128 v[146:149], v5 offset:3072
	v_lshl_add_u64 v[214:215], v[212:213], 0, s[4:5]
	s_add_i32 m0, s40, 0xc000
	s_waitcnt lgkmcnt(0)
	ds_read_b128 v[166:169], v231
	ds_read_b128 v[170:173], v231 offset:1024
	ds_read_b128 v[174:177], v231 offset:2048
	ds_read_b128 v[178:181], v231 offset:3072
	ds_read_b128 v[182:185], v231 offset:4096
	ds_read_b128 v[186:189], v231 offset:5120
	ds_read_b128 v[190:193], v231 offset:6144
	ds_read_b128 v[194:197], v231 offset:7168
	global_load_lds_dwordx4 v[214:215], off
	v_lshl_add_u64 v[214:215], v[210:211], 0, s[4:5]
	s_add_i32 m0, s40, 0xe000
	s_nop 0
	global_load_lds_dwordx4 v[214:215], off
	s_waitcnt vmcnt(8)
	s_waitcnt lgkmcnt(0)
	s_barrier
	s_waitcnt lgkmcnt(0)
	v_mfma_f32_16x16x32_bf16 v[130:133], v[150:153], v[166:169], v[130:133]
	v_mfma_f32_16x16x32_bf16 v[126:129], v[158:161], v[166:169], v[126:129]
	v_mfma_f32_16x16x32_bf16 v[114:117], v[150:153], v[174:177], v[114:117]
	v_mfma_f32_16x16x32_bf16 v[110:113], v[158:161], v[174:177], v[110:113]
	v_mfma_f32_16x16x32_bf16 v[98:101], v[150:153], v[182:185], v[98:101]
	v_mfma_f32_16x16x32_bf16 v[94:97], v[158:161], v[182:185], v[94:97]
	v_mfma_f32_16x16x32_bf16 v[82:85], v[150:153], v[190:193], v[82:85]
	v_mfma_f32_16x16x32_bf16 v[78:81], v[158:161], v[190:193], v[78:81]
	v_mfma_f32_16x16x32_bf16 v[130:133], v[154:157], v[170:173], v[130:133]
	v_mfma_f32_16x16x32_bf16 v[126:129], v[162:165], v[170:173], v[126:129]
	v_mfma_f32_16x16x32_bf16 v[114:117], v[154:157], v[178:181], v[114:117]
	v_mfma_f32_16x16x32_bf16 v[110:113], v[162:165], v[178:181], v[110:113]
	v_mfma_f32_16x16x32_bf16 v[98:101], v[154:157], v[186:189], v[98:101]
	v_mfma_f32_16x16x32_bf16 v[94:97], v[162:165], v[186:189], v[94:97]
	v_mfma_f32_16x16x32_bf16 v[82:85], v[154:157], v[194:197], v[82:85]
	v_mfma_f32_16x16x32_bf16 v[78:81], v[162:165], v[194:197], v[78:81]
	v_mfma_f32_16x16x32_bf16 v[122:125], v[134:137], v[166:169], v[122:125]
	v_mfma_f32_16x16x32_bf16 v[118:121], v[142:145], v[166:169], v[118:121]
	v_mfma_f32_16x16x32_bf16 v[106:109], v[134:137], v[174:177], v[106:109]
	v_mfma_f32_16x16x32_bf16 v[102:105], v[142:145], v[174:177], v[102:105]
	v_mfma_f32_16x16x32_bf16 v[90:93], v[134:137], v[182:185], v[90:93]
	v_mfma_f32_16x16x32_bf16 v[86:89], v[142:145], v[182:185], v[86:89]
	v_mfma_f32_16x16x32_bf16 v[74:77], v[134:137], v[190:193], v[74:77]
	v_mfma_f32_16x16x32_bf16 v[70:73], v[142:145], v[190:193], v[70:73]
	v_mfma_f32_16x16x32_bf16 v[122:125], v[138:141], v[170:173], v[122:125]
	v_mfma_f32_16x16x32_bf16 v[118:121], v[146:149], v[170:173], v[118:121]
	v_mfma_f32_16x16x32_bf16 v[106:109], v[138:141], v[178:181], v[106:109]
	v_mfma_f32_16x16x32_bf16 v[102:105], v[146:149], v[178:181], v[102:105]
	v_mfma_f32_16x16x32_bf16 v[90:93], v[138:141], v[186:189], v[90:93]
	v_mfma_f32_16x16x32_bf16 v[86:89], v[146:149], v[186:189], v[86:89]
	v_mfma_f32_16x16x32_bf16 v[74:77], v[138:141], v[194:197], v[74:77]
	v_mfma_f32_16x16x32_bf16 v[70:73], v[146:149], v[194:197], v[70:73]
	s_barrier
	s_add_i32 s4, s54, s19
	v_lshl_add_u64 v[214:215], s[36:37], 0, v[198:199]
	s_mov_b32 m0, s4
	ds_read_b128 v[190:193], v231 offset:16384
	ds_read_b128 v[194:197], v231 offset:17408
	ds_read_b128 v[182:185], v231 offset:18432
	ds_read_b128 v[186:189], v231 offset:19456
	ds_read_b128 v[174:177], v231 offset:20480
	ds_read_b128 v[178:181], v231 offset:21504
	ds_read_b128 v[166:169], v231 offset:22528
	ds_read_b128 v[170:173], v231 offset:23552
	global_load_lds_dwordx4 v[214:215], off
	s_add_i32 m0, s4, 0x2000
	s_add_u32 s4, s36, 0x40000
	v_lshl_add_u64 v[216:217], s[36:37], 0, v[200:201]
	s_addc_u32 s5, s37, 0
	s_add_i32 s39, s55, s19
	global_load_lds_dwordx4 v[216:217], off
	v_lshl_add_u64 v[238:239], s[4:5], 0, v[198:199]
	s_mov_b32 m0, s39
	v_cndmask_b32_e64 v5, 0, 1, s[28:29]
	global_load_lds_dwordx4 v[238:239], off
	v_lshl_add_u64 v[238:239], s[4:5], 0, v[200:201]
	s_add_i32 m0, s39, 0x2000
	v_readlane_b32 s4, v253, 52
	v_readlane_b32 s5, v253, 53
	s_add_u32 s38, s4, s38
	global_load_lds_dwordx4 v[238:239], off
	s_addc_u32 s39, s5, 0
	s_mov_b32 m0, s40
	v_cmp_ne_u32_e64 s[4:5], 1, v5
	global_load_lds_dwordx4 v2, s[38:39]
	s_mov_b32 m0, s41
	s_andn2_b64 vcc, exec, s[28:29]
	global_load_lds_dwordx4 v4, s[38:39]
	s_waitcnt vmcnt(8)
	s_waitcnt lgkmcnt(0)
	s_barrier
	s_cbranch_vccnz .LBB0_160
	s_waitcnt lgkmcnt(0)
	v_mfma_f32_16x16x32_bf16 v[66:69], v[150:153], v[190:193], v[66:69]
	v_mfma_f32_16x16x32_bf16 v[62:65], v[158:161], v[190:193], v[62:65]
	v_mfma_f32_16x16x32_bf16 v[50:53], v[150:153], v[182:185], v[50:53]
	v_mfma_f32_16x16x32_bf16 v[46:49], v[158:161], v[182:185], v[46:49]
	v_mfma_f32_16x16x32_bf16 v[34:37], v[150:153], v[174:177], v[34:37]
	v_mfma_f32_16x16x32_bf16 v[30:33], v[158:161], v[174:177], v[30:33]
	v_mfma_f32_16x16x32_bf16 v[18:21], v[150:153], v[166:169], v[18:21]
	v_mfma_f32_16x16x32_bf16 v[14:17], v[158:161], v[166:169], v[14:17]
	v_mfma_f32_16x16x32_bf16 v[66:69], v[154:157], v[194:197], v[66:69]
	v_mfma_f32_16x16x32_bf16 v[62:65], v[162:165], v[194:197], v[62:65]
	v_mfma_f32_16x16x32_bf16 v[50:53], v[154:157], v[186:189], v[50:53]
	v_mfma_f32_16x16x32_bf16 v[46:49], v[162:165], v[186:189], v[46:49]
	v_mfma_f32_16x16x32_bf16 v[34:37], v[154:157], v[178:181], v[34:37]
	v_mfma_f32_16x16x32_bf16 v[30:33], v[162:165], v[178:181], v[30:33]
	v_mfma_f32_16x16x32_bf16 v[18:21], v[154:157], v[170:173], v[18:21]
	v_mfma_f32_16x16x32_bf16 v[14:17], v[162:165], v[170:173], v[14:17]
	v_mfma_f32_16x16x32_bf16 v[58:61], v[134:137], v[190:193], v[58:61]
	v_mfma_f32_16x16x32_bf16 v[54:57], v[142:145], v[190:193], v[54:57]
	v_mfma_f32_16x16x32_bf16 v[42:45], v[134:137], v[182:185], v[42:45]
	v_mfma_f32_16x16x32_bf16 v[38:41], v[142:145], v[182:185], v[38:41]
	v_mfma_f32_16x16x32_bf16 v[26:29], v[134:137], v[174:177], v[26:29]
	v_mfma_f32_16x16x32_bf16 v[22:25], v[142:145], v[174:177], v[22:25]
	v_mfma_f32_16x16x32_bf16 v[10:13], v[134:137], v[166:169], v[10:13]
	v_mfma_f32_16x16x32_bf16 v[6:9], v[142:145], v[166:169], v[6:9]
	v_mfma_f32_16x16x32_bf16 v[58:61], v[138:141], v[194:197], v[58:61]
	v_mfma_f32_16x16x32_bf16 v[54:57], v[146:149], v[194:197], v[54:57]
	v_mfma_f32_16x16x32_bf16 v[42:45], v[138:141], v[186:189], v[42:45]
	v_mfma_f32_16x16x32_bf16 v[38:41], v[146:149], v[186:189], v[38:41]
	v_mfma_f32_16x16x32_bf16 v[26:29], v[138:141], v[178:181], v[26:29]
	v_mfma_f32_16x16x32_bf16 v[22:25], v[146:149], v[178:181], v[22:25]
	v_mfma_f32_16x16x32_bf16 v[10:13], v[138:141], v[170:173], v[10:13]
	v_mfma_f32_16x16x32_bf16 v[6:9], v[146:149], v[170:173], v[6:9]
; #define PG8_STAGE_B(bufoff, gbase) do { _Pragma("unroll") for (int _i = 0; _i < 2; ++_i) \
;         __builtin_amdgcn_global_load_lds((const unsigned*)((const char*)(gbase) + voffB[_i]), (LAS unsigned*)(lds + (bufoff) + ldsw + _i * 8192), 16, 0, 0); } while (0)
; #define PG8_STAGE_A(bufoff, V0, V1, kb) do { \
;         __builtin_amdgcn_global_load_lds((const unsigned*)((Abase + (kb)) + (V0)), (LAS unsigned*)(lds + (bufoff) + ldsw), 16, 0, 0); \
;         __builtin_amdgcn_global_load_lds((const unsigned*)((Abase + (kb)) + (V1)), (LAS unsigned*)(lds + (bufoff) + ldsw + 8192), 16, 0, 0); } while (0)
; #define PG8_LDA(dst, b, h) do { _Pragma("unroll") for (int m = 0; m < 4; ++m) _Pragma("unroll") for (int k = 0; k < 2; ++k) dst[m][k] = *(const LAS bf16x8*)(lds + PG8_SA(b, h) + aoff + m * 2048 + k * 1024); } while (0)
; #define PG8_LDB(dst, b, h) do { _Pragma("unroll") for (int n = 0; n < 2; ++n) _Pragma("unroll") for (int k = 0; k < 2; ++k) dst[n][k] = *(const LAS bf16x8*)(lds + PG8_SB(b, h) + boff + n * 2048 + k * 1024); } while (0)
; #define PG8_MMA(ai, bj, At, Bt) do { __builtin_amdgcn_s_setprio(1); _Pragma("unroll") for (int m = 0; m < 4; ++m) _Pragma("unroll") for (int n = 0; n < 2; ++n) _Pragma("unroll") for (int k = 0; k < 2; ++k) \
;         acc[ai][bj][m][n] = __builtin_amdgcn_mfma_f32_16x16x32_bf16(Bt[n][k], At[m][k], acc[ai][bj][m][n], 0, 0, 0); __builtin_amdgcn_s_setprio(0); } while (0)
; #define PG8_WAIT_V(n) asm volatile("s_waitcnt vmcnt(" #n ")" ::: "memory")
; #define PG8_WAIT_L(n) asm volatile("s_waitcnt lgkmcnt(" #n ")" ::: "memory")
; #define PG8_BAR __builtin_amdgcn_s_barrier()
; #define PG8_SCHED __builtin_amdgcn_sched_barrier(0)
; template <class Epi, class Sched, bool ALIGN_EPI>
; __device__ __forceinline__ void gemm_phase(LAS unsigned char* lds, const Gemm g, const Sched& S, const Epi& E) {
;     ...
;             PG8_LDB(B0, 1, 0); PG8_LDB(B1, 1, 1); PG8_SCHED; PG8_LDA(At, 1, 0); PG8_STAGE_A(PG8_SA(0, 1), s10, s11, kb2);
;             PG8_WAIT_V(8); PG8_WAIT_L(0); PG8_BAR; PG8_MMA(0, 0, At, B0); PG8_MMA(0, 1, At, B1); PG8_BAR; PG8_SCHED;
;             PG8_LDA(At, 1, 1); PG8_STAGE_B(PG8_SB(1, 0), b3); PG8_STAGE_B(PG8_SB(1, 1), b3 + hstepB); PG8_STAGE_A(PG8_SA(1, 0), s00, s01, kb3);
;             PG8_WAIT_V(8); PG8_WAIT_L(0); PG8_BAR; if (half1) { PG8_MMA(1, 0, At, B0); PG8_MMA(1, 1, At, B1); } PG8_BAR; PG8_SCHED;
.LBB0_160:
	v_mov_b32_e32 v5, v3
	v_lshl_add_u64 v[238:239], s[38:39], 0, v[2:3]
	v_lshl_add_u64 v[4:5], s[38:39], 0, v[4:5]
	s_barrier
	v_add_u32_e32 v2, s56, v223
	ds_read_b128 v[150:153], v2
	ds_read_b128 v[154:157], v2 offset:1024
	ds_read_b128 v[158:161], v2 offset:2048
	ds_read_b128 v[162:165], v2 offset:3072
	v_add_u32_e32 v2, s57, v223
	ds_read_b128 v[134:137], v2
	ds_read_b128 v[138:141], v2 offset:1024
	ds_read_b128 v[142:145], v2 offset:2048
	ds_read_b128 v[146:149], v2 offset:3072
	s_mov_b32 m0, s46
	s_waitcnt lgkmcnt(0)
	ds_read_b128 v[166:169], v231 offset:32768
	ds_read_b128 v[170:173], v231 offset:33792
	ds_read_b128 v[174:177], v231 offset:34816
	ds_read_b128 v[178:181], v231 offset:35840
	ds_read_b128 v[182:185], v231 offset:36864
	ds_read_b128 v[186:189], v231 offset:37888
	ds_read_b128 v[190:193], v231 offset:38912
	ds_read_b128 v[194:197], v231 offset:39936
	global_load_lds_dwordx4 v207, s[38:39]
	s_mov_b32 m0, s47
	s_nop 0
	global_load_lds_dwordx4 v209, s[38:39]
	s_waitcnt vmcnt(8)
	s_waitcnt lgkmcnt(0)
	s_barrier
	s_waitcnt lgkmcnt(0)
	v_mfma_f32_16x16x32_bf16 v[130:133], v[150:153], v[166:169], v[130:133]
	v_mfma_f32_16x16x32_bf16 v[126:129], v[158:161], v[166:169], v[126:129]
	v_mfma_f32_16x16x32_bf16 v[114:117], v[150:153], v[174:177], v[114:117]
	v_mfma_f32_16x16x32_bf16 v[110:113], v[158:161], v[174:177], v[110:113]
	v_mfma_f32_16x16x32_bf16 v[98:101], v[150:153], v[182:185], v[98:101]
	v_mfma_f32_16x16x32_bf16 v[94:97], v[158:161], v[182:185], v[94:97]
	v_mfma_f32_16x16x32_bf16 v[82:85], v[150:153], v[190:193], v[82:85]
	v_mfma_f32_16x16x32_bf16 v[78:81], v[158:161], v[190:193], v[78:81]
	v_mfma_f32_16x16x32_bf16 v[130:133], v[154:157], v[170:173], v[130:133]
	v_mfma_f32_16x16x32_bf16 v[126:129], v[162:165], v[170:173], v[126:129]
	v_mfma_f32_16x16x32_bf16 v[114:117], v[154:157], v[178:181], v[114:117]
	v_mfma_f32_16x16x32_bf16 v[110:113], v[162:165], v[178:181], v[110:113]
	v_mfma_f32_16x16x32_bf16 v[98:101], v[154:157], v[186:189], v[98:101]
	v_mfma_f32_16x16x32_bf16 v[94:97], v[162:165], v[186:189], v[94:97]
	v_mfma_f32_16x16x32_bf16 v[82:85], v[154:157], v[194:197], v[82:85]
	v_mfma_f32_16x16x32_bf16 v[78:81], v[162:165], v[194:197], v[78:81]
	v_mfma_f32_16x16x32_bf16 v[122:125], v[134:137], v[166:169], v[122:125]
	v_mfma_f32_16x16x32_bf16 v[118:121], v[142:145], v[166:169], v[118:121]
	v_mfma_f32_16x16x32_bf16 v[106:109], v[134:137], v[174:177], v[106:109]
	v_mfma_f32_16x16x32_bf16 v[102:105], v[142:145], v[174:177], v[102:105]
	v_mfma_f32_16x16x32_bf16 v[90:93], v[134:137], v[182:185], v[90:93]
	v_mfma_f32_16x16x32_bf16 v[86:89], v[142:145], v[182:185], v[86:89]
	v_mfma_f32_16x16x32_bf16 v[74:77], v[134:137], v[190:193], v[74:77]
	v_mfma_f32_16x16x32_bf16 v[70:73], v[142:145], v[190:193], v[70:73]
	v_mfma_f32_16x16x32_bf16 v[122:125], v[138:141], v[170:173], v[122:125]
	v_mfma_f32_16x16x32_bf16 v[118:121], v[146:149], v[170:173], v[118:121]
	v_mfma_f32_16x16x32_bf16 v[106:109], v[138:141], v[178:181], v[106:109]
	v_mfma_f32_16x16x32_bf16 v[102:105], v[146:149], v[178:181], v[102:105]
	v_mfma_f32_16x16x32_bf16 v[90:93], v[138:141], v[186:189], v[90:93]
	v_mfma_f32_16x16x32_bf16 v[86:89], v[146:149], v[186:189], v[86:89]
	v_mfma_f32_16x16x32_bf16 v[74:77], v[138:141], v[194:197], v[74:77]
	v_mfma_f32_16x16x32_bf16 v[70:73], v[146:149], v[194:197], v[70:73]
	s_barrier
	s_add_i32 s38, s56, s19
	v_lshl_add_u64 v[214:215], v[214:215], 0, s[8:9]
	s_mov_b32 m0, s38
	ds_read_b128 v[190:193], v231 offset:49152
	ds_read_b128 v[194:197], v231 offset:50176
	ds_read_b128 v[182:185], v231 offset:51200
	ds_read_b128 v[186:189], v231 offset:52224
	ds_read_b128 v[174:177], v231 offset:53248
	ds_read_b128 v[178:181], v231 offset:54272
	ds_read_b128 v[166:169], v231 offset:55296
	ds_read_b128 v[170:173], v231 offset:56320
	global_load_lds_dwordx4 v[214:215], off
	s_add_i32 m0, s38, 0x2000
	s_add_u32 s36, s36, 0x40080
	v_lshl_add_u64 v[214:215], v[216:217], 0, s[8:9]
	s_addc_u32 s37, s37, 0
	s_add_i32 s38, s57, s19
	global_load_lds_dwordx4 v[214:215], off
	v_lshl_add_u64 v[214:215], s[36:37], 0, v[198:199]
	s_mov_b32 m0, s38
	v_lshl_add_u64 v[4:5], v[4:5], 0, s[8:9]
	global_load_lds_dwordx4 v[214:215], off
	v_lshl_add_u64 v[214:215], s[36:37], 0, v[200:201]
	s_add_i32 m0, s38, 0x2000
	s_and_b64 vcc, exec, s[4:5]
	global_load_lds_dwordx4 v[214:215], off
	v_lshl_add_u64 v[214:215], v[238:239], 0, s[8:9]
	s_mov_b32 m0, s48
	s_nop 0
	global_load_lds_dwordx4 v[214:215], off
	s_mov_b32 m0, s49
	s_nop 0
	global_load_lds_dwordx4 v[4:5], off
	s_waitcnt vmcnt(8)
	s_waitcnt lgkmcnt(0)
	s_barrier
	s_cbranch_vccnz .LBB0_162
	s_waitcnt lgkmcnt(0)
	v_mfma_f32_16x16x32_bf16 v[66:69], v[150:153], v[190:193], v[66:69]
	v_mfma_f32_16x16x32_bf16 v[62:65], v[158:161], v[190:193], v[62:65]
	v_mfma_f32_16x16x32_bf16 v[50:53], v[150:153], v[182:185], v[50:53]
	v_mfma_f32_16x16x32_bf16 v[46:49], v[158:161], v[182:185], v[46:49]
	v_mfma_f32_16x16x32_bf16 v[34:37], v[150:153], v[174:177], v[34:37]
	v_mfma_f32_16x16x32_bf16 v[30:33], v[158:161], v[174:177], v[30:33]
	v_mfma_f32_16x16x32_bf16 v[18:21], v[150:153], v[166:169], v[18:21]
	v_mfma_f32_16x16x32_bf16 v[14:17], v[158:161], v[166:169], v[14:17]
	v_mfma_f32_16x16x32_bf16 v[66:69], v[154:157], v[194:197], v[66:69]
	v_mfma_f32_16x16x32_bf16 v[62:65], v[162:165], v[194:197], v[62:65]
	v_mfma_f32_16x16x32_bf16 v[50:53], v[154:157], v[186:189], v[50:53]
	v_mfma_f32_16x16x32_bf16 v[46:49], v[162:165], v[186:189], v[46:49]
	v_mfma_f32_16x16x32_bf16 v[34:37], v[154:157], v[178:181], v[34:37]
	v_mfma_f32_16x16x32_bf16 v[30:33], v[162:165], v[178:181], v[30:33]
	v_mfma_f32_16x16x32_bf16 v[18:21], v[154:157], v[170:173], v[18:21]
	v_mfma_f32_16x16x32_bf16 v[14:17], v[162:165], v[170:173], v[14:17]
	v_mfma_f32_16x16x32_bf16 v[58:61], v[134:137], v[190:193], v[58:61]
	v_mfma_f32_16x16x32_bf16 v[54:57], v[142:145], v[190:193], v[54:57]
	v_mfma_f32_16x16x32_bf16 v[42:45], v[134:137], v[182:185], v[42:45]
	v_mfma_f32_16x16x32_bf16 v[38:41], v[142:145], v[182:185], v[38:41]
	v_mfma_f32_16x16x32_bf16 v[26:29], v[134:137], v[174:177], v[26:29]
	v_mfma_f32_16x16x32_bf16 v[22:25], v[142:145], v[174:177], v[22:25]
	v_mfma_f32_16x16x32_bf16 v[10:13], v[134:137], v[166:169], v[10:13]
	v_mfma_f32_16x16x32_bf16 v[4:7], v[142:145], v[166:169], v[6:9]
	v_mfma_f32_16x16x32_bf16 v[58:61], v[138:141], v[194:197], v[58:61]
	v_mfma_f32_16x16x32_bf16 v[54:57], v[146:149], v[194:197], v[54:57]
	v_mfma_f32_16x16x32_bf16 v[42:45], v[138:141], v[186:189], v[42:45]
	v_mfma_f32_16x16x32_bf16 v[38:41], v[146:149], v[186:189], v[38:41]
	v_mfma_f32_16x16x32_bf16 v[26:29], v[138:141], v[178:181], v[26:29]
	v_mfma_f32_16x16x32_bf16 v[22:25], v[146:149], v[178:181], v[22:25]
	v_mfma_f32_16x16x32_bf16 v[10:13], v[138:141], v[170:173], v[10:13]
	v_mfma_f32_16x16x32_bf16 v[6:9], v[146:149], v[170:173], v[4:7]

; #define PG8_STAGE_B(bufoff, gbase) do { _Pragma("unroll") for (int _i = 0; _i < 2; ++_i) \
;         __builtin_amdgcn_global_load_lds((const unsigned*)((const char*)(gbase) + voffB[_i]), (LAS unsigned*)(lds + (bufoff) + ldsw + _i * 8192), 16, 0, 0); } while (0)
; #define PG8_STAGE_A(bufoff, V0, V1, kb) do { \
;         __builtin_amdgcn_global_load_lds((const unsigned*)((Abase + (kb)) + (V0)), (LAS unsigned*)(lds + (bufoff) + ldsw), 16, 0, 0); \
;         __builtin_amdgcn_global_load_lds((const unsigned*)((Abase + (kb)) + (V1)), (LAS unsigned*)(lds + (bufoff) + ldsw + 8192), 16, 0, 0); } while (0)
; #define PG8_LDA(dst, b, h) do { _Pragma("unroll") for (int m = 0; m < 4; ++m) _Pragma("unroll") for (int k = 0; k < 2; ++k) dst[m][k] = *(const LAS bf16x8*)(lds + PG8_SA(b, h) + aoff + m * 2048 + k * 1024); } while (0)
; #define PG8_LDB(dst, b, h) do { _Pragma("unroll") for (int n = 0; n < 2; ++n) _Pragma("unroll") for (int k = 0; k < 2; ++k) dst[n][k] = *(const LAS bf16x8*)(lds + PG8_SB(b, h) + boff + n * 2048 + k * 1024); } while (0)
; #define PG8_MMA(ai, bj, At, Bt) do { __builtin_amdgcn_s_setprio(1); _Pragma("unroll") for (int m = 0; m < 4; ++m) _Pragma("unroll") for (int n = 0; n < 2; ++n) _Pragma("unroll") for (int k = 0; k < 2; ++k) \
;         acc[ai][bj][m][n] = __builtin_amdgcn_mfma_f32_16x16x32_bf16(Bt[n][k], At[m][k], acc[ai][bj][m][n], 0, 0, 0); __builtin_amdgcn_s_setprio(0); } while (0)
; #define PG8_WAIT_V(n) asm volatile("s_waitcnt vmcnt(" #n ")" ::: "memory")
; #define PG8_WAIT_L(n) asm volatile("s_waitcnt lgkmcnt(" #n ")" ::: "memory")
; #define PG8_BAR __builtin_amdgcn_s_barrier()
; #define PG8_SCHED __builtin_amdgcn_sched_barrier(0)
; template <class Epi, class Sched, bool ALIGN_EPI>
; __device__ __forceinline__ void gemm_phase(LAS unsigned char* lds, const Gemm g, const Sched& S, const Epi& E) {
;     ...
;             PG8_LDB(B0, 0, 0); PG8_LDB(B1, 0, 1); PG8_SCHED; PG8_LDA(At, 0, 0); PG8_STAGE_A(PG8_SA(1, 1), vc10, vc11, kb1);
;             PG8_WAIT_V(8); PG8_WAIT_L(0); PG8_BAR; PG8_MMA(0, 0, At, B0); PG8_MMA(0, 1, At, B1); PG8_BAR; PG8_SCHED;
;             PG8_LDA(At, 0, 1); PG8_STAGE_B(PG8_SB(0, 0), b2); PG8_STAGE_B(PG8_SB(0, 1), b2 + hstepB); PG8_STAGE_A(PG8_SA(0, 0), s00, s01, kb2);
;             PG8_WAIT_V(8); PG8_WAIT_L(0); PG8_BAR; if (half1) { PG8_MMA(1, 0, At, B0); PG8_MMA(1, 1, At, B1); } PG8_BAR; PG8_SCHED;
.LBB0_453:
	v_add_u32_e32 v5, s54, v219
	ds_read_b128 v[150:153], v5
	ds_read_b128 v[154:157], v5 offset:1024
	ds_read_b128 v[158:161], v5 offset:2048
	ds_read_b128 v[162:165], v5 offset:3072
	v_add_u32_e32 v5, s55, v219
	ds_read_b128 v[134:137], v5
	ds_read_b128 v[138:141], v5 offset:1024
	ds_read_b128 v[142:145], v5 offset:2048
	ds_read_b128 v[146:149], v5 offset:3072
	v_readlane_b32 s64, v253, 60
	v_readlane_b32 s65, v253, 61
	s_add_u32 s36, s64, s3
	s_addc_u32 s37, s65, 0
	v_lshl_add_u64 v[212:213], s[36:37], 0, v[208:209]
	v_lshl_add_u64 v[212:213], v[212:213], 0, s[6:7]
	s_add_i32 m0, s41, 0xc000
	s_waitcnt lgkmcnt(0)
	ds_read_b128 v[166:169], v220
	ds_read_b128 v[170:173], v220 offset:1024
	ds_read_b128 v[174:177], v220 offset:2048
	ds_read_b128 v[178:181], v220 offset:3072
	ds_read_b128 v[182:185], v220 offset:4096
	ds_read_b128 v[186:189], v220 offset:5120
	ds_read_b128 v[190:193], v220 offset:6144
	ds_read_b128 v[194:197], v220 offset:7168
	global_load_lds_dwordx4 v[212:213], off
	v_lshl_add_u64 v[212:213], s[36:37], 0, v[210:211]
	v_lshl_add_u64 v[212:213], v[212:213], 0, s[6:7]
	s_add_i32 m0, s41, 0xe000
	s_nop 0
	global_load_lds_dwordx4 v[212:213], off
	s_waitcnt vmcnt(8)
	s_waitcnt lgkmcnt(0)
	s_barrier
	s_waitcnt lgkmcnt(0)
	v_mfma_f32_16x16x32_bf16 v[130:133], v[150:153], v[166:169], v[130:133]
	v_mfma_f32_16x16x32_bf16 v[126:129], v[158:161], v[166:169], v[126:129]
	v_mfma_f32_16x16x32_bf16 v[114:117], v[150:153], v[174:177], v[114:117]
	v_mfma_f32_16x16x32_bf16 v[110:113], v[158:161], v[174:177], v[110:113]
	v_mfma_f32_16x16x32_bf16 v[98:101], v[150:153], v[182:185], v[98:101]
	v_mfma_f32_16x16x32_bf16 v[94:97], v[158:161], v[182:185], v[94:97]
	v_mfma_f32_16x16x32_bf16 v[82:85], v[150:153], v[190:193], v[82:85]
	v_mfma_f32_16x16x32_bf16 v[78:81], v[158:161], v[190:193], v[78:81]
	v_mfma_f32_16x16x32_bf16 v[130:133], v[154:157], v[170:173], v[130:133]
	v_mfma_f32_16x16x32_bf16 v[126:129], v[162:165], v[170:173], v[126:129]
	v_mfma_f32_16x16x32_bf16 v[114:117], v[154:157], v[178:181], v[114:117]
	v_mfma_f32_16x16x32_bf16 v[110:113], v[162:165], v[178:181], v[110:113]
	v_mfma_f32_16x16x32_bf16 v[98:101], v[154:157], v[186:189], v[98:101]
	v_mfma_f32_16x16x32_bf16 v[94:97], v[162:165], v[186:189], v[94:97]
	v_mfma_f32_16x16x32_bf16 v[82:85], v[154:157], v[194:197], v[82:85]
	v_mfma_f32_16x16x32_bf16 v[78:81], v[162:165], v[194:197], v[78:81]
	v_mfma_f32_16x16x32_bf16 v[122:125], v[134:137], v[166:169], v[122:125]
	v_mfma_f32_16x16x32_bf16 v[118:121], v[142:145], v[166:169], v[118:121]
	v_mfma_f32_16x16x32_bf16 v[106:109], v[134:137], v[174:177], v[106:109]
	v_mfma_f32_16x16x32_bf16 v[102:105], v[142:145], v[174:177], v[102:105]
	v_mfma_f32_16x16x32_bf16 v[90:93], v[134:137], v[182:185], v[90:93]
	v_mfma_f32_16x16x32_bf16 v[86:89], v[142:145], v[182:185], v[86:89]
	v_mfma_f32_16x16x32_bf16 v[74:77], v[134:137], v[190:193], v[74:77]
	v_mfma_f32_16x16x32_bf16 v[70:73], v[142:145], v[190:193], v[70:73]
	v_mfma_f32_16x16x32_bf16 v[122:125], v[138:141], v[170:173], v[122:125]
	v_mfma_f32_16x16x32_bf16 v[118:121], v[146:149], v[170:173], v[118:121]
	v_mfma_f32_16x16x32_bf16 v[106:109], v[138:141], v[178:181], v[106:109]
	v_mfma_f32_16x16x32_bf16 v[102:105], v[146:149], v[178:181], v[102:105]
	v_mfma_f32_16x16x32_bf16 v[90:93], v[138:141], v[186:189], v[90:93]
	v_mfma_f32_16x16x32_bf16 v[86:89], v[146:149], v[186:189], v[86:89]
	v_mfma_f32_16x16x32_bf16 v[74:77], v[138:141], v[194:197], v[74:77]
	v_mfma_f32_16x16x32_bf16 v[70:73], v[146:149], v[194:197], v[70:73]
	s_barrier
	s_add_i32 s3, s54, s40
	v_lshl_add_u64 v[212:213], s[30:31], 0, v[198:199]
	s_mov_b32 m0, s3
	ds_read_b128 v[190:193], v220 offset:16384
	ds_read_b128 v[194:197], v220 offset:17408
	ds_read_b128 v[182:185], v220 offset:18432
	ds_read_b128 v[186:189], v220 offset:19456
	ds_read_b128 v[174:177], v220 offset:20480
	ds_read_b128 v[178:181], v220 offset:21504
	ds_read_b128 v[166:169], v220 offset:22528
	ds_read_b128 v[170:173], v220 offset:23552
	global_load_lds_dwordx4 v[212:213], off
	s_add_i32 m0, s3, 0x2000
	s_add_u32 s36, s30, 0x10000
	v_lshl_add_u64 v[214:215], s[30:31], 0, v[200:201]
	s_addc_u32 s37, s31, 0
	s_add_i32 s3, s55, s40
	global_load_lds_dwordx4 v[214:215], off
	v_lshl_add_u64 v[230:231], s[36:37], 0, v[198:199]
	s_mov_b32 m0, s3
	v_cndmask_b32_e64 v5, 0, 1, s[26:27]
	global_load_lds_dwordx4 v[230:231], off
	s_add_i32 m0, s3, 0x2000
	v_lshl_add_u64 v[230:231], s[36:37], 0, v[200:201]
	s_add_u32 s36, s64, s4
	global_load_lds_dwordx4 v[230:231], off
	s_addc_u32 s37, s65, 0
	s_mov_b32 m0, s41
	v_cmp_ne_u32_e64 s[4:5], 1, v5
	global_load_lds_dwordx4 v2, s[36:37]
	s_mov_b32 m0, s46
	s_andn2_b64 vcc, exec, s[26:27]
	global_load_lds_dwordx4 v4, s[36:37]
	s_waitcnt vmcnt(8)
	s_waitcnt lgkmcnt(0)
	s_barrier
	s_cbranch_vccnz .LBB0_455
	s_waitcnt lgkmcnt(0)
	v_mfma_f32_16x16x32_bf16 v[66:69], v[150:153], v[190:193], v[66:69]
	v_mfma_f32_16x16x32_bf16 v[62:65], v[158:161], v[190:193], v[62:65]
	v_mfma_f32_16x16x32_bf16 v[50:53], v[150:153], v[182:185], v[50:53]
	v_mfma_f32_16x16x32_bf16 v[46:49], v[158:161], v[182:185], v[46:49]
	v_mfma_f32_16x16x32_bf16 v[34:37], v[150:153], v[174:177], v[34:37]
	v_mfma_f32_16x16x32_bf16 v[30:33], v[158:161], v[174:177], v[30:33]
	v_mfma_f32_16x16x32_bf16 v[18:21], v[150:153], v[166:169], v[18:21]
	v_mfma_f32_16x16x32_bf16 v[14:17], v[158:161], v[166:169], v[14:17]
	v_mfma_f32_16x16x32_bf16 v[66:69], v[154:157], v[194:197], v[66:69]
	v_mfma_f32_16x16x32_bf16 v[62:65], v[162:165], v[194:197], v[62:65]
	v_mfma_f32_16x16x32_bf16 v[50:53], v[154:157], v[186:189], v[50:53]
	v_mfma_f32_16x16x32_bf16 v[46:49], v[162:165], v[186:189], v[46:49]
	v_mfma_f32_16x16x32_bf16 v[34:37], v[154:157], v[178:181], v[34:37]
	v_mfma_f32_16x16x32_bf16 v[30:33], v[162:165], v[178:181], v[30:33]
	v_mfma_f32_16x16x32_bf16 v[18:21], v[154:157], v[170:173], v[18:21]
	v_mfma_f32_16x16x32_bf16 v[14:17], v[162:165], v[170:173], v[14:17]
	v_mfma_f32_16x16x32_bf16 v[58:61], v[134:137], v[190:193], v[58:61]
	v_mfma_f32_16x16x32_bf16 v[54:57], v[142:145], v[190:193], v[54:57]
	v_mfma_f32_16x16x32_bf16 v[42:45], v[134:137], v[182:185], v[42:45]
	v_mfma_f32_16x16x32_bf16 v[38:41], v[142:145], v[182:185], v[38:41]
	v_mfma_f32_16x16x32_bf16 v[26:29], v[134:137], v[174:177], v[26:29]
	v_mfma_f32_16x16x32_bf16 v[22:25], v[142:145], v[174:177], v[22:25]
	v_mfma_f32_16x16x32_bf16 v[10:13], v[134:137], v[166:169], v[10:13]
	v_mfma_f32_16x16x32_bf16 v[6:9], v[142:145], v[166:169], v[6:9]
	v_mfma_f32_16x16x32_bf16 v[58:61], v[138:141], v[194:197], v[58:61]
	v_mfma_f32_16x16x32_bf16 v[54:57], v[146:149], v[194:197], v[54:57]
	v_mfma_f32_16x16x32_bf16 v[42:45], v[138:141], v[186:189], v[42:45]
	v_mfma_f32_16x16x32_bf16 v[38:41], v[146:149], v[186:189], v[38:41]
	v_mfma_f32_16x16x32_bf16 v[26:29], v[138:141], v[178:181], v[26:29]
	v_mfma_f32_16x16x32_bf16 v[22:25], v[146:149], v[178:181], v[22:25]
	v_mfma_f32_16x16x32_bf16 v[10:13], v[138:141], v[170:173], v[10:13]
	v_mfma_f32_16x16x32_bf16 v[6:9], v[146:149], v[170:173], v[6:9]
; #define PG8_STAGE_B(bufoff, gbase) do { _Pragma("unroll") for (int _i = 0; _i < 2; ++_i) \
;         __builtin_amdgcn_global_load_lds((const unsigned*)((const char*)(gbase) + voffB[_i]), (LAS unsigned*)(lds + (bufoff) + ldsw + _i * 8192), 16, 0, 0); } while (0)
; #define PG8_STAGE_A(bufoff, V0, V1, kb) do { \
;         __builtin_amdgcn_global_load_lds((const unsigned*)((Abase + (kb)) + (V0)), (LAS unsigned*)(lds + (bufoff) + ldsw), 16, 0, 0); \
;         __builtin_amdgcn_global_load_lds((const unsigned*)((Abase + (kb)) + (V1)), (LAS unsigned*)(lds + (bufoff) + ldsw + 8192), 16, 0, 0); } while (0)
; #define PG8_LDA(dst, b, h) do { _Pragma("unroll") for (int m = 0; m < 4; ++m) _Pragma("unroll") for (int k = 0; k < 2; ++k) dst[m][k] = *(const LAS bf16x8*)(lds + PG8_SA(b, h) + aoff + m * 2048 + k * 1024); } while (0)
; #define PG8_LDB(dst, b, h) do { _Pragma("unroll") for (int n = 0; n < 2; ++n) _Pragma("unroll") for (int k = 0; k < 2; ++k) dst[n][k] = *(const LAS bf16x8*)(lds + PG8_SB(b, h) + boff + n * 2048 + k * 1024); } while (0)
; #define PG8_MMA(ai, bj, At, Bt) do { __builtin_amdgcn_s_setprio(1); _Pragma("unroll") for (int m = 0; m < 4; ++m) _Pragma("unroll") for (int n = 0; n < 2; ++n) _Pragma("unroll") for (int k = 0; k < 2; ++k) \
;         acc[ai][bj][m][n] = __builtin_amdgcn_mfma_f32_16x16x32_bf16(Bt[n][k], At[m][k], acc[ai][bj][m][n], 0, 0, 0); __builtin_amdgcn_s_setprio(0); } while (0)
; #define PG8_WAIT_V(n) asm volatile("s_waitcnt vmcnt(" #n ")" ::: "memory")
; #define PG8_WAIT_L(n) asm volatile("s_waitcnt lgkmcnt(" #n ")" ::: "memory")
; #define PG8_BAR __builtin_amdgcn_s_barrier()
; #define PG8_SCHED __builtin_amdgcn_sched_barrier(0)
; template <class Epi, class Sched, bool ALIGN_EPI>
; __device__ __forceinline__ void gemm_phase(LAS unsigned char* lds, const Gemm g, const Sched& S, const Epi& E) {
;     ...
;             PG8_LDB(B0, 1, 0); PG8_LDB(B1, 1, 1); PG8_SCHED; PG8_LDA(At, 1, 0); PG8_STAGE_A(PG8_SA(0, 1), s10, s11, kb2);
;             PG8_WAIT_V(8); PG8_WAIT_L(0); PG8_BAR; PG8_MMA(0, 0, At, B0); PG8_MMA(0, 1, At, B1); PG8_BAR; PG8_SCHED;
;             PG8_LDA(At, 1, 1); PG8_STAGE_B(PG8_SB(1, 0), b3); PG8_STAGE_B(PG8_SB(1, 1), b3 + hstepB); PG8_STAGE_A(PG8_SA(1, 0), s00, s01, kb3);
;             PG8_WAIT_V(8); PG8_WAIT_L(0); PG8_BAR; if (half1) { PG8_MMA(1, 0, At, B0); PG8_MMA(1, 1, At, B1); } PG8_BAR; PG8_SCHED;
.LBB0_455:
	v_mov_b32_e32 v5, v3
	v_lshl_add_u64 v[230:231], s[36:37], 0, v[2:3]
	v_lshl_add_u64 v[4:5], s[36:37], 0, v[4:5]
	s_barrier
	v_add_u32_e32 v2, s56, v219
	ds_read_b128 v[150:153], v2
	ds_read_b128 v[154:157], v2 offset:1024
	ds_read_b128 v[158:161], v2 offset:2048
	ds_read_b128 v[162:165], v2 offset:3072
	v_add_u32_e32 v2, s57, v219
	ds_read_b128 v[134:137], v2
	ds_read_b128 v[138:141], v2 offset:1024
	ds_read_b128 v[142:145], v2 offset:2048
	ds_read_b128 v[146:149], v2 offset:3072
	s_mov_b32 m0, s47
	s_waitcnt lgkmcnt(0)
	ds_read_b128 v[166:169], v220 offset:32768
	ds_read_b128 v[170:173], v220 offset:33792
	ds_read_b128 v[174:177], v220 offset:34816
	ds_read_b128 v[178:181], v220 offset:35840
	ds_read_b128 v[182:185], v220 offset:36864
	ds_read_b128 v[186:189], v220 offset:37888
	ds_read_b128 v[190:193], v220 offset:38912
	ds_read_b128 v[194:197], v220 offset:39936
	global_load_lds_dwordx4 v227, s[36:37]
	s_mov_b32 m0, s48
	s_nop 0
	global_load_lds_dwordx4 v228, s[36:37]
	s_waitcnt vmcnt(8)
	s_waitcnt lgkmcnt(0)
	s_barrier
	s_waitcnt lgkmcnt(0)
	v_mfma_f32_16x16x32_bf16 v[130:133], v[150:153], v[166:169], v[130:133]
	v_mfma_f32_16x16x32_bf16 v[126:129], v[158:161], v[166:169], v[126:129]
	v_mfma_f32_16x16x32_bf16 v[114:117], v[150:153], v[174:177], v[114:117]
	v_mfma_f32_16x16x32_bf16 v[110:113], v[158:161], v[174:177], v[110:113]
	v_mfma_f32_16x16x32_bf16 v[98:101], v[150:153], v[182:185], v[98:101]
	v_mfma_f32_16x16x32_bf16 v[94:97], v[158:161], v[182:185], v[94:97]
	v_mfma_f32_16x16x32_bf16 v[82:85], v[150:153], v[190:193], v[82:85]
	v_mfma_f32_16x16x32_bf16 v[78:81], v[158:161], v[190:193], v[78:81]
	v_mfma_f32_16x16x32_bf16 v[130:133], v[154:157], v[170:173], v[130:133]
	v_mfma_f32_16x16x32_bf16 v[126:129], v[162:165], v[170:173], v[126:129]
	v_mfma_f32_16x16x32_bf16 v[114:117], v[154:157], v[178:181], v[114:117]
	v_mfma_f32_16x16x32_bf16 v[110:113], v[162:165], v[178:181], v[110:113]
	v_mfma_f32_16x16x32_bf16 v[98:101], v[154:157], v[186:189], v[98:101]
	v_mfma_f32_16x16x32_bf16 v[94:97], v[162:165], v[186:189], v[94:97]
	v_mfma_f32_16x16x32_bf16 v[82:85], v[154:157], v[194:197], v[82:85]
	v_mfma_f32_16x16x32_bf16 v[78:81], v[162:165], v[194:197], v[78:81]
	v_mfma_f32_16x16x32_bf16 v[122:125], v[134:137], v[166:169], v[122:125]
	v_mfma_f32_16x16x32_bf16 v[118:121], v[142:145], v[166:169], v[118:121]
	v_mfma_f32_16x16x32_bf16 v[106:109], v[134:137], v[174:177], v[106:109]
	v_mfma_f32_16x16x32_bf16 v[102:105], v[142:145], v[174:177], v[102:105]
	v_mfma_f32_16x16x32_bf16 v[90:93], v[134:137], v[182:185], v[90:93]
	v_mfma_f32_16x16x32_bf16 v[86:89], v[142:145], v[182:185], v[86:89]
	v_mfma_f32_16x16x32_bf16 v[74:77], v[134:137], v[190:193], v[74:77]
	v_mfma_f32_16x16x32_bf16 v[70:73], v[142:145], v[190:193], v[70:73]
	v_mfma_f32_16x16x32_bf16 v[122:125], v[138:141], v[170:173], v[122:125]
	v_mfma_f32_16x16x32_bf16 v[118:121], v[146:149], v[170:173], v[118:121]
	v_mfma_f32_16x16x32_bf16 v[106:109], v[138:141], v[178:181], v[106:109]
	v_mfma_f32_16x16x32_bf16 v[102:105], v[146:149], v[178:181], v[102:105]
	v_mfma_f32_16x16x32_bf16 v[90:93], v[138:141], v[186:189], v[90:93]
	v_mfma_f32_16x16x32_bf16 v[86:89], v[146:149], v[186:189], v[86:89]
	v_mfma_f32_16x16x32_bf16 v[74:77], v[138:141], v[194:197], v[74:77]
	v_mfma_f32_16x16x32_bf16 v[70:73], v[146:149], v[194:197], v[70:73]
	s_barrier
	s_add_i32 s3, s56, s40
	v_lshl_add_u64 v[212:213], v[212:213], 0, s[6:7]
	s_mov_b32 m0, s3
	ds_read_b128 v[190:193], v220 offset:49152
	ds_read_b128 v[194:197], v220 offset:50176
	ds_read_b128 v[182:185], v220 offset:51200
	ds_read_b128 v[186:189], v220 offset:52224
	ds_read_b128 v[174:177], v220 offset:53248
	ds_read_b128 v[178:181], v220 offset:54272
	ds_read_b128 v[166:169], v220 offset:55296
	ds_read_b128 v[170:173], v220 offset:56320
	global_load_lds_dwordx4 v[212:213], off
	s_add_i32 m0, s3, 0x2000
	s_add_u32 s30, s30, 0x10080
	v_lshl_add_u64 v[212:213], v[214:215], 0, s[6:7]
	s_addc_u32 s31, s31, 0
	s_add_i32 s3, s57, s40
	global_load_lds_dwordx4 v[212:213], off
	v_lshl_add_u64 v[212:213], s[30:31], 0, v[198:199]
	s_mov_b32 m0, s3
	v_lshl_add_u64 v[4:5], v[4:5], 0, s[6:7]
	global_load_lds_dwordx4 v[212:213], off
	v_lshl_add_u64 v[212:213], s[30:31], 0, v[200:201]
	s_add_i32 m0, s3, 0x2000
	s_and_b64 vcc, exec, s[4:5]
	global_load_lds_dwordx4 v[212:213], off
	v_lshl_add_u64 v[212:213], v[230:231], 0, s[6:7]
	s_mov_b32 m0, s49
	s_nop 0
	global_load_lds_dwordx4 v[212:213], off
	s_mov_b32 m0, s50
	s_nop 0
	global_load_lds_dwordx4 v[4:5], off
	s_waitcnt vmcnt(8)
	s_waitcnt lgkmcnt(0)
	s_barrier
	s_cbranch_vccnz .LBB0_449
	s_waitcnt lgkmcnt(0)
	v_mfma_f32_16x16x32_bf16 v[66:69], v[150:153], v[190:193], v[66:69]
	v_mfma_f32_16x16x32_bf16 v[62:65], v[158:161], v[190:193], v[62:65]
	v_mfma_f32_16x16x32_bf16 v[50:53], v[150:153], v[182:185], v[50:53]
	v_mfma_f32_16x16x32_bf16 v[46:49], v[158:161], v[182:185], v[46:49]
	v_mfma_f32_16x16x32_bf16 v[34:37], v[150:153], v[174:177], v[34:37]
	v_mfma_f32_16x16x32_bf16 v[30:33], v[158:161], v[174:177], v[30:33]
	v_mfma_f32_16x16x32_bf16 v[18:21], v[150:153], v[166:169], v[18:21]
	v_mfma_f32_16x16x32_bf16 v[14:17], v[158:161], v[166:169], v[14:17]
	v_mfma_f32_16x16x32_bf16 v[66:69], v[154:157], v[194:197], v[66:69]
	v_mfma_f32_16x16x32_bf16 v[62:65], v[162:165], v[194:197], v[62:65]
	v_mfma_f32_16x16x32_bf16 v[50:53], v[154:157], v[186:189], v[50:53]
	v_mfma_f32_16x16x32_bf16 v[46:49], v[162:165], v[186:189], v[46:49]
	v_mfma_f32_16x16x32_bf16 v[34:37], v[154:157], v[178:181], v[34:37]
	v_mfma_f32_16x16x32_bf16 v[30:33], v[162:165], v[178:181], v[30:33]
	v_mfma_f32_16x16x32_bf16 v[18:21], v[154:157], v[170:173], v[18:21]
	v_mfma_f32_16x16x32_bf16 v[14:17], v[162:165], v[170:173], v[14:17]
	v_mfma_f32_16x16x32_bf16 v[58:61], v[134:137], v[190:193], v[58:61]
	v_mfma_f32_16x16x32_bf16 v[54:57], v[142:145], v[190:193], v[54:57]
	v_mfma_f32_16x16x32_bf16 v[42:45], v[134:137], v[182:185], v[42:45]
	v_mfma_f32_16x16x32_bf16 v[38:41], v[142:145], v[182:185], v[38:41]
	v_mfma_f32_16x16x32_bf16 v[26:29], v[134:137], v[174:177], v[26:29]
	v_mfma_f32_16x16x32_bf16 v[22:25], v[142:145], v[174:177], v[22:25]
	v_mfma_f32_16x16x32_bf16 v[10:13], v[134:137], v[166:169], v[10:13]
	v_mfma_f32_16x16x32_bf16 v[4:7], v[142:145], v[166:169], v[6:9]
	v_mfma_f32_16x16x32_bf16 v[58:61], v[138:141], v[194:197], v[58:61]
	v_mfma_f32_16x16x32_bf16 v[54:57], v[146:149], v[194:197], v[54:57]
	v_mfma_f32_16x16x32_bf16 v[42:45], v[138:141], v[186:189], v[42:45]
	v_mfma_f32_16x16x32_bf16 v[38:41], v[146:149], v[186:189], v[38:41]
	v_mfma_f32_16x16x32_bf16 v[26:29], v[138:141], v[178:181], v[26:29]
	v_mfma_f32_16x16x32_bf16 v[22:25], v[146:149], v[178:181], v[22:25]
	v_mfma_f32_16x16x32_bf16 v[10:13], v[138:141], v[170:173], v[10:13]
	v_mfma_f32_16x16x32_bf16 v[6:9], v[146:149], v[170:173], v[4:7]
	s_branch .LBB0_449

; #define PG8_STAGE_B(bufoff, gbase) do { _Pragma("unroll") for (int _i = 0; _i < 2; ++_i) \
;         __builtin_amdgcn_global_load_lds((const unsigned*)((const char*)(gbase) + voffB[_i]), (LAS unsigned*)(lds + (bufoff) + ldsw + _i * 8192), 16, 0, 0); } while (0)
; #define PG8_STAGE_A(bufoff, V0, V1, kb) do { \
;         __builtin_amdgcn_global_load_lds((const unsigned*)((Abase + (kb)) + (V0)), (LAS unsigned*)(lds + (bufoff) + ldsw), 16, 0, 0); \
;         __builtin_amdgcn_global_load_lds((const unsigned*)((Abase + (kb)) + (V1)), (LAS unsigned*)(lds + (bufoff) + ldsw + 8192), 16, 0, 0); } while (0)
; #define PG8_LDA(dst, b, h) do { _Pragma("unroll") for (int m = 0; m < 4; ++m) _Pragma("unroll") for (int k = 0; k < 2; ++k) dst[m][k] = *(const LAS bf16x8*)(lds + PG8_SA(b, h) + aoff + m * 2048 + k * 1024); } while (0)
; #define PG8_LDB(dst, b, h) do { _Pragma("unroll") for (int n = 0; n < 2; ++n) _Pragma("unroll") for (int k = 0; k < 2; ++k) dst[n][k] = *(const LAS bf16x8*)(lds + PG8_SB(b, h) + boff + n * 2048 + k * 1024); } while (0)
; #define PG8_MMA(ai, bj, At, Bt) do { __builtin_amdgcn_s_setprio(1); _Pragma("unroll") for (int m = 0; m < 4; ++m) _Pragma("unroll") for (int n = 0; n < 2; ++n) _Pragma("unroll") for (int k = 0; k < 2; ++k) \
;         acc[ai][bj][m][n] = __builtin_amdgcn_mfma_f32_16x16x32_bf16(Bt[n][k], At[m][k], acc[ai][bj][m][n], 0, 0, 0); __builtin_amdgcn_s_setprio(0); } while (0)
; #define PG8_WAIT_V(n) asm volatile("s_waitcnt vmcnt(" #n ")" ::: "memory")
; #define PG8_WAIT_L(n) asm volatile("s_waitcnt lgkmcnt(" #n ")" ::: "memory")
; #define PG8_BAR __builtin_amdgcn_s_barrier()
; #define PG8_SCHED __builtin_amdgcn_sched_barrier(0)
; template <class Epi, class Sched, bool ALIGN_EPI>
; __device__ __forceinline__ void gemm_phase(LAS unsigned char* lds, const Gemm g, const Sched& S, const Epi& E) {
;     ...
;             PG8_LDB(B0, 0, 0); PG8_LDB(B1, 0, 1); PG8_SCHED; PG8_LDA(At, 0, 0); PG8_STAGE_A(PG8_SA(1, 1), vc10, vc11, kb1);
;             PG8_WAIT_V(8); PG8_WAIT_L(0); PG8_BAR; PG8_MMA(0, 0, At, B0); PG8_MMA(0, 1, At, B1); PG8_BAR; PG8_SCHED;
;             PG8_LDA(At, 0, 1); PG8_STAGE_B(PG8_SB(0, 0), b2); PG8_STAGE_B(PG8_SB(0, 1), b2 + hstepB); PG8_STAGE_A(PG8_SA(0, 0), s00, s01, kb2);
;             PG8_WAIT_V(8); PG8_WAIT_L(0); PG8_BAR; if (half1) { PG8_MMA(1, 0, At, B0); PG8_MMA(1, 1, At, B1); } PG8_BAR; PG8_SCHED;
.LBB0_544:
	v_add_u32_e32 v5, s41, v221
	ds_read_b128 v[150:153], v5
	ds_read_b128 v[154:157], v5 offset:1024
	ds_read_b128 v[158:161], v5 offset:2048
	ds_read_b128 v[162:165], v5 offset:3072
	v_add_u32_e32 v5, s44, v221
	ds_read_b128 v[134:137], v5
	ds_read_b128 v[138:141], v5 offset:1024
	ds_read_b128 v[142:145], v5 offset:2048
	ds_read_b128 v[146:149], v5 offset:3072
	v_lshl_add_u64 v[230:231], v[228:229], 0, s[4:5]
	s_add_i32 m0, s26, 0xc000
	s_waitcnt lgkmcnt(0)
	ds_read_b128 v[166:169], v234
	ds_read_b128 v[170:173], v234 offset:1024
	ds_read_b128 v[174:177], v234 offset:2048
	ds_read_b128 v[178:181], v234 offset:3072
	ds_read_b128 v[182:185], v234 offset:4096
	ds_read_b128 v[186:189], v234 offset:5120
	ds_read_b128 v[190:193], v234 offset:6144
	ds_read_b128 v[194:197], v234 offset:7168
	global_load_lds_dwordx4 v[230:231], off
	v_lshl_add_u64 v[230:231], v[226:227], 0, s[4:5]
	s_add_i32 m0, s26, 0xe000
	s_nop 0
	global_load_lds_dwordx4 v[230:231], off
	s_waitcnt vmcnt(8)
	s_waitcnt lgkmcnt(0)
	s_barrier
	s_waitcnt lgkmcnt(0)
	v_mfma_f32_16x16x32_bf16 v[130:133], v[150:153], v[166:169], v[130:133]
	v_mfma_f32_16x16x32_bf16 v[126:129], v[158:161], v[166:169], v[126:129]
	v_mfma_f32_16x16x32_bf16 v[114:117], v[150:153], v[174:177], v[114:117]
	v_mfma_f32_16x16x32_bf16 v[110:113], v[158:161], v[174:177], v[110:113]
	v_mfma_f32_16x16x32_bf16 v[98:101], v[150:153], v[182:185], v[98:101]
	v_mfma_f32_16x16x32_bf16 v[94:97], v[158:161], v[182:185], v[94:97]
	v_mfma_f32_16x16x32_bf16 v[82:85], v[150:153], v[190:193], v[82:85]
	v_mfma_f32_16x16x32_bf16 v[78:81], v[158:161], v[190:193], v[78:81]
	v_mfma_f32_16x16x32_bf16 v[130:133], v[154:157], v[170:173], v[130:133]
	v_mfma_f32_16x16x32_bf16 v[126:129], v[162:165], v[170:173], v[126:129]
	v_mfma_f32_16x16x32_bf16 v[114:117], v[154:157], v[178:181], v[114:117]
	v_mfma_f32_16x16x32_bf16 v[110:113], v[162:165], v[178:181], v[110:113]
	v_mfma_f32_16x16x32_bf16 v[98:101], v[154:157], v[186:189], v[98:101]
	v_mfma_f32_16x16x32_bf16 v[94:97], v[162:165], v[186:189], v[94:97]
	v_mfma_f32_16x16x32_bf16 v[82:85], v[154:157], v[194:197], v[82:85]
	v_mfma_f32_16x16x32_bf16 v[78:81], v[162:165], v[194:197], v[78:81]
	v_mfma_f32_16x16x32_bf16 v[122:125], v[134:137], v[166:169], v[122:125]
	v_mfma_f32_16x16x32_bf16 v[118:121], v[142:145], v[166:169], v[118:121]
	v_mfma_f32_16x16x32_bf16 v[106:109], v[134:137], v[174:177], v[106:109]
	v_mfma_f32_16x16x32_bf16 v[102:105], v[142:145], v[174:177], v[102:105]
	v_mfma_f32_16x16x32_bf16 v[90:93], v[134:137], v[182:185], v[90:93]
	v_mfma_f32_16x16x32_bf16 v[86:89], v[142:145], v[182:185], v[86:89]
	v_mfma_f32_16x16x32_bf16 v[74:77], v[134:137], v[190:193], v[74:77]
	v_mfma_f32_16x16x32_bf16 v[70:73], v[142:145], v[190:193], v[70:73]
	v_mfma_f32_16x16x32_bf16 v[122:125], v[138:141], v[170:173], v[122:125]
	v_mfma_f32_16x16x32_bf16 v[118:121], v[146:149], v[170:173], v[118:121]
	v_mfma_f32_16x16x32_bf16 v[106:109], v[138:141], v[178:181], v[106:109]
	v_mfma_f32_16x16x32_bf16 v[102:105], v[146:149], v[178:181], v[102:105]
	v_mfma_f32_16x16x32_bf16 v[90:93], v[138:141], v[186:189], v[90:93]
	v_mfma_f32_16x16x32_bf16 v[86:89], v[146:149], v[186:189], v[86:89]
	v_mfma_f32_16x16x32_bf16 v[74:77], v[138:141], v[194:197], v[74:77]
	v_mfma_f32_16x16x32_bf16 v[70:73], v[146:149], v[194:197], v[70:73]
	s_barrier
	s_add_i32 s4, s41, s15
	v_lshl_add_u64 v[230:231], s[22:23], 0, v[200:201]
	s_mov_b32 m0, s4
	ds_read_b128 v[190:193], v234 offset:16384
	ds_read_b128 v[194:197], v234 offset:17408
	ds_read_b128 v[182:185], v234 offset:18432
	ds_read_b128 v[186:189], v234 offset:19456
	ds_read_b128 v[174:177], v234 offset:20480
	ds_read_b128 v[178:181], v234 offset:21504
	ds_read_b128 v[166:169], v234 offset:22528
	ds_read_b128 v[170:173], v234 offset:23552
	global_load_lds_dwordx4 v[230:231], off
	s_add_i32 m0, s4, 0x2000
	s_add_u32 s4, s22, 0x18000
	v_lshl_add_u64 v[232:233], s[22:23], 0, v[204:205]
	s_addc_u32 s5, s23, 0
	s_add_i32 s25, s44, s15
	global_load_lds_dwordx4 v[232:233], off
	v_lshl_add_u64 v[236:237], s[4:5], 0, v[200:201]
	s_mov_b32 m0, s25
	v_cndmask_b32_e64 v5, 0, 1, s[18:19]
	global_load_lds_dwordx4 v[236:237], off
	v_lshl_add_u64 v[236:237], s[4:5], 0, v[204:205]
	s_add_i32 m0, s25, 0x2000
	v_readlane_b32 s4, v253, 58
	v_readlane_b32 s5, v253, 59
	s_add_u32 s24, s4, s24
	global_load_lds_dwordx4 v[236:237], off
	s_addc_u32 s25, s5, 0
	s_mov_b32 m0, s26
	v_cmp_ne_u32_e64 s[4:5], 1, v5
	global_load_lds_dwordx4 v2, s[24:25]
	s_mov_b32 m0, s28
	s_andn2_b64 vcc, exec, s[18:19]
	global_load_lds_dwordx4 v4, s[24:25]
	s_waitcnt vmcnt(8)
	s_waitcnt lgkmcnt(0)
	s_barrier
	s_cbranch_vccnz .LBB0_546
	s_waitcnt lgkmcnt(0)
	v_mfma_f32_16x16x32_bf16 v[66:69], v[150:153], v[190:193], v[66:69]
	v_mfma_f32_16x16x32_bf16 v[62:65], v[158:161], v[190:193], v[62:65]
	v_mfma_f32_16x16x32_bf16 v[50:53], v[150:153], v[182:185], v[50:53]
	v_mfma_f32_16x16x32_bf16 v[46:49], v[158:161], v[182:185], v[46:49]
	v_mfma_f32_16x16x32_bf16 v[34:37], v[150:153], v[174:177], v[34:37]
	v_mfma_f32_16x16x32_bf16 v[30:33], v[158:161], v[174:177], v[30:33]
	v_mfma_f32_16x16x32_bf16 v[18:21], v[150:153], v[166:169], v[18:21]
	v_mfma_f32_16x16x32_bf16 v[14:17], v[158:161], v[166:169], v[14:17]
	v_mfma_f32_16x16x32_bf16 v[66:69], v[154:157], v[194:197], v[66:69]
	v_mfma_f32_16x16x32_bf16 v[62:65], v[162:165], v[194:197], v[62:65]
	v_mfma_f32_16x16x32_bf16 v[50:53], v[154:157], v[186:189], v[50:53]
	v_mfma_f32_16x16x32_bf16 v[46:49], v[162:165], v[186:189], v[46:49]
	v_mfma_f32_16x16x32_bf16 v[34:37], v[154:157], v[178:181], v[34:37]
	v_mfma_f32_16x16x32_bf16 v[30:33], v[162:165], v[178:181], v[30:33]
	v_mfma_f32_16x16x32_bf16 v[18:21], v[154:157], v[170:173], v[18:21]
	v_mfma_f32_16x16x32_bf16 v[14:17], v[162:165], v[170:173], v[14:17]
	v_mfma_f32_16x16x32_bf16 v[58:61], v[134:137], v[190:193], v[58:61]
	v_mfma_f32_16x16x32_bf16 v[54:57], v[142:145], v[190:193], v[54:57]
	v_mfma_f32_16x16x32_bf16 v[42:45], v[134:137], v[182:185], v[42:45]
	v_mfma_f32_16x16x32_bf16 v[38:41], v[142:145], v[182:185], v[38:41]
	v_mfma_f32_16x16x32_bf16 v[26:29], v[134:137], v[174:177], v[26:29]
	v_mfma_f32_16x16x32_bf16 v[22:25], v[142:145], v[174:177], v[22:25]
	v_mfma_f32_16x16x32_bf16 v[10:13], v[134:137], v[166:169], v[10:13]
	v_mfma_f32_16x16x32_bf16 v[6:9], v[142:145], v[166:169], v[6:9]
	v_mfma_f32_16x16x32_bf16 v[58:61], v[138:141], v[194:197], v[58:61]
	v_mfma_f32_16x16x32_bf16 v[54:57], v[146:149], v[194:197], v[54:57]
	v_mfma_f32_16x16x32_bf16 v[42:45], v[138:141], v[186:189], v[42:45]
	v_mfma_f32_16x16x32_bf16 v[38:41], v[146:149], v[186:189], v[38:41]
	v_mfma_f32_16x16x32_bf16 v[26:29], v[138:141], v[178:181], v[26:29]
	v_mfma_f32_16x16x32_bf16 v[22:25], v[146:149], v[178:181], v[22:25]
	v_mfma_f32_16x16x32_bf16 v[10:13], v[138:141], v[170:173], v[10:13]
	v_mfma_f32_16x16x32_bf16 v[6:9], v[146:149], v[170:173], v[6:9]
; #define PG8_STAGE_B(bufoff, gbase) do { _Pragma("unroll") for (int _i = 0; _i < 2; ++_i) \
;         __builtin_amdgcn_global_load_lds((const unsigned*)((const char*)(gbase) + voffB[_i]), (LAS unsigned*)(lds + (bufoff) + ldsw + _i * 8192), 16, 0, 0); } while (0)
; #define PG8_STAGE_A(bufoff, V0, V1, kb) do { \
;         __builtin_amdgcn_global_load_lds((const unsigned*)((Abase + (kb)) + (V0)), (LAS unsigned*)(lds + (bufoff) + ldsw), 16, 0, 0); \
;         __builtin_amdgcn_global_load_lds((const unsigned*)((Abase + (kb)) + (V1)), (LAS unsigned*)(lds + (bufoff) + ldsw + 8192), 16, 0, 0); } while (0)
; #define PG8_LDA(dst, b, h) do { _Pragma("unroll") for (int m = 0; m < 4; ++m) _Pragma("unroll") for (int k = 0; k < 2; ++k) dst[m][k] = *(const LAS bf16x8*)(lds + PG8_SA(b, h) + aoff + m * 2048 + k * 1024); } while (0)
; #define PG8_LDB(dst, b, h) do { _Pragma("unroll") for (int n = 0; n < 2; ++n) _Pragma("unroll") for (int k = 0; k < 2; ++k) dst[n][k] = *(const LAS bf16x8*)(lds + PG8_SB(b, h) + boff + n * 2048 + k * 1024); } while (0)
; #define PG8_MMA(ai, bj, At, Bt) do { __builtin_amdgcn_s_setprio(1); _Pragma("unroll") for (int m = 0; m < 4; ++m) _Pragma("unroll") for (int n = 0; n < 2; ++n) _Pragma("unroll") for (int k = 0; k < 2; ++k) \
;         acc[ai][bj][m][n] = __builtin_amdgcn_mfma_f32_16x16x32_bf16(Bt[n][k], At[m][k], acc[ai][bj][m][n], 0, 0, 0); __builtin_amdgcn_s_setprio(0); } while (0)
; #define PG8_WAIT_V(n) asm volatile("s_waitcnt vmcnt(" #n ")" ::: "memory")
; #define PG8_WAIT_L(n) asm volatile("s_waitcnt lgkmcnt(" #n ")" ::: "memory")
; #define PG8_BAR __builtin_amdgcn_s_barrier()
; #define PG8_SCHED __builtin_amdgcn_sched_barrier(0)
; template <class Epi, class Sched, bool ALIGN_EPI>
; __device__ __forceinline__ void gemm_phase(LAS unsigned char* lds, const Gemm g, const Sched& S, const Epi& E) {
;     ...
;             PG8_LDB(B0, 1, 0); PG8_LDB(B1, 1, 1); PG8_SCHED; PG8_LDA(At, 1, 0); PG8_STAGE_A(PG8_SA(0, 1), s10, s11, kb2);
;             PG8_WAIT_V(8); PG8_WAIT_L(0); PG8_BAR; PG8_MMA(0, 0, At, B0); PG8_MMA(0, 1, At, B1); PG8_BAR; PG8_SCHED;
;             PG8_LDA(At, 1, 1); PG8_STAGE_B(PG8_SB(1, 0), b3); PG8_STAGE_B(PG8_SB(1, 1), b3 + hstepB); PG8_STAGE_A(PG8_SA(1, 0), s00, s01, kb3);
;             PG8_WAIT_V(8); PG8_WAIT_L(0); PG8_BAR; if (half1) { PG8_MMA(1, 0, At, B0); PG8_MMA(1, 1, At, B1); } PG8_BAR; PG8_SCHED;
.LBB0_546:
	v_mov_b32_e32 v5, v3
	v_lshl_add_u64 v[236:237], s[24:25], 0, v[2:3]
	v_lshl_add_u64 v[4:5], s[24:25], 0, v[4:5]
	s_barrier
	v_add_u32_e32 v2, s45, v221
	ds_read_b128 v[150:153], v2
	ds_read_b128 v[154:157], v2 offset:1024
	ds_read_b128 v[158:161], v2 offset:2048
	ds_read_b128 v[162:165], v2 offset:3072
	v_add_u32_e32 v2, s46, v221
	ds_read_b128 v[134:137], v2
	ds_read_b128 v[138:141], v2 offset:1024
	ds_read_b128 v[142:145], v2 offset:2048
	ds_read_b128 v[146:149], v2 offset:3072
	s_mov_b32 m0, s29
	s_waitcnt lgkmcnt(0)
	ds_read_b128 v[166:169], v234 offset:32768
	ds_read_b128 v[170:173], v234 offset:33792
	ds_read_b128 v[174:177], v234 offset:34816
	ds_read_b128 v[178:181], v234 offset:35840
	ds_read_b128 v[182:185], v234 offset:36864
	ds_read_b128 v[186:189], v234 offset:37888
	ds_read_b128 v[190:193], v234 offset:38912
	ds_read_b128 v[194:197], v234 offset:39936
	global_load_lds_dwordx4 v211, s[24:25]
	s_mov_b32 m0, s30
	s_nop 0
	global_load_lds_dwordx4 v213, s[24:25]
	s_waitcnt vmcnt(8)
	s_waitcnt lgkmcnt(0)
	s_barrier
	s_waitcnt lgkmcnt(0)
	v_mfma_f32_16x16x32_bf16 v[130:133], v[150:153], v[166:169], v[130:133]
	v_mfma_f32_16x16x32_bf16 v[126:129], v[158:161], v[166:169], v[126:129]
	v_mfma_f32_16x16x32_bf16 v[114:117], v[150:153], v[174:177], v[114:117]
	v_mfma_f32_16x16x32_bf16 v[110:113], v[158:161], v[174:177], v[110:113]
	v_mfma_f32_16x16x32_bf16 v[98:101], v[150:153], v[182:185], v[98:101]
	v_mfma_f32_16x16x32_bf16 v[94:97], v[158:161], v[182:185], v[94:97]
	v_mfma_f32_16x16x32_bf16 v[82:85], v[150:153], v[190:193], v[82:85]
	v_mfma_f32_16x16x32_bf16 v[78:81], v[158:161], v[190:193], v[78:81]
	v_mfma_f32_16x16x32_bf16 v[130:133], v[154:157], v[170:173], v[130:133]
	v_mfma_f32_16x16x32_bf16 v[126:129], v[162:165], v[170:173], v[126:129]
	v_mfma_f32_16x16x32_bf16 v[114:117], v[154:157], v[178:181], v[114:117]
	v_mfma_f32_16x16x32_bf16 v[110:113], v[162:165], v[178:181], v[110:113]
	v_mfma_f32_16x16x32_bf16 v[98:101], v[154:157], v[186:189], v[98:101]
	v_mfma_f32_16x16x32_bf16 v[94:97], v[162:165], v[186:189], v[94:97]
	v_mfma_f32_16x16x32_bf16 v[82:85], v[154:157], v[194:197], v[82:85]
	v_mfma_f32_16x16x32_bf16 v[78:81], v[162:165], v[194:197], v[78:81]
	v_mfma_f32_16x16x32_bf16 v[122:125], v[134:137], v[166:169], v[122:125]
	v_mfma_f32_16x16x32_bf16 v[118:121], v[142:145], v[166:169], v[118:121]
	v_mfma_f32_16x16x32_bf16 v[106:109], v[134:137], v[174:177], v[106:109]
	v_mfma_f32_16x16x32_bf16 v[102:105], v[142:145], v[174:177], v[102:105]
	v_mfma_f32_16x16x32_bf16 v[90:93], v[134:137], v[182:185], v[90:93]
	v_mfma_f32_16x16x32_bf16 v[86:89], v[142:145], v[182:185], v[86:89]
	v_mfma_f32_16x16x32_bf16 v[74:77], v[134:137], v[190:193], v[74:77]
	v_mfma_f32_16x16x32_bf16 v[70:73], v[142:145], v[190:193], v[70:73]
	v_mfma_f32_16x16x32_bf16 v[122:125], v[138:141], v[170:173], v[122:125]
	v_mfma_f32_16x16x32_bf16 v[118:121], v[146:149], v[170:173], v[118:121]
	v_mfma_f32_16x16x32_bf16 v[106:109], v[138:141], v[178:181], v[106:109]
	v_mfma_f32_16x16x32_bf16 v[102:105], v[146:149], v[178:181], v[102:105]
	v_mfma_f32_16x16x32_bf16 v[90:93], v[138:141], v[186:189], v[90:93]
	v_mfma_f32_16x16x32_bf16 v[86:89], v[146:149], v[186:189], v[86:89]
	v_mfma_f32_16x16x32_bf16 v[74:77], v[138:141], v[194:197], v[74:77]
	v_mfma_f32_16x16x32_bf16 v[70:73], v[146:149], v[194:197], v[70:73]
	s_barrier
	s_add_i32 s24, s45, s15
	v_lshl_add_u64 v[230:231], v[230:231], 0, s[2:3]
	s_mov_b32 m0, s24
	ds_read_b128 v[190:193], v234 offset:49152
	ds_read_b128 v[194:197], v234 offset:50176
	ds_read_b128 v[182:185], v234 offset:51200
	ds_read_b128 v[186:189], v234 offset:52224
	ds_read_b128 v[174:177], v234 offset:53248
	ds_read_b128 v[178:181], v234 offset:54272
	ds_read_b128 v[166:169], v234 offset:55296
	ds_read_b128 v[170:173], v234 offset:56320
	global_load_lds_dwordx4 v[230:231], off
	s_add_i32 m0, s24, 0x2000
	s_add_u32 s22, s22, 0x18080
	v_lshl_add_u64 v[230:231], v[232:233], 0, s[2:3]
	s_addc_u32 s23, s23, 0
	s_add_i32 s24, s46, s15
	global_load_lds_dwordx4 v[230:231], off
	v_lshl_add_u64 v[230:231], s[22:23], 0, v[200:201]
	s_mov_b32 m0, s24
	v_lshl_add_u64 v[4:5], v[4:5], 0, s[2:3]
	global_load_lds_dwordx4 v[230:231], off
	v_lshl_add_u64 v[230:231], s[22:23], 0, v[204:205]
	s_add_i32 m0, s24, 0x2000
	s_and_b64 vcc, exec, s[4:5]
	global_load_lds_dwordx4 v[230:231], off
	v_lshl_add_u64 v[230:231], v[236:237], 0, s[2:3]
	s_mov_b32 m0, s31
	s_nop 0
	global_load_lds_dwordx4 v[230:231], off
	s_mov_b32 m0, s33
	s_nop 0
	global_load_lds_dwordx4 v[4:5], off
	s_waitcnt vmcnt(8)
	s_waitcnt lgkmcnt(0)
	s_barrier
	s_cbranch_vccnz .LBB0_548
	s_waitcnt lgkmcnt(0)
	v_mfma_f32_16x16x32_bf16 v[66:69], v[150:153], v[190:193], v[66:69]
	v_mfma_f32_16x16x32_bf16 v[62:65], v[158:161], v[190:193], v[62:65]
	v_mfma_f32_16x16x32_bf16 v[50:53], v[150:153], v[182:185], v[50:53]
	v_mfma_f32_16x16x32_bf16 v[46:49], v[158:161], v[182:185], v[46:49]
	v_mfma_f32_16x16x32_bf16 v[34:37], v[150:153], v[174:177], v[34:37]
	v_mfma_f32_16x16x32_bf16 v[30:33], v[158:161], v[174:177], v[30:33]
	v_mfma_f32_16x16x32_bf16 v[18:21], v[150:153], v[166:169], v[18:21]
	v_mfma_f32_16x16x32_bf16 v[14:17], v[158:161], v[166:169], v[14:17]
	v_mfma_f32_16x16x32_bf16 v[66:69], v[154:157], v[194:197], v[66:69]
	v_mfma_f32_16x16x32_bf16 v[62:65], v[162:165], v[194:197], v[62:65]
	v_mfma_f32_16x16x32_bf16 v[50:53], v[154:157], v[186:189], v[50:53]
	v_mfma_f32_16x16x32_bf16 v[46:49], v[162:165], v[186:189], v[46:49]
	v_mfma_f32_16x16x32_bf16 v[34:37], v[154:157], v[178:181], v[34:37]
	v_mfma_f32_16x16x32_bf16 v[30:33], v[162:165], v[178:181], v[30:33]
	v_mfma_f32_16x16x32_bf16 v[18:21], v[154:157], v[170:173], v[18:21]
	v_mfma_f32_16x16x32_bf16 v[14:17], v[162:165], v[170:173], v[14:17]
	v_mfma_f32_16x16x32_bf16 v[58:61], v[134:137], v[190:193], v[58:61]
	v_mfma_f32_16x16x32_bf16 v[54:57], v[142:145], v[190:193], v[54:57]
	v_mfma_f32_16x16x32_bf16 v[42:45], v[134:137], v[182:185], v[42:45]
	v_mfma_f32_16x16x32_bf16 v[38:41], v[142:145], v[182:185], v[38:41]
	v_mfma_f32_16x16x32_bf16 v[26:29], v[134:137], v[174:177], v[26:29]
	v_mfma_f32_16x16x32_bf16 v[22:25], v[142:145], v[174:177], v[22:25]
	v_mfma_f32_16x16x32_bf16 v[10:13], v[134:137], v[166:169], v[10:13]
	v_mfma_f32_16x16x32_bf16 v[4:7], v[142:145], v[166:169], v[6:9]
	v_mfma_f32_16x16x32_bf16 v[58:61], v[138:141], v[194:197], v[58:61]
	v_mfma_f32_16x16x32_bf16 v[54:57], v[146:149], v[194:197], v[54:57]
	v_mfma_f32_16x16x32_bf16 v[42:45], v[138:141], v[186:189], v[42:45]
	v_mfma_f32_16x16x32_bf16 v[38:41], v[146:149], v[186:189], v[38:41]
	v_mfma_f32_16x16x32_bf16 v[26:29], v[138:141], v[178:181], v[26:29]
	v_mfma_f32_16x16x32_bf16 v[22:25], v[146:149], v[178:181], v[22:25]
	v_mfma_f32_16x16x32_bf16 v[10:13], v[138:141], v[170:173], v[10:13]
	v_mfma_f32_16x16x32_bf16 v[6:9], v[146:149], v[170:173], v[4:7]

; #define PG8_STAGE_B(bufoff, gbase) do { _Pragma("unroll") for (int _i = 0; _i < 2; ++_i) \
;         __builtin_amdgcn_global_load_lds((const unsigned*)((const char*)(gbase) + voffB[_i]), (LAS unsigned*)(lds + (bufoff) + ldsw + _i * 8192), 16, 0, 0); } while (0)
; #define PG8_STAGE_A(bufoff, V0, V1, kb) do { \
;         __builtin_amdgcn_global_load_lds((const unsigned*)((Abase + (kb)) + (V0)), (LAS unsigned*)(lds + (bufoff) + ldsw), 16, 0, 0); \
;         __builtin_amdgcn_global_load_lds((const unsigned*)((Abase + (kb)) + (V1)), (LAS unsigned*)(lds + (bufoff) + ldsw + 8192), 16, 0, 0); } while (0)
; #define PG8_LDA(dst, b, h) do { _Pragma("unroll") for (int m = 0; m < 4; ++m) _Pragma("unroll") for (int k = 0; k < 2; ++k) dst[m][k] = *(const LAS bf16x8*)(lds + PG8_SA(b, h) + aoff + m * 2048 + k * 1024); } while (0)
; #define PG8_LDB(dst, b, h) do { _Pragma("unroll") for (int n = 0; n < 2; ++n) _Pragma("unroll") for (int k = 0; k < 2; ++k) dst[n][k] = *(const LAS bf16x8*)(lds + PG8_SB(b, h) + boff + n * 2048 + k * 1024); } while (0)
; #define PG8_MMA(ai, bj, At, Bt) do { __builtin_amdgcn_s_setprio(1); _Pragma("unroll") for (int m = 0; m < 4; ++m) _Pragma("unroll") for (int n = 0; n < 2; ++n) _Pragma("unroll") for (int k = 0; k < 2; ++k) \
;         acc[ai][bj][m][n] = __builtin_amdgcn_mfma_f32_16x16x32_bf16(Bt[n][k], At[m][k], acc[ai][bj][m][n], 0, 0, 0); __builtin_amdgcn_s_setprio(0); } while (0)
; #define PG8_WAIT_V(n) asm volatile("s_waitcnt vmcnt(" #n ")" ::: "memory")
; #define PG8_WAIT_L(n) asm volatile("s_waitcnt lgkmcnt(" #n ")" ::: "memory")
; #define PG8_BAR __builtin_amdgcn_s_barrier()
; #define PG8_SCHED __builtin_amdgcn_sched_barrier(0)
; template <class Epi, class Sched, bool ALIGN_EPI>
; __device__ __forceinline__ void gemm_phase(LAS unsigned char* lds, const Gemm g, const Sched& S, const Epi& E) {
;     ...
;             PG8_LDB(B0, 0, 0); PG8_LDB(B1, 0, 1); PG8_SCHED; PG8_LDA(At, 0, 0); PG8_STAGE_A(PG8_SA(1, 1), vc10, vc11, kb1);
;             PG8_WAIT_V(8); PG8_WAIT_L(0); PG8_BAR; PG8_MMA(0, 0, At, B0); PG8_MMA(0, 1, At, B1); PG8_BAR; PG8_SCHED;
;             PG8_LDA(At, 0, 1); PG8_STAGE_B(PG8_SB(0, 0), b2); PG8_STAGE_B(PG8_SB(0, 1), b2 + hstepB); PG8_STAGE_A(PG8_SA(0, 0), s00, s01, kb2);
;             PG8_WAIT_V(8); PG8_WAIT_L(0); PG8_BAR; if (half1) { PG8_MMA(1, 0, At, B0); PG8_MMA(1, 1, At, B1); } PG8_BAR; PG8_SCHED;
.LBB0_611:
	v_add_u32_e32 v5, s49, v219
	ds_read_b128 v[150:153], v5
	ds_read_b128 v[154:157], v5 offset:1024
	ds_read_b128 v[158:161], v5 offset:2048
	ds_read_b128 v[162:165], v5 offset:3072
	v_add_u32_e32 v5, s50, v219
	ds_read_b128 v[134:137], v5
	ds_read_b128 v[138:141], v5 offset:1024
	ds_read_b128 v[142:145], v5 offset:2048
	ds_read_b128 v[146:149], v5 offset:3072
	v_lshl_add_u64 v[210:211], v[208:209], 0, s[4:5]
	s_add_i32 m0, s40, 0xc000
	s_waitcnt lgkmcnt(0)
	ds_read_b128 v[166:169], v227
	ds_read_b128 v[170:173], v227 offset:1024
	ds_read_b128 v[174:177], v227 offset:2048
	ds_read_b128 v[178:181], v227 offset:3072
	ds_read_b128 v[182:185], v227 offset:4096
	ds_read_b128 v[186:189], v227 offset:5120
	ds_read_b128 v[190:193], v227 offset:6144
	ds_read_b128 v[194:197], v227 offset:7168
	global_load_lds_dwordx4 v[210:211], off
	v_lshl_add_u64 v[210:211], v[206:207], 0, s[4:5]
	s_add_i32 m0, s40, 0xe000
	s_nop 0
	global_load_lds_dwordx4 v[210:211], off
	s_waitcnt vmcnt(8)
	s_waitcnt lgkmcnt(0)
	s_barrier
	s_waitcnt lgkmcnt(0)
	v_mfma_f32_16x16x32_bf16 v[130:133], v[150:153], v[166:169], v[130:133]
	v_mfma_f32_16x16x32_bf16 v[126:129], v[158:161], v[166:169], v[126:129]
	v_mfma_f32_16x16x32_bf16 v[114:117], v[150:153], v[174:177], v[114:117]
	v_mfma_f32_16x16x32_bf16 v[110:113], v[158:161], v[174:177], v[110:113]
	v_mfma_f32_16x16x32_bf16 v[98:101], v[150:153], v[182:185], v[98:101]
	v_mfma_f32_16x16x32_bf16 v[94:97], v[158:161], v[182:185], v[94:97]
	v_mfma_f32_16x16x32_bf16 v[82:85], v[150:153], v[190:193], v[82:85]
	v_mfma_f32_16x16x32_bf16 v[78:81], v[158:161], v[190:193], v[78:81]
	v_mfma_f32_16x16x32_bf16 v[130:133], v[154:157], v[170:173], v[130:133]
	v_mfma_f32_16x16x32_bf16 v[126:129], v[162:165], v[170:173], v[126:129]
	v_mfma_f32_16x16x32_bf16 v[114:117], v[154:157], v[178:181], v[114:117]
	v_mfma_f32_16x16x32_bf16 v[110:113], v[162:165], v[178:181], v[110:113]
	v_mfma_f32_16x16x32_bf16 v[98:101], v[154:157], v[186:189], v[98:101]
	v_mfma_f32_16x16x32_bf16 v[94:97], v[162:165], v[186:189], v[94:97]
	v_mfma_f32_16x16x32_bf16 v[82:85], v[154:157], v[194:197], v[82:85]
	v_mfma_f32_16x16x32_bf16 v[78:81], v[162:165], v[194:197], v[78:81]
	v_mfma_f32_16x16x32_bf16 v[122:125], v[134:137], v[166:169], v[122:125]
	v_mfma_f32_16x16x32_bf16 v[118:121], v[142:145], v[166:169], v[118:121]
	v_mfma_f32_16x16x32_bf16 v[106:109], v[134:137], v[174:177], v[106:109]
	v_mfma_f32_16x16x32_bf16 v[102:105], v[142:145], v[174:177], v[102:105]
	v_mfma_f32_16x16x32_bf16 v[90:93], v[134:137], v[182:185], v[90:93]
	v_mfma_f32_16x16x32_bf16 v[86:89], v[142:145], v[182:185], v[86:89]
	v_mfma_f32_16x16x32_bf16 v[74:77], v[134:137], v[190:193], v[74:77]
	v_mfma_f32_16x16x32_bf16 v[70:73], v[142:145], v[190:193], v[70:73]
	v_mfma_f32_16x16x32_bf16 v[122:125], v[138:141], v[170:173], v[122:125]
	v_mfma_f32_16x16x32_bf16 v[118:121], v[146:149], v[170:173], v[118:121]
	v_mfma_f32_16x16x32_bf16 v[106:109], v[138:141], v[178:181], v[106:109]
	v_mfma_f32_16x16x32_bf16 v[102:105], v[146:149], v[178:181], v[102:105]
	v_mfma_f32_16x16x32_bf16 v[90:93], v[138:141], v[186:189], v[90:93]
	v_mfma_f32_16x16x32_bf16 v[86:89], v[146:149], v[186:189], v[86:89]
	v_mfma_f32_16x16x32_bf16 v[74:77], v[138:141], v[194:197], v[74:77]
	v_mfma_f32_16x16x32_bf16 v[70:73], v[146:149], v[194:197], v[70:73]
	s_barrier
	s_add_i32 s4, s49, s39
	v_lshl_add_u64 v[210:211], s[30:31], 0, v[198:199]
	s_mov_b32 m0, s4
	ds_read_b128 v[190:193], v227 offset:16384
	ds_read_b128 v[194:197], v227 offset:17408
	ds_read_b128 v[182:185], v227 offset:18432
	ds_read_b128 v[186:189], v227 offset:19456
	ds_read_b128 v[174:177], v227 offset:20480
	ds_read_b128 v[178:181], v227 offset:21504
	ds_read_b128 v[166:169], v227 offset:22528
	ds_read_b128 v[170:173], v227 offset:23552
	global_load_lds_dwordx4 v[210:211], off
	s_add_i32 m0, s4, 0x2000
	s_add_u32 s4, s30, 0x40000
	v_lshl_add_u64 v[212:213], s[30:31], 0, v[200:201]
	s_addc_u32 s5, s31, 0
	s_add_i32 s37, s50, s39
	global_load_lds_dwordx4 v[212:213], off
	v_lshl_add_u64 v[234:235], s[4:5], 0, v[198:199]
	s_mov_b32 m0, s37
	v_cndmask_b32_e64 v5, 0, 1, s[6:7]
	global_load_lds_dwordx4 v[234:235], off
	v_lshl_add_u64 v[234:235], s[4:5], 0, v[200:201]
	s_add_i32 m0, s37, 0x2000
	v_readlane_b32 s4, v253, 52
	v_readlane_b32 s5, v253, 53
	s_add_u32 s36, s4, s36
	global_load_lds_dwordx4 v[234:235], off
	s_addc_u32 s37, s5, 0
	s_mov_b32 m0, s40
	v_cmp_ne_u32_e64 s[4:5], 1, v5
	global_load_lds_dwordx4 v2, s[36:37]
	s_mov_b32 m0, s41
	s_andn2_b64 vcc, exec, s[6:7]
	global_load_lds_dwordx4 v4, s[36:37]
	s_waitcnt vmcnt(8)
	s_waitcnt lgkmcnt(0)
	s_barrier
	s_cbranch_vccnz .LBB0_613
	s_waitcnt lgkmcnt(0)
	v_mfma_f32_16x16x32_bf16 v[66:69], v[150:153], v[190:193], v[66:69]
	v_mfma_f32_16x16x32_bf16 v[62:65], v[158:161], v[190:193], v[62:65]
	v_mfma_f32_16x16x32_bf16 v[50:53], v[150:153], v[182:185], v[50:53]
	v_mfma_f32_16x16x32_bf16 v[46:49], v[158:161], v[182:185], v[46:49]
	v_mfma_f32_16x16x32_bf16 v[34:37], v[150:153], v[174:177], v[34:37]
	v_mfma_f32_16x16x32_bf16 v[30:33], v[158:161], v[174:177], v[30:33]
	v_mfma_f32_16x16x32_bf16 v[18:21], v[150:153], v[166:169], v[18:21]
	v_mfma_f32_16x16x32_bf16 v[14:17], v[158:161], v[166:169], v[14:17]
	v_mfma_f32_16x16x32_bf16 v[66:69], v[154:157], v[194:197], v[66:69]
	v_mfma_f32_16x16x32_bf16 v[62:65], v[162:165], v[194:197], v[62:65]
	v_mfma_f32_16x16x32_bf16 v[50:53], v[154:157], v[186:189], v[50:53]
	v_mfma_f32_16x16x32_bf16 v[46:49], v[162:165], v[186:189], v[46:49]
	v_mfma_f32_16x16x32_bf16 v[34:37], v[154:157], v[178:181], v[34:37]
	v_mfma_f32_16x16x32_bf16 v[30:33], v[162:165], v[178:181], v[30:33]
	v_mfma_f32_16x16x32_bf16 v[18:21], v[154:157], v[170:173], v[18:21]
	v_mfma_f32_16x16x32_bf16 v[14:17], v[162:165], v[170:173], v[14:17]
	v_mfma_f32_16x16x32_bf16 v[58:61], v[134:137], v[190:193], v[58:61]
	v_mfma_f32_16x16x32_bf16 v[54:57], v[142:145], v[190:193], v[54:57]
	v_mfma_f32_16x16x32_bf16 v[42:45], v[134:137], v[182:185], v[42:45]
	v_mfma_f32_16x16x32_bf16 v[38:41], v[142:145], v[182:185], v[38:41]
	v_mfma_f32_16x16x32_bf16 v[26:29], v[134:137], v[174:177], v[26:29]
	v_mfma_f32_16x16x32_bf16 v[22:25], v[142:145], v[174:177], v[22:25]
	v_mfma_f32_16x16x32_bf16 v[10:13], v[134:137], v[166:169], v[10:13]
	v_mfma_f32_16x16x32_bf16 v[6:9], v[142:145], v[166:169], v[6:9]
	v_mfma_f32_16x16x32_bf16 v[58:61], v[138:141], v[194:197], v[58:61]
	v_mfma_f32_16x16x32_bf16 v[54:57], v[146:149], v[194:197], v[54:57]
	v_mfma_f32_16x16x32_bf16 v[42:45], v[138:141], v[186:189], v[42:45]
	v_mfma_f32_16x16x32_bf16 v[38:41], v[146:149], v[186:189], v[38:41]
	v_mfma_f32_16x16x32_bf16 v[26:29], v[138:141], v[178:181], v[26:29]
	v_mfma_f32_16x16x32_bf16 v[22:25], v[146:149], v[178:181], v[22:25]
	v_mfma_f32_16x16x32_bf16 v[10:13], v[138:141], v[170:173], v[10:13]
	v_mfma_f32_16x16x32_bf16 v[6:9], v[146:149], v[170:173], v[6:9]
; #define PG8_STAGE_B(bufoff, gbase) do { _Pragma("unroll") for (int _i = 0; _i < 2; ++_i) \
;         __builtin_amdgcn_global_load_lds((const unsigned*)((const char*)(gbase) + voffB[_i]), (LAS unsigned*)(lds + (bufoff) + ldsw + _i * 8192), 16, 0, 0); } while (0)
; #define PG8_STAGE_A(bufoff, V0, V1, kb) do { \
;         __builtin_amdgcn_global_load_lds((const unsigned*)((Abase + (kb)) + (V0)), (LAS unsigned*)(lds + (bufoff) + ldsw), 16, 0, 0); \
;         __builtin_amdgcn_global_load_lds((const unsigned*)((Abase + (kb)) + (V1)), (LAS unsigned*)(lds + (bufoff) + ldsw + 8192), 16, 0, 0); } while (0)
; #define PG8_LDA(dst, b, h) do { _Pragma("unroll") for (int m = 0; m < 4; ++m) _Pragma("unroll") for (int k = 0; k < 2; ++k) dst[m][k] = *(const LAS bf16x8*)(lds + PG8_SA(b, h) + aoff + m * 2048 + k * 1024); } while (0)
; #define PG8_LDB(dst, b, h) do { _Pragma("unroll") for (int n = 0; n < 2; ++n) _Pragma("unroll") for (int k = 0; k < 2; ++k) dst[n][k] = *(const LAS bf16x8*)(lds + PG8_SB(b, h) + boff + n * 2048 + k * 1024); } while (0)
; #define PG8_MMA(ai, bj, At, Bt) do { __builtin_amdgcn_s_setprio(1); _Pragma("unroll") for (int m = 0; m < 4; ++m) _Pragma("unroll") for (int n = 0; n < 2; ++n) _Pragma("unroll") for (int k = 0; k < 2; ++k) \
;         acc[ai][bj][m][n] = __builtin_amdgcn_mfma_f32_16x16x32_bf16(Bt[n][k], At[m][k], acc[ai][bj][m][n], 0, 0, 0); __builtin_amdgcn_s_setprio(0); } while (0)
; #define PG8_WAIT_V(n) asm volatile("s_waitcnt vmcnt(" #n ")" ::: "memory")
; #define PG8_WAIT_L(n) asm volatile("s_waitcnt lgkmcnt(" #n ")" ::: "memory")
; #define PG8_BAR __builtin_amdgcn_s_barrier()
; #define PG8_SCHED __builtin_amdgcn_sched_barrier(0)
; template <class Epi, class Sched, bool ALIGN_EPI>
; __device__ __forceinline__ void gemm_phase(LAS unsigned char* lds, const Gemm g, const Sched& S, const Epi& E) {
;     ...
;             PG8_LDB(B0, 1, 0); PG8_LDB(B1, 1, 1); PG8_SCHED; PG8_LDA(At, 1, 0); PG8_STAGE_A(PG8_SA(0, 1), s10, s11, kb2);
;             PG8_WAIT_V(8); PG8_WAIT_L(0); PG8_BAR; PG8_MMA(0, 0, At, B0); PG8_MMA(0, 1, At, B1); PG8_BAR; PG8_SCHED;
;             PG8_LDA(At, 1, 1); PG8_STAGE_B(PG8_SB(1, 0), b3); PG8_STAGE_B(PG8_SB(1, 1), b3 + hstepB); PG8_STAGE_A(PG8_SA(1, 0), s00, s01, kb3);
;             PG8_WAIT_V(8); PG8_WAIT_L(0); PG8_BAR; if (half1) { PG8_MMA(1, 0, At, B0); PG8_MMA(1, 1, At, B1); } PG8_BAR; PG8_SCHED;
.LBB0_613:
	v_mov_b32_e32 v5, v3
	v_lshl_add_u64 v[234:235], s[36:37], 0, v[2:3]
	v_lshl_add_u64 v[4:5], s[36:37], 0, v[4:5]
	s_barrier
	v_add_u32_e32 v2, s51, v219
	ds_read_b128 v[150:153], v2
	ds_read_b128 v[154:157], v2 offset:1024
	ds_read_b128 v[158:161], v2 offset:2048
	ds_read_b128 v[162:165], v2 offset:3072
	v_add_u32_e32 v2, s52, v219
	ds_read_b128 v[134:137], v2
	ds_read_b128 v[138:141], v2 offset:1024
	ds_read_b128 v[142:145], v2 offset:2048
	ds_read_b128 v[146:149], v2 offset:3072
	s_mov_b32 m0, s42
	s_waitcnt lgkmcnt(0)
	ds_read_b128 v[166:169], v227 offset:32768
	ds_read_b128 v[170:173], v227 offset:33792
	ds_read_b128 v[174:177], v227 offset:34816
	ds_read_b128 v[178:181], v227 offset:35840
	ds_read_b128 v[182:185], v227 offset:36864
	ds_read_b128 v[186:189], v227 offset:37888
	ds_read_b128 v[190:193], v227 offset:38912
	ds_read_b128 v[194:197], v227 offset:39936
	global_load_lds_dwordx4 v203, s[36:37]
	s_mov_b32 m0, s43
	s_nop 0
	global_load_lds_dwordx4 v205, s[36:37]
	s_waitcnt vmcnt(8)
	s_waitcnt lgkmcnt(0)
	s_barrier
	s_waitcnt lgkmcnt(0)
	v_mfma_f32_16x16x32_bf16 v[130:133], v[150:153], v[166:169], v[130:133]
	v_mfma_f32_16x16x32_bf16 v[126:129], v[158:161], v[166:169], v[126:129]
	v_mfma_f32_16x16x32_bf16 v[114:117], v[150:153], v[174:177], v[114:117]
	v_mfma_f32_16x16x32_bf16 v[110:113], v[158:161], v[174:177], v[110:113]
	v_mfma_f32_16x16x32_bf16 v[98:101], v[150:153], v[182:185], v[98:101]
	v_mfma_f32_16x16x32_bf16 v[94:97], v[158:161], v[182:185], v[94:97]
	v_mfma_f32_16x16x32_bf16 v[82:85], v[150:153], v[190:193], v[82:85]
	v_mfma_f32_16x16x32_bf16 v[78:81], v[158:161], v[190:193], v[78:81]
	v_mfma_f32_16x16x32_bf16 v[130:133], v[154:157], v[170:173], v[130:133]
	v_mfma_f32_16x16x32_bf16 v[126:129], v[162:165], v[170:173], v[126:129]
	v_mfma_f32_16x16x32_bf16 v[114:117], v[154:157], v[178:181], v[114:117]
	v_mfma_f32_16x16x32_bf16 v[110:113], v[162:165], v[178:181], v[110:113]
	v_mfma_f32_16x16x32_bf16 v[98:101], v[154:157], v[186:189], v[98:101]
	v_mfma_f32_16x16x32_bf16 v[94:97], v[162:165], v[186:189], v[94:97]
	v_mfma_f32_16x16x32_bf16 v[82:85], v[154:157], v[194:197], v[82:85]
	v_mfma_f32_16x16x32_bf16 v[78:81], v[162:165], v[194:197], v[78:81]
	v_mfma_f32_16x16x32_bf16 v[122:125], v[134:137], v[166:169], v[122:125]
	v_mfma_f32_16x16x32_bf16 v[118:121], v[142:145], v[166:169], v[118:121]
	v_mfma_f32_16x16x32_bf16 v[106:109], v[134:137], v[174:177], v[106:109]
	v_mfma_f32_16x16x32_bf16 v[102:105], v[142:145], v[174:177], v[102:105]
	v_mfma_f32_16x16x32_bf16 v[90:93], v[134:137], v[182:185], v[90:93]
	v_mfma_f32_16x16x32_bf16 v[86:89], v[142:145], v[182:185], v[86:89]
	v_mfma_f32_16x16x32_bf16 v[74:77], v[134:137], v[190:193], v[74:77]
	v_mfma_f32_16x16x32_bf16 v[70:73], v[142:145], v[190:193], v[70:73]
	v_mfma_f32_16x16x32_bf16 v[122:125], v[138:141], v[170:173], v[122:125]
	v_mfma_f32_16x16x32_bf16 v[118:121], v[146:149], v[170:173], v[118:121]
	v_mfma_f32_16x16x32_bf16 v[106:109], v[138:141], v[178:181], v[106:109]
	v_mfma_f32_16x16x32_bf16 v[102:105], v[146:149], v[178:181], v[102:105]
	v_mfma_f32_16x16x32_bf16 v[90:93], v[138:141], v[186:189], v[90:93]
	v_mfma_f32_16x16x32_bf16 v[86:89], v[146:149], v[186:189], v[86:89]
	v_mfma_f32_16x16x32_bf16 v[74:77], v[138:141], v[194:197], v[74:77]
	v_mfma_f32_16x16x32_bf16 v[70:73], v[146:149], v[194:197], v[70:73]
	s_barrier
	s_add_i32 s36, s51, s39
	v_lshl_add_u64 v[210:211], v[210:211], 0, s[16:17]
	s_mov_b32 m0, s36
	ds_read_b128 v[190:193], v227 offset:49152
	ds_read_b128 v[194:197], v227 offset:50176
	ds_read_b128 v[182:185], v227 offset:51200
	ds_read_b128 v[186:189], v227 offset:52224
	ds_read_b128 v[174:177], v227 offset:53248
	ds_read_b128 v[178:181], v227 offset:54272
	ds_read_b128 v[166:169], v227 offset:55296
	ds_read_b128 v[170:173], v227 offset:56320
	global_load_lds_dwordx4 v[210:211], off
	s_add_i32 m0, s36, 0x2000
	s_add_u32 s30, s30, 0x40080
	v_lshl_add_u64 v[210:211], v[212:213], 0, s[16:17]
	s_addc_u32 s31, s31, 0
	s_add_i32 s36, s52, s39
	global_load_lds_dwordx4 v[210:211], off
	v_lshl_add_u64 v[210:211], s[30:31], 0, v[198:199]
	s_mov_b32 m0, s36
	v_lshl_add_u64 v[4:5], v[4:5], 0, s[16:17]
	global_load_lds_dwordx4 v[210:211], off
	v_lshl_add_u64 v[210:211], s[30:31], 0, v[200:201]
	s_add_i32 m0, s36, 0x2000
	s_and_b64 vcc, exec, s[4:5]
	global_load_lds_dwordx4 v[210:211], off
	v_lshl_add_u64 v[210:211], v[234:235], 0, s[16:17]
	s_mov_b32 m0, s44
	s_nop 0
	global_load_lds_dwordx4 v[210:211], off
	s_mov_b32 m0, s45
	s_nop 0
	global_load_lds_dwordx4 v[4:5], off
	s_waitcnt vmcnt(8)
	s_waitcnt lgkmcnt(0)
	s_barrier
	s_cbranch_vccnz .LBB0_615
	s_waitcnt lgkmcnt(0)
	v_mfma_f32_16x16x32_bf16 v[66:69], v[150:153], v[190:193], v[66:69]
	v_mfma_f32_16x16x32_bf16 v[62:65], v[158:161], v[190:193], v[62:65]
	v_mfma_f32_16x16x32_bf16 v[50:53], v[150:153], v[182:185], v[50:53]
	v_mfma_f32_16x16x32_bf16 v[46:49], v[158:161], v[182:185], v[46:49]
	v_mfma_f32_16x16x32_bf16 v[34:37], v[150:153], v[174:177], v[34:37]
	v_mfma_f32_16x16x32_bf16 v[30:33], v[158:161], v[174:177], v[30:33]
	v_mfma_f32_16x16x32_bf16 v[18:21], v[150:153], v[166:169], v[18:21]
	v_mfma_f32_16x16x32_bf16 v[14:17], v[158:161], v[166:169], v[14:17]
	v_mfma_f32_16x16x32_bf16 v[66:69], v[154:157], v[194:197], v[66:69]
	v_mfma_f32_16x16x32_bf16 v[62:65], v[162:165], v[194:197], v[62:65]
	v_mfma_f32_16x16x32_bf16 v[50:53], v[154:157], v[186:189], v[50:53]
	v_mfma_f32_16x16x32_bf16 v[46:49], v[162:165], v[186:189], v[46:49]
	v_mfma_f32_16x16x32_bf16 v[34:37], v[154:157], v[178:181], v[34:37]
	v_mfma_f32_16x16x32_bf16 v[30:33], v[162:165], v[178:181], v[30:33]
	v_mfma_f32_16x16x32_bf16 v[18:21], v[154:157], v[170:173], v[18:21]
	v_mfma_f32_16x16x32_bf16 v[14:17], v[162:165], v[170:173], v[14:17]
	v_mfma_f32_16x16x32_bf16 v[58:61], v[134:137], v[190:193], v[58:61]
	v_mfma_f32_16x16x32_bf16 v[54:57], v[142:145], v[190:193], v[54:57]
	v_mfma_f32_16x16x32_bf16 v[42:45], v[134:137], v[182:185], v[42:45]
	v_mfma_f32_16x16x32_bf16 v[38:41], v[142:145], v[182:185], v[38:41]
	v_mfma_f32_16x16x32_bf16 v[26:29], v[134:137], v[174:177], v[26:29]
	v_mfma_f32_16x16x32_bf16 v[22:25], v[142:145], v[174:177], v[22:25]
	v_mfma_f32_16x16x32_bf16 v[10:13], v[134:137], v[166:169], v[10:13]
	v_mfma_f32_16x16x32_bf16 v[4:7], v[142:145], v[166:169], v[6:9]
	v_mfma_f32_16x16x32_bf16 v[58:61], v[138:141], v[194:197], v[58:61]
	v_mfma_f32_16x16x32_bf16 v[54:57], v[146:149], v[194:197], v[54:57]
	v_mfma_f32_16x16x32_bf16 v[42:45], v[138:141], v[186:189], v[42:45]
	v_mfma_f32_16x16x32_bf16 v[38:41], v[146:149], v[186:189], v[38:41]
	v_mfma_f32_16x16x32_bf16 v[26:29], v[138:141], v[178:181], v[26:29]
	v_mfma_f32_16x16x32_bf16 v[22:25], v[146:149], v[178:181], v[22:25]
	v_mfma_f32_16x16x32_bf16 v[10:13], v[138:141], v[170:173], v[10:13]
	v_mfma_f32_16x16x32_bf16 v[6:9], v[146:149], v[170:173], v[4:7]

; #define PG8_STAGE_B(bufoff, gbase) do { _Pragma("unroll") for (int _i = 0; _i < 2; ++_i) \
;         __builtin_amdgcn_global_load_lds((const unsigned*)((const char*)(gbase) + voffB[_i]), (LAS unsigned*)(lds + (bufoff) + ldsw + _i * 8192), 16, 0, 0); } while (0)
; #define PG8_STAGE_A(bufoff, V0, V1, kb) do { \
;         __builtin_amdgcn_global_load_lds((const unsigned*)((Abase + (kb)) + (V0)), (LAS unsigned*)(lds + (bufoff) + ldsw), 16, 0, 0); \
;         __builtin_amdgcn_global_load_lds((const unsigned*)((Abase + (kb)) + (V1)), (LAS unsigned*)(lds + (bufoff) + ldsw + 8192), 16, 0, 0); } while (0)
; #define PG8_LDA(dst, b, h) do { _Pragma("unroll") for (int m = 0; m < 4; ++m) _Pragma("unroll") for (int k = 0; k < 2; ++k) dst[m][k] = *(const LAS bf16x8*)(lds + PG8_SA(b, h) + aoff + m * 2048 + k * 1024); } while (0)
; #define PG8_LDB(dst, b, h) do { _Pragma("unroll") for (int n = 0; n < 2; ++n) _Pragma("unroll") for (int k = 0; k < 2; ++k) dst[n][k] = *(const LAS bf16x8*)(lds + PG8_SB(b, h) + boff + n * 2048 + k * 1024); } while (0)
; #define PG8_MMA(ai, bj, At, Bt) do { __builtin_amdgcn_s_setprio(1); _Pragma("unroll") for (int m = 0; m < 4; ++m) _Pragma("unroll") for (int n = 0; n < 2; ++n) _Pragma("unroll") for (int k = 0; k < 2; ++k) \
;         acc[ai][bj][m][n] = __builtin_amdgcn_mfma_f32_16x16x32_bf16(Bt[n][k], At[m][k], acc[ai][bj][m][n], 0, 0, 0); __builtin_amdgcn_s_setprio(0); } while (0)
; #define PG8_WAIT_V(n) asm volatile("s_waitcnt vmcnt(" #n ")" ::: "memory")
; #define PG8_WAIT_L(n) asm volatile("s_waitcnt lgkmcnt(" #n ")" ::: "memory")
; #define PG8_BAR __builtin_amdgcn_s_barrier()
; #define PG8_SCHED __builtin_amdgcn_sched_barrier(0)
; template <class Epi, class Sched, bool ALIGN_EPI>
; __device__ __forceinline__ void gemm_phase(LAS unsigned char* lds, const Gemm g, const Sched& S, const Epi& E) {
;     ...
;             PG8_LDB(B0, 0, 0); PG8_LDB(B1, 0, 1); PG8_SCHED; PG8_LDA(At, 0, 0); PG8_STAGE_A(PG8_SA(1, 1), vc10, vc11, kb1);
;             PG8_WAIT_V(8); PG8_WAIT_L(0); PG8_BAR; PG8_MMA(0, 0, At, B0); PG8_MMA(0, 1, At, B1); PG8_BAR; PG8_SCHED;
;             PG8_LDA(At, 0, 1); PG8_STAGE_B(PG8_SB(0, 0), b2); PG8_STAGE_B(PG8_SB(0, 1), b2 + hstepB); PG8_STAGE_A(PG8_SA(0, 0), s00, s01, kb2);
;             PG8_WAIT_V(8); PG8_WAIT_L(0); PG8_BAR; if (half1) { PG8_MMA(1, 0, At, B0); PG8_MMA(1, 1, At, B1); } PG8_BAR; PG8_SCHED;
.LBB0_1142:
	v_add_u32_e32 v5, s48, v227
	ds_read_b128 v[150:153], v5
	ds_read_b128 v[154:157], v5 offset:1024
	ds_read_b128 v[158:161], v5 offset:2048
	ds_read_b128 v[162:165], v5 offset:3072
	v_add_u32_e32 v5, s49, v227
	ds_read_b128 v[134:137], v5
	ds_read_b128 v[138:141], v5 offset:1024
	ds_read_b128 v[142:145], v5 offset:2048
	ds_read_b128 v[146:149], v5 offset:3072
	v_lshl_add_u64 v[218:219], v[216:217], 0, s[4:5]
	s_add_i32 m0, s35, 0xc000
	s_waitcnt lgkmcnt(0)
	ds_read_b128 v[166:169], v229
	ds_read_b128 v[170:173], v229 offset:1024
	ds_read_b128 v[174:177], v229 offset:2048
	ds_read_b128 v[178:181], v229 offset:3072
	ds_read_b128 v[182:185], v229 offset:4096
	ds_read_b128 v[186:189], v229 offset:5120
	ds_read_b128 v[190:193], v229 offset:6144
	ds_read_b128 v[194:197], v229 offset:7168
	global_load_lds_dwordx4 v[218:219], off
	v_lshl_add_u64 v[218:219], v[214:215], 0, s[4:5]
	s_add_i32 m0, s35, 0xe000
	s_nop 0
	global_load_lds_dwordx4 v[218:219], off
	s_waitcnt vmcnt(8)
	s_waitcnt lgkmcnt(0)
	s_barrier
	s_waitcnt lgkmcnt(0)
	v_mfma_f32_16x16x32_bf16 v[130:133], v[150:153], v[166:169], v[130:133]
	v_mfma_f32_16x16x32_bf16 v[126:129], v[158:161], v[166:169], v[126:129]
	v_mfma_f32_16x16x32_bf16 v[114:117], v[150:153], v[174:177], v[114:117]
	v_mfma_f32_16x16x32_bf16 v[110:113], v[158:161], v[174:177], v[110:113]
	v_mfma_f32_16x16x32_bf16 v[98:101], v[150:153], v[182:185], v[98:101]
	v_mfma_f32_16x16x32_bf16 v[94:97], v[158:161], v[182:185], v[94:97]
	v_mfma_f32_16x16x32_bf16 v[82:85], v[150:153], v[190:193], v[82:85]
	v_mfma_f32_16x16x32_bf16 v[78:81], v[158:161], v[190:193], v[78:81]
	v_mfma_f32_16x16x32_bf16 v[130:133], v[154:157], v[170:173], v[130:133]
	v_mfma_f32_16x16x32_bf16 v[126:129], v[162:165], v[170:173], v[126:129]
	v_mfma_f32_16x16x32_bf16 v[114:117], v[154:157], v[178:181], v[114:117]
	v_mfma_f32_16x16x32_bf16 v[110:113], v[162:165], v[178:181], v[110:113]
	v_mfma_f32_16x16x32_bf16 v[98:101], v[154:157], v[186:189], v[98:101]
	v_mfma_f32_16x16x32_bf16 v[94:97], v[162:165], v[186:189], v[94:97]
	v_mfma_f32_16x16x32_bf16 v[82:85], v[154:157], v[194:197], v[82:85]
	v_mfma_f32_16x16x32_bf16 v[78:81], v[162:165], v[194:197], v[78:81]
	v_mfma_f32_16x16x32_bf16 v[122:125], v[134:137], v[166:169], v[122:125]
	v_mfma_f32_16x16x32_bf16 v[118:121], v[142:145], v[166:169], v[118:121]
	v_mfma_f32_16x16x32_bf16 v[106:109], v[134:137], v[174:177], v[106:109]
	v_mfma_f32_16x16x32_bf16 v[102:105], v[142:145], v[174:177], v[102:105]
	v_mfma_f32_16x16x32_bf16 v[90:93], v[134:137], v[182:185], v[90:93]
	v_mfma_f32_16x16x32_bf16 v[86:89], v[142:145], v[182:185], v[86:89]
	v_mfma_f32_16x16x32_bf16 v[74:77], v[134:137], v[190:193], v[74:77]
	v_mfma_f32_16x16x32_bf16 v[70:73], v[142:145], v[190:193], v[70:73]
	v_mfma_f32_16x16x32_bf16 v[122:125], v[138:141], v[170:173], v[122:125]
	v_mfma_f32_16x16x32_bf16 v[118:121], v[146:149], v[170:173], v[118:121]
	v_mfma_f32_16x16x32_bf16 v[106:109], v[138:141], v[178:181], v[106:109]
	v_mfma_f32_16x16x32_bf16 v[102:105], v[146:149], v[178:181], v[102:105]
	v_mfma_f32_16x16x32_bf16 v[90:93], v[138:141], v[186:189], v[90:93]
	v_mfma_f32_16x16x32_bf16 v[86:89], v[146:149], v[186:189], v[86:89]
	v_mfma_f32_16x16x32_bf16 v[74:77], v[138:141], v[194:197], v[74:77]
	v_mfma_f32_16x16x32_bf16 v[70:73], v[146:149], v[194:197], v[70:73]
	s_barrier
	s_add_i32 s4, s48, s34
	v_lshl_add_u64 v[218:219], s[28:29], 0, v[198:199]
	s_mov_b32 m0, s4
	ds_read_b128 v[190:193], v229 offset:16384
	ds_read_b128 v[194:197], v229 offset:17408
	ds_read_b128 v[182:185], v229 offset:18432
	ds_read_b128 v[186:189], v229 offset:19456
	ds_read_b128 v[174:177], v229 offset:20480
	ds_read_b128 v[178:181], v229 offset:21504
	ds_read_b128 v[166:169], v229 offset:22528
	ds_read_b128 v[170:173], v229 offset:23552
	global_load_lds_dwordx4 v[218:219], off
	s_add_i32 m0, s4, 0x2000
	s_add_u32 s4, s28, 0x40000
	v_lshl_add_u64 v[220:221], s[28:29], 0, v[200:201]
	s_addc_u32 s5, s29, 0
	s_add_i32 s31, s49, s34
	global_load_lds_dwordx4 v[220:221], off
	v_lshl_add_u64 v[236:237], s[4:5], 0, v[198:199]
	s_mov_b32 m0, s31
	v_cndmask_b32_e64 v5, 0, 1, s[24:25]
	global_load_lds_dwordx4 v[236:237], off
	v_lshl_add_u64 v[236:237], s[4:5], 0, v[200:201]
	s_add_i32 m0, s31, 0x2000
	v_readlane_b32 s4, v255, 11
	v_readlane_b32 s5, v255, 12
	s_add_u32 s30, s4, s30
	global_load_lds_dwordx4 v[236:237], off
	s_addc_u32 s31, s5, 0
	s_mov_b32 m0, s35
	v_cmp_ne_u32_e64 s[4:5], 1, v5
	global_load_lds_dwordx4 v2, s[30:31]
	s_mov_b32 m0, s36
	s_andn2_b64 vcc, exec, s[24:25]
	global_load_lds_dwordx4 v4, s[30:31]
	s_waitcnt vmcnt(8)
	s_waitcnt lgkmcnt(0)
	s_barrier
	s_cbranch_vccnz .LBB0_1144
	s_waitcnt lgkmcnt(0)
	v_mfma_f32_16x16x32_bf16 v[66:69], v[150:153], v[190:193], v[66:69]
	v_mfma_f32_16x16x32_bf16 v[62:65], v[158:161], v[190:193], v[62:65]
	v_mfma_f32_16x16x32_bf16 v[50:53], v[150:153], v[182:185], v[50:53]
	v_mfma_f32_16x16x32_bf16 v[46:49], v[158:161], v[182:185], v[46:49]
	v_mfma_f32_16x16x32_bf16 v[34:37], v[150:153], v[174:177], v[34:37]
	v_mfma_f32_16x16x32_bf16 v[30:33], v[158:161], v[174:177], v[30:33]
	v_mfma_f32_16x16x32_bf16 v[18:21], v[150:153], v[166:169], v[18:21]
	v_mfma_f32_16x16x32_bf16 v[14:17], v[158:161], v[166:169], v[14:17]
	v_mfma_f32_16x16x32_bf16 v[66:69], v[154:157], v[194:197], v[66:69]
	v_mfma_f32_16x16x32_bf16 v[62:65], v[162:165], v[194:197], v[62:65]
	v_mfma_f32_16x16x32_bf16 v[50:53], v[154:157], v[186:189], v[50:53]
	v_mfma_f32_16x16x32_bf16 v[46:49], v[162:165], v[186:189], v[46:49]
	v_mfma_f32_16x16x32_bf16 v[34:37], v[154:157], v[178:181], v[34:37]
	v_mfma_f32_16x16x32_bf16 v[30:33], v[162:165], v[178:181], v[30:33]
	v_mfma_f32_16x16x32_bf16 v[18:21], v[154:157], v[170:173], v[18:21]
	v_mfma_f32_16x16x32_bf16 v[14:17], v[162:165], v[170:173], v[14:17]
	v_mfma_f32_16x16x32_bf16 v[58:61], v[134:137], v[190:193], v[58:61]
	v_mfma_f32_16x16x32_bf16 v[54:57], v[142:145], v[190:193], v[54:57]
	v_mfma_f32_16x16x32_bf16 v[42:45], v[134:137], v[182:185], v[42:45]
	v_mfma_f32_16x16x32_bf16 v[38:41], v[142:145], v[182:185], v[38:41]
	v_mfma_f32_16x16x32_bf16 v[26:29], v[134:137], v[174:177], v[26:29]
	v_mfma_f32_16x16x32_bf16 v[22:25], v[142:145], v[174:177], v[22:25]
	v_mfma_f32_16x16x32_bf16 v[10:13], v[134:137], v[166:169], v[10:13]
	v_mfma_f32_16x16x32_bf16 v[6:9], v[142:145], v[166:169], v[6:9]
	v_mfma_f32_16x16x32_bf16 v[58:61], v[138:141], v[194:197], v[58:61]
	v_mfma_f32_16x16x32_bf16 v[54:57], v[146:149], v[194:197], v[54:57]
	v_mfma_f32_16x16x32_bf16 v[42:45], v[138:141], v[186:189], v[42:45]
	v_mfma_f32_16x16x32_bf16 v[38:41], v[146:149], v[186:189], v[38:41]
	v_mfma_f32_16x16x32_bf16 v[26:29], v[138:141], v[178:181], v[26:29]
	v_mfma_f32_16x16x32_bf16 v[22:25], v[146:149], v[178:181], v[22:25]
	v_mfma_f32_16x16x32_bf16 v[10:13], v[138:141], v[170:173], v[10:13]
	v_mfma_f32_16x16x32_bf16 v[6:9], v[146:149], v[170:173], v[6:9]
; #define PG8_STAGE_B(bufoff, gbase) do { _Pragma("unroll") for (int _i = 0; _i < 2; ++_i) \
;         __builtin_amdgcn_global_load_lds((const unsigned*)((const char*)(gbase) + voffB[_i]), (LAS unsigned*)(lds + (bufoff) + ldsw + _i * 8192), 16, 0, 0); } while (0)
; #define PG8_STAGE_A(bufoff, V0, V1, kb) do { \
;         __builtin_amdgcn_global_load_lds((const unsigned*)((Abase + (kb)) + (V0)), (LAS unsigned*)(lds + (bufoff) + ldsw), 16, 0, 0); \
;         __builtin_amdgcn_global_load_lds((const unsigned*)((Abase + (kb)) + (V1)), (LAS unsigned*)(lds + (bufoff) + ldsw + 8192), 16, 0, 0); } while (0)
; #define PG8_LDA(dst, b, h) do { _Pragma("unroll") for (int m = 0; m < 4; ++m) _Pragma("unroll") for (int k = 0; k < 2; ++k) dst[m][k] = *(const LAS bf16x8*)(lds + PG8_SA(b, h) + aoff + m * 2048 + k * 1024); } while (0)
; #define PG8_LDB(dst, b, h) do { _Pragma("unroll") for (int n = 0; n < 2; ++n) _Pragma("unroll") for (int k = 0; k < 2; ++k) dst[n][k] = *(const LAS bf16x8*)(lds + PG8_SB(b, h) + boff + n * 2048 + k * 1024); } while (0)
; #define PG8_MMA(ai, bj, At, Bt) do { __builtin_amdgcn_s_setprio(1); _Pragma("unroll") for (int m = 0; m < 4; ++m) _Pragma("unroll") for (int n = 0; n < 2; ++n) _Pragma("unroll") for (int k = 0; k < 2; ++k) \
;         acc[ai][bj][m][n] = __builtin_amdgcn_mfma_f32_16x16x32_bf16(Bt[n][k], At[m][k], acc[ai][bj][m][n], 0, 0, 0); __builtin_amdgcn_s_setprio(0); } while (0)
; #define PG8_WAIT_V(n) asm volatile("s_waitcnt vmcnt(" #n ")" ::: "memory")
; #define PG8_WAIT_L(n) asm volatile("s_waitcnt lgkmcnt(" #n ")" ::: "memory")
; #define PG8_BAR __builtin_amdgcn_s_barrier()
; #define PG8_SCHED __builtin_amdgcn_sched_barrier(0)
; template <class Epi, class Sched, bool ALIGN_EPI>
; __device__ __forceinline__ void gemm_phase(LAS unsigned char* lds, const Gemm g, const Sched& S, const Epi& E) {
;     ...
;             PG8_LDB(B0, 1, 0); PG8_LDB(B1, 1, 1); PG8_SCHED; PG8_LDA(At, 1, 0); PG8_STAGE_A(PG8_SA(0, 1), s10, s11, kb2);
;             PG8_WAIT_V(8); PG8_WAIT_L(0); PG8_BAR; PG8_MMA(0, 0, At, B0); PG8_MMA(0, 1, At, B1); PG8_BAR; PG8_SCHED;
;             PG8_LDA(At, 1, 1); PG8_STAGE_B(PG8_SB(1, 0), b3); PG8_STAGE_B(PG8_SB(1, 1), b3 + hstepB); PG8_STAGE_A(PG8_SA(1, 0), s00, s01, kb3);
;             PG8_WAIT_V(8); PG8_WAIT_L(0); PG8_BAR; if (half1) { PG8_MMA(1, 0, At, B0); PG8_MMA(1, 1, At, B1); } PG8_BAR; PG8_SCHED;
.LBB0_1144:
	v_mov_b32_e32 v5, v3
	v_lshl_add_u64 v[236:237], s[30:31], 0, v[2:3]
	v_lshl_add_u64 v[4:5], s[30:31], 0, v[4:5]
	s_barrier
	v_add_u32_e32 v2, s50, v227
	ds_read_b128 v[150:153], v2
	ds_read_b128 v[154:157], v2 offset:1024
	ds_read_b128 v[158:161], v2 offset:2048
	ds_read_b128 v[162:165], v2 offset:3072
	v_add_u32_e32 v2, s51, v227
	ds_read_b128 v[134:137], v2
	ds_read_b128 v[138:141], v2 offset:1024
	ds_read_b128 v[142:145], v2 offset:2048
	ds_read_b128 v[146:149], v2 offset:3072
	s_mov_b32 m0, s37
	s_waitcnt lgkmcnt(0)
	ds_read_b128 v[166:169], v229 offset:32768
	ds_read_b128 v[170:173], v229 offset:33792
	ds_read_b128 v[174:177], v229 offset:34816
	ds_read_b128 v[178:181], v229 offset:35840
	ds_read_b128 v[182:185], v229 offset:36864
	ds_read_b128 v[186:189], v229 offset:37888
	ds_read_b128 v[190:193], v229 offset:38912
	ds_read_b128 v[194:197], v229 offset:39936
	global_load_lds_dwordx4 v209, s[30:31]
	s_mov_b32 m0, s38
	s_nop 0
	global_load_lds_dwordx4 v211, s[30:31]
	s_waitcnt vmcnt(8)
	s_waitcnt lgkmcnt(0)
	s_barrier
	s_waitcnt lgkmcnt(0)
	v_mfma_f32_16x16x32_bf16 v[130:133], v[150:153], v[166:169], v[130:133]
	v_mfma_f32_16x16x32_bf16 v[126:129], v[158:161], v[166:169], v[126:129]
	v_mfma_f32_16x16x32_bf16 v[114:117], v[150:153], v[174:177], v[114:117]
	v_mfma_f32_16x16x32_bf16 v[110:113], v[158:161], v[174:177], v[110:113]
	v_mfma_f32_16x16x32_bf16 v[98:101], v[150:153], v[182:185], v[98:101]
	v_mfma_f32_16x16x32_bf16 v[94:97], v[158:161], v[182:185], v[94:97]
	v_mfma_f32_16x16x32_bf16 v[82:85], v[150:153], v[190:193], v[82:85]
	v_mfma_f32_16x16x32_bf16 v[78:81], v[158:161], v[190:193], v[78:81]
	v_mfma_f32_16x16x32_bf16 v[130:133], v[154:157], v[170:173], v[130:133]
	v_mfma_f32_16x16x32_bf16 v[126:129], v[162:165], v[170:173], v[126:129]
	v_mfma_f32_16x16x32_bf16 v[114:117], v[154:157], v[178:181], v[114:117]
	v_mfma_f32_16x16x32_bf16 v[110:113], v[162:165], v[178:181], v[110:113]
	v_mfma_f32_16x16x32_bf16 v[98:101], v[154:157], v[186:189], v[98:101]
	v_mfma_f32_16x16x32_bf16 v[94:97], v[162:165], v[186:189], v[94:97]
	v_mfma_f32_16x16x32_bf16 v[82:85], v[154:157], v[194:197], v[82:85]
	v_mfma_f32_16x16x32_bf16 v[78:81], v[162:165], v[194:197], v[78:81]
	v_mfma_f32_16x16x32_bf16 v[122:125], v[134:137], v[166:169], v[122:125]
	v_mfma_f32_16x16x32_bf16 v[118:121], v[142:145], v[166:169], v[118:121]
	v_mfma_f32_16x16x32_bf16 v[106:109], v[134:137], v[174:177], v[106:109]
	v_mfma_f32_16x16x32_bf16 v[102:105], v[142:145], v[174:177], v[102:105]
	v_mfma_f32_16x16x32_bf16 v[90:93], v[134:137], v[182:185], v[90:93]
	v_mfma_f32_16x16x32_bf16 v[86:89], v[142:145], v[182:185], v[86:89]
	v_mfma_f32_16x16x32_bf16 v[74:77], v[134:137], v[190:193], v[74:77]
	v_mfma_f32_16x16x32_bf16 v[70:73], v[142:145], v[190:193], v[70:73]
	v_mfma_f32_16x16x32_bf16 v[122:125], v[138:141], v[170:173], v[122:125]
	v_mfma_f32_16x16x32_bf16 v[118:121], v[146:149], v[170:173], v[118:121]
	v_mfma_f32_16x16x32_bf16 v[106:109], v[138:141], v[178:181], v[106:109]
	v_mfma_f32_16x16x32_bf16 v[102:105], v[146:149], v[178:181], v[102:105]
	v_mfma_f32_16x16x32_bf16 v[90:93], v[138:141], v[186:189], v[90:93]
	v_mfma_f32_16x16x32_bf16 v[86:89], v[146:149], v[186:189], v[86:89]
	v_mfma_f32_16x16x32_bf16 v[74:77], v[138:141], v[194:197], v[74:77]
	v_mfma_f32_16x16x32_bf16 v[70:73], v[146:149], v[194:197], v[70:73]
	s_barrier
	s_add_i32 s30, s50, s34
	v_lshl_add_u64 v[218:219], v[218:219], 0, s[8:9]
	s_mov_b32 m0, s30
	ds_read_b128 v[190:193], v229 offset:49152
	ds_read_b128 v[194:197], v229 offset:50176
	ds_read_b128 v[182:185], v229 offset:51200
	ds_read_b128 v[186:189], v229 offset:52224
	ds_read_b128 v[174:177], v229 offset:53248
	ds_read_b128 v[178:181], v229 offset:54272
	ds_read_b128 v[166:169], v229 offset:55296
	ds_read_b128 v[170:173], v229 offset:56320
	global_load_lds_dwordx4 v[218:219], off
	s_add_i32 m0, s30, 0x2000
	s_add_u32 s28, s28, 0x40080
	v_lshl_add_u64 v[218:219], v[220:221], 0, s[8:9]
	s_addc_u32 s29, s29, 0
	s_add_i32 s30, s51, s34
	global_load_lds_dwordx4 v[218:219], off
	v_lshl_add_u64 v[218:219], s[28:29], 0, v[198:199]
	s_mov_b32 m0, s30
	v_lshl_add_u64 v[4:5], v[4:5], 0, s[8:9]
	global_load_lds_dwordx4 v[218:219], off
	v_lshl_add_u64 v[218:219], s[28:29], 0, v[200:201]
	s_add_i32 m0, s30, 0x2000
	s_and_b64 vcc, exec, s[4:5]
	global_load_lds_dwordx4 v[218:219], off
	v_lshl_add_u64 v[218:219], v[236:237], 0, s[8:9]
	s_mov_b32 m0, s39
	s_nop 0
	global_load_lds_dwordx4 v[218:219], off
	s_mov_b32 m0, s40
	s_nop 0
	global_load_lds_dwordx4 v[4:5], off
	s_waitcnt vmcnt(8)
	s_waitcnt lgkmcnt(0)
	s_barrier
	s_cbranch_vccnz .LBB0_1146
	s_waitcnt lgkmcnt(0)
	v_mfma_f32_16x16x32_bf16 v[66:69], v[150:153], v[190:193], v[66:69]
	v_mfma_f32_16x16x32_bf16 v[62:65], v[158:161], v[190:193], v[62:65]
	v_mfma_f32_16x16x32_bf16 v[50:53], v[150:153], v[182:185], v[50:53]
	v_mfma_f32_16x16x32_bf16 v[46:49], v[158:161], v[182:185], v[46:49]
	v_mfma_f32_16x16x32_bf16 v[34:37], v[150:153], v[174:177], v[34:37]
	v_mfma_f32_16x16x32_bf16 v[30:33], v[158:161], v[174:177], v[30:33]
	v_mfma_f32_16x16x32_bf16 v[18:21], v[150:153], v[166:169], v[18:21]
	v_mfma_f32_16x16x32_bf16 v[14:17], v[158:161], v[166:169], v[14:17]
	v_mfma_f32_16x16x32_bf16 v[66:69], v[154:157], v[194:197], v[66:69]
	v_mfma_f32_16x16x32_bf16 v[62:65], v[162:165], v[194:197], v[62:65]
	v_mfma_f32_16x16x32_bf16 v[50:53], v[154:157], v[186:189], v[50:53]
	v_mfma_f32_16x16x32_bf16 v[46:49], v[162:165], v[186:189], v[46:49]
	v_mfma_f32_16x16x32_bf16 v[34:37], v[154:157], v[178:181], v[34:37]
	v_mfma_f32_16x16x32_bf16 v[30:33], v[162:165], v[178:181], v[30:33]
	v_mfma_f32_16x16x32_bf16 v[18:21], v[154:157], v[170:173], v[18:21]
	v_mfma_f32_16x16x32_bf16 v[14:17], v[162:165], v[170:173], v[14:17]
	v_mfma_f32_16x16x32_bf16 v[58:61], v[134:137], v[190:193], v[58:61]
	v_mfma_f32_16x16x32_bf16 v[54:57], v[142:145], v[190:193], v[54:57]
	v_mfma_f32_16x16x32_bf16 v[42:45], v[134:137], v[182:185], v[42:45]
	v_mfma_f32_16x16x32_bf16 v[38:41], v[142:145], v[182:185], v[38:41]
	v_mfma_f32_16x16x32_bf16 v[26:29], v[134:137], v[174:177], v[26:29]
	v_mfma_f32_16x16x32_bf16 v[22:25], v[142:145], v[174:177], v[22:25]
	v_mfma_f32_16x16x32_bf16 v[10:13], v[134:137], v[166:169], v[10:13]
	v_mfma_f32_16x16x32_bf16 v[4:7], v[142:145], v[166:169], v[6:9]
	v_mfma_f32_16x16x32_bf16 v[58:61], v[138:141], v[194:197], v[58:61]
	v_mfma_f32_16x16x32_bf16 v[54:57], v[146:149], v[194:197], v[54:57]
	v_mfma_f32_16x16x32_bf16 v[42:45], v[138:141], v[186:189], v[42:45]
	v_mfma_f32_16x16x32_bf16 v[38:41], v[146:149], v[186:189], v[38:41]
	v_mfma_f32_16x16x32_bf16 v[26:29], v[138:141], v[178:181], v[26:29]
	v_mfma_f32_16x16x32_bf16 v[22:25], v[146:149], v[178:181], v[22:25]
	v_mfma_f32_16x16x32_bf16 v[10:13], v[138:141], v[170:173], v[10:13]
	v_mfma_f32_16x16x32_bf16 v[6:9], v[146:149], v[170:173], v[4:7]

; #define PG8_STAGE_B(bufoff, gbase) do { _Pragma("unroll") for (int _i = 0; _i < 2; ++_i) \
;         __builtin_amdgcn_global_load_lds((const unsigned*)((const char*)(gbase) + voffB[_i]), (LAS unsigned*)(lds + (bufoff) + ldsw + _i * 8192), 16, 0, 0); } while (0)
; #define PG8_STAGE_A(bufoff, V0, V1, kb) do { \
;         __builtin_amdgcn_global_load_lds((const unsigned*)((Abase + (kb)) + (V0)), (LAS unsigned*)(lds + (bufoff) + ldsw), 16, 0, 0); \
;         __builtin_amdgcn_global_load_lds((const unsigned*)((Abase + (kb)) + (V1)), (LAS unsigned*)(lds + (bufoff) + ldsw + 8192), 16, 0, 0); } while (0)
; #define PG8_LDA(dst, b, h) do { _Pragma("unroll") for (int m = 0; m < 4; ++m) _Pragma("unroll") for (int k = 0; k < 2; ++k) dst[m][k] = *(const LAS bf16x8*)(lds + PG8_SA(b, h) + aoff + m * 2048 + k * 1024); } while (0)
; #define PG8_LDB(dst, b, h) do { _Pragma("unroll") for (int n = 0; n < 2; ++n) _Pragma("unroll") for (int k = 0; k < 2; ++k) dst[n][k] = *(const LAS bf16x8*)(lds + PG8_SB(b, h) + boff + n * 2048 + k * 1024); } while (0)
; #define PG8_MMA(ai, bj, At, Bt) do { __builtin_amdgcn_s_setprio(1); _Pragma("unroll") for (int m = 0; m < 4; ++m) _Pragma("unroll") for (int n = 0; n < 2; ++n) _Pragma("unroll") for (int k = 0; k < 2; ++k) \
;         acc[ai][bj][m][n] = __builtin_amdgcn_mfma_f32_16x16x32_bf16(Bt[n][k], At[m][k], acc[ai][bj][m][n], 0, 0, 0); __builtin_amdgcn_s_setprio(0); } while (0)
; #define PG8_WAIT_V(n) asm volatile("s_waitcnt vmcnt(" #n ")" ::: "memory")
; #define PG8_WAIT_L(n) asm volatile("s_waitcnt lgkmcnt(" #n ")" ::: "memory")
; #define PG8_BAR __builtin_amdgcn_s_barrier()
; #define PG8_SCHED __builtin_amdgcn_sched_barrier(0)
; template <class Epi, class Sched, bool ALIGN_EPI>
; __device__ __forceinline__ void gemm_phase(LAS unsigned char* lds, const Gemm g, const Sched& S, const Epi& E) {
;     ...
;             PG8_LDB(B0, 0, 0); PG8_LDB(B1, 0, 1); PG8_SCHED; PG8_LDA(At, 0, 0); PG8_STAGE_A(PG8_SA(1, 1), vc10, vc11, kb1);
;             PG8_WAIT_V(8); PG8_WAIT_L(0); PG8_BAR; PG8_MMA(0, 0, At, B0); PG8_MMA(0, 1, At, B1); PG8_BAR; PG8_SCHED;
;             PG8_LDA(At, 0, 1); PG8_STAGE_B(PG8_SB(0, 0), b2); PG8_STAGE_B(PG8_SB(0, 1), b2 + hstepB); PG8_STAGE_A(PG8_SA(0, 0), s00, s01, kb2);
;             PG8_WAIT_V(8); PG8_WAIT_L(0); PG8_BAR; if (half1) { PG8_MMA(1, 0, At, B0); PG8_MMA(1, 1, At, B1); } PG8_BAR; PG8_SCHED;
.LBB0_1227:
	v_add_u32_e32 v100, s47, v228
	ds_read_b128 v[150:153], v100
	ds_read_b128 v[154:157], v100 offset:1024
	ds_read_b128 v[158:161], v100 offset:2048
	ds_read_b128 v[162:165], v100 offset:3072
	v_add_u32_e32 v100, s48, v228
	ds_read_b128 v[134:137], v100
	ds_read_b128 v[138:141], v100 offset:1024
	ds_read_b128 v[142:145], v100 offset:2048
	ds_read_b128 v[146:149], v100 offset:3072
	v_lshl_add_u64 v[100:101], v[212:213], 0, s[6:7]
	s_add_i32 m0, s39, 0xc000
	s_waitcnt lgkmcnt(0)
	ds_read_b128 v[166:169], v229
	ds_read_b128 v[170:173], v229 offset:1024
	ds_read_b128 v[174:177], v229 offset:2048
	ds_read_b128 v[178:181], v229 offset:3072
	ds_read_b128 v[182:185], v229 offset:4096
	ds_read_b128 v[186:189], v229 offset:5120
	ds_read_b128 v[190:193], v229 offset:6144
	ds_read_b128 v[194:197], v229 offset:7168
	global_load_lds_dwordx4 v[100:101], off
	v_lshl_add_u64 v[100:101], v[210:211], 0, s[6:7]
	s_add_i32 m0, s39, 0xe000
	s_nop 0
	global_load_lds_dwordx4 v[100:101], off
	s_waitcnt vmcnt(8)
	s_waitcnt lgkmcnt(0)
	s_barrier
	s_waitcnt lgkmcnt(0)
	v_mfma_f32_16x16x32_bf16 v[130:133], v[150:153], v[166:169], v[130:133]
	v_mfma_f32_16x16x32_bf16 v[126:129], v[158:161], v[166:169], v[126:129]
	v_mfma_f32_16x16x32_bf16 v[114:117], v[150:153], v[174:177], v[114:117]
	v_mfma_f32_16x16x32_bf16 v[110:113], v[158:161], v[174:177], v[110:113]
	v_mfma_f32_16x16x32_bf16 v[94:97], v[150:153], v[182:185], v[94:97]
	v_mfma_f32_16x16x32_bf16 v[90:93], v[158:161], v[182:185], v[90:93]
	v_mfma_f32_16x16x32_bf16 v[78:81], v[150:153], v[190:193], v[78:81]
	v_mfma_f32_16x16x32_bf16 v[74:77], v[158:161], v[190:193], v[74:77]
	v_mfma_f32_16x16x32_bf16 v[130:133], v[154:157], v[170:173], v[130:133]
	v_mfma_f32_16x16x32_bf16 v[126:129], v[162:165], v[170:173], v[126:129]
	v_mfma_f32_16x16x32_bf16 v[114:117], v[154:157], v[178:181], v[114:117]
	v_mfma_f32_16x16x32_bf16 v[110:113], v[162:165], v[178:181], v[110:113]
	v_mfma_f32_16x16x32_bf16 v[94:97], v[154:157], v[186:189], v[94:97]
	v_mfma_f32_16x16x32_bf16 v[90:93], v[162:165], v[186:189], v[90:93]
	v_mfma_f32_16x16x32_bf16 v[78:81], v[154:157], v[194:197], v[78:81]
	v_mfma_f32_16x16x32_bf16 v[74:77], v[162:165], v[194:197], v[74:77]
	v_mfma_f32_16x16x32_bf16 v[122:125], v[134:137], v[166:169], v[122:125]
	v_mfma_f32_16x16x32_bf16 v[118:121], v[142:145], v[166:169], v[118:121]
	v_mfma_f32_16x16x32_bf16 v[106:109], v[134:137], v[174:177], v[106:109]
	v_mfma_f32_16x16x32_bf16 v[100:103], v[142:145], v[174:177], v[102:105]
	v_mfma_f32_16x16x32_bf16 v[86:89], v[134:137], v[182:185], v[86:89]
	v_mfma_f32_16x16x32_bf16 v[82:85], v[142:145], v[182:185], v[82:85]
	v_mfma_f32_16x16x32_bf16 v[70:73], v[134:137], v[190:193], v[70:73]
	v_mfma_f32_16x16x32_bf16 v[66:69], v[142:145], v[190:193], v[66:69]
	v_mfma_f32_16x16x32_bf16 v[122:125], v[138:141], v[170:173], v[122:125]
	v_mfma_f32_16x16x32_bf16 v[118:121], v[146:149], v[170:173], v[118:121]
	v_mfma_f32_16x16x32_bf16 v[106:109], v[138:141], v[178:181], v[106:109]
	v_mfma_f32_16x16x32_bf16 v[100:103], v[146:149], v[178:181], v[100:103]
	v_mfma_f32_16x16x32_bf16 v[86:89], v[138:141], v[186:189], v[86:89]
	v_mfma_f32_16x16x32_bf16 v[82:85], v[146:149], v[186:189], v[82:85]
	v_mfma_f32_16x16x32_bf16 v[70:73], v[138:141], v[194:197], v[70:73]
	v_mfma_f32_16x16x32_bf16 v[66:69], v[146:149], v[194:197], v[66:69]
	s_barrier
	s_add_i32 s6, s47, s38
	v_lshl_add_u64 v[216:217], s[28:29], 0, v[198:199]
	s_mov_b32 m0, s6
	ds_read_b128 v[190:193], v229 offset:16384
	ds_read_b128 v[194:197], v229 offset:17408
	ds_read_b128 v[182:185], v229 offset:18432
	ds_read_b128 v[186:189], v229 offset:19456
	ds_read_b128 v[174:177], v229 offset:20480
	ds_read_b128 v[178:181], v229 offset:21504
	ds_read_b128 v[166:169], v229 offset:22528
	ds_read_b128 v[170:173], v229 offset:23552
	global_load_lds_dwordx4 v[216:217], off
	s_add_i32 m0, s6, 0x2000
	s_add_u32 s6, s28, 0x40000
	v_lshl_add_u64 v[218:219], s[28:29], 0, v[200:201]
	s_addc_u32 s7, s29, 0
	s_add_i32 s31, s48, s38
	global_load_lds_dwordx4 v[218:219], off
	v_lshl_add_u64 v[104:105], s[6:7], 0, v[198:199]
	s_mov_b32 m0, s31
	s_nop 0
	global_load_lds_dwordx4 v[104:105], off
	v_lshl_add_u64 v[104:105], s[6:7], 0, v[200:201]
	s_add_i32 m0, s31, 0x2000
	v_readlane_b32 s6, v254, 59
	v_readlane_b32 s7, v254, 60
	s_add_u32 s30, s6, s30
	global_load_lds_dwordx4 v[104:105], off
	s_addc_u32 s31, s7, 0
	s_mov_b32 m0, s39
	v_cndmask_b32_e64 v104, 0, 1, s[24:25]
	global_load_lds_dwordx4 v98, s[30:31]
	s_mov_b32 m0, s41
	v_cmp_ne_u32_e64 s[6:7], 1, v104
	global_load_lds_dwordx4 v214, s[30:31]
	s_waitcnt vmcnt(8)
	s_waitcnt lgkmcnt(0)
	s_andn2_b64 vcc, exec, s[24:25]
	s_barrier
	s_cbranch_vccnz .LBB0_1229
	s_waitcnt lgkmcnt(0)
	v_mfma_f32_16x16x32_bf16 v[62:65], v[150:153], v[190:193], v[62:65]
	v_mfma_f32_16x16x32_bf16 v[58:61], v[158:161], v[190:193], v[58:61]
	v_mfma_f32_16x16x32_bf16 v[46:49], v[150:153], v[182:185], v[46:49]
	v_mfma_f32_16x16x32_bf16 v[42:45], v[158:161], v[182:185], v[42:45]
	v_mfma_f32_16x16x32_bf16 v[30:33], v[150:153], v[174:177], v[30:33]
	v_mfma_f32_16x16x32_bf16 v[26:29], v[158:161], v[174:177], v[26:29]
	v_mfma_f32_16x16x32_bf16 v[14:17], v[150:153], v[166:169], v[14:17]
	v_mfma_f32_16x16x32_bf16 v[10:13], v[158:161], v[166:169], v[10:13]
	v_mfma_f32_16x16x32_bf16 v[62:65], v[154:157], v[194:197], v[62:65]
	v_mfma_f32_16x16x32_bf16 v[58:61], v[162:165], v[194:197], v[58:61]
	v_mfma_f32_16x16x32_bf16 v[46:49], v[154:157], v[186:189], v[46:49]
	v_mfma_f32_16x16x32_bf16 v[42:45], v[162:165], v[186:189], v[42:45]
	v_mfma_f32_16x16x32_bf16 v[30:33], v[154:157], v[178:181], v[30:33]
	v_mfma_f32_16x16x32_bf16 v[26:29], v[162:165], v[178:181], v[26:29]
	v_mfma_f32_16x16x32_bf16 v[14:17], v[154:157], v[170:173], v[14:17]
	v_mfma_f32_16x16x32_bf16 v[10:13], v[162:165], v[170:173], v[10:13]
	v_mfma_f32_16x16x32_bf16 v[54:57], v[134:137], v[190:193], v[54:57]
	v_mfma_f32_16x16x32_bf16 v[50:53], v[142:145], v[190:193], v[50:53]
	v_mfma_f32_16x16x32_bf16 v[38:41], v[134:137], v[182:185], v[38:41]
	v_mfma_f32_16x16x32_bf16 v[34:37], v[142:145], v[182:185], v[34:37]
	v_mfma_f32_16x16x32_bf16 v[22:25], v[134:137], v[174:177], v[22:25]
	v_mfma_f32_16x16x32_bf16 v[18:21], v[142:145], v[174:177], v[18:21]
	v_mfma_f32_16x16x32_bf16 v[6:9], v[134:137], v[166:169], v[6:9]
	v_mfma_f32_16x16x32_bf16 v[2:5], v[142:145], v[166:169], v[2:5]
	v_mfma_f32_16x16x32_bf16 v[54:57], v[138:141], v[194:197], v[54:57]
	v_mfma_f32_16x16x32_bf16 v[50:53], v[146:149], v[194:197], v[50:53]
	v_mfma_f32_16x16x32_bf16 v[38:41], v[138:141], v[186:189], v[38:41]
	v_mfma_f32_16x16x32_bf16 v[34:37], v[146:149], v[186:189], v[34:37]
	v_mfma_f32_16x16x32_bf16 v[22:25], v[138:141], v[178:181], v[22:25]
	v_mfma_f32_16x16x32_bf16 v[18:21], v[146:149], v[178:181], v[18:21]
	v_mfma_f32_16x16x32_bf16 v[6:9], v[138:141], v[170:173], v[6:9]
	v_mfma_f32_16x16x32_bf16 v[2:5], v[146:149], v[170:173], v[2:5]
; #define PG8_STAGE_B(bufoff, gbase) do { _Pragma("unroll") for (int _i = 0; _i < 2; ++_i) \
;         __builtin_amdgcn_global_load_lds((const unsigned*)((const char*)(gbase) + voffB[_i]), (LAS unsigned*)(lds + (bufoff) + ldsw + _i * 8192), 16, 0, 0); } while (0)
; #define PG8_STAGE_A(bufoff, V0, V1, kb) do { \
;         __builtin_amdgcn_global_load_lds((const unsigned*)((Abase + (kb)) + (V0)), (LAS unsigned*)(lds + (bufoff) + ldsw), 16, 0, 0); \
;         __builtin_amdgcn_global_load_lds((const unsigned*)((Abase + (kb)) + (V1)), (LAS unsigned*)(lds + (bufoff) + ldsw + 8192), 16, 0, 0); } while (0)
; #define PG8_LDA(dst, b, h) do { _Pragma("unroll") for (int m = 0; m < 4; ++m) _Pragma("unroll") for (int k = 0; k < 2; ++k) dst[m][k] = *(const LAS bf16x8*)(lds + PG8_SA(b, h) + aoff + m * 2048 + k * 1024); } while (0)
; #define PG8_LDB(dst, b, h) do { _Pragma("unroll") for (int n = 0; n < 2; ++n) _Pragma("unroll") for (int k = 0; k < 2; ++k) dst[n][k] = *(const LAS bf16x8*)(lds + PG8_SB(b, h) + boff + n * 2048 + k * 1024); } while (0)
; #define PG8_MMA(ai, bj, At, Bt) do { __builtin_amdgcn_s_setprio(1); _Pragma("unroll") for (int m = 0; m < 4; ++m) _Pragma("unroll") for (int n = 0; n < 2; ++n) _Pragma("unroll") for (int k = 0; k < 2; ++k) \
;         acc[ai][bj][m][n] = __builtin_amdgcn_mfma_f32_16x16x32_bf16(Bt[n][k], At[m][k], acc[ai][bj][m][n], 0, 0, 0); __builtin_amdgcn_s_setprio(0); } while (0)
; #define PG8_WAIT_V(n) asm volatile("s_waitcnt vmcnt(" #n ")" ::: "memory")
; #define PG8_WAIT_L(n) asm volatile("s_waitcnt lgkmcnt(" #n ")" ::: "memory")
; #define PG8_BAR __builtin_amdgcn_s_barrier()
; #define PG8_SCHED __builtin_amdgcn_sched_barrier(0)
; template <class Epi, class Sched, bool ALIGN_EPI>
; __device__ __forceinline__ void gemm_phase(LAS unsigned char* lds, const Gemm g, const Sched& S, const Epi& E) {
;     ...
;             PG8_LDB(B0, 1, 0); PG8_LDB(B1, 1, 1); PG8_SCHED; PG8_LDA(At, 1, 0); PG8_STAGE_A(PG8_SA(0, 1), s10, s11, kb2);
;             PG8_WAIT_V(8); PG8_WAIT_L(0); PG8_BAR; PG8_MMA(0, 0, At, B0); PG8_MMA(0, 1, At, B1); PG8_BAR; PG8_SCHED;
;             PG8_LDA(At, 1, 1); PG8_STAGE_B(PG8_SB(1, 0), b3); PG8_STAGE_B(PG8_SB(1, 1), b3 + hstepB); PG8_STAGE_A(PG8_SA(1, 0), s00, s01, kb3);
;             PG8_WAIT_V(8); PG8_WAIT_L(0); PG8_BAR; if (half1) { PG8_MMA(1, 0, At, B0); PG8_MMA(1, 1, At, B1); } PG8_BAR; PG8_SCHED;
.LBB0_1229:
	v_mov_b32_e32 v215, v99
	v_lshl_add_u64 v[236:237], s[30:31], 0, v[98:99]
	v_lshl_add_u64 v[214:215], s[30:31], 0, v[214:215]
	s_barrier
	v_add_u32_e32 v98, s49, v228
	ds_read_b128 v[150:153], v98
	ds_read_b128 v[154:157], v98 offset:1024
	ds_read_b128 v[158:161], v98 offset:2048
	ds_read_b128 v[162:165], v98 offset:3072
	v_add_u32_e32 v98, s50, v228
	ds_read_b128 v[134:137], v98
	ds_read_b128 v[138:141], v98 offset:1024
	ds_read_b128 v[142:145], v98 offset:2048
	ds_read_b128 v[146:149], v98 offset:3072
	s_mov_b32 m0, s42
	s_waitcnt lgkmcnt(0)
	ds_read_b128 v[166:169], v229 offset:32768
	ds_read_b128 v[170:173], v229 offset:33792
	ds_read_b128 v[174:177], v229 offset:34816
	ds_read_b128 v[178:181], v229 offset:35840
	ds_read_b128 v[182:185], v229 offset:36864
	ds_read_b128 v[186:189], v229 offset:37888
	ds_read_b128 v[190:193], v229 offset:38912
	ds_read_b128 v[194:197], v229 offset:39936
	global_load_lds_dwordx4 v207, s[30:31]
	s_mov_b32 m0, s43
	s_nop 0
	global_load_lds_dwordx4 v209, s[30:31]
	s_waitcnt vmcnt(8)
	s_waitcnt lgkmcnt(0)
	s_barrier
	s_waitcnt lgkmcnt(0)
	v_mfma_f32_16x16x32_bf16 v[130:133], v[150:153], v[166:169], v[130:133]
	v_mfma_f32_16x16x32_bf16 v[126:129], v[158:161], v[166:169], v[126:129]
	v_mfma_f32_16x16x32_bf16 v[114:117], v[150:153], v[174:177], v[114:117]
	v_mfma_f32_16x16x32_bf16 v[110:113], v[158:161], v[174:177], v[110:113]
	v_mfma_f32_16x16x32_bf16 v[94:97], v[150:153], v[182:185], v[94:97]
	v_mfma_f32_16x16x32_bf16 v[90:93], v[158:161], v[182:185], v[90:93]
	v_mfma_f32_16x16x32_bf16 v[78:81], v[150:153], v[190:193], v[78:81]
	v_mfma_f32_16x16x32_bf16 v[74:77], v[158:161], v[190:193], v[74:77]
	v_mfma_f32_16x16x32_bf16 v[130:133], v[154:157], v[170:173], v[130:133]
	v_mfma_f32_16x16x32_bf16 v[126:129], v[162:165], v[170:173], v[126:129]
	v_mfma_f32_16x16x32_bf16 v[114:117], v[154:157], v[178:181], v[114:117]
	v_mfma_f32_16x16x32_bf16 v[110:113], v[162:165], v[178:181], v[110:113]
	v_mfma_f32_16x16x32_bf16 v[94:97], v[154:157], v[186:189], v[94:97]
	v_mfma_f32_16x16x32_bf16 v[90:93], v[162:165], v[186:189], v[90:93]
	v_mfma_f32_16x16x32_bf16 v[78:81], v[154:157], v[194:197], v[78:81]
	v_mfma_f32_16x16x32_bf16 v[74:77], v[162:165], v[194:197], v[74:77]
	v_mfma_f32_16x16x32_bf16 v[122:125], v[134:137], v[166:169], v[122:125]
	v_mfma_f32_16x16x32_bf16 v[118:121], v[142:145], v[166:169], v[118:121]
	v_mfma_f32_16x16x32_bf16 v[104:107], v[134:137], v[174:177], v[106:109]
	v_mfma_f32_16x16x32_bf16 v[100:103], v[142:145], v[174:177], v[100:103]
	v_mfma_f32_16x16x32_bf16 v[86:89], v[134:137], v[182:185], v[86:89]
	v_mfma_f32_16x16x32_bf16 v[82:85], v[142:145], v[182:185], v[82:85]
	v_mfma_f32_16x16x32_bf16 v[70:73], v[134:137], v[190:193], v[70:73]
	v_mfma_f32_16x16x32_bf16 v[66:69], v[142:145], v[190:193], v[66:69]
	v_mfma_f32_16x16x32_bf16 v[122:125], v[138:141], v[170:173], v[122:125]
	v_mfma_f32_16x16x32_bf16 v[118:121], v[146:149], v[170:173], v[118:121]
	v_mfma_f32_16x16x32_bf16 v[106:109], v[138:141], v[178:181], v[104:107]
	v_mfma_f32_16x16x32_bf16 v[102:105], v[146:149], v[178:181], v[100:103]
	v_mfma_f32_16x16x32_bf16 v[86:89], v[138:141], v[186:189], v[86:89]
	v_mfma_f32_16x16x32_bf16 v[82:85], v[146:149], v[186:189], v[82:85]
	v_mfma_f32_16x16x32_bf16 v[70:73], v[138:141], v[194:197], v[70:73]
	v_mfma_f32_16x16x32_bf16 v[66:69], v[146:149], v[194:197], v[66:69]
	s_barrier
	s_add_i32 s30, s49, s38
	v_lshl_add_u64 v[100:101], v[216:217], 0, s[10:11]
	s_mov_b32 m0, s30
	ds_read_b128 v[190:193], v229 offset:49152
	ds_read_b128 v[194:197], v229 offset:50176
	ds_read_b128 v[182:185], v229 offset:51200
	ds_read_b128 v[186:189], v229 offset:52224
	ds_read_b128 v[174:177], v229 offset:53248
	ds_read_b128 v[178:181], v229 offset:54272
	ds_read_b128 v[166:169], v229 offset:55296
	ds_read_b128 v[170:173], v229 offset:56320
	global_load_lds_dwordx4 v[100:101], off
	s_add_i32 m0, s30, 0x2000
	s_add_u32 s28, s28, 0x40080
	v_lshl_add_u64 v[100:101], v[218:219], 0, s[10:11]
	s_addc_u32 s29, s29, 0
	s_add_i32 s30, s50, s38
	global_load_lds_dwordx4 v[100:101], off
	v_lshl_add_u64 v[100:101], s[28:29], 0, v[198:199]
	s_mov_b32 m0, s30
	s_and_b64 vcc, exec, s[6:7]
	global_load_lds_dwordx4 v[100:101], off
	v_lshl_add_u64 v[100:101], s[28:29], 0, v[200:201]
	s_add_i32 m0, s30, 0x2000
	s_nop 0
	global_load_lds_dwordx4 v[100:101], off
	v_lshl_add_u64 v[100:101], v[236:237], 0, s[10:11]
	s_mov_b32 m0, s44
	s_nop 0
	global_load_lds_dwordx4 v[100:101], off
	v_lshl_add_u64 v[100:101], v[214:215], 0, s[10:11]
	s_mov_b32 m0, s45
	s_nop 0
	global_load_lds_dwordx4 v[100:101], off
	s_waitcnt vmcnt(8)
	s_waitcnt lgkmcnt(0)
	s_barrier
	s_cbranch_vccnz .LBB0_1231
	s_waitcnt lgkmcnt(0)
	v_mfma_f32_16x16x32_bf16 v[62:65], v[150:153], v[190:193], v[62:65]
	v_mfma_f32_16x16x32_bf16 v[58:61], v[158:161], v[190:193], v[58:61]
	v_mfma_f32_16x16x32_bf16 v[46:49], v[150:153], v[182:185], v[46:49]
	v_mfma_f32_16x16x32_bf16 v[42:45], v[158:161], v[182:185], v[42:45]
	v_mfma_f32_16x16x32_bf16 v[30:33], v[150:153], v[174:177], v[30:33]
	v_mfma_f32_16x16x32_bf16 v[26:29], v[158:161], v[174:177], v[26:29]
	v_mfma_f32_16x16x32_bf16 v[14:17], v[150:153], v[166:169], v[14:17]
	v_mfma_f32_16x16x32_bf16 v[10:13], v[158:161], v[166:169], v[10:13]
	v_mfma_f32_16x16x32_bf16 v[62:65], v[154:157], v[194:197], v[62:65]
	v_mfma_f32_16x16x32_bf16 v[58:61], v[162:165], v[194:197], v[58:61]
	v_mfma_f32_16x16x32_bf16 v[46:49], v[154:157], v[186:189], v[46:49]
	v_mfma_f32_16x16x32_bf16 v[42:45], v[162:165], v[186:189], v[42:45]
	v_mfma_f32_16x16x32_bf16 v[30:33], v[154:157], v[178:181], v[30:33]
	v_mfma_f32_16x16x32_bf16 v[26:29], v[162:165], v[178:181], v[26:29]
	v_mfma_f32_16x16x32_bf16 v[14:17], v[154:157], v[170:173], v[14:17]
	v_mfma_f32_16x16x32_bf16 v[10:13], v[162:165], v[170:173], v[10:13]
	v_mfma_f32_16x16x32_bf16 v[54:57], v[134:137], v[190:193], v[54:57]
	v_mfma_f32_16x16x32_bf16 v[50:53], v[142:145], v[190:193], v[50:53]
	v_mfma_f32_16x16x32_bf16 v[38:41], v[134:137], v[182:185], v[38:41]
	v_mfma_f32_16x16x32_bf16 v[34:37], v[142:145], v[182:185], v[34:37]
	v_mfma_f32_16x16x32_bf16 v[22:25], v[134:137], v[174:177], v[22:25]
	v_mfma_f32_16x16x32_bf16 v[18:21], v[142:145], v[174:177], v[18:21]
	v_mfma_f32_16x16x32_bf16 v[6:9], v[134:137], v[166:169], v[6:9]
	v_mfma_f32_16x16x32_bf16 v[2:5], v[142:145], v[166:169], v[2:5]
	v_mfma_f32_16x16x32_bf16 v[54:57], v[138:141], v[194:197], v[54:57]
	v_mfma_f32_16x16x32_bf16 v[50:53], v[146:149], v[194:197], v[50:53]
	v_mfma_f32_16x16x32_bf16 v[38:41], v[138:141], v[186:189], v[38:41]
	v_mfma_f32_16x16x32_bf16 v[34:37], v[146:149], v[186:189], v[34:37]
	v_mfma_f32_16x16x32_bf16 v[22:25], v[138:141], v[178:181], v[22:25]
	v_mfma_f32_16x16x32_bf16 v[18:21], v[146:149], v[178:181], v[18:21]
	v_mfma_f32_16x16x32_bf16 v[6:9], v[138:141], v[170:173], v[6:9]
	v_mfma_f32_16x16x32_bf16 v[2:5], v[146:149], v[170:173], v[2:5]

; #define PG8_STAGE_B(bufoff, gbase) do { _Pragma("unroll") for (int _i = 0; _i < 2; ++_i) \
;         __builtin_amdgcn_global_load_lds((const unsigned*)((const char*)(gbase) + voffB[_i]), (LAS unsigned*)(lds + (bufoff) + ldsw + _i * 8192), 16, 0, 0); } while (0)
; #define PG8_STAGE_A(bufoff, V0, V1, kb) do { \
;         __builtin_amdgcn_global_load_lds((const unsigned*)((Abase + (kb)) + (V0)), (LAS unsigned*)(lds + (bufoff) + ldsw), 16, 0, 0); \
;         __builtin_amdgcn_global_load_lds((const unsigned*)((Abase + (kb)) + (V1)), (LAS unsigned*)(lds + (bufoff) + ldsw + 8192), 16, 0, 0); } while (0)
; #define PG8_LDA(dst, b, h) do { _Pragma("unroll") for (int m = 0; m < 4; ++m) _Pragma("unroll") for (int k = 0; k < 2; ++k) dst[m][k] = *(const LAS bf16x8*)(lds + PG8_SA(b, h) + aoff + m * 2048 + k * 1024); } while (0)
; #define PG8_LDB(dst, b, h) do { _Pragma("unroll") for (int n = 0; n < 2; ++n) _Pragma("unroll") for (int k = 0; k < 2; ++k) dst[n][k] = *(const LAS bf16x8*)(lds + PG8_SB(b, h) + boff + n * 2048 + k * 1024); } while (0)
; #define PG8_MMA(ai, bj, At, Bt) do { __builtin_amdgcn_s_setprio(1); _Pragma("unroll") for (int m = 0; m < 4; ++m) _Pragma("unroll") for (int n = 0; n < 2; ++n) _Pragma("unroll") for (int k = 0; k < 2; ++k) \
;         acc[ai][bj][m][n] = __builtin_amdgcn_mfma_f32_16x16x32_bf16(Bt[n][k], At[m][k], acc[ai][bj][m][n], 0, 0, 0); __builtin_amdgcn_s_setprio(0); } while (0)
; #define PG8_WAIT_V(n) asm volatile("s_waitcnt vmcnt(" #n ")" ::: "memory")
; #define PG8_WAIT_L(n) asm volatile("s_waitcnt lgkmcnt(" #n ")" ::: "memory")
; #define PG8_BAR __builtin_amdgcn_s_barrier()
; #define PG8_SCHED __builtin_amdgcn_sched_barrier(0)
; template <class Epi, class Sched, bool ALIGN_EPI>
; __device__ __forceinline__ void gemm_phase(LAS unsigned char* lds, const Gemm g, const Sched& S, const Epi& E) {
;     ...
;             PG8_LDB(B0, 0, 0); PG8_LDB(B1, 0, 1); PG8_SCHED; PG8_LDA(At, 0, 0); PG8_STAGE_A(PG8_SA(1, 1), vc10, vc11, kb1);
;             PG8_WAIT_V(8); PG8_WAIT_L(0); PG8_BAR; PG8_MMA(0, 0, At, B0); PG8_MMA(0, 1, At, B1); PG8_BAR; PG8_SCHED;
;             PG8_LDA(At, 0, 1); PG8_STAGE_B(PG8_SB(0, 0), b2); PG8_STAGE_B(PG8_SB(0, 1), b2 + hstepB); PG8_STAGE_A(PG8_SA(0, 0), s00, s01, kb2);
;             PG8_WAIT_V(8); PG8_WAIT_L(0); PG8_BAR; if (half1) { PG8_MMA(1, 0, At, B0); PG8_MMA(1, 1, At, B1); } PG8_BAR; PG8_SCHED;
.LBB0_1354:
	v_add_u32_e32 v5, s38, v220
	ds_read_b128 v[150:153], v5
	ds_read_b128 v[154:157], v5 offset:1024
	ds_read_b128 v[158:161], v5 offset:2048
	ds_read_b128 v[162:165], v5 offset:3072
	v_add_u32_e32 v5, s39, v220
	ds_read_b128 v[134:137], v5
	ds_read_b128 v[138:141], v5 offset:1024
	ds_read_b128 v[142:145], v5 offset:2048
	ds_read_b128 v[146:149], v5 offset:3072
	v_lshl_add_u64 v[212:213], v[210:211], 0, s[4:5]
	s_add_i32 m0, s30, 0xc000
	s_waitcnt lgkmcnt(0)
	ds_read_b128 v[166:169], v221
	ds_read_b128 v[170:173], v221 offset:1024
	ds_read_b128 v[174:177], v221 offset:2048
	ds_read_b128 v[178:181], v221 offset:3072
	ds_read_b128 v[182:185], v221 offset:4096
	ds_read_b128 v[186:189], v221 offset:5120
	ds_read_b128 v[190:193], v221 offset:6144
	ds_read_b128 v[194:197], v221 offset:7168
	global_load_lds_dwordx4 v[212:213], off
	v_lshl_add_u64 v[212:213], v[208:209], 0, s[4:5]
	s_add_i32 m0, s30, 0xe000
	s_nop 0
	global_load_lds_dwordx4 v[212:213], off
	s_waitcnt vmcnt(8)
	s_waitcnt lgkmcnt(0)
	s_barrier
	s_waitcnt lgkmcnt(0)
	v_mfma_f32_16x16x32_bf16 v[130:133], v[150:153], v[166:169], v[130:133]
	v_mfma_f32_16x16x32_bf16 v[126:129], v[158:161], v[166:169], v[126:129]
	v_mfma_f32_16x16x32_bf16 v[122:125], v[150:153], v[174:177], v[122:125]
	v_mfma_f32_16x16x32_bf16 v[118:121], v[158:161], v[174:177], v[118:121]
	v_mfma_f32_16x16x32_bf16 v[106:109], v[150:153], v[182:185], v[106:109]
	v_mfma_f32_16x16x32_bf16 v[102:105], v[158:161], v[182:185], v[102:105]
	v_mfma_f32_16x16x32_bf16 v[90:93], v[150:153], v[190:193], v[90:93]
	v_mfma_f32_16x16x32_bf16 v[86:89], v[158:161], v[190:193], v[86:89]
	v_mfma_f32_16x16x32_bf16 v[130:133], v[154:157], v[170:173], v[130:133]
	v_mfma_f32_16x16x32_bf16 v[126:129], v[162:165], v[170:173], v[126:129]
	v_mfma_f32_16x16x32_bf16 v[122:125], v[154:157], v[178:181], v[122:125]
	v_mfma_f32_16x16x32_bf16 v[118:121], v[162:165], v[178:181], v[118:121]
	v_mfma_f32_16x16x32_bf16 v[106:109], v[154:157], v[186:189], v[106:109]
	v_mfma_f32_16x16x32_bf16 v[102:105], v[162:165], v[186:189], v[102:105]
	v_mfma_f32_16x16x32_bf16 v[90:93], v[154:157], v[194:197], v[90:93]
	v_mfma_f32_16x16x32_bf16 v[86:89], v[162:165], v[194:197], v[86:89]
	v_mfma_f32_16x16x32_bf16 v[114:117], v[134:137], v[166:169], v[114:117]
	v_mfma_f32_16x16x32_bf16 v[110:113], v[142:145], v[166:169], v[110:113]
	v_mfma_f32_16x16x32_bf16 v[98:101], v[134:137], v[174:177], v[98:101]
	v_mfma_f32_16x16x32_bf16 v[94:97], v[142:145], v[174:177], v[94:97]
	v_mfma_f32_16x16x32_bf16 v[82:85], v[134:137], v[182:185], v[82:85]
	v_mfma_f32_16x16x32_bf16 v[78:81], v[142:145], v[182:185], v[78:81]
	v_mfma_f32_16x16x32_bf16 v[74:77], v[134:137], v[190:193], v[74:77]
	v_mfma_f32_16x16x32_bf16 v[70:73], v[142:145], v[190:193], v[70:73]
	v_mfma_f32_16x16x32_bf16 v[114:117], v[138:141], v[170:173], v[114:117]
	v_mfma_f32_16x16x32_bf16 v[110:113], v[146:149], v[170:173], v[110:113]
	v_mfma_f32_16x16x32_bf16 v[98:101], v[138:141], v[178:181], v[98:101]
	v_mfma_f32_16x16x32_bf16 v[94:97], v[146:149], v[178:181], v[94:97]
	v_mfma_f32_16x16x32_bf16 v[82:85], v[138:141], v[186:189], v[82:85]
	v_mfma_f32_16x16x32_bf16 v[78:81], v[146:149], v[186:189], v[78:81]
	v_mfma_f32_16x16x32_bf16 v[74:77], v[138:141], v[194:197], v[74:77]
	v_mfma_f32_16x16x32_bf16 v[70:73], v[146:149], v[194:197], v[70:73]
	s_barrier
	s_add_i32 s4, s38, s29
	v_lshl_add_u64 v[212:213], s[24:25], 0, v[198:199]
	s_mov_b32 m0, s4
	ds_read_b128 v[190:193], v221 offset:16384
	ds_read_b128 v[194:197], v221 offset:17408
	ds_read_b128 v[182:185], v221 offset:18432
	ds_read_b128 v[186:189], v221 offset:19456
	ds_read_b128 v[174:177], v221 offset:20480
	ds_read_b128 v[178:181], v221 offset:21504
	ds_read_b128 v[166:169], v221 offset:22528
	ds_read_b128 v[170:173], v221 offset:23552
	global_load_lds_dwordx4 v[212:213], off
	s_add_i32 m0, s4, 0x2000
	s_add_u32 s4, s24, 0x40000
	v_lshl_add_u64 v[214:215], s[24:25], 0, v[200:201]
	s_addc_u32 s5, s25, 0
	s_add_i32 s27, s39, s29
	global_load_lds_dwordx4 v[214:215], off
	v_lshl_add_u64 v[228:229], s[4:5], 0, v[198:199]
	s_mov_b32 m0, s27
	v_cndmask_b32_e64 v5, 0, 1, s[20:21]
	global_load_lds_dwordx4 v[228:229], off
	v_lshl_add_u64 v[228:229], s[4:5], 0, v[200:201]
	s_add_i32 m0, s27, 0x2000
	v_readlane_b32 s4, v255, 13
	v_readlane_b32 s5, v255, 14
	s_add_u32 s26, s4, s26
	global_load_lds_dwordx4 v[228:229], off
	s_addc_u32 s27, s5, 0
	s_mov_b32 m0, s30
	v_cmp_ne_u32_e64 s[4:5], 1, v5
	global_load_lds_dwordx4 v2, s[26:27]
	s_mov_b32 m0, s31
	s_andn2_b64 vcc, exec, s[20:21]
	global_load_lds_dwordx4 v4, s[26:27]
	s_waitcnt vmcnt(8)
	s_waitcnt lgkmcnt(0)
	s_barrier
	s_cbranch_vccnz .LBB0_1356
	s_waitcnt lgkmcnt(0)
	v_mfma_f32_16x16x32_bf16 v[66:69], v[150:153], v[190:193], v[66:69]
	v_mfma_f32_16x16x32_bf16 v[62:65], v[158:161], v[190:193], v[62:65]
	v_mfma_f32_16x16x32_bf16 v[50:53], v[150:153], v[182:185], v[50:53]
	v_mfma_f32_16x16x32_bf16 v[46:49], v[158:161], v[182:185], v[46:49]
	v_mfma_f32_16x16x32_bf16 v[34:37], v[150:153], v[174:177], v[34:37]
	v_mfma_f32_16x16x32_bf16 v[30:33], v[158:161], v[174:177], v[30:33]
	v_mfma_f32_16x16x32_bf16 v[18:21], v[150:153], v[166:169], v[18:21]
	v_mfma_f32_16x16x32_bf16 v[14:17], v[158:161], v[166:169], v[14:17]
	v_mfma_f32_16x16x32_bf16 v[66:69], v[154:157], v[194:197], v[66:69]
	v_mfma_f32_16x16x32_bf16 v[62:65], v[162:165], v[194:197], v[62:65]
	v_mfma_f32_16x16x32_bf16 v[50:53], v[154:157], v[186:189], v[50:53]
	v_mfma_f32_16x16x32_bf16 v[46:49], v[162:165], v[186:189], v[46:49]
	v_mfma_f32_16x16x32_bf16 v[34:37], v[154:157], v[178:181], v[34:37]
	v_mfma_f32_16x16x32_bf16 v[30:33], v[162:165], v[178:181], v[30:33]
	v_mfma_f32_16x16x32_bf16 v[18:21], v[154:157], v[170:173], v[18:21]
	v_mfma_f32_16x16x32_bf16 v[14:17], v[162:165], v[170:173], v[14:17]
	v_mfma_f32_16x16x32_bf16 v[58:61], v[134:137], v[190:193], v[58:61]
	v_mfma_f32_16x16x32_bf16 v[54:57], v[142:145], v[190:193], v[54:57]
	v_mfma_f32_16x16x32_bf16 v[42:45], v[134:137], v[182:185], v[42:45]
	v_mfma_f32_16x16x32_bf16 v[38:41], v[142:145], v[182:185], v[38:41]
	v_mfma_f32_16x16x32_bf16 v[26:29], v[134:137], v[174:177], v[26:29]
	v_mfma_f32_16x16x32_bf16 v[22:25], v[142:145], v[174:177], v[22:25]
	v_mfma_f32_16x16x32_bf16 v[10:13], v[134:137], v[166:169], v[10:13]
	v_mfma_f32_16x16x32_bf16 v[6:9], v[142:145], v[166:169], v[6:9]
	v_mfma_f32_16x16x32_bf16 v[58:61], v[138:141], v[194:197], v[58:61]
	v_mfma_f32_16x16x32_bf16 v[54:57], v[146:149], v[194:197], v[54:57]
	v_mfma_f32_16x16x32_bf16 v[42:45], v[138:141], v[186:189], v[42:45]
	v_mfma_f32_16x16x32_bf16 v[38:41], v[146:149], v[186:189], v[38:41]
	v_mfma_f32_16x16x32_bf16 v[26:29], v[138:141], v[178:181], v[26:29]
	v_mfma_f32_16x16x32_bf16 v[22:25], v[146:149], v[178:181], v[22:25]
	v_mfma_f32_16x16x32_bf16 v[10:13], v[138:141], v[170:173], v[10:13]
	v_mfma_f32_16x16x32_bf16 v[6:9], v[146:149], v[170:173], v[6:9]
; #define PG8_STAGE_B(bufoff, gbase) do { _Pragma("unroll") for (int _i = 0; _i < 2; ++_i) \
;         __builtin_amdgcn_global_load_lds((const unsigned*)((const char*)(gbase) + voffB[_i]), (LAS unsigned*)(lds + (bufoff) + ldsw + _i * 8192), 16, 0, 0); } while (0)
; #define PG8_STAGE_A(bufoff, V0, V1, kb) do { \
;         __builtin_amdgcn_global_load_lds((const unsigned*)((Abase + (kb)) + (V0)), (LAS unsigned*)(lds + (bufoff) + ldsw), 16, 0, 0); \
;         __builtin_amdgcn_global_load_lds((const unsigned*)((Abase + (kb)) + (V1)), (LAS unsigned*)(lds + (bufoff) + ldsw + 8192), 16, 0, 0); } while (0)
; #define PG8_LDA(dst, b, h) do { _Pragma("unroll") for (int m = 0; m < 4; ++m) _Pragma("unroll") for (int k = 0; k < 2; ++k) dst[m][k] = *(const LAS bf16x8*)(lds + PG8_SA(b, h) + aoff + m * 2048 + k * 1024); } while (0)
; #define PG8_LDB(dst, b, h) do { _Pragma("unroll") for (int n = 0; n < 2; ++n) _Pragma("unroll") for (int k = 0; k < 2; ++k) dst[n][k] = *(const LAS bf16x8*)(lds + PG8_SB(b, h) + boff + n * 2048 + k * 1024); } while (0)
; #define PG8_MMA(ai, bj, At, Bt) do { __builtin_amdgcn_s_setprio(1); _Pragma("unroll") for (int m = 0; m < 4; ++m) _Pragma("unroll") for (int n = 0; n < 2; ++n) _Pragma("unroll") for (int k = 0; k < 2; ++k) \
;         acc[ai][bj][m][n] = __builtin_amdgcn_mfma_f32_16x16x32_bf16(Bt[n][k], At[m][k], acc[ai][bj][m][n], 0, 0, 0); __builtin_amdgcn_s_setprio(0); } while (0)
; #define PG8_WAIT_V(n) asm volatile("s_waitcnt vmcnt(" #n ")" ::: "memory")
; #define PG8_WAIT_L(n) asm volatile("s_waitcnt lgkmcnt(" #n ")" ::: "memory")
; #define PG8_BAR __builtin_amdgcn_s_barrier()
; #define PG8_SCHED __builtin_amdgcn_sched_barrier(0)
; template <class Epi, class Sched, bool ALIGN_EPI>
; __device__ __forceinline__ void gemm_phase(LAS unsigned char* lds, const Gemm g, const Sched& S, const Epi& E) {
;     ...
;             PG8_LDB(B0, 1, 0); PG8_LDB(B1, 1, 1); PG8_SCHED; PG8_LDA(At, 1, 0); PG8_STAGE_A(PG8_SA(0, 1), s10, s11, kb2);
;             PG8_WAIT_V(8); PG8_WAIT_L(0); PG8_BAR; PG8_MMA(0, 0, At, B0); PG8_MMA(0, 1, At, B1); PG8_BAR; PG8_SCHED;
;             PG8_LDA(At, 1, 1); PG8_STAGE_B(PG8_SB(1, 0), b3); PG8_STAGE_B(PG8_SB(1, 1), b3 + hstepB); PG8_STAGE_A(PG8_SA(1, 0), s00, s01, kb3);
;             PG8_WAIT_V(8); PG8_WAIT_L(0); PG8_BAR; if (half1) { PG8_MMA(1, 0, At, B0); PG8_MMA(1, 1, At, B1); } PG8_BAR; PG8_SCHED;
.LBB0_1356:
	v_mov_b32_e32 v5, v3
	v_lshl_add_u64 v[228:229], s[26:27], 0, v[2:3]
	v_lshl_add_u64 v[4:5], s[26:27], 0, v[4:5]
	s_barrier
	v_add_u32_e32 v2, s40, v220
	ds_read_b128 v[150:153], v2
	ds_read_b128 v[154:157], v2 offset:1024
	ds_read_b128 v[158:161], v2 offset:2048
	ds_read_b128 v[162:165], v2 offset:3072
	v_add_u32_e32 v2, s41, v220
	ds_read_b128 v[134:137], v2
	ds_read_b128 v[138:141], v2 offset:1024
	ds_read_b128 v[142:145], v2 offset:2048
	ds_read_b128 v[146:149], v2 offset:3072
	s_mov_b32 m0, s33
	s_waitcnt lgkmcnt(0)
	ds_read_b128 v[166:169], v221 offset:32768
	ds_read_b128 v[170:173], v221 offset:33792
	ds_read_b128 v[174:177], v221 offset:34816
	ds_read_b128 v[178:181], v221 offset:35840
	ds_read_b128 v[182:185], v221 offset:36864
	ds_read_b128 v[186:189], v221 offset:37888
	ds_read_b128 v[190:193], v221 offset:38912
	ds_read_b128 v[194:197], v221 offset:39936
	global_load_lds_dwordx4 v205, s[26:27]
	s_mov_b32 m0, s34
	s_nop 0
	global_load_lds_dwordx4 v207, s[26:27]
	s_waitcnt vmcnt(8)
	s_waitcnt lgkmcnt(0)
	s_barrier
	s_waitcnt lgkmcnt(0)
	v_mfma_f32_16x16x32_bf16 v[130:133], v[150:153], v[166:169], v[130:133]
	v_mfma_f32_16x16x32_bf16 v[126:129], v[158:161], v[166:169], v[126:129]
	v_mfma_f32_16x16x32_bf16 v[122:125], v[150:153], v[174:177], v[122:125]
	v_mfma_f32_16x16x32_bf16 v[118:121], v[158:161], v[174:177], v[118:121]
	v_mfma_f32_16x16x32_bf16 v[106:109], v[150:153], v[182:185], v[106:109]
	v_mfma_f32_16x16x32_bf16 v[102:105], v[158:161], v[182:185], v[102:105]
	v_mfma_f32_16x16x32_bf16 v[90:93], v[150:153], v[190:193], v[90:93]
	v_mfma_f32_16x16x32_bf16 v[86:89], v[158:161], v[190:193], v[86:89]
	v_mfma_f32_16x16x32_bf16 v[130:133], v[154:157], v[170:173], v[130:133]
	v_mfma_f32_16x16x32_bf16 v[126:129], v[162:165], v[170:173], v[126:129]
	v_mfma_f32_16x16x32_bf16 v[122:125], v[154:157], v[178:181], v[122:125]
	v_mfma_f32_16x16x32_bf16 v[118:121], v[162:165], v[178:181], v[118:121]
	v_mfma_f32_16x16x32_bf16 v[106:109], v[154:157], v[186:189], v[106:109]
	v_mfma_f32_16x16x32_bf16 v[102:105], v[162:165], v[186:189], v[102:105]
	v_mfma_f32_16x16x32_bf16 v[90:93], v[154:157], v[194:197], v[90:93]
	v_mfma_f32_16x16x32_bf16 v[86:89], v[162:165], v[194:197], v[86:89]
	v_mfma_f32_16x16x32_bf16 v[114:117], v[134:137], v[166:169], v[114:117]
	v_mfma_f32_16x16x32_bf16 v[110:113], v[142:145], v[166:169], v[110:113]
	v_mfma_f32_16x16x32_bf16 v[98:101], v[134:137], v[174:177], v[98:101]
	v_mfma_f32_16x16x32_bf16 v[94:97], v[142:145], v[174:177], v[94:97]
	v_mfma_f32_16x16x32_bf16 v[82:85], v[134:137], v[182:185], v[82:85]
	v_mfma_f32_16x16x32_bf16 v[78:81], v[142:145], v[182:185], v[78:81]
	v_mfma_f32_16x16x32_bf16 v[74:77], v[134:137], v[190:193], v[74:77]
	v_mfma_f32_16x16x32_bf16 v[70:73], v[142:145], v[190:193], v[70:73]
	v_mfma_f32_16x16x32_bf16 v[114:117], v[138:141], v[170:173], v[114:117]
	v_mfma_f32_16x16x32_bf16 v[110:113], v[146:149], v[170:173], v[110:113]
	v_mfma_f32_16x16x32_bf16 v[98:101], v[138:141], v[178:181], v[98:101]
	v_mfma_f32_16x16x32_bf16 v[94:97], v[146:149], v[178:181], v[94:97]
	v_mfma_f32_16x16x32_bf16 v[82:85], v[138:141], v[186:189], v[82:85]
	v_mfma_f32_16x16x32_bf16 v[78:81], v[146:149], v[186:189], v[78:81]
	v_mfma_f32_16x16x32_bf16 v[74:77], v[138:141], v[194:197], v[74:77]
	v_mfma_f32_16x16x32_bf16 v[70:73], v[146:149], v[194:197], v[70:73]
	s_barrier
	s_add_i32 s26, s40, s29
	v_lshl_add_u64 v[212:213], v[212:213], 0, s[12:13]
	s_mov_b32 m0, s26
	ds_read_b128 v[190:193], v221 offset:49152
	ds_read_b128 v[194:197], v221 offset:50176
	ds_read_b128 v[182:185], v221 offset:51200
	ds_read_b128 v[186:189], v221 offset:52224
	ds_read_b128 v[174:177], v221 offset:53248
	ds_read_b128 v[178:181], v221 offset:54272
	ds_read_b128 v[166:169], v221 offset:55296
	ds_read_b128 v[170:173], v221 offset:56320
	global_load_lds_dwordx4 v[212:213], off
	s_add_i32 m0, s26, 0x2000
	s_add_u32 s24, s24, 0x40080
	v_lshl_add_u64 v[212:213], v[214:215], 0, s[12:13]
	s_addc_u32 s25, s25, 0
	s_add_i32 s26, s41, s29
	global_load_lds_dwordx4 v[212:213], off
	v_lshl_add_u64 v[212:213], s[24:25], 0, v[198:199]
	s_mov_b32 m0, s26
	v_lshl_add_u64 v[4:5], v[4:5], 0, s[12:13]
	global_load_lds_dwordx4 v[212:213], off
	v_lshl_add_u64 v[212:213], s[24:25], 0, v[200:201]
	s_add_i32 m0, s26, 0x2000
	s_and_b64 vcc, exec, s[4:5]
	global_load_lds_dwordx4 v[212:213], off
	v_lshl_add_u64 v[212:213], v[228:229], 0, s[12:13]
	s_mov_b32 m0, s35
	s_nop 0
	global_load_lds_dwordx4 v[212:213], off
	s_mov_b32 m0, s36
	s_nop 0
	global_load_lds_dwordx4 v[4:5], off
	s_waitcnt vmcnt(8)
	s_waitcnt lgkmcnt(0)
	s_barrier
	s_cbranch_vccnz .LBB0_1358
	s_waitcnt lgkmcnt(0)
	v_mfma_f32_16x16x32_bf16 v[66:69], v[150:153], v[190:193], v[66:69]
	v_mfma_f32_16x16x32_bf16 v[62:65], v[158:161], v[190:193], v[62:65]
	v_mfma_f32_16x16x32_bf16 v[50:53], v[150:153], v[182:185], v[50:53]
	v_mfma_f32_16x16x32_bf16 v[46:49], v[158:161], v[182:185], v[46:49]
	v_mfma_f32_16x16x32_bf16 v[34:37], v[150:153], v[174:177], v[34:37]
	v_mfma_f32_16x16x32_bf16 v[30:33], v[158:161], v[174:177], v[30:33]
	v_mfma_f32_16x16x32_bf16 v[18:21], v[150:153], v[166:169], v[18:21]
	v_mfma_f32_16x16x32_bf16 v[14:17], v[158:161], v[166:169], v[14:17]
	v_mfma_f32_16x16x32_bf16 v[66:69], v[154:157], v[194:197], v[66:69]
	v_mfma_f32_16x16x32_bf16 v[62:65], v[162:165], v[194:197], v[62:65]
	v_mfma_f32_16x16x32_bf16 v[50:53], v[154:157], v[186:189], v[50:53]
	v_mfma_f32_16x16x32_bf16 v[46:49], v[162:165], v[186:189], v[46:49]
	v_mfma_f32_16x16x32_bf16 v[34:37], v[154:157], v[178:181], v[34:37]
	v_mfma_f32_16x16x32_bf16 v[30:33], v[162:165], v[178:181], v[30:33]
	v_mfma_f32_16x16x32_bf16 v[18:21], v[154:157], v[170:173], v[18:21]
	v_mfma_f32_16x16x32_bf16 v[14:17], v[162:165], v[170:173], v[14:17]
	v_mfma_f32_16x16x32_bf16 v[58:61], v[134:137], v[190:193], v[58:61]
	v_mfma_f32_16x16x32_bf16 v[54:57], v[142:145], v[190:193], v[54:57]
	v_mfma_f32_16x16x32_bf16 v[42:45], v[134:137], v[182:185], v[42:45]
	v_mfma_f32_16x16x32_bf16 v[38:41], v[142:145], v[182:185], v[38:41]
	v_mfma_f32_16x16x32_bf16 v[26:29], v[134:137], v[174:177], v[26:29]
	v_mfma_f32_16x16x32_bf16 v[22:25], v[142:145], v[174:177], v[22:25]
	v_mfma_f32_16x16x32_bf16 v[10:13], v[134:137], v[166:169], v[10:13]
	v_mfma_f32_16x16x32_bf16 v[4:7], v[142:145], v[166:169], v[6:9]
	v_mfma_f32_16x16x32_bf16 v[58:61], v[138:141], v[194:197], v[58:61]
	v_mfma_f32_16x16x32_bf16 v[54:57], v[146:149], v[194:197], v[54:57]
	v_mfma_f32_16x16x32_bf16 v[42:45], v[138:141], v[186:189], v[42:45]
	v_mfma_f32_16x16x32_bf16 v[38:41], v[146:149], v[186:189], v[38:41]
	v_mfma_f32_16x16x32_bf16 v[26:29], v[138:141], v[178:181], v[26:29]
	v_mfma_f32_16x16x32_bf16 v[22:25], v[146:149], v[178:181], v[22:25]
	v_mfma_f32_16x16x32_bf16 v[10:13], v[138:141], v[170:173], v[10:13]
	v_mfma_f32_16x16x32_bf16 v[6:9], v[146:149], v[170:173], v[4:7]

; #define PG8_STAGE_B(bufoff, gbase) do { _Pragma("unroll") for (int _i = 0; _i < 2; ++_i) \
;         __builtin_amdgcn_global_load_lds((const unsigned*)((const char*)(gbase) + voffB[_i]), (LAS unsigned*)(lds + (bufoff) + ldsw + _i * 8192), 16, 0, 0); } while (0)
; #define PG8_STAGE_A(bufoff, V0, V1, kb) do { \
;         __builtin_amdgcn_global_load_lds((const unsigned*)((Abase + (kb)) + (V0)), (LAS unsigned*)(lds + (bufoff) + ldsw), 16, 0, 0); \
;         __builtin_amdgcn_global_load_lds((const unsigned*)((Abase + (kb)) + (V1)), (LAS unsigned*)(lds + (bufoff) + ldsw + 8192), 16, 0, 0); } while (0)
; #define PG8_LDA(dst, b, h) do { _Pragma("unroll") for (int m = 0; m < 4; ++m) _Pragma("unroll") for (int k = 0; k < 2; ++k) dst[m][k] = *(const LAS bf16x8*)(lds + PG8_SA(b, h) + aoff + m * 2048 + k * 1024); } while (0)
; #define PG8_LDB(dst, b, h) do { _Pragma("unroll") for (int n = 0; n < 2; ++n) _Pragma("unroll") for (int k = 0; k < 2; ++k) dst[n][k] = *(const LAS bf16x8*)(lds + PG8_SB(b, h) + boff + n * 2048 + k * 1024); } while (0)
; #define PG8_MMA(ai, bj, At, Bt) do { __builtin_amdgcn_s_setprio(1); _Pragma("unroll") for (int m = 0; m < 4; ++m) _Pragma("unroll") for (int n = 0; n < 2; ++n) _Pragma("unroll") for (int k = 0; k < 2; ++k) \
;         acc[ai][bj][m][n] = __builtin_amdgcn_mfma_f32_16x16x32_bf16(Bt[n][k], At[m][k], acc[ai][bj][m][n], 0, 0, 0); __builtin_amdgcn_s_setprio(0); } while (0)
; #define PG8_WAIT_V(n) asm volatile("s_waitcnt vmcnt(" #n ")" ::: "memory")
; #define PG8_WAIT_L(n) asm volatile("s_waitcnt lgkmcnt(" #n ")" ::: "memory")
; #define PG8_BAR __builtin_amdgcn_s_barrier()
; #define PG8_SCHED __builtin_amdgcn_sched_barrier(0)
; template <class Epi, class Sched, bool ALIGN_EPI>
; __device__ __forceinline__ void gemm_phase(LAS unsigned char* lds, const Gemm g, const Sched& S, const Epi& E) {
;     ...
;             PG8_LDB(B0, 0, 0); PG8_LDB(B1, 0, 1); PG8_SCHED; PG8_LDA(At, 0, 0); PG8_STAGE_A(PG8_SA(1, 1), vc10, vc11, kb1);
;             PG8_WAIT_V(8); PG8_WAIT_L(0); PG8_BAR; PG8_MMA(0, 0, At, B0); PG8_MMA(0, 1, At, B1); PG8_BAR; PG8_SCHED;
;             PG8_LDA(At, 0, 1); PG8_STAGE_B(PG8_SB(0, 0), b2); PG8_STAGE_B(PG8_SB(0, 1), b2 + hstepB); PG8_STAGE_A(PG8_SA(0, 0), s00, s01, kb2);
;             PG8_WAIT_V(8); PG8_WAIT_L(0); PG8_BAR; if (half1) { PG8_MMA(1, 0, At, B0); PG8_MMA(1, 1, At, B1); } PG8_BAR; PG8_SCHED;
.LBB0_1389:
	v_add_u32_e32 v5, s44, v223
	ds_read_b128 v[150:153], v5
	ds_read_b128 v[154:157], v5 offset:1024
	ds_read_b128 v[158:161], v5 offset:2048
	ds_read_b128 v[162:165], v5 offset:3072
	v_add_u32_e32 v5, s45, v223
	ds_read_b128 v[134:137], v5
	ds_read_b128 v[138:141], v5 offset:1024
	ds_read_b128 v[142:145], v5 offset:2048
	ds_read_b128 v[146:149], v5 offset:3072
	v_lshl_add_u64 v[216:217], v[214:215], 0, s[4:5]
	s_add_i32 m0, s7, 0xc000
	s_waitcnt lgkmcnt(0)
	ds_read_b128 v[166:169], v227
	ds_read_b128 v[170:173], v227 offset:1024
	ds_read_b128 v[174:177], v227 offset:2048
	ds_read_b128 v[178:181], v227 offset:3072
	ds_read_b128 v[182:185], v227 offset:4096
	ds_read_b128 v[186:189], v227 offset:5120
	ds_read_b128 v[190:193], v227 offset:6144
	ds_read_b128 v[194:197], v227 offset:7168
	global_load_lds_dwordx4 v[216:217], off
	v_lshl_add_u64 v[216:217], v[212:213], 0, s[4:5]
	s_add_i32 m0, s7, 0xe000
	s_nop 0
	global_load_lds_dwordx4 v[216:217], off
	s_waitcnt vmcnt(8)
	s_waitcnt lgkmcnt(0)
	s_barrier
	s_waitcnt lgkmcnt(0)
	v_mfma_f32_16x16x32_bf16 v[130:133], v[150:153], v[166:169], v[130:133]
	v_mfma_f32_16x16x32_bf16 v[122:125], v[158:161], v[166:169], v[122:125]
	v_mfma_f32_16x16x32_bf16 v[114:117], v[150:153], v[174:177], v[114:117]
	v_mfma_f32_16x16x32_bf16 v[106:109], v[158:161], v[174:177], v[106:109]
	v_mfma_f32_16x16x32_bf16 v[98:101], v[150:153], v[182:185], v[98:101]
	v_mfma_f32_16x16x32_bf16 v[90:93], v[158:161], v[182:185], v[90:93]
	v_mfma_f32_16x16x32_bf16 v[82:85], v[150:153], v[190:193], v[82:85]
	v_mfma_f32_16x16x32_bf16 v[74:77], v[158:161], v[190:193], v[74:77]
	v_mfma_f32_16x16x32_bf16 v[130:133], v[154:157], v[170:173], v[130:133]
	v_mfma_f32_16x16x32_bf16 v[122:125], v[162:165], v[170:173], v[122:125]
	v_mfma_f32_16x16x32_bf16 v[114:117], v[154:157], v[178:181], v[114:117]
	v_mfma_f32_16x16x32_bf16 v[106:109], v[162:165], v[178:181], v[106:109]
	v_mfma_f32_16x16x32_bf16 v[98:101], v[154:157], v[186:189], v[98:101]
	v_mfma_f32_16x16x32_bf16 v[90:93], v[162:165], v[186:189], v[90:93]
	v_mfma_f32_16x16x32_bf16 v[82:85], v[154:157], v[194:197], v[82:85]
	v_mfma_f32_16x16x32_bf16 v[74:77], v[162:165], v[194:197], v[74:77]
	v_mfma_f32_16x16x32_bf16 v[126:129], v[134:137], v[166:169], v[126:129]
	v_mfma_f32_16x16x32_bf16 v[118:121], v[142:145], v[166:169], v[118:121]
	v_mfma_f32_16x16x32_bf16 v[110:113], v[134:137], v[174:177], v[110:113]
	v_mfma_f32_16x16x32_bf16 v[102:105], v[142:145], v[174:177], v[102:105]
	v_mfma_f32_16x16x32_bf16 v[94:97], v[134:137], v[182:185], v[94:97]
	v_mfma_f32_16x16x32_bf16 v[86:89], v[142:145], v[182:185], v[86:89]
	v_mfma_f32_16x16x32_bf16 v[78:81], v[134:137], v[190:193], v[78:81]
	v_mfma_f32_16x16x32_bf16 v[70:73], v[142:145], v[190:193], v[70:73]
	v_mfma_f32_16x16x32_bf16 v[126:129], v[138:141], v[170:173], v[126:129]
	v_mfma_f32_16x16x32_bf16 v[118:121], v[146:149], v[170:173], v[118:121]
	v_mfma_f32_16x16x32_bf16 v[110:113], v[138:141], v[178:181], v[110:113]
	v_mfma_f32_16x16x32_bf16 v[102:105], v[146:149], v[178:181], v[102:105]
	v_mfma_f32_16x16x32_bf16 v[94:97], v[138:141], v[186:189], v[94:97]
	v_mfma_f32_16x16x32_bf16 v[86:89], v[146:149], v[186:189], v[86:89]
	v_mfma_f32_16x16x32_bf16 v[78:81], v[138:141], v[194:197], v[78:81]
	v_mfma_f32_16x16x32_bf16 v[70:73], v[146:149], v[194:197], v[70:73]
	s_barrier
	s_add_i32 s4, s44, s34
	v_lshl_add_u64 v[216:217], s[28:29], 0, v[198:199]
	s_mov_b32 m0, s4
	ds_read_b128 v[190:193], v227 offset:16384
	ds_read_b128 v[194:197], v227 offset:17408
	ds_read_b128 v[182:185], v227 offset:18432
	ds_read_b128 v[186:189], v227 offset:19456
	ds_read_b128 v[174:177], v227 offset:20480
	ds_read_b128 v[178:181], v227 offset:21504
	ds_read_b128 v[166:169], v227 offset:22528
	ds_read_b128 v[170:173], v227 offset:23552
	global_load_lds_dwordx4 v[216:217], off
	s_add_i32 m0, s4, 0x2000
	s_add_u32 s4, s28, 0x40000
	v_lshl_add_u64 v[218:219], s[28:29], 0, v[200:201]
	s_addc_u32 s5, s29, 0
	s_add_i32 s31, s45, s34
	global_load_lds_dwordx4 v[218:219], off
	v_lshl_add_u64 v[234:235], s[4:5], 0, v[198:199]
	s_mov_b32 m0, s31
	v_cndmask_b32_e64 v5, 0, 1, s[24:25]
	global_load_lds_dwordx4 v[234:235], off
	v_lshl_add_u64 v[234:235], s[4:5], 0, v[200:201]
	s_add_i32 m0, s31, 0x2000
	v_readlane_b32 s4, v255, 13
	v_readlane_b32 s5, v255, 14
	s_add_u32 s30, s4, s30
	global_load_lds_dwordx4 v[234:235], off
	s_addc_u32 s31, s5, 0
	s_mov_b32 m0, s7
	v_cmp_ne_u32_e64 s[4:5], 1, v5
	global_load_lds_dwordx4 v2, s[30:31]
	s_mov_b32 m0, s35
	s_andn2_b64 vcc, exec, s[24:25]
	global_load_lds_dwordx4 v4, s[30:31]
	s_waitcnt vmcnt(8)
	s_waitcnt lgkmcnt(0)
	s_barrier
	s_cbranch_vccnz .LBB0_1391
	s_waitcnt lgkmcnt(0)
	v_mfma_f32_16x16x32_bf16 v[66:69], v[150:153], v[190:193], v[66:69]
	v_mfma_f32_16x16x32_bf16 v[58:61], v[158:161], v[190:193], v[58:61]
	v_mfma_f32_16x16x32_bf16 v[50:53], v[150:153], v[182:185], v[50:53]
	v_mfma_f32_16x16x32_bf16 v[42:45], v[158:161], v[182:185], v[42:45]
	v_mfma_f32_16x16x32_bf16 v[34:37], v[150:153], v[174:177], v[34:37]
	v_mfma_f32_16x16x32_bf16 v[26:29], v[158:161], v[174:177], v[26:29]
	v_mfma_f32_16x16x32_bf16 v[18:21], v[150:153], v[166:169], v[18:21]
	v_mfma_f32_16x16x32_bf16 v[10:13], v[158:161], v[166:169], v[10:13]
	v_mfma_f32_16x16x32_bf16 v[66:69], v[154:157], v[194:197], v[66:69]
	v_mfma_f32_16x16x32_bf16 v[58:61], v[162:165], v[194:197], v[58:61]
	v_mfma_f32_16x16x32_bf16 v[50:53], v[154:157], v[186:189], v[50:53]
	v_mfma_f32_16x16x32_bf16 v[42:45], v[162:165], v[186:189], v[42:45]
	v_mfma_f32_16x16x32_bf16 v[34:37], v[154:157], v[178:181], v[34:37]
	v_mfma_f32_16x16x32_bf16 v[26:29], v[162:165], v[178:181], v[26:29]
	v_mfma_f32_16x16x32_bf16 v[18:21], v[154:157], v[170:173], v[18:21]
	v_mfma_f32_16x16x32_bf16 v[10:13], v[162:165], v[170:173], v[10:13]
	v_mfma_f32_16x16x32_bf16 v[62:65], v[134:137], v[190:193], v[62:65]
	v_mfma_f32_16x16x32_bf16 v[54:57], v[142:145], v[190:193], v[54:57]
	v_mfma_f32_16x16x32_bf16 v[46:49], v[134:137], v[182:185], v[46:49]
	v_mfma_f32_16x16x32_bf16 v[38:41], v[142:145], v[182:185], v[38:41]
	v_mfma_f32_16x16x32_bf16 v[30:33], v[134:137], v[174:177], v[30:33]
	v_mfma_f32_16x16x32_bf16 v[22:25], v[142:145], v[174:177], v[22:25]
	v_mfma_f32_16x16x32_bf16 v[14:17], v[134:137], v[166:169], v[14:17]
	v_mfma_f32_16x16x32_bf16 v[6:9], v[142:145], v[166:169], v[6:9]
	v_mfma_f32_16x16x32_bf16 v[62:65], v[138:141], v[194:197], v[62:65]
	v_mfma_f32_16x16x32_bf16 v[54:57], v[146:149], v[194:197], v[54:57]
	v_mfma_f32_16x16x32_bf16 v[46:49], v[138:141], v[186:189], v[46:49]
	v_mfma_f32_16x16x32_bf16 v[38:41], v[146:149], v[186:189], v[38:41]
	v_mfma_f32_16x16x32_bf16 v[30:33], v[138:141], v[178:181], v[30:33]
	v_mfma_f32_16x16x32_bf16 v[22:25], v[146:149], v[178:181], v[22:25]
	v_mfma_f32_16x16x32_bf16 v[14:17], v[138:141], v[170:173], v[14:17]
	v_mfma_f32_16x16x32_bf16 v[6:9], v[146:149], v[170:173], v[6:9]
; #define PG8_STAGE_B(bufoff, gbase) do { _Pragma("unroll") for (int _i = 0; _i < 2; ++_i) \
;         __builtin_amdgcn_global_load_lds((const unsigned*)((const char*)(gbase) + voffB[_i]), (LAS unsigned*)(lds + (bufoff) + ldsw + _i * 8192), 16, 0, 0); } while (0)
; #define PG8_STAGE_A(bufoff, V0, V1, kb) do { \
;         __builtin_amdgcn_global_load_lds((const unsigned*)((Abase + (kb)) + (V0)), (LAS unsigned*)(lds + (bufoff) + ldsw), 16, 0, 0); \
;         __builtin_amdgcn_global_load_lds((const unsigned*)((Abase + (kb)) + (V1)), (LAS unsigned*)(lds + (bufoff) + ldsw + 8192), 16, 0, 0); } while (0)
; #define PG8_LDA(dst, b, h) do { _Pragma("unroll") for (int m = 0; m < 4; ++m) _Pragma("unroll") for (int k = 0; k < 2; ++k) dst[m][k] = *(const LAS bf16x8*)(lds + PG8_SA(b, h) + aoff + m * 2048 + k * 1024); } while (0)
; #define PG8_LDB(dst, b, h) do { _Pragma("unroll") for (int n = 0; n < 2; ++n) _Pragma("unroll") for (int k = 0; k < 2; ++k) dst[n][k] = *(const LAS bf16x8*)(lds + PG8_SB(b, h) + boff + n * 2048 + k * 1024); } while (0)
; #define PG8_MMA(ai, bj, At, Bt) do { __builtin_amdgcn_s_setprio(1); _Pragma("unroll") for (int m = 0; m < 4; ++m) _Pragma("unroll") for (int n = 0; n < 2; ++n) _Pragma("unroll") for (int k = 0; k < 2; ++k) \
;         acc[ai][bj][m][n] = __builtin_amdgcn_mfma_f32_16x16x32_bf16(Bt[n][k], At[m][k], acc[ai][bj][m][n], 0, 0, 0); __builtin_amdgcn_s_setprio(0); } while (0)
; #define PG8_WAIT_V(n) asm volatile("s_waitcnt vmcnt(" #n ")" ::: "memory")
; #define PG8_WAIT_L(n) asm volatile("s_waitcnt lgkmcnt(" #n ")" ::: "memory")
; #define PG8_BAR __builtin_amdgcn_s_barrier()
; #define PG8_SCHED __builtin_amdgcn_sched_barrier(0)
; template <class Epi, class Sched, bool ALIGN_EPI>
; __device__ __forceinline__ void gemm_phase(LAS unsigned char* lds, const Gemm g, const Sched& S, const Epi& E) {
;     ...
;             PG8_LDB(B0, 1, 0); PG8_LDB(B1, 1, 1); PG8_SCHED; PG8_LDA(At, 1, 0); PG8_STAGE_A(PG8_SA(0, 1), s10, s11, kb2);
;             PG8_WAIT_V(8); PG8_WAIT_L(0); PG8_BAR; PG8_MMA(0, 0, At, B0); PG8_MMA(0, 1, At, B1); PG8_BAR; PG8_SCHED;
;             PG8_LDA(At, 1, 1); PG8_STAGE_B(PG8_SB(1, 0), b3); PG8_STAGE_B(PG8_SB(1, 1), b3 + hstepB); PG8_STAGE_A(PG8_SA(1, 0), s00, s01, kb3);
;             PG8_WAIT_V(8); PG8_WAIT_L(0); PG8_BAR; if (half1) { PG8_MMA(1, 0, At, B0); PG8_MMA(1, 1, At, B1); } PG8_BAR; PG8_SCHED;
.LBB0_1391:
	v_mov_b32_e32 v5, v3
	v_lshl_add_u64 v[234:235], s[30:31], 0, v[2:3]
	v_lshl_add_u64 v[4:5], s[30:31], 0, v[4:5]
	s_barrier
	v_add_u32_e32 v2, s46, v223
	ds_read_b128 v[150:153], v2
	ds_read_b128 v[154:157], v2 offset:1024
	ds_read_b128 v[158:161], v2 offset:2048
	ds_read_b128 v[162:165], v2 offset:3072
	v_add_u32_e32 v2, s47, v223
	ds_read_b128 v[134:137], v2
	ds_read_b128 v[138:141], v2 offset:1024
	ds_read_b128 v[142:145], v2 offset:2048
	ds_read_b128 v[146:149], v2 offset:3072
	s_mov_b32 m0, s36
	s_waitcnt lgkmcnt(0)
	ds_read_b128 v[166:169], v227 offset:32768
	ds_read_b128 v[170:173], v227 offset:33792
	ds_read_b128 v[174:177], v227 offset:34816
	ds_read_b128 v[178:181], v227 offset:35840
	ds_read_b128 v[182:185], v227 offset:36864
	ds_read_b128 v[186:189], v227 offset:37888
	ds_read_b128 v[190:193], v227 offset:38912
	ds_read_b128 v[194:197], v227 offset:39936
	global_load_lds_dwordx4 v209, s[30:31]
	s_mov_b32 m0, s37
	s_nop 0
	global_load_lds_dwordx4 v211, s[30:31]
	s_waitcnt vmcnt(8)
	s_waitcnt lgkmcnt(0)
	s_barrier
	s_waitcnt lgkmcnt(0)
	v_mfma_f32_16x16x32_bf16 v[130:133], v[150:153], v[166:169], v[130:133]
	v_mfma_f32_16x16x32_bf16 v[122:125], v[158:161], v[166:169], v[122:125]
	v_mfma_f32_16x16x32_bf16 v[114:117], v[150:153], v[174:177], v[114:117]
	v_mfma_f32_16x16x32_bf16 v[106:109], v[158:161], v[174:177], v[106:109]
	v_mfma_f32_16x16x32_bf16 v[98:101], v[150:153], v[182:185], v[98:101]
	v_mfma_f32_16x16x32_bf16 v[90:93], v[158:161], v[182:185], v[90:93]
	v_mfma_f32_16x16x32_bf16 v[82:85], v[150:153], v[190:193], v[82:85]
	v_mfma_f32_16x16x32_bf16 v[74:77], v[158:161], v[190:193], v[74:77]
	v_mfma_f32_16x16x32_bf16 v[130:133], v[154:157], v[170:173], v[130:133]
	v_mfma_f32_16x16x32_bf16 v[122:125], v[162:165], v[170:173], v[122:125]
	v_mfma_f32_16x16x32_bf16 v[114:117], v[154:157], v[178:181], v[114:117]
	v_mfma_f32_16x16x32_bf16 v[106:109], v[162:165], v[178:181], v[106:109]
	v_mfma_f32_16x16x32_bf16 v[98:101], v[154:157], v[186:189], v[98:101]
	v_mfma_f32_16x16x32_bf16 v[90:93], v[162:165], v[186:189], v[90:93]
	v_mfma_f32_16x16x32_bf16 v[82:85], v[154:157], v[194:197], v[82:85]
	v_mfma_f32_16x16x32_bf16 v[74:77], v[162:165], v[194:197], v[74:77]
	v_mfma_f32_16x16x32_bf16 v[126:129], v[134:137], v[166:169], v[126:129]
	v_mfma_f32_16x16x32_bf16 v[118:121], v[142:145], v[166:169], v[118:121]
	v_mfma_f32_16x16x32_bf16 v[110:113], v[134:137], v[174:177], v[110:113]
	v_mfma_f32_16x16x32_bf16 v[102:105], v[142:145], v[174:177], v[102:105]
	v_mfma_f32_16x16x32_bf16 v[94:97], v[134:137], v[182:185], v[94:97]
	v_mfma_f32_16x16x32_bf16 v[86:89], v[142:145], v[182:185], v[86:89]
	v_mfma_f32_16x16x32_bf16 v[78:81], v[134:137], v[190:193], v[78:81]
	v_mfma_f32_16x16x32_bf16 v[70:73], v[142:145], v[190:193], v[70:73]
	v_mfma_f32_16x16x32_bf16 v[126:129], v[138:141], v[170:173], v[126:129]
	v_mfma_f32_16x16x32_bf16 v[118:121], v[146:149], v[170:173], v[118:121]
	v_mfma_f32_16x16x32_bf16 v[110:113], v[138:141], v[178:181], v[110:113]
	v_mfma_f32_16x16x32_bf16 v[102:105], v[146:149], v[178:181], v[102:105]
	v_mfma_f32_16x16x32_bf16 v[94:97], v[138:141], v[186:189], v[94:97]
	v_mfma_f32_16x16x32_bf16 v[86:89], v[146:149], v[186:189], v[86:89]
	v_mfma_f32_16x16x32_bf16 v[78:81], v[138:141], v[194:197], v[78:81]
	v_mfma_f32_16x16x32_bf16 v[70:73], v[146:149], v[194:197], v[70:73]
	s_barrier
	s_add_i32 s30, s46, s34
	v_lshl_add_u64 v[216:217], v[216:217], 0, s[8:9]
	s_mov_b32 m0, s30
	ds_read_b128 v[190:193], v227 offset:49152
	ds_read_b128 v[194:197], v227 offset:50176
	ds_read_b128 v[182:185], v227 offset:51200
	ds_read_b128 v[186:189], v227 offset:52224
	ds_read_b128 v[174:177], v227 offset:53248
	ds_read_b128 v[178:181], v227 offset:54272
	ds_read_b128 v[166:169], v227 offset:55296
	ds_read_b128 v[170:173], v227 offset:56320
	global_load_lds_dwordx4 v[216:217], off
	s_add_i32 m0, s30, 0x2000
	s_add_u32 s28, s28, 0x40080
	v_lshl_add_u64 v[216:217], v[218:219], 0, s[8:9]
	s_addc_u32 s29, s29, 0
	s_add_i32 s30, s47, s34
	global_load_lds_dwordx4 v[216:217], off
	v_lshl_add_u64 v[216:217], s[28:29], 0, v[198:199]
	s_mov_b32 m0, s30
	v_lshl_add_u64 v[4:5], v[4:5], 0, s[8:9]
	global_load_lds_dwordx4 v[216:217], off
	v_lshl_add_u64 v[216:217], s[28:29], 0, v[200:201]
	s_add_i32 m0, s30, 0x2000
	s_and_b64 vcc, exec, s[4:5]
	global_load_lds_dwordx4 v[216:217], off
	v_lshl_add_u64 v[216:217], v[234:235], 0, s[8:9]
	s_mov_b32 m0, s38
	s_nop 0
	global_load_lds_dwordx4 v[216:217], off
	s_mov_b32 m0, s39
	s_nop 0
	global_load_lds_dwordx4 v[4:5], off
	s_waitcnt vmcnt(8)
	s_waitcnt lgkmcnt(0)
	s_barrier
	s_cbranch_vccnz .LBB0_1393
	s_waitcnt lgkmcnt(0)
	v_mfma_f32_16x16x32_bf16 v[66:69], v[150:153], v[190:193], v[66:69]
	v_mfma_f32_16x16x32_bf16 v[58:61], v[158:161], v[190:193], v[58:61]
	v_mfma_f32_16x16x32_bf16 v[50:53], v[150:153], v[182:185], v[50:53]
	v_mfma_f32_16x16x32_bf16 v[42:45], v[158:161], v[182:185], v[42:45]
	v_mfma_f32_16x16x32_bf16 v[34:37], v[150:153], v[174:177], v[34:37]
	v_mfma_f32_16x16x32_bf16 v[26:29], v[158:161], v[174:177], v[26:29]
	v_mfma_f32_16x16x32_bf16 v[18:21], v[150:153], v[166:169], v[18:21]
	v_mfma_f32_16x16x32_bf16 v[10:13], v[158:161], v[166:169], v[10:13]
	v_mfma_f32_16x16x32_bf16 v[66:69], v[154:157], v[194:197], v[66:69]
	v_mfma_f32_16x16x32_bf16 v[58:61], v[162:165], v[194:197], v[58:61]
	v_mfma_f32_16x16x32_bf16 v[50:53], v[154:157], v[186:189], v[50:53]
	v_mfma_f32_16x16x32_bf16 v[42:45], v[162:165], v[186:189], v[42:45]
	v_mfma_f32_16x16x32_bf16 v[34:37], v[154:157], v[178:181], v[34:37]
	v_mfma_f32_16x16x32_bf16 v[26:29], v[162:165], v[178:181], v[26:29]
	v_mfma_f32_16x16x32_bf16 v[18:21], v[154:157], v[170:173], v[18:21]
	v_mfma_f32_16x16x32_bf16 v[10:13], v[162:165], v[170:173], v[10:13]
	v_mfma_f32_16x16x32_bf16 v[62:65], v[134:137], v[190:193], v[62:65]
	v_mfma_f32_16x16x32_bf16 v[54:57], v[142:145], v[190:193], v[54:57]
	v_mfma_f32_16x16x32_bf16 v[46:49], v[134:137], v[182:185], v[46:49]
	v_mfma_f32_16x16x32_bf16 v[38:41], v[142:145], v[182:185], v[38:41]
	v_mfma_f32_16x16x32_bf16 v[30:33], v[134:137], v[174:177], v[30:33]
	v_mfma_f32_16x16x32_bf16 v[22:25], v[142:145], v[174:177], v[22:25]
	v_mfma_f32_16x16x32_bf16 v[14:17], v[134:137], v[166:169], v[14:17]
	v_mfma_f32_16x16x32_bf16 v[4:7], v[142:145], v[166:169], v[6:9]
	v_mfma_f32_16x16x32_bf16 v[62:65], v[138:141], v[194:197], v[62:65]
	v_mfma_f32_16x16x32_bf16 v[54:57], v[146:149], v[194:197], v[54:57]
	v_mfma_f32_16x16x32_bf16 v[46:49], v[138:141], v[186:189], v[46:49]
	v_mfma_f32_16x16x32_bf16 v[38:41], v[146:149], v[186:189], v[38:41]
	v_mfma_f32_16x16x32_bf16 v[30:33], v[138:141], v[178:181], v[30:33]
	v_mfma_f32_16x16x32_bf16 v[22:25], v[146:149], v[178:181], v[22:25]
	v_mfma_f32_16x16x32_bf16 v[14:17], v[138:141], v[170:173], v[14:17]
	v_mfma_f32_16x16x32_bf16 v[6:9], v[146:149], v[170:173], v[4:7]

; #define PG8_STAGE_A(bufoff, V0, V1, kb) do { \
;         __builtin_amdgcn_global_load_lds((const unsigned*)((Abase + (kb)) + (V0)), (LAS unsigned*)(lds + (bufoff) + ldsw), 16, 0, 0); \
;         __builtin_amdgcn_global_load_lds((const unsigned*)((Abase + (kb)) + (V1)), (LAS unsigned*)(lds + (bufoff) + ldsw + 8192), 16, 0, 0); } while (0)
; #define PG8_LDA(dst, b, h) do { _Pragma("unroll") for (int m = 0; m < 4; ++m) _Pragma("unroll") for (int k = 0; k < 2; ++k) dst[m][k] = *(const LAS bf16x8*)(lds + PG8_SA(b, h) + aoff + m * 2048 + k * 1024); } while (0)
; #define PG8_LDB(dst, b, h) do { _Pragma("unroll") for (int n = 0; n < 2; ++n) _Pragma("unroll") for (int k = 0; k < 2; ++k) dst[n][k] = *(const LAS bf16x8*)(lds + PG8_SB(b, h) + boff + n * 2048 + k * 1024); } while (0)
; #define PG8_MMA(ai, bj, At, Bt) do { __builtin_amdgcn_s_setprio(1); _Pragma("unroll") for (int m = 0; m < 4; ++m) _Pragma("unroll") for (int n = 0; n < 2; ++n) _Pragma("unroll") for (int k = 0; k < 2; ++k) \
;         acc[ai][bj][m][n] = __builtin_amdgcn_mfma_f32_16x16x32_bf16(Bt[n][k], At[m][k], acc[ai][bj][m][n], 0, 0, 0); __builtin_amdgcn_s_setprio(0); } while (0)
; #define PG8_WAIT_V(n) asm volatile("s_waitcnt vmcnt(" #n ")" ::: "memory")
; #define PG8_WAIT_L(n) asm volatile("s_waitcnt lgkmcnt(" #n ")" ::: "memory")
; #define PG8_BAR __builtin_amdgcn_s_barrier()
; #define PG8_SCHED __builtin_amdgcn_sched_barrier(0)
; template <class Epi, class Sched, bool ALIGN_EPI>
; __device__ __forceinline__ void gemm_phase(LAS unsigned char* lds, const Gemm g, const Sched& S, const Epi& E) {
;     ...
;             PG8_LDB(B0, 0, 0); PG8_LDB(B1, 0, 1); PG8_SCHED; PG8_LDA(At, 0, 0); PG8_STAGE_A(PG8_SA(1, 1), vc10, vc11, kb1);
;             PG8_WAIT_V(12); PG8_WAIT_L(0); PG8_BAR; PG8_MMA(0, 0, At, B0); PG8_MMA(0, 1, At, B1); PG8_BAR; PG8_SCHED;
.LBB0_2251:
	v_add_u32_e32 v162, 0x10000, v240
	v_add_u32_e32 v174, 0x14000, v240
	ds_read_b128 v[178:181], v162
	ds_read_b128 v[182:185], v162 offset:1024
	ds_read_b128 v[186:189], v162 offset:2048
	ds_read_b128 v[190:193], v162 offset:3072
	ds_read_b128 v[162:165], v174
	ds_read_b128 v[166:169], v174 offset:1024
	ds_read_b128 v[170:173], v174 offset:2048
	ds_read_b128 v[174:177], v174 offset:3072
	s_add_i32 s54, s53, 2
	s_add_i32 m0, s40, 0xc000
	s_add_u32 s4, s90, s22
	s_addc_u32 s5, s91, s23
	s_waitcnt lgkmcnt(0)
	ds_read_b128 v[194:197], v241
	ds_read_b128 v[198:201], v241 offset:1024
	ds_read_b128 v[202:205], v241 offset:2048
	ds_read_b128 v[206:209], v241 offset:3072
	ds_read_b128 v[210:213], v241 offset:4096
	ds_read_b128 v[214:217], v241 offset:5120
	ds_read_b128 v[218:221], v241 offset:6144
	ds_read_b128 v[222:225], v241 offset:7168
	global_load_lds_dwordx4 v234, s[4:5]
	s_add_i32 m0, s40, 0xe000
	s_nop 0
	global_load_lds_dwordx4 v235, s[4:5]
	s_waitcnt vmcnt(12)
	s_waitcnt lgkmcnt(0)
	s_barrier
	s_waitcnt lgkmcnt(0)
	v_mfma_f32_16x16x32_bf16 v[158:161], v[178:181], v[194:197], v[158:161]
	v_mfma_f32_16x16x32_bf16 v[150:153], v[186:189], v[194:197], v[150:153]
	v_mfma_f32_16x16x32_bf16 v[142:145], v[178:181], v[202:205], v[142:145]
	v_mfma_f32_16x16x32_bf16 v[134:137], v[186:189], v[202:205], v[134:137]
	v_mfma_f32_16x16x32_bf16 v[126:129], v[178:181], v[210:213], v[126:129]
	v_mfma_f32_16x16x32_bf16 v[118:121], v[186:189], v[210:213], v[118:121]
	v_mfma_f32_16x16x32_bf16 v[110:113], v[178:181], v[218:221], v[110:113]
	v_mfma_f32_16x16x32_bf16 v[102:105], v[186:189], v[218:221], v[102:105]
	v_mfma_f32_16x16x32_bf16 v[158:161], v[182:185], v[198:201], v[158:161]
	v_mfma_f32_16x16x32_bf16 v[150:153], v[190:193], v[198:201], v[150:153]
	v_mfma_f32_16x16x32_bf16 v[142:145], v[182:185], v[206:209], v[142:145]
	v_mfma_f32_16x16x32_bf16 v[134:137], v[190:193], v[206:209], v[134:137]
	v_mfma_f32_16x16x32_bf16 v[126:129], v[182:185], v[214:217], v[126:129]
	v_mfma_f32_16x16x32_bf16 v[118:121], v[190:193], v[214:217], v[118:121]
	v_mfma_f32_16x16x32_bf16 v[110:113], v[182:185], v[222:225], v[110:113]
	v_mfma_f32_16x16x32_bf16 v[102:105], v[190:193], v[222:225], v[102:105]
	v_mfma_f32_16x16x32_bf16 v[154:157], v[162:165], v[194:197], v[154:157]
	v_mfma_f32_16x16x32_bf16 v[146:149], v[170:173], v[194:197], v[146:149]
	v_mfma_f32_16x16x32_bf16 v[138:141], v[162:165], v[202:205], v[138:141]
	v_mfma_f32_16x16x32_bf16 v[130:133], v[170:173], v[202:205], v[130:133]
	v_mfma_f32_16x16x32_bf16 v[122:125], v[162:165], v[210:213], v[122:125]
	v_mfma_f32_16x16x32_bf16 v[114:117], v[170:173], v[210:213], v[114:117]
	v_mfma_f32_16x16x32_bf16 v[106:109], v[162:165], v[218:221], v[106:109]
	v_mfma_f32_16x16x32_bf16 v[98:101], v[170:173], v[218:221], v[98:101]
	v_mfma_f32_16x16x32_bf16 v[154:157], v[166:169], v[198:201], v[154:157]
	v_mfma_f32_16x16x32_bf16 v[146:149], v[174:177], v[198:201], v[146:149]
	v_mfma_f32_16x16x32_bf16 v[138:141], v[166:169], v[206:209], v[138:141]
	v_mfma_f32_16x16x32_bf16 v[130:133], v[174:177], v[206:209], v[130:133]
	v_mfma_f32_16x16x32_bf16 v[122:125], v[166:169], v[214:217], v[122:125]
	v_mfma_f32_16x16x32_bf16 v[114:117], v[174:177], v[214:217], v[114:117]
	v_mfma_f32_16x16x32_bf16 v[106:109], v[166:169], v[222:225], v[106:109]
	v_mfma_f32_16x16x32_bf16 v[98:101], v[174:177], v[222:225], v[98:101]
	s_barrier
	s_cmp_lt_u32 s54, 13
	s_mov_b64 s[6:7], -1
	s_cbranch_scc0 .LBB0_2253
	s_add_u32 s4, s20, 0x30000
	s_addc_u32 s5, s21, 0
	s_mov_b64 s[6:7], 0

; #define PG8_BWAIT(n) asm volatile("s_waitcnt vmcnt(" #n ")" : "+v"(bv[0]), "+v"(bv[1]), "+v"(bv[2]), "+v"(bv[3]), "+v"(bv[4]), "+v"(bv[5]), "+v"(bv[6]), "+v"(bv[7]) :: "memory")
; #define PG8_STAGE_A(bufoff, V0, V1, kb) do { \
;         __builtin_amdgcn_global_load_lds((const unsigned*)((Abase + (kb)) + (V0)), (LAS unsigned*)(lds + (bufoff) + ldsw), 16, 0, 0); \
;         __builtin_amdgcn_global_load_lds((const unsigned*)((Abase + (kb)) + (V1)), (LAS unsigned*)(lds + (bufoff) + ldsw + 8192), 16, 0, 0); } while (0)
; #define PG8_LDA(dst, b, h) do { _Pragma("unroll") for (int m = 0; m < 4; ++m) _Pragma("unroll") for (int k = 0; k < 2; ++k) dst[m][k] = *(const LAS bf16x8*)(lds + PG8_SA(b, h) + aoff + m * 2048 + k * 1024); } while (0)
; #define PG8_MMA(ai, bj, At, Bt) do { __builtin_amdgcn_s_setprio(1); _Pragma("unroll") for (int m = 0; m < 4; ++m) _Pragma("unroll") for (int n = 0; n < 2; ++n) _Pragma("unroll") for (int k = 0; k < 2; ++k) \
;         acc[ai][bj][m][n] = __builtin_amdgcn_mfma_f32_16x16x32_bf16(Bt[n][k], At[m][k], acc[ai][bj][m][n], 0, 0, 0); __builtin_amdgcn_s_setprio(0); } while (0)
; #define PG8_WAIT_V(n) asm volatile("s_waitcnt vmcnt(" #n ")" ::: "memory")
; #define PG8_WAIT_L(n) asm volatile("s_waitcnt lgkmcnt(" #n ")" ::: "memory")
; #define PG8_BAR __builtin_amdgcn_s_barrier()
; #define PG8_SCHED __builtin_amdgcn_sched_barrier(0)
; template <class Epi, class Sched, bool ALIGN_EPI>
; __device__ __forceinline__ void gemm_phase(LAS unsigned char* lds, const Gemm g, const Sched& S, const Epi& E) {
;     ...
;             PG8_BWAIT(2); PG8_BCOMMIT(0); PG8_SCHED; PG8_LDA(At, 0, 1); PG8_BISSUE(t + 3 >= nt ? pbn + (size_t)(t + 3 - nt) * 64 * Sched::LDN : pbc + (size_t)(t + 3) * 64 * Sched::LDN); PG8_STAGE_A(PG8_SA(0, 0), vc00, vc01, kb2);
;             PG8_WAIT_V(12); PG8_WAIT_L(0); PG8_BAR; if (half1) { PG8_MMA(1, 0, At, B0); PG8_MMA(1, 1, At, B1); } PG8_BAR; PG8_SCHED;
.LBB0_2255:
	s_add_i32 s2, s22, 0xe8940080
	s_cmp_eq_u32 s53, 12
	s_waitcnt vmcnt(2)
	s_nop 0
	v_cvt_pk_bf16_f32 v194, v2, v6
	v_cvt_pk_bf16_f32 v198, v3, v7
	v_cvt_pk_bf16_f32 v202, v4, v8
	v_cvt_pk_bf16_f32 v206, v5, v9
	global_load_dwordx4 v[2:5], v231, s[4:5] offset:0
	s_cselect_b64 s[6:7], -1, 0
	global_load_dwordx4 v[6:9], v231, s[4:5] offset:0x400
	v_cvt_pk_bf16_f32 v195, v10, v14
	v_cvt_pk_bf16_f32 v199, v11, v15
	v_cvt_pk_bf16_f32 v203, v12, v16
	v_cvt_pk_bf16_f32 v207, v13, v17
	s_and_b64 s[26:27], s[6:7], exec
	global_load_dwordx4 v[10:13], v231, s[4:5] offset:0x800
	s_cselect_b32 s2, 0, s2
	global_load_dwordx4 v[14:17], v231, s[4:5] offset:0xc00
	v_cvt_pk_bf16_f32 v196, v18, v22
	v_cvt_pk_bf16_f32 v200, v19, v23
	v_cvt_pk_bf16_f32 v204, v20, v24
	v_cvt_pk_bf16_f32 v208, v21, v25
	s_add_u32 s4, s4, 0x1000
	s_addc_u32 s5, s5, 0
	global_load_dwordx4 v[18:21], v231, s[4:5] offset:0
	global_load_dwordx4 v[22:25], v231, s[4:5] offset:0x400
	v_cvt_pk_bf16_f32 v197, v26, v30
	v_cvt_pk_bf16_f32 v201, v27, v31
	v_cvt_pk_bf16_f32 v205, v28, v32
	v_cvt_pk_bf16_f32 v209, v29, v33
	global_load_dwordx4 v[26:29], v231, s[4:5] offset:0x800
	global_load_dwordx4 v[30:33], v231, s[4:5] offset:0xc00
	v_add_u32_e32 v210, 0x10000, v232
	v_xor_b32_e32 v211, 64, v210
	v_xor_b32_e32 v212, 0x80, v210
	v_xor_b32_e32 v213, 0xc0, v210
	ds_write_b128 v210, v[194:197]
	ds_write_b128 v211, v[198:201]
	ds_write_b128 v212, v[202:205]
	ds_write_b128 v213, v[206:209]
	ds_read_b128 v[218:221], v241 offset:16384
	ds_read_b128 v[222:225], v241 offset:17408
	ds_read_b128 v[210:213], v241 offset:18432
	ds_read_b128 v[214:217], v241 offset:19456
	ds_read_b128 v[202:205], v241 offset:20480
	ds_read_b128 v[206:209], v241 offset:21504
	ds_read_b128 v[194:197], v241 offset:22528
	ds_read_b128 v[198:201], v241 offset:23552
	v_readlane_b32 s4, v255, 13
	v_readlane_b32 s5, v255, 14
	s_add_u32 s26, s4, s2
	s_mov_b32 m0, s40
	v_cndmask_b32_e64 v226, v226, v242, s[6:7]
	s_addc_u32 s27, s5, 0
	v_cndmask_b32_e64 v228, v228, v243, s[6:7]
	global_load_lds_dwordx4 v226, s[26:27]
	s_mov_b32 m0, s41
	v_cndmask_b32_e64 v229, 0, 1, s[24:25]
	global_load_lds_dwordx4 v228, s[26:27]
	s_waitcnt vmcnt(12)
	s_waitcnt lgkmcnt(0)
	v_cmp_ne_u32_e64 s[4:5], 1, v229
	s_andn2_b64 vcc, exec, s[24:25]
	s_barrier
	s_cbranch_vccnz .LBB0_2257
	s_waitcnt lgkmcnt(0)
	v_mfma_f32_16x16x32_bf16 v[94:97], v[178:181], v[218:221], v[94:97]
	v_mfma_f32_16x16x32_bf16 v[86:89], v[186:189], v[218:221], v[86:89]
	v_mfma_f32_16x16x32_bf16 v[78:81], v[178:181], v[210:213], v[78:81]
	v_mfma_f32_16x16x32_bf16 v[70:73], v[186:189], v[210:213], v[70:73]
	v_mfma_f32_16x16x32_bf16 v[62:65], v[178:181], v[202:205], v[62:65]
	v_mfma_f32_16x16x32_bf16 v[54:57], v[186:189], v[202:205], v[54:57]
	v_mfma_f32_16x16x32_bf16 v[46:49], v[178:181], v[194:197], v[46:49]
	v_mfma_f32_16x16x32_bf16 v[38:41], v[186:189], v[194:197], v[38:41]
	v_mfma_f32_16x16x32_bf16 v[94:97], v[182:185], v[222:225], v[94:97]
	v_mfma_f32_16x16x32_bf16 v[86:89], v[190:193], v[222:225], v[86:89]
	v_mfma_f32_16x16x32_bf16 v[78:81], v[182:185], v[214:217], v[78:81]
	v_mfma_f32_16x16x32_bf16 v[70:73], v[190:193], v[214:217], v[70:73]
	v_mfma_f32_16x16x32_bf16 v[62:65], v[182:185], v[206:209], v[62:65]
	v_mfma_f32_16x16x32_bf16 v[54:57], v[190:193], v[206:209], v[54:57]
	v_mfma_f32_16x16x32_bf16 v[46:49], v[182:185], v[198:201], v[46:49]
	v_mfma_f32_16x16x32_bf16 v[38:41], v[190:193], v[198:201], v[38:41]
	v_mfma_f32_16x16x32_bf16 v[90:93], v[162:165], v[218:221], v[90:93]
	v_mfma_f32_16x16x32_bf16 v[82:85], v[170:173], v[218:221], v[82:85]
	v_mfma_f32_16x16x32_bf16 v[74:77], v[162:165], v[210:213], v[74:77]
	v_mfma_f32_16x16x32_bf16 v[66:69], v[170:173], v[210:213], v[66:69]
	v_mfma_f32_16x16x32_bf16 v[58:61], v[162:165], v[202:205], v[58:61]
	v_mfma_f32_16x16x32_bf16 v[50:53], v[170:173], v[202:205], v[50:53]
	v_mfma_f32_16x16x32_bf16 v[42:45], v[162:165], v[194:197], v[42:45]
	v_mfma_f32_16x16x32_bf16 v[34:37], v[170:173], v[194:197], v[34:37]
	v_mfma_f32_16x16x32_bf16 v[90:93], v[166:169], v[222:225], v[90:93]
	v_mfma_f32_16x16x32_bf16 v[82:85], v[174:177], v[222:225], v[82:85]
	v_mfma_f32_16x16x32_bf16 v[74:77], v[166:169], v[214:217], v[74:77]
	v_mfma_f32_16x16x32_bf16 v[66:69], v[174:177], v[214:217], v[66:69]
	v_mfma_f32_16x16x32_bf16 v[58:61], v[166:169], v[206:209], v[58:61]
	v_mfma_f32_16x16x32_bf16 v[50:53], v[174:177], v[206:209], v[50:53]
	v_mfma_f32_16x16x32_bf16 v[42:45], v[166:169], v[198:201], v[42:45]
	v_mfma_f32_16x16x32_bf16 v[34:37], v[174:177], v[198:201], v[34:37]
; #define PG8_STAGE_A(bufoff, V0, V1, kb) do { \
;         __builtin_amdgcn_global_load_lds((const unsigned*)((Abase + (kb)) + (V0)), (LAS unsigned*)(lds + (bufoff) + ldsw), 16, 0, 0); \
;         __builtin_amdgcn_global_load_lds((const unsigned*)((Abase + (kb)) + (V1)), (LAS unsigned*)(lds + (bufoff) + ldsw + 8192), 16, 0, 0); } while (0)
; #define PG8_LDA(dst, b, h) do { _Pragma("unroll") for (int m = 0; m < 4; ++m) _Pragma("unroll") for (int k = 0; k < 2; ++k) dst[m][k] = *(const LAS bf16x8*)(lds + PG8_SA(b, h) + aoff + m * 2048 + k * 1024); } while (0)
; #define PG8_LDB(dst, b, h) do { _Pragma("unroll") for (int n = 0; n < 2; ++n) _Pragma("unroll") for (int k = 0; k < 2; ++k) dst[n][k] = *(const LAS bf16x8*)(lds + PG8_SB(b, h) + boff + n * 2048 + k * 1024); } while (0)
; #define PG8_MMA(ai, bj, At, Bt) do { __builtin_amdgcn_s_setprio(1); _Pragma("unroll") for (int m = 0; m < 4; ++m) _Pragma("unroll") for (int n = 0; n < 2; ++n) _Pragma("unroll") for (int k = 0; k < 2; ++k) \
;         acc[ai][bj][m][n] = __builtin_amdgcn_mfma_f32_16x16x32_bf16(Bt[n][k], At[m][k], acc[ai][bj][m][n], 0, 0, 0); __builtin_amdgcn_s_setprio(0); } while (0)
; #define PG8_WAIT_V(n) asm volatile("s_waitcnt vmcnt(" #n ")" ::: "memory")
; #define PG8_WAIT_L(n) asm volatile("s_waitcnt lgkmcnt(" #n ")" ::: "memory")
; #define PG8_BAR __builtin_amdgcn_s_barrier()
; #define PG8_SCHED __builtin_amdgcn_sched_barrier(0)
; template <class Epi, class Sched, bool ALIGN_EPI>
; __device__ __forceinline__ void gemm_phase(LAS unsigned char* lds, const Gemm g, const Sched& S, const Epi& E) {
;     ...
;             PG8_LDB(B0, 1, 0); PG8_LDB(B1, 1, 1); PG8_SCHED; PG8_LDA(At, 1, 0); PG8_STAGE_A(PG8_SA(0, 1), vc10, vc11, kb2);
;             PG8_WAIT_V(12); PG8_WAIT_L(0); PG8_BAR; PG8_MMA(0, 0, At, B0); PG8_MMA(0, 1, At, B1); PG8_BAR; PG8_SCHED;
.LBB0_2257:
	v_cndmask_b32_e64 v235, v235, v245, s[6:7]
	v_cndmask_b32_e64 v234, v234, v244, s[6:7]
	s_barrier
	v_add_u32_e32 v162, 0x18000, v240
	v_add_u32_e32 v174, 0x1c000, v240
	ds_read_b128 v[178:181], v162
	ds_read_b128 v[182:185], v162 offset:1024
	ds_read_b128 v[186:189], v162 offset:2048
	ds_read_b128 v[190:193], v162 offset:3072
	ds_read_b128 v[162:165], v174
	ds_read_b128 v[166:169], v174 offset:1024
	ds_read_b128 v[170:173], v174 offset:2048
	ds_read_b128 v[174:177], v174 offset:3072
	s_mov_b32 m0, s42
	s_waitcnt lgkmcnt(0)
	ds_read_b128 v[194:197], v241 offset:32768
	ds_read_b128 v[198:201], v241 offset:33792
	ds_read_b128 v[202:205], v241 offset:34816
	ds_read_b128 v[206:209], v241 offset:35840
	ds_read_b128 v[210:213], v241 offset:36864
	ds_read_b128 v[214:217], v241 offset:37888
	ds_read_b128 v[218:221], v241 offset:38912
	ds_read_b128 v[222:225], v241 offset:39936
	global_load_lds_dwordx4 v234, s[26:27]
	s_mov_b32 m0, s43
	s_nop 0
	global_load_lds_dwordx4 v235, s[26:27]
	s_waitcnt vmcnt(12)
	s_waitcnt lgkmcnt(0)
	s_barrier
	s_waitcnt lgkmcnt(0)
	v_mfma_f32_16x16x32_bf16 v[158:161], v[178:181], v[194:197], v[158:161]
	v_mfma_f32_16x16x32_bf16 v[150:153], v[186:189], v[194:197], v[150:153]
	v_mfma_f32_16x16x32_bf16 v[142:145], v[178:181], v[202:205], v[142:145]
	v_mfma_f32_16x16x32_bf16 v[134:137], v[186:189], v[202:205], v[134:137]
	v_mfma_f32_16x16x32_bf16 v[126:129], v[178:181], v[210:213], v[126:129]
	v_mfma_f32_16x16x32_bf16 v[118:121], v[186:189], v[210:213], v[118:121]
	v_mfma_f32_16x16x32_bf16 v[110:113], v[178:181], v[218:221], v[110:113]
	v_mfma_f32_16x16x32_bf16 v[102:105], v[186:189], v[218:221], v[102:105]
	v_mfma_f32_16x16x32_bf16 v[158:161], v[182:185], v[198:201], v[158:161]
	v_mfma_f32_16x16x32_bf16 v[150:153], v[190:193], v[198:201], v[150:153]
	v_mfma_f32_16x16x32_bf16 v[142:145], v[182:185], v[206:209], v[142:145]
	v_mfma_f32_16x16x32_bf16 v[134:137], v[190:193], v[206:209], v[134:137]
	v_mfma_f32_16x16x32_bf16 v[126:129], v[182:185], v[214:217], v[126:129]
	v_mfma_f32_16x16x32_bf16 v[118:121], v[190:193], v[214:217], v[118:121]
	v_mfma_f32_16x16x32_bf16 v[110:113], v[182:185], v[222:225], v[110:113]
	v_mfma_f32_16x16x32_bf16 v[102:105], v[190:193], v[222:225], v[102:105]
	v_mfma_f32_16x16x32_bf16 v[154:157], v[162:165], v[194:197], v[154:157]
	v_mfma_f32_16x16x32_bf16 v[146:149], v[170:173], v[194:197], v[146:149]
	v_mfma_f32_16x16x32_bf16 v[138:141], v[162:165], v[202:205], v[138:141]
	v_mfma_f32_16x16x32_bf16 v[130:133], v[170:173], v[202:205], v[130:133]
	v_mfma_f32_16x16x32_bf16 v[122:125], v[162:165], v[210:213], v[122:125]
	v_mfma_f32_16x16x32_bf16 v[114:117], v[170:173], v[210:213], v[114:117]
	v_mfma_f32_16x16x32_bf16 v[106:109], v[162:165], v[218:221], v[106:109]
	v_mfma_f32_16x16x32_bf16 v[98:101], v[170:173], v[218:221], v[98:101]
	v_mfma_f32_16x16x32_bf16 v[154:157], v[166:169], v[198:201], v[154:157]
	v_mfma_f32_16x16x32_bf16 v[146:149], v[174:177], v[198:201], v[146:149]
	v_mfma_f32_16x16x32_bf16 v[138:141], v[166:169], v[206:209], v[138:141]
	v_mfma_f32_16x16x32_bf16 v[130:133], v[174:177], v[206:209], v[130:133]
	v_mfma_f32_16x16x32_bf16 v[122:125], v[166:169], v[214:217], v[122:125]
	v_mfma_f32_16x16x32_bf16 v[114:117], v[174:177], v[214:217], v[114:117]
	v_mfma_f32_16x16x32_bf16 v[106:109], v[166:169], v[222:225], v[106:109]
	v_mfma_f32_16x16x32_bf16 v[98:101], v[174:177], v[222:225], v[98:101]
	s_barrier
	s_cmp_lt_u32 s54, 12
	s_mov_b64 s[28:29], -1
	s_cbranch_scc0 .LBB0_2259
	s_add_u32 s6, s20, 0x40000
	s_addc_u32 s7, s21, 0
	s_mov_b64 s[28:29], 0

; #define PG8_BWAIT(n) asm volatile("s_waitcnt vmcnt(" #n ")" : "+v"(bv[0]), "+v"(bv[1]), "+v"(bv[2]), "+v"(bv[3]), "+v"(bv[4]), "+v"(bv[5]), "+v"(bv[6]), "+v"(bv[7]) :: "memory")
; #define PG8_STAGE_A(bufoff, V0, V1, kb) do { \
;         __builtin_amdgcn_global_load_lds((const unsigned*)((Abase + (kb)) + (V0)), (LAS unsigned*)(lds + (bufoff) + ldsw), 16, 0, 0); \
;         __builtin_amdgcn_global_load_lds((const unsigned*)((Abase + (kb)) + (V1)), (LAS unsigned*)(lds + (bufoff) + ldsw + 8192), 16, 0, 0); } while (0)
; #define PG8_LDA(dst, b, h) do { _Pragma("unroll") for (int m = 0; m < 4; ++m) _Pragma("unroll") for (int k = 0; k < 2; ++k) dst[m][k] = *(const LAS bf16x8*)(lds + PG8_SA(b, h) + aoff + m * 2048 + k * 1024); } while (0)
; #define PG8_MMA(ai, bj, At, Bt) do { __builtin_amdgcn_s_setprio(1); _Pragma("unroll") for (int m = 0; m < 4; ++m) _Pragma("unroll") for (int n = 0; n < 2; ++n) _Pragma("unroll") for (int k = 0; k < 2; ++k) \
;         acc[ai][bj][m][n] = __builtin_amdgcn_mfma_f32_16x16x32_bf16(Bt[n][k], At[m][k], acc[ai][bj][m][n], 0, 0, 0); __builtin_amdgcn_s_setprio(0); } while (0)
; #define PG8_WAIT_V(n) asm volatile("s_waitcnt vmcnt(" #n ")" ::: "memory")
; #define PG8_WAIT_L(n) asm volatile("s_waitcnt lgkmcnt(" #n ")" ::: "memory")
; #define PG8_BAR __builtin_amdgcn_s_barrier()
; #define PG8_SCHED __builtin_amdgcn_sched_barrier(0)
; template <class Epi, class Sched, bool ALIGN_EPI>
; __device__ __forceinline__ void gemm_phase(LAS unsigned char* lds, const Gemm g, const Sched& S, const Epi& E) {
;     ...
;             PG8_BWAIT(2); PG8_BCOMMIT(1); PG8_SCHED; PG8_LDA(At, 1, 1); PG8_BISSUE(t + 4 >= nt ? pbn + (size_t)(t + 4 - nt) * 64 * Sched::LDN : pbc + (size_t)(t + 4) * 64 * Sched::LDN); PG8_STAGE_A(PG8_SA(1, 0), vc00, vc01, kb2 + 128u);
;             PG8_WAIT_V(12); PG8_WAIT_L(0); PG8_BAR; if (half1) { PG8_MMA(1, 0, At, B0); PG8_MMA(1, 1, At, B1); } PG8_BAR; PG8_SCHED;
.LBB0_2261:
	s_waitcnt vmcnt(2)
	s_nop 0
	v_cvt_pk_bf16_f32 v194, v2, v6
	v_cvt_pk_bf16_f32 v198, v3, v7
	v_cvt_pk_bf16_f32 v202, v4, v8
	v_cvt_pk_bf16_f32 v206, v5, v9
	global_load_dwordx4 v[2:5], v231, s[6:7] offset:0
	global_load_dwordx4 v[6:9], v231, s[6:7] offset:0x400
	v_cvt_pk_bf16_f32 v195, v10, v14
	v_cvt_pk_bf16_f32 v199, v11, v15
	v_cvt_pk_bf16_f32 v203, v12, v16
	v_cvt_pk_bf16_f32 v207, v13, v17
	global_load_dwordx4 v[10:13], v231, s[6:7] offset:0x800
	global_load_dwordx4 v[14:17], v231, s[6:7] offset:0xc00
	v_cvt_pk_bf16_f32 v196, v18, v22
	v_cvt_pk_bf16_f32 v200, v19, v23
	v_cvt_pk_bf16_f32 v204, v20, v24
	v_cvt_pk_bf16_f32 v208, v21, v25
	s_add_u32 s6, s6, 0x1000
	s_addc_u32 s7, s7, 0
	global_load_dwordx4 v[18:21], v231, s[6:7] offset:0
	global_load_dwordx4 v[22:25], v231, s[6:7] offset:0x400
	v_cvt_pk_bf16_f32 v197, v26, v30
	v_cvt_pk_bf16_f32 v201, v27, v31
	v_cvt_pk_bf16_f32 v205, v28, v32
	v_cvt_pk_bf16_f32 v209, v29, v33
	v_lshl_add_u64 v[246:247], s[26:27], 0, v[226:227]
	v_mov_b32_e32 v229, v227
	global_load_dwordx4 v[26:29], v231, s[6:7] offset:0x800
	s_mov_b32 m0, s44
	v_lshl_add_u64 v[248:249], s[26:27], 0, v[228:229]
	global_load_dwordx4 v[30:33], v231, s[6:7] offset:0xc00
	v_add_u32_e32 v210, 0x18000, v232
	v_xor_b32_e32 v211, 64, v210
	v_xor_b32_e32 v212, 0x80, v210
	v_xor_b32_e32 v213, 0xc0, v210
	ds_write_b128 v210, v[194:197]
	ds_write_b128 v211, v[198:201]
	ds_write_b128 v212, v[202:205]
	ds_write_b128 v213, v[206:209]
	ds_read_b128 v[218:221], v241 offset:49152
	ds_read_b128 v[222:225], v241 offset:50176
	ds_read_b128 v[210:213], v241 offset:51200
	ds_read_b128 v[214:217], v241 offset:52224
	ds_read_b128 v[202:205], v241 offset:53248
	ds_read_b128 v[206:209], v241 offset:54272
	ds_read_b128 v[194:197], v241 offset:55296
	ds_read_b128 v[198:201], v241 offset:56320
	v_lshl_add_u64 v[246:247], v[246:247], 0, s[12:13]
	global_load_lds_dwordx4 v[246:247], off
	v_lshl_add_u64 v[246:247], v[248:249], 0, s[12:13]
	s_mov_b32 m0, s45
	s_and_b64 vcc, exec, s[4:5]
	global_load_lds_dwordx4 v[246:247], off
	s_waitcnt vmcnt(12)
	s_waitcnt lgkmcnt(0)
	s_barrier
	s_cbranch_vccnz .LBB0_2263
	s_waitcnt lgkmcnt(0)
	v_mfma_f32_16x16x32_bf16 v[94:97], v[178:181], v[218:221], v[94:97]
	v_mfma_f32_16x16x32_bf16 v[86:89], v[186:189], v[218:221], v[86:89]
	v_mfma_f32_16x16x32_bf16 v[78:81], v[178:181], v[210:213], v[78:81]
	v_mfma_f32_16x16x32_bf16 v[70:73], v[186:189], v[210:213], v[70:73]
	v_mfma_f32_16x16x32_bf16 v[62:65], v[178:181], v[202:205], v[62:65]
	v_mfma_f32_16x16x32_bf16 v[54:57], v[186:189], v[202:205], v[54:57]
	v_mfma_f32_16x16x32_bf16 v[46:49], v[178:181], v[194:197], v[46:49]
	v_mfma_f32_16x16x32_bf16 v[38:41], v[186:189], v[194:197], v[38:41]
	v_mfma_f32_16x16x32_bf16 v[94:97], v[182:185], v[222:225], v[94:97]
	v_mfma_f32_16x16x32_bf16 v[86:89], v[190:193], v[222:225], v[86:89]
	v_mfma_f32_16x16x32_bf16 v[78:81], v[182:185], v[214:217], v[78:81]
	v_mfma_f32_16x16x32_bf16 v[70:73], v[190:193], v[214:217], v[70:73]
	v_mfma_f32_16x16x32_bf16 v[62:65], v[182:185], v[206:209], v[62:65]
	v_mfma_f32_16x16x32_bf16 v[54:57], v[190:193], v[206:209], v[54:57]
	v_mfma_f32_16x16x32_bf16 v[46:49], v[182:185], v[198:201], v[46:49]
	v_mfma_f32_16x16x32_bf16 v[38:41], v[190:193], v[198:201], v[38:41]
	v_mfma_f32_16x16x32_bf16 v[90:93], v[162:165], v[218:221], v[90:93]
	v_mfma_f32_16x16x32_bf16 v[82:85], v[170:173], v[218:221], v[82:85]
	v_mfma_f32_16x16x32_bf16 v[74:77], v[162:165], v[210:213], v[74:77]
	v_mfma_f32_16x16x32_bf16 v[66:69], v[170:173], v[210:213], v[66:69]
	v_mfma_f32_16x16x32_bf16 v[58:61], v[162:165], v[202:205], v[58:61]
	v_mfma_f32_16x16x32_bf16 v[50:53], v[170:173], v[202:205], v[50:53]
	v_mfma_f32_16x16x32_bf16 v[42:45], v[162:165], v[194:197], v[42:45]
	v_mfma_f32_16x16x32_bf16 v[34:37], v[170:173], v[194:197], v[34:37]
	v_mfma_f32_16x16x32_bf16 v[90:93], v[166:169], v[222:225], v[90:93]
	v_mfma_f32_16x16x32_bf16 v[82:85], v[174:177], v[222:225], v[82:85]
	v_mfma_f32_16x16x32_bf16 v[74:77], v[166:169], v[214:217], v[74:77]
	v_mfma_f32_16x16x32_bf16 v[66:69], v[174:177], v[214:217], v[66:69]
	v_mfma_f32_16x16x32_bf16 v[58:61], v[166:169], v[206:209], v[58:61]
	v_mfma_f32_16x16x32_bf16 v[50:53], v[174:177], v[206:209], v[50:53]
	v_mfma_f32_16x16x32_bf16 v[42:45], v[166:169], v[198:201], v[42:45]
	v_mfma_f32_16x16x32_bf16 v[34:37], v[174:177], v[198:201], v[34:37]

; #define PG8_STAGE_B(bufoff, gbase) do { _Pragma("unroll") for (int _i = 0; _i < 2; ++_i) \
;         __builtin_amdgcn_global_load_lds((const unsigned*)((const char*)(gbase) + voffB[_i]), (LAS unsigned*)(lds + (bufoff) + ldsw + _i * 8192), 16, 0, 0); } while (0)
; #define PG8_STAGE_A(bufoff, V0, V1, kb) do { \
;         __builtin_amdgcn_global_load_lds((const unsigned*)((Abase + (kb)) + (V0)), (LAS unsigned*)(lds + (bufoff) + ldsw), 16, 0, 0); \
;         __builtin_amdgcn_global_load_lds((const unsigned*)((Abase + (kb)) + (V1)), (LAS unsigned*)(lds + (bufoff) + ldsw + 8192), 16, 0, 0); } while (0)
; #define PG8_LDA(dst, b, h) do { _Pragma("unroll") for (int m = 0; m < 4; ++m) _Pragma("unroll") for (int k = 0; k < 2; ++k) dst[m][k] = *(const LAS bf16x8*)(lds + PG8_SA(b, h) + aoff + m * 2048 + k * 1024); } while (0)
; #define PG8_LDB(dst, b, h) do { _Pragma("unroll") for (int n = 0; n < 2; ++n) _Pragma("unroll") for (int k = 0; k < 2; ++k) dst[n][k] = *(const LAS bf16x8*)(lds + PG8_SB(b, h) + boff + n * 2048 + k * 1024); } while (0)
; #define PG8_MMA(ai, bj, At, Bt) do { __builtin_amdgcn_s_setprio(1); _Pragma("unroll") for (int m = 0; m < 4; ++m) _Pragma("unroll") for (int n = 0; n < 2; ++n) _Pragma("unroll") for (int k = 0; k < 2; ++k) \
;         acc[ai][bj][m][n] = __builtin_amdgcn_mfma_f32_16x16x32_bf16(Bt[n][k], At[m][k], acc[ai][bj][m][n], 0, 0, 0); __builtin_amdgcn_s_setprio(0); } while (0)
; #define PG8_WAIT_V(n) asm volatile("s_waitcnt vmcnt(" #n ")" ::: "memory")
; #define PG8_WAIT_L(n) asm volatile("s_waitcnt lgkmcnt(" #n ")" ::: "memory")
; #define PG8_BAR __builtin_amdgcn_s_barrier()
; #define PG8_SCHED __builtin_amdgcn_sched_barrier(0)
; template <class Epi, class Sched, bool ALIGN_EPI>
; __device__ __forceinline__ void gemm_phase(LAS unsigned char* lds, const Gemm g, const Sched& S, const Epi& E) {
;     ...
;             PG8_LDB(B0, 0, 0); PG8_LDB(B1, 0, 1); PG8_SCHED; PG8_LDA(At, 0, 0); PG8_STAGE_A(PG8_SA(1, 1), vc10, vc11, kb1);
;             PG8_WAIT_V(8); PG8_WAIT_L(0); PG8_BAR; PG8_MMA(0, 0, At, B0); PG8_MMA(0, 1, At, B1); PG8_BAR; PG8_SCHED;
;             PG8_LDA(At, 0, 1); PG8_STAGE_B(PG8_SB(0, 0), b2); PG8_STAGE_B(PG8_SB(0, 1), b2 + hstepB); PG8_STAGE_A(PG8_SA(0, 0), s00, s01, kb2);
;             PG8_WAIT_V(8); PG8_WAIT_L(0); PG8_BAR; if (half1) { PG8_MMA(1, 0, At, B0); PG8_MMA(1, 1, At, B1); } PG8_BAR; PG8_SCHED;
.LBB0_2327:
	v_add_u32_e32 v5, s47, v216
	ds_read_b128 v[150:153], v5
	ds_read_b128 v[154:157], v5 offset:1024
	ds_read_b128 v[158:161], v5 offset:2048
	ds_read_b128 v[162:165], v5 offset:3072
	v_add_u32_e32 v5, s48, v216
	ds_read_b128 v[134:137], v5
	ds_read_b128 v[138:141], v5 offset:1024
	ds_read_b128 v[142:145], v5 offset:2048
	ds_read_b128 v[146:149], v5 offset:3072
	v_readlane_b32 s18, v254, 55
	v_readlane_b32 s19, v254, 56
	s_add_u32 s30, s18, s13
	s_addc_u32 s31, s19, 0
	v_lshl_add_u64 v[210:211], s[30:31], 0, v[206:207]
	v_lshl_add_u64 v[210:211], v[210:211], 0, s[2:3]
	s_add_i32 m0, s17, 0xc000
	s_waitcnt lgkmcnt(0)
	ds_read_b128 v[166:169], v217
	ds_read_b128 v[170:173], v217 offset:1024
	ds_read_b128 v[174:177], v217 offset:2048
	ds_read_b128 v[178:181], v217 offset:3072
	ds_read_b128 v[182:185], v217 offset:4096
	ds_read_b128 v[186:189], v217 offset:5120
	ds_read_b128 v[190:193], v217 offset:6144
	ds_read_b128 v[194:197], v217 offset:7168
	global_load_lds_dwordx4 v[210:211], off
	v_lshl_add_u64 v[210:211], s[30:31], 0, v[208:209]
	v_lshl_add_u64 v[210:211], v[210:211], 0, s[2:3]
	s_add_i32 m0, s17, 0xe000
	s_nop 0
	global_load_lds_dwordx4 v[210:211], off
	s_waitcnt vmcnt(8)
	s_waitcnt lgkmcnt(0)
	s_barrier
	s_waitcnt lgkmcnt(0)
	v_mfma_f32_16x16x32_bf16 v[130:133], v[150:153], v[166:169], v[130:133]
	v_mfma_f32_16x16x32_bf16 v[126:129], v[158:161], v[166:169], v[126:129]
	v_mfma_f32_16x16x32_bf16 v[114:117], v[150:153], v[174:177], v[114:117]
	v_mfma_f32_16x16x32_bf16 v[110:113], v[158:161], v[174:177], v[110:113]
	v_mfma_f32_16x16x32_bf16 v[98:101], v[150:153], v[182:185], v[98:101]
	v_mfma_f32_16x16x32_bf16 v[94:97], v[158:161], v[182:185], v[94:97]
	v_mfma_f32_16x16x32_bf16 v[82:85], v[150:153], v[190:193], v[82:85]
	v_mfma_f32_16x16x32_bf16 v[78:81], v[158:161], v[190:193], v[78:81]
	v_mfma_f32_16x16x32_bf16 v[130:133], v[154:157], v[170:173], v[130:133]
	v_mfma_f32_16x16x32_bf16 v[126:129], v[162:165], v[170:173], v[126:129]
	v_mfma_f32_16x16x32_bf16 v[114:117], v[154:157], v[178:181], v[114:117]
	v_mfma_f32_16x16x32_bf16 v[110:113], v[162:165], v[178:181], v[110:113]
	v_mfma_f32_16x16x32_bf16 v[98:101], v[154:157], v[186:189], v[98:101]
	v_mfma_f32_16x16x32_bf16 v[94:97], v[162:165], v[186:189], v[94:97]
	v_mfma_f32_16x16x32_bf16 v[82:85], v[154:157], v[194:197], v[82:85]
	v_mfma_f32_16x16x32_bf16 v[78:81], v[162:165], v[194:197], v[78:81]
	v_mfma_f32_16x16x32_bf16 v[122:125], v[134:137], v[166:169], v[122:125]
	v_mfma_f32_16x16x32_bf16 v[118:121], v[142:145], v[166:169], v[118:121]
	v_mfma_f32_16x16x32_bf16 v[106:109], v[134:137], v[174:177], v[106:109]
	v_mfma_f32_16x16x32_bf16 v[102:105], v[142:145], v[174:177], v[102:105]
	v_mfma_f32_16x16x32_bf16 v[90:93], v[134:137], v[182:185], v[90:93]
	v_mfma_f32_16x16x32_bf16 v[86:89], v[142:145], v[182:185], v[86:89]
	v_mfma_f32_16x16x32_bf16 v[74:77], v[134:137], v[190:193], v[74:77]
	v_mfma_f32_16x16x32_bf16 v[70:73], v[142:145], v[190:193], v[70:73]
	v_mfma_f32_16x16x32_bf16 v[122:125], v[138:141], v[170:173], v[122:125]
	v_mfma_f32_16x16x32_bf16 v[118:121], v[146:149], v[170:173], v[118:121]
	v_mfma_f32_16x16x32_bf16 v[106:109], v[138:141], v[178:181], v[106:109]
	v_mfma_f32_16x16x32_bf16 v[102:105], v[146:149], v[178:181], v[102:105]
	v_mfma_f32_16x16x32_bf16 v[90:93], v[138:141], v[186:189], v[90:93]
	v_mfma_f32_16x16x32_bf16 v[86:89], v[146:149], v[186:189], v[86:89]
	v_mfma_f32_16x16x32_bf16 v[74:77], v[138:141], v[194:197], v[74:77]
	v_mfma_f32_16x16x32_bf16 v[70:73], v[146:149], v[194:197], v[70:73]
	s_barrier
	s_add_i32 s5, s47, s38
	v_lshl_add_u64 v[210:211], s[28:29], 0, v[198:199]
	s_mov_b32 m0, s5
	ds_read_b128 v[190:193], v217 offset:16384
	ds_read_b128 v[194:197], v217 offset:17408
	ds_read_b128 v[182:185], v217 offset:18432
	ds_read_b128 v[186:189], v217 offset:19456
	ds_read_b128 v[174:177], v217 offset:20480
	ds_read_b128 v[178:181], v217 offset:21504
	ds_read_b128 v[166:169], v217 offset:22528
	ds_read_b128 v[170:173], v217 offset:23552
	global_load_lds_dwordx4 v[210:211], off
	s_add_i32 m0, s5, 0x2000
	s_add_u32 s30, s28, 0x10000
	v_lshl_add_u64 v[212:213], s[28:29], 0, v[200:201]
	s_addc_u32 s31, s29, 0
	s_add_i32 s5, s48, s38
	global_load_lds_dwordx4 v[212:213], off
	v_lshl_add_u64 v[226:227], s[30:31], 0, v[198:199]
	s_mov_b32 m0, s5
	v_cndmask_b32_e64 v5, 0, 1, s[24:25]
	global_load_lds_dwordx4 v[226:227], off
	s_add_i32 m0, s5, 0x2000
	v_lshl_add_u64 v[226:227], s[30:31], 0, v[200:201]
	s_add_u32 s30, s18, s4
	global_load_lds_dwordx4 v[226:227], off
	s_addc_u32 s31, s19, 0
	s_mov_b32 m0, s17
	v_cmp_ne_u32_e64 s[4:5], 1, v5
	global_load_lds_dwordx4 v2, s[30:31]
	s_mov_b32 m0, s39
	s_andn2_b64 vcc, exec, s[24:25]
	global_load_lds_dwordx4 v4, s[30:31]
	s_waitcnt vmcnt(8)
	s_waitcnt lgkmcnt(0)
	s_barrier
	s_cbranch_vccnz .LBB0_2329
	s_waitcnt lgkmcnt(0)
	v_mfma_f32_16x16x32_bf16 v[66:69], v[150:153], v[190:193], v[66:69]
	v_mfma_f32_16x16x32_bf16 v[62:65], v[158:161], v[190:193], v[62:65]
	v_mfma_f32_16x16x32_bf16 v[50:53], v[150:153], v[182:185], v[50:53]
	v_mfma_f32_16x16x32_bf16 v[46:49], v[158:161], v[182:185], v[46:49]
	v_mfma_f32_16x16x32_bf16 v[34:37], v[150:153], v[174:177], v[34:37]
	v_mfma_f32_16x16x32_bf16 v[30:33], v[158:161], v[174:177], v[30:33]
	v_mfma_f32_16x16x32_bf16 v[18:21], v[150:153], v[166:169], v[18:21]
	v_mfma_f32_16x16x32_bf16 v[14:17], v[158:161], v[166:169], v[14:17]
	v_mfma_f32_16x16x32_bf16 v[66:69], v[154:157], v[194:197], v[66:69]
	v_mfma_f32_16x16x32_bf16 v[62:65], v[162:165], v[194:197], v[62:65]
	v_mfma_f32_16x16x32_bf16 v[50:53], v[154:157], v[186:189], v[50:53]
	v_mfma_f32_16x16x32_bf16 v[46:49], v[162:165], v[186:189], v[46:49]
	v_mfma_f32_16x16x32_bf16 v[34:37], v[154:157], v[178:181], v[34:37]
	v_mfma_f32_16x16x32_bf16 v[30:33], v[162:165], v[178:181], v[30:33]
	v_mfma_f32_16x16x32_bf16 v[18:21], v[154:157], v[170:173], v[18:21]
	v_mfma_f32_16x16x32_bf16 v[14:17], v[162:165], v[170:173], v[14:17]
	v_mfma_f32_16x16x32_bf16 v[58:61], v[134:137], v[190:193], v[58:61]
	v_mfma_f32_16x16x32_bf16 v[54:57], v[142:145], v[190:193], v[54:57]
	v_mfma_f32_16x16x32_bf16 v[42:45], v[134:137], v[182:185], v[42:45]
	v_mfma_f32_16x16x32_bf16 v[38:41], v[142:145], v[182:185], v[38:41]
	v_mfma_f32_16x16x32_bf16 v[26:29], v[134:137], v[174:177], v[26:29]
	v_mfma_f32_16x16x32_bf16 v[22:25], v[142:145], v[174:177], v[22:25]
	v_mfma_f32_16x16x32_bf16 v[10:13], v[134:137], v[166:169], v[10:13]
	v_mfma_f32_16x16x32_bf16 v[6:9], v[142:145], v[166:169], v[6:9]
	v_mfma_f32_16x16x32_bf16 v[58:61], v[138:141], v[194:197], v[58:61]
	v_mfma_f32_16x16x32_bf16 v[54:57], v[146:149], v[194:197], v[54:57]
	v_mfma_f32_16x16x32_bf16 v[42:45], v[138:141], v[186:189], v[42:45]
	v_mfma_f32_16x16x32_bf16 v[38:41], v[146:149], v[186:189], v[38:41]
	v_mfma_f32_16x16x32_bf16 v[26:29], v[138:141], v[178:181], v[26:29]
	v_mfma_f32_16x16x32_bf16 v[22:25], v[146:149], v[178:181], v[22:25]
	v_mfma_f32_16x16x32_bf16 v[10:13], v[138:141], v[170:173], v[10:13]
	v_mfma_f32_16x16x32_bf16 v[6:9], v[146:149], v[170:173], v[6:9]
; #define PG8_STAGE_B(bufoff, gbase) do { _Pragma("unroll") for (int _i = 0; _i < 2; ++_i) \
;         __builtin_amdgcn_global_load_lds((const unsigned*)((const char*)(gbase) + voffB[_i]), (LAS unsigned*)(lds + (bufoff) + ldsw + _i * 8192), 16, 0, 0); } while (0)
; #define PG8_STAGE_A(bufoff, V0, V1, kb) do { \
;         __builtin_amdgcn_global_load_lds((const unsigned*)((Abase + (kb)) + (V0)), (LAS unsigned*)(lds + (bufoff) + ldsw), 16, 0, 0); \
;         __builtin_amdgcn_global_load_lds((const unsigned*)((Abase + (kb)) + (V1)), (LAS unsigned*)(lds + (bufoff) + ldsw + 8192), 16, 0, 0); } while (0)
; #define PG8_LDA(dst, b, h) do { _Pragma("unroll") for (int m = 0; m < 4; ++m) _Pragma("unroll") for (int k = 0; k < 2; ++k) dst[m][k] = *(const LAS bf16x8*)(lds + PG8_SA(b, h) + aoff + m * 2048 + k * 1024); } while (0)
; #define PG8_LDB(dst, b, h) do { _Pragma("unroll") for (int n = 0; n < 2; ++n) _Pragma("unroll") for (int k = 0; k < 2; ++k) dst[n][k] = *(const LAS bf16x8*)(lds + PG8_SB(b, h) + boff + n * 2048 + k * 1024); } while (0)
; #define PG8_MMA(ai, bj, At, Bt) do { __builtin_amdgcn_s_setprio(1); _Pragma("unroll") for (int m = 0; m < 4; ++m) _Pragma("unroll") for (int n = 0; n < 2; ++n) _Pragma("unroll") for (int k = 0; k < 2; ++k) \
;         acc[ai][bj][m][n] = __builtin_amdgcn_mfma_f32_16x16x32_bf16(Bt[n][k], At[m][k], acc[ai][bj][m][n], 0, 0, 0); __builtin_amdgcn_s_setprio(0); } while (0)
; #define PG8_WAIT_V(n) asm volatile("s_waitcnt vmcnt(" #n ")" ::: "memory")
; #define PG8_WAIT_L(n) asm volatile("s_waitcnt lgkmcnt(" #n ")" ::: "memory")
; #define PG8_BAR __builtin_amdgcn_s_barrier()
; #define PG8_SCHED __builtin_amdgcn_sched_barrier(0)
; template <class Epi, class Sched, bool ALIGN_EPI>
; __device__ __forceinline__ void gemm_phase(LAS unsigned char* lds, const Gemm g, const Sched& S, const Epi& E) {
;     ...
;             PG8_LDB(B0, 1, 0); PG8_LDB(B1, 1, 1); PG8_SCHED; PG8_LDA(At, 1, 0); PG8_STAGE_A(PG8_SA(0, 1), s10, s11, kb2);
;             PG8_WAIT_V(8); PG8_WAIT_L(0); PG8_BAR; PG8_MMA(0, 0, At, B0); PG8_MMA(0, 1, At, B1); PG8_BAR; PG8_SCHED;
;             PG8_LDA(At, 1, 1); PG8_STAGE_B(PG8_SB(1, 0), b3); PG8_STAGE_B(PG8_SB(1, 1), b3 + hstepB); PG8_STAGE_A(PG8_SA(1, 0), s00, s01, kb3);
;             PG8_WAIT_V(8); PG8_WAIT_L(0); PG8_BAR; if (half1) { PG8_MMA(1, 0, At, B0); PG8_MMA(1, 1, At, B1); } PG8_BAR; PG8_SCHED;
.LBB0_2329:
	v_mov_b32_e32 v5, v3
	v_lshl_add_u64 v[226:227], s[30:31], 0, v[2:3]
	v_lshl_add_u64 v[4:5], s[30:31], 0, v[4:5]
	s_barrier
	v_add_u32_e32 v2, s49, v216
	ds_read_b128 v[150:153], v2
	ds_read_b128 v[154:157], v2 offset:1024
	ds_read_b128 v[158:161], v2 offset:2048
	ds_read_b128 v[162:165], v2 offset:3072
	v_add_u32_e32 v2, s50, v216
	ds_read_b128 v[134:137], v2
	ds_read_b128 v[138:141], v2 offset:1024
	ds_read_b128 v[142:145], v2 offset:2048
	ds_read_b128 v[146:149], v2 offset:3072
	s_mov_b32 m0, s40
	s_waitcnt lgkmcnt(0)
	ds_read_b128 v[166:169], v217 offset:32768
	ds_read_b128 v[170:173], v217 offset:33792
	ds_read_b128 v[174:177], v217 offset:34816
	ds_read_b128 v[178:181], v217 offset:35840
	ds_read_b128 v[182:185], v217 offset:36864
	ds_read_b128 v[186:189], v217 offset:37888
	ds_read_b128 v[190:193], v217 offset:38912
	ds_read_b128 v[194:197], v217 offset:39936
	global_load_lds_dwordx4 v224, s[30:31]
	s_mov_b32 m0, s41
	s_nop 0
	global_load_lds_dwordx4 v225, s[30:31]
	s_waitcnt vmcnt(8)
	s_waitcnt lgkmcnt(0)
	s_barrier
	s_waitcnt lgkmcnt(0)
	v_mfma_f32_16x16x32_bf16 v[130:133], v[150:153], v[166:169], v[130:133]
	v_mfma_f32_16x16x32_bf16 v[126:129], v[158:161], v[166:169], v[126:129]
	v_mfma_f32_16x16x32_bf16 v[114:117], v[150:153], v[174:177], v[114:117]
	v_mfma_f32_16x16x32_bf16 v[110:113], v[158:161], v[174:177], v[110:113]
	v_mfma_f32_16x16x32_bf16 v[98:101], v[150:153], v[182:185], v[98:101]
	v_mfma_f32_16x16x32_bf16 v[94:97], v[158:161], v[182:185], v[94:97]
	v_mfma_f32_16x16x32_bf16 v[82:85], v[150:153], v[190:193], v[82:85]
	v_mfma_f32_16x16x32_bf16 v[78:81], v[158:161], v[190:193], v[78:81]
	v_mfma_f32_16x16x32_bf16 v[130:133], v[154:157], v[170:173], v[130:133]
	v_mfma_f32_16x16x32_bf16 v[126:129], v[162:165], v[170:173], v[126:129]
	v_mfma_f32_16x16x32_bf16 v[114:117], v[154:157], v[178:181], v[114:117]
	v_mfma_f32_16x16x32_bf16 v[110:113], v[162:165], v[178:181], v[110:113]
	v_mfma_f32_16x16x32_bf16 v[98:101], v[154:157], v[186:189], v[98:101]
	v_mfma_f32_16x16x32_bf16 v[94:97], v[162:165], v[186:189], v[94:97]
	v_mfma_f32_16x16x32_bf16 v[82:85], v[154:157], v[194:197], v[82:85]
	v_mfma_f32_16x16x32_bf16 v[78:81], v[162:165], v[194:197], v[78:81]
	v_mfma_f32_16x16x32_bf16 v[122:125], v[134:137], v[166:169], v[122:125]
	v_mfma_f32_16x16x32_bf16 v[118:121], v[142:145], v[166:169], v[118:121]
	v_mfma_f32_16x16x32_bf16 v[106:109], v[134:137], v[174:177], v[106:109]
	v_mfma_f32_16x16x32_bf16 v[102:105], v[142:145], v[174:177], v[102:105]
	v_mfma_f32_16x16x32_bf16 v[90:93], v[134:137], v[182:185], v[90:93]
	v_mfma_f32_16x16x32_bf16 v[86:89], v[142:145], v[182:185], v[86:89]
	v_mfma_f32_16x16x32_bf16 v[74:77], v[134:137], v[190:193], v[74:77]
	v_mfma_f32_16x16x32_bf16 v[70:73], v[142:145], v[190:193], v[70:73]
	v_mfma_f32_16x16x32_bf16 v[122:125], v[138:141], v[170:173], v[122:125]
	v_mfma_f32_16x16x32_bf16 v[118:121], v[146:149], v[170:173], v[118:121]
	v_mfma_f32_16x16x32_bf16 v[106:109], v[138:141], v[178:181], v[106:109]
	v_mfma_f32_16x16x32_bf16 v[102:105], v[146:149], v[178:181], v[102:105]
	v_mfma_f32_16x16x32_bf16 v[90:93], v[138:141], v[186:189], v[90:93]
	v_mfma_f32_16x16x32_bf16 v[86:89], v[146:149], v[186:189], v[86:89]
	v_mfma_f32_16x16x32_bf16 v[74:77], v[138:141], v[194:197], v[74:77]
	v_mfma_f32_16x16x32_bf16 v[70:73], v[146:149], v[194:197], v[70:73]
	s_barrier
	s_add_i32 s13, s49, s38
	v_lshl_add_u64 v[210:211], v[210:211], 0, s[2:3]
	s_mov_b32 m0, s13
	ds_read_b128 v[190:193], v217 offset:49152
	ds_read_b128 v[194:197], v217 offset:50176
	ds_read_b128 v[182:185], v217 offset:51200
	ds_read_b128 v[186:189], v217 offset:52224
	ds_read_b128 v[174:177], v217 offset:53248
	ds_read_b128 v[178:181], v217 offset:54272
	ds_read_b128 v[166:169], v217 offset:55296
	ds_read_b128 v[170:173], v217 offset:56320
	global_load_lds_dwordx4 v[210:211], off
	s_add_i32 m0, s13, 0x2000
	s_add_u32 s28, s28, 0x10080
	v_lshl_add_u64 v[210:211], v[212:213], 0, s[2:3]
	s_addc_u32 s29, s29, 0
	s_add_i32 s13, s50, s38
	global_load_lds_dwordx4 v[210:211], off
	v_lshl_add_u64 v[210:211], s[28:29], 0, v[198:199]
	s_mov_b32 m0, s13
	v_lshl_add_u64 v[4:5], v[4:5], 0, s[2:3]
	global_load_lds_dwordx4 v[210:211], off
	v_lshl_add_u64 v[210:211], s[28:29], 0, v[200:201]
	s_add_i32 m0, s13, 0x2000
	s_and_b64 vcc, exec, s[4:5]
	global_load_lds_dwordx4 v[210:211], off
	v_lshl_add_u64 v[210:211], v[226:227], 0, s[2:3]
	s_mov_b32 m0, s42
	s_nop 0
	global_load_lds_dwordx4 v[210:211], off
	s_mov_b32 m0, s43
	s_nop 0
	global_load_lds_dwordx4 v[4:5], off
	s_waitcnt vmcnt(8)
	s_waitcnt lgkmcnt(0)
	s_barrier
	s_cbranch_vccnz .LBB0_2323
	s_waitcnt lgkmcnt(0)
	v_mfma_f32_16x16x32_bf16 v[66:69], v[150:153], v[190:193], v[66:69]
	v_mfma_f32_16x16x32_bf16 v[62:65], v[158:161], v[190:193], v[62:65]
	v_mfma_f32_16x16x32_bf16 v[50:53], v[150:153], v[182:185], v[50:53]
	v_mfma_f32_16x16x32_bf16 v[46:49], v[158:161], v[182:185], v[46:49]
	v_mfma_f32_16x16x32_bf16 v[34:37], v[150:153], v[174:177], v[34:37]
	v_mfma_f32_16x16x32_bf16 v[30:33], v[158:161], v[174:177], v[30:33]
	v_mfma_f32_16x16x32_bf16 v[18:21], v[150:153], v[166:169], v[18:21]
	v_mfma_f32_16x16x32_bf16 v[14:17], v[158:161], v[166:169], v[14:17]
	v_mfma_f32_16x16x32_bf16 v[66:69], v[154:157], v[194:197], v[66:69]
	v_mfma_f32_16x16x32_bf16 v[62:65], v[162:165], v[194:197], v[62:65]
	v_mfma_f32_16x16x32_bf16 v[50:53], v[154:157], v[186:189], v[50:53]
	v_mfma_f32_16x16x32_bf16 v[46:49], v[162:165], v[186:189], v[46:49]
	v_mfma_f32_16x16x32_bf16 v[34:37], v[154:157], v[178:181], v[34:37]
	v_mfma_f32_16x16x32_bf16 v[30:33], v[162:165], v[178:181], v[30:33]
	v_mfma_f32_16x16x32_bf16 v[18:21], v[154:157], v[170:173], v[18:21]
	v_mfma_f32_16x16x32_bf16 v[14:17], v[162:165], v[170:173], v[14:17]
	v_mfma_f32_16x16x32_bf16 v[58:61], v[134:137], v[190:193], v[58:61]
	v_mfma_f32_16x16x32_bf16 v[54:57], v[142:145], v[190:193], v[54:57]
	v_mfma_f32_16x16x32_bf16 v[42:45], v[134:137], v[182:185], v[42:45]
	v_mfma_f32_16x16x32_bf16 v[38:41], v[142:145], v[182:185], v[38:41]
	v_mfma_f32_16x16x32_bf16 v[26:29], v[134:137], v[174:177], v[26:29]
	v_mfma_f32_16x16x32_bf16 v[22:25], v[142:145], v[174:177], v[22:25]
	v_mfma_f32_16x16x32_bf16 v[10:13], v[134:137], v[166:169], v[10:13]
	v_mfma_f32_16x16x32_bf16 v[4:7], v[142:145], v[166:169], v[6:9]
	v_mfma_f32_16x16x32_bf16 v[58:61], v[138:141], v[194:197], v[58:61]
	v_mfma_f32_16x16x32_bf16 v[54:57], v[146:149], v[194:197], v[54:57]
	v_mfma_f32_16x16x32_bf16 v[42:45], v[138:141], v[186:189], v[42:45]
	v_mfma_f32_16x16x32_bf16 v[38:41], v[146:149], v[186:189], v[38:41]
	v_mfma_f32_16x16x32_bf16 v[26:29], v[138:141], v[178:181], v[26:29]
	v_mfma_f32_16x16x32_bf16 v[22:25], v[146:149], v[178:181], v[22:25]
	v_mfma_f32_16x16x32_bf16 v[10:13], v[138:141], v[170:173], v[10:13]
	v_mfma_f32_16x16x32_bf16 v[6:9], v[146:149], v[170:173], v[4:7]
	s_branch .LBB0_2323

; #define PG8_BWAIT(n) asm volatile("s_waitcnt vmcnt(" #n ")" : "+v"(bv[0]), "+v"(bv[1]), "+v"(bv[2]), "+v"(bv[3]), "+v"(bv[4]), "+v"(bv[5]), "+v"(bv[6]), "+v"(bv[7]) :: "memory")
; #define PG8_STAGE_A(bufoff, V0, V1, kb) do { \
;         __builtin_amdgcn_global_load_lds((const unsigned*)((Abase + (kb)) + (V0)), (LAS unsigned*)(lds + (bufoff) + ldsw), 16, 0, 0); \
;         __builtin_amdgcn_global_load_lds((const unsigned*)((Abase + (kb)) + (V1)), (LAS unsigned*)(lds + (bufoff) + ldsw + 8192), 16, 0, 0); } while (0)
; #define PG8_LDA(dst, b, h) do { _Pragma("unroll") for (int m = 0; m < 4; ++m) _Pragma("unroll") for (int k = 0; k < 2; ++k) dst[m][k] = *(const LAS bf16x8*)(lds + PG8_SA(b, h) + aoff + m * 2048 + k * 1024); } while (0)
; #define PG8_LDB(dst, b, h) do { _Pragma("unroll") for (int n = 0; n < 2; ++n) _Pragma("unroll") for (int k = 0; k < 2; ++k) dst[n][k] = *(const LAS bf16x8*)(lds + PG8_SB(b, h) + boff + n * 2048 + k * 1024); } while (0)
; #define PG8_MMA(ai, bj, At, Bt) do { __builtin_amdgcn_s_setprio(1); _Pragma("unroll") for (int m = 0; m < 4; ++m) _Pragma("unroll") for (int n = 0; n < 2; ++n) _Pragma("unroll") for (int k = 0; k < 2; ++k) \
;         acc[ai][bj][m][n] = __builtin_amdgcn_mfma_f32_16x16x32_bf16(Bt[n][k], At[m][k], acc[ai][bj][m][n], 0, 0, 0); __builtin_amdgcn_s_setprio(0); } while (0)
; #define PG8_WAIT_V(n) asm volatile("s_waitcnt vmcnt(" #n ")" ::: "memory")
; #define PG8_WAIT_L(n) asm volatile("s_waitcnt lgkmcnt(" #n ")" ::: "memory")
; #define PG8_BAR __builtin_amdgcn_s_barrier()
; template <class Epi, class Sched, bool ALIGN_EPI>
; __device__ __forceinline__ void gemm_phase(LAS unsigned char* lds, const Gemm g, const Sched& S, const Epi& E) {
;     ...
;             PG8_LDB(B0, 0, 0); PG8_LDB(B1, 0, 1); PG8_SCHED; PG8_LDA(At, 0, 0); PG8_STAGE_A(PG8_SA(1, 1), vc10, vc11, kb1);
;             PG8_WAIT_V(12); PG8_WAIT_L(0); PG8_BAR; PG8_MMA(0, 0, At, B0); PG8_MMA(0, 1, At, B1); PG8_BAR; PG8_SCHED;
;             if (last) { vc10 = vn10; vc11 = vn11; }
;             PG8_BWAIT(2); PG8_BCOMMIT(0); PG8_SCHED; PG8_LDA(At, 0, 1); PG8_BISSUE(t + 3 >= nt ? pbn + (size_t)(t + 3 - nt) * 64 * Sched::LDN : pbc + (size_t)(t + 3) * 64 * Sched::LDN); PG8_STAGE_A(PG8_SA(0, 0), vc00, vc01, kb2);
;             PG8_WAIT_V(12); PG8_WAIT_L(0); PG8_BAR; if (half1) { PG8_MMA(1, 0, At, B0); PG8_MMA(1, 1, At, B1); } PG8_BAR; PG8_SCHED;
.LBB0_2448:
	v_add_u32_e32 v162, 0x10000, v247
	v_add_u32_e32 v174, 0x14000, v247
	ds_read_b128 v[178:181], v162
	ds_read_b128 v[182:185], v162 offset:1024
	ds_read_b128 v[186:189], v162 offset:2048
	ds_read_b128 v[190:193], v162 offset:3072
	ds_read_b128 v[162:165], v174
	ds_read_b128 v[166:169], v174 offset:1024
	ds_read_b128 v[170:173], v174 offset:2048
	ds_read_b128 v[174:177], v174 offset:3072
	s_lshl_b32 s5, s50, 7
	s_add_i32 s4, s5, 0x100
	v_cndmask_b32_e64 v228, v228, v250, s[28:29]
	v_readlane_b32 s54, v254, 53
	v_readlane_b32 s55, v254, 54
	s_add_u32 s30, s54, s5
	s_addc_u32 s31, s55, 0
	v_lshl_add_u64 v[236:237], s[30:31], 0, v[230:231]
	v_lshl_add_u64 v[236:237], v[236:237], 0, s[16:17]
	s_add_i32 m0, s35, 0xc000
	v_mov_b32_e32 v233, v231
	s_waitcnt lgkmcnt(0)
	ds_read_b128 v[194:197], v248
	ds_read_b128 v[198:201], v248 offset:1024
	ds_read_b128 v[202:205], v248 offset:2048
	ds_read_b128 v[206:209], v248 offset:3072
	ds_read_b128 v[210:213], v248 offset:4096
	ds_read_b128 v[214:217], v248 offset:5120
	ds_read_b128 v[218:221], v248 offset:6144
	ds_read_b128 v[222:225], v248 offset:7168
	global_load_lds_dwordx4 v[236:237], off
	v_lshl_add_u64 v[236:237], s[30:31], 0, v[232:233]
	v_lshl_add_u64 v[236:237], v[236:237], 0, s[16:17]
	s_add_i32 m0, s35, 0xe000
	s_nop 0
	global_load_lds_dwordx4 v[236:237], off
	s_waitcnt vmcnt(12)
	s_waitcnt lgkmcnt(0)
	s_barrier
	s_waitcnt lgkmcnt(0)
	v_mfma_f32_16x16x32_bf16 v[158:161], v[178:181], v[194:197], v[158:161]
	v_mfma_f32_16x16x32_bf16 v[154:157], v[186:189], v[194:197], v[154:157]
	v_mfma_f32_16x16x32_bf16 v[142:145], v[178:181], v[202:205], v[142:145]
	v_mfma_f32_16x16x32_bf16 v[138:141], v[186:189], v[202:205], v[138:141]
	v_mfma_f32_16x16x32_bf16 v[126:129], v[178:181], v[210:213], v[126:129]
	v_mfma_f32_16x16x32_bf16 v[122:125], v[186:189], v[210:213], v[122:125]
	v_mfma_f32_16x16x32_bf16 v[110:113], v[178:181], v[218:221], v[110:113]
	v_mfma_f32_16x16x32_bf16 v[106:109], v[186:189], v[218:221], v[106:109]
	v_mfma_f32_16x16x32_bf16 v[158:161], v[182:185], v[198:201], v[158:161]
	v_mfma_f32_16x16x32_bf16 v[154:157], v[190:193], v[198:201], v[154:157]
	v_mfma_f32_16x16x32_bf16 v[142:145], v[182:185], v[206:209], v[142:145]
	v_mfma_f32_16x16x32_bf16 v[138:141], v[190:193], v[206:209], v[138:141]
	v_mfma_f32_16x16x32_bf16 v[126:129], v[182:185], v[214:217], v[126:129]
	v_mfma_f32_16x16x32_bf16 v[122:125], v[190:193], v[214:217], v[122:125]
	v_mfma_f32_16x16x32_bf16 v[110:113], v[182:185], v[222:225], v[110:113]
	v_mfma_f32_16x16x32_bf16 v[106:109], v[190:193], v[222:225], v[106:109]
	v_mfma_f32_16x16x32_bf16 v[150:153], v[162:165], v[194:197], v[150:153]
	v_mfma_f32_16x16x32_bf16 v[146:149], v[170:173], v[194:197], v[146:149]
	v_mfma_f32_16x16x32_bf16 v[134:137], v[162:165], v[202:205], v[134:137]
	v_mfma_f32_16x16x32_bf16 v[130:133], v[170:173], v[202:205], v[130:133]
	v_mfma_f32_16x16x32_bf16 v[118:121], v[162:165], v[210:213], v[118:121]
	v_mfma_f32_16x16x32_bf16 v[114:117], v[170:173], v[210:213], v[114:117]
	v_mfma_f32_16x16x32_bf16 v[102:105], v[162:165], v[218:221], v[102:105]
	v_mfma_f32_16x16x32_bf16 v[98:101], v[170:173], v[218:221], v[98:101]
	v_mfma_f32_16x16x32_bf16 v[150:153], v[166:169], v[198:201], v[150:153]
	v_mfma_f32_16x16x32_bf16 v[146:149], v[174:177], v[198:201], v[146:149]
	v_mfma_f32_16x16x32_bf16 v[134:137], v[166:169], v[206:209], v[134:137]
	v_mfma_f32_16x16x32_bf16 v[130:133], v[174:177], v[206:209], v[130:133]
	v_mfma_f32_16x16x32_bf16 v[118:121], v[166:169], v[214:217], v[118:121]
	v_mfma_f32_16x16x32_bf16 v[114:117], v[174:177], v[214:217], v[114:117]
	v_mfma_f32_16x16x32_bf16 v[102:105], v[166:169], v[222:225], v[102:105]
	v_mfma_f32_16x16x32_bf16 v[98:101], v[174:177], v[222:225], v[98:101]
	s_barrier
	s_add_i32 s10, s50, -1
	s_lshl_b64 s[30:31], s[10:11], 18
	s_add_u32 s5, s47, s30
	s_addc_u32 s10, s21, s31
	s_and_b64 s[30:31], s[26:27], exec
	s_cselect_b32 s30, s48, s5
	s_cselect_b32 s31, s49, s10
	s_add_u32 s52, s30, 0x1000
	s_waitcnt vmcnt(2)
	v_cndmask_b32_e64 v226, v226, v249, s[28:29]
	v_cvt_pk_bf16_f32 v194, v2, v6
	v_cvt_pk_bf16_f32 v198, v3, v7
	v_cvt_pk_bf16_f32 v202, v4, v8
	v_cvt_pk_bf16_f32 v206, v5, v9
	global_load_dwordx4 v[2:5], v240, s[30:31] offset:0
	s_addc_u32 s53, s31, 0
	global_load_dwordx4 v[6:9], v240, s[52:53] offset:0
	v_cvt_pk_bf16_f32 v195, v10, v14
	v_cvt_pk_bf16_f32 v199, v11, v15
	v_cvt_pk_bf16_f32 v203, v12, v16
	v_cvt_pk_bf16_f32 v207, v13, v17
	s_add_u32 s52, s30, 0x2000
	s_addc_u32 s53, s31, 0
	global_load_dwordx4 v[10:13], v240, s[52:53] offset:0
	s_add_u32 s52, s30, 0x3000
	s_addc_u32 s53, s31, 0
	global_load_dwordx4 v[14:17], v240, s[52:53] offset:0
	v_cvt_pk_bf16_f32 v196, v18, v22
	v_cvt_pk_bf16_f32 v200, v19, v23
	v_cvt_pk_bf16_f32 v204, v20, v24
	v_cvt_pk_bf16_f32 v208, v21, v25
	s_add_u32 s52, s30, 0x4000
	s_addc_u32 s53, s31, 0
	global_load_dwordx4 v[18:21], v240, s[52:53] offset:0
	s_add_u32 s52, s30, 0x5000
	s_addc_u32 s53, s31, 0
	global_load_dwordx4 v[22:25], v240, s[52:53] offset:0
	v_cvt_pk_bf16_f32 v197, v26, v30
	v_cvt_pk_bf16_f32 v201, v27, v31
	v_cvt_pk_bf16_f32 v205, v28, v32
	v_cvt_pk_bf16_f32 v209, v29, v33
	s_add_u32 s52, s30, 0x6000
	s_addc_u32 s53, s31, 0
	s_add_u32 s30, s30, 0x7000
	global_load_dwordx4 v[26:29], v240, s[52:53] offset:0
	s_addc_u32 s31, s31, 0
	global_load_dwordx4 v[30:33], v240, s[30:31] offset:0
	v_add_u32_e32 v210, 0x10000, v242
	v_xor_b32_e32 v211, 64, v210
	v_xor_b32_e32 v212, 0x80, v210
	v_xor_b32_e32 v213, 0xc0, v210
	ds_write_b128 v210, v[194:197]
	ds_write_b128 v211, v[198:201]
	ds_write_b128 v212, v[202:205]
	ds_write_b128 v213, v[206:209]
	ds_read_b128 v[218:221], v248 offset:16384
	ds_read_b128 v[222:225], v248 offset:17408
	ds_read_b128 v[210:213], v248 offset:18432
	ds_read_b128 v[214:217], v248 offset:19456
	ds_read_b128 v[202:205], v248 offset:20480
	ds_read_b128 v[206:209], v248 offset:21504
	ds_read_b128 v[194:197], v248 offset:22528
	ds_read_b128 v[198:201], v248 offset:23552
	s_and_b64 s[30:31], s[28:29], exec
	s_cselect_b32 s4, 0, s4
	s_cselect_b32 s5, 0, 0
	s_add_u32 s30, s54, s4
	s_mov_b32 m0, s35
	s_addc_u32 s31, s55, s5
	global_load_lds_dwordx4 v226, s[30:31]
	s_mov_b32 m0, s36
	v_mov_b32_e32 v227, v231
	global_load_lds_dwordx4 v228, s[30:31]
	s_waitcnt vmcnt(12)
	s_waitcnt lgkmcnt(0)
	v_lshl_add_u64 v[238:239], s[30:31], 0, v[226:227]
	v_mov_b32_e32 v229, v231
	v_cndmask_b32_e64 v227, 0, 1, s[24:25]
	v_lshl_add_u64 v[236:237], s[30:31], 0, v[228:229]
	v_cmp_ne_u32_e64 s[4:5], 1, v227
	s_andn2_b64 vcc, exec, s[24:25]
	s_barrier
; #define PG8_STAGE_A(bufoff, V0, V1, kb) do { \
;         __builtin_amdgcn_global_load_lds((const unsigned*)((Abase + (kb)) + (V0)), (LAS unsigned*)(lds + (bufoff) + ldsw), 16, 0, 0); \
;         __builtin_amdgcn_global_load_lds((const unsigned*)((Abase + (kb)) + (V1)), (LAS unsigned*)(lds + (bufoff) + ldsw + 8192), 16, 0, 0); } while (0)
; #define PG8_LDA(dst, b, h) do { _Pragma("unroll") for (int m = 0; m < 4; ++m) _Pragma("unroll") for (int k = 0; k < 2; ++k) dst[m][k] = *(const LAS bf16x8*)(lds + PG8_SA(b, h) + aoff + m * 2048 + k * 1024); } while (0)
; #define PG8_LDB(dst, b, h) do { _Pragma("unroll") for (int n = 0; n < 2; ++n) _Pragma("unroll") for (int k = 0; k < 2; ++k) dst[n][k] = *(const LAS bf16x8*)(lds + PG8_SB(b, h) + boff + n * 2048 + k * 1024); } while (0)
; #define PG8_MMA(ai, bj, At, Bt) do { __builtin_amdgcn_s_setprio(1); _Pragma("unroll") for (int m = 0; m < 4; ++m) _Pragma("unroll") for (int n = 0; n < 2; ++n) _Pragma("unroll") for (int k = 0; k < 2; ++k) \
;         acc[ai][bj][m][n] = __builtin_amdgcn_mfma_f32_16x16x32_bf16(Bt[n][k], At[m][k], acc[ai][bj][m][n], 0, 0, 0); __builtin_amdgcn_s_setprio(0); } while (0)
; #define PG8_WAIT_V(n) asm volatile("s_waitcnt vmcnt(" #n ")" ::: "memory")
; #define PG8_WAIT_L(n) asm volatile("s_waitcnt lgkmcnt(" #n ")" ::: "memory")
; #define PG8_BAR __builtin_amdgcn_s_barrier()
; #define PG8_SCHED __builtin_amdgcn_sched_barrier(0)
; template <class Epi, class Sched, bool ALIGN_EPI>
; __device__ __forceinline__ void gemm_phase(LAS unsigned char* lds, const Gemm g, const Sched& S, const Epi& E) {
;     ...
;             PG8_WAIT_V(12); PG8_WAIT_L(0); PG8_BAR; if (half1) { PG8_MMA(1, 0, At, B0); PG8_MMA(1, 1, At, B1); } PG8_BAR; PG8_SCHED;
;             PG8_LDB(B0, 1, 0); PG8_LDB(B1, 1, 1); PG8_SCHED; PG8_LDA(At, 1, 0); PG8_STAGE_A(PG8_SA(0, 1), vc10, vc11, kb2);
;             PG8_WAIT_V(12); PG8_WAIT_L(0); PG8_BAR; PG8_MMA(0, 0, At, B0); PG8_MMA(0, 1, At, B1); PG8_BAR; PG8_SCHED;
	s_cbranch_vccnz .LBB0_2450
	s_waitcnt lgkmcnt(0)
	v_mfma_f32_16x16x32_bf16 v[94:97], v[178:181], v[218:221], v[94:97]
	v_mfma_f32_16x16x32_bf16 v[90:93], v[186:189], v[218:221], v[90:93]
	v_mfma_f32_16x16x32_bf16 v[78:81], v[178:181], v[210:213], v[78:81]
	v_mfma_f32_16x16x32_bf16 v[74:77], v[186:189], v[210:213], v[74:77]
	v_mfma_f32_16x16x32_bf16 v[62:65], v[178:181], v[202:205], v[62:65]
	v_mfma_f32_16x16x32_bf16 v[58:61], v[186:189], v[202:205], v[58:61]
	v_mfma_f32_16x16x32_bf16 v[46:49], v[178:181], v[194:197], v[46:49]
	v_mfma_f32_16x16x32_bf16 v[42:45], v[186:189], v[194:197], v[42:45]
	v_mfma_f32_16x16x32_bf16 v[94:97], v[182:185], v[222:225], v[94:97]
	v_mfma_f32_16x16x32_bf16 v[90:93], v[190:193], v[222:225], v[90:93]
	v_mfma_f32_16x16x32_bf16 v[78:81], v[182:185], v[214:217], v[78:81]
	v_mfma_f32_16x16x32_bf16 v[74:77], v[190:193], v[214:217], v[74:77]
	v_mfma_f32_16x16x32_bf16 v[62:65], v[182:185], v[206:209], v[62:65]
	v_mfma_f32_16x16x32_bf16 v[58:61], v[190:193], v[206:209], v[58:61]
	v_mfma_f32_16x16x32_bf16 v[46:49], v[182:185], v[198:201], v[46:49]
	v_mfma_f32_16x16x32_bf16 v[42:45], v[190:193], v[198:201], v[42:45]
	v_mfma_f32_16x16x32_bf16 v[86:89], v[162:165], v[218:221], v[86:89]
	v_mfma_f32_16x16x32_bf16 v[82:85], v[170:173], v[218:221], v[82:85]
	v_mfma_f32_16x16x32_bf16 v[70:73], v[162:165], v[210:213], v[70:73]
	v_mfma_f32_16x16x32_bf16 v[66:69], v[170:173], v[210:213], v[66:69]
	v_mfma_f32_16x16x32_bf16 v[54:57], v[162:165], v[202:205], v[54:57]
	v_mfma_f32_16x16x32_bf16 v[50:53], v[170:173], v[202:205], v[50:53]
	v_mfma_f32_16x16x32_bf16 v[38:41], v[162:165], v[194:197], v[38:41]
	v_mfma_f32_16x16x32_bf16 v[34:37], v[170:173], v[194:197], v[34:37]
	v_mfma_f32_16x16x32_bf16 v[86:89], v[166:169], v[222:225], v[86:89]
	v_mfma_f32_16x16x32_bf16 v[82:85], v[174:177], v[222:225], v[82:85]
	v_mfma_f32_16x16x32_bf16 v[70:73], v[166:169], v[214:217], v[70:73]
	v_mfma_f32_16x16x32_bf16 v[66:69], v[174:177], v[214:217], v[66:69]
	v_mfma_f32_16x16x32_bf16 v[54:57], v[166:169], v[206:209], v[54:57]
	v_mfma_f32_16x16x32_bf16 v[50:53], v[174:177], v[206:209], v[50:53]
	v_mfma_f32_16x16x32_bf16 v[38:41], v[166:169], v[198:201], v[38:41]
	v_mfma_f32_16x16x32_bf16 v[34:37], v[174:177], v[198:201], v[34:37]
.LBB0_2450:
	v_cndmask_b32_e64 v232, v232, v252, s[28:29]
	v_cndmask_b32_e64 v230, v230, v251, s[28:29]
	s_barrier
	v_add_u32_e32 v162, 0x18000, v247
	v_add_u32_e32 v174, 0x1c000, v247
	ds_read_b128 v[178:181], v162
	ds_read_b128 v[182:185], v162 offset:1024
	ds_read_b128 v[186:189], v162 offset:2048
	ds_read_b128 v[190:193], v162 offset:3072
	ds_read_b128 v[162:165], v174
	ds_read_b128 v[166:169], v174 offset:1024
	ds_read_b128 v[170:173], v174 offset:2048
	ds_read_b128 v[174:177], v174 offset:3072
	s_mov_b32 m0, s37
	s_waitcnt lgkmcnt(0)
	ds_read_b128 v[194:197], v248 offset:32768
	ds_read_b128 v[198:201], v248 offset:33792
	ds_read_b128 v[202:205], v248 offset:34816
	ds_read_b128 v[206:209], v248 offset:35840
	ds_read_b128 v[210:213], v248 offset:36864
	ds_read_b128 v[214:217], v248 offset:37888
	ds_read_b128 v[218:221], v248 offset:38912
	ds_read_b128 v[222:225], v248 offset:39936
	global_load_lds_dwordx4 v230, s[30:31]
	s_mov_b32 m0, s38
	s_nop 0
	global_load_lds_dwordx4 v232, s[30:31]
	s_waitcnt vmcnt(12)
	s_waitcnt lgkmcnt(0)
	s_barrier
	s_waitcnt lgkmcnt(0)
	v_mfma_f32_16x16x32_bf16 v[158:161], v[178:181], v[194:197], v[158:161]
	v_mfma_f32_16x16x32_bf16 v[154:157], v[186:189], v[194:197], v[154:157]
	v_mfma_f32_16x16x32_bf16 v[142:145], v[178:181], v[202:205], v[142:145]
	v_mfma_f32_16x16x32_bf16 v[138:141], v[186:189], v[202:205], v[138:141]
	v_mfma_f32_16x16x32_bf16 v[126:129], v[178:181], v[210:213], v[126:129]
	v_mfma_f32_16x16x32_bf16 v[122:125], v[186:189], v[210:213], v[122:125]
	v_mfma_f32_16x16x32_bf16 v[110:113], v[178:181], v[218:221], v[110:113]
	v_mfma_f32_16x16x32_bf16 v[106:109], v[186:189], v[218:221], v[106:109]
	v_mfma_f32_16x16x32_bf16 v[158:161], v[182:185], v[198:201], v[158:161]
	v_mfma_f32_16x16x32_bf16 v[154:157], v[190:193], v[198:201], v[154:157]
	v_mfma_f32_16x16x32_bf16 v[142:145], v[182:185], v[206:209], v[142:145]
	v_mfma_f32_16x16x32_bf16 v[138:141], v[190:193], v[206:209], v[138:141]
	v_mfma_f32_16x16x32_bf16 v[126:129], v[182:185], v[214:217], v[126:129]
	v_mfma_f32_16x16x32_bf16 v[122:125], v[190:193], v[214:217], v[122:125]
	v_mfma_f32_16x16x32_bf16 v[110:113], v[182:185], v[222:225], v[110:113]
	v_mfma_f32_16x16x32_bf16 v[106:109], v[190:193], v[222:225], v[106:109]
	v_mfma_f32_16x16x32_bf16 v[150:153], v[162:165], v[194:197], v[150:153]
	v_mfma_f32_16x16x32_bf16 v[146:149], v[170:173], v[194:197], v[146:149]
	v_mfma_f32_16x16x32_bf16 v[134:137], v[162:165], v[202:205], v[134:137]
	v_mfma_f32_16x16x32_bf16 v[130:133], v[170:173], v[202:205], v[130:133]
	v_mfma_f32_16x16x32_bf16 v[118:121], v[162:165], v[210:213], v[118:121]
	v_mfma_f32_16x16x32_bf16 v[114:117], v[170:173], v[210:213], v[114:117]
	v_mfma_f32_16x16x32_bf16 v[102:105], v[162:165], v[218:221], v[102:105]
	v_mfma_f32_16x16x32_bf16 v[98:101], v[170:173], v[218:221], v[98:101]
	v_mfma_f32_16x16x32_bf16 v[150:153], v[166:169], v[198:201], v[150:153]
	v_mfma_f32_16x16x32_bf16 v[146:149], v[174:177], v[198:201], v[146:149]
	v_mfma_f32_16x16x32_bf16 v[134:137], v[166:169], v[206:209], v[134:137]
	v_mfma_f32_16x16x32_bf16 v[130:133], v[174:177], v[206:209], v[130:133]
	v_mfma_f32_16x16x32_bf16 v[118:121], v[166:169], v[214:217], v[118:121]
	v_mfma_f32_16x16x32_bf16 v[114:117], v[174:177], v[214:217], v[114:117]
	v_mfma_f32_16x16x32_bf16 v[102:105], v[166:169], v[222:225], v[102:105]
	v_mfma_f32_16x16x32_bf16 v[98:101], v[174:177], v[222:225], v[98:101]
	s_barrier
; #define PG8_BWAIT(n) asm volatile("s_waitcnt vmcnt(" #n ")" : "+v"(bv[0]), "+v"(bv[1]), "+v"(bv[2]), "+v"(bv[3]), "+v"(bv[4]), "+v"(bv[5]), "+v"(bv[6]), "+v"(bv[7]) :: "memory")
; #define PG8_STAGE_A(bufoff, V0, V1, kb) do { \
;         __builtin_amdgcn_global_load_lds((const unsigned*)((Abase + (kb)) + (V0)), (LAS unsigned*)(lds + (bufoff) + ldsw), 16, 0, 0); \
;         __builtin_amdgcn_global_load_lds((const unsigned*)((Abase + (kb)) + (V1)), (LAS unsigned*)(lds + (bufoff) + ldsw + 8192), 16, 0, 0); } while (0)
; #define PG8_LDA(dst, b, h) do { _Pragma("unroll") for (int m = 0; m < 4; ++m) _Pragma("unroll") for (int k = 0; k < 2; ++k) dst[m][k] = *(const LAS bf16x8*)(lds + PG8_SA(b, h) + aoff + m * 2048 + k * 1024); } while (0)
; #define PG8_MMA(ai, bj, At, Bt) do { __builtin_amdgcn_s_setprio(1); _Pragma("unroll") for (int m = 0; m < 4; ++m) _Pragma("unroll") for (int n = 0; n < 2; ++n) _Pragma("unroll") for (int k = 0; k < 2; ++k) \
;         acc[ai][bj][m][n] = __builtin_amdgcn_mfma_f32_16x16x32_bf16(Bt[n][k], At[m][k], acc[ai][bj][m][n], 0, 0, 0); __builtin_amdgcn_s_setprio(0); } while (0)
; #define PG8_WAIT_V(n) asm volatile("s_waitcnt vmcnt(" #n ")" ::: "memory")
; #define PG8_WAIT_L(n) asm volatile("s_waitcnt lgkmcnt(" #n ")" ::: "memory")
; #define PG8_BAR __builtin_amdgcn_s_barrier()
; #define PG8_SCHED __builtin_amdgcn_sched_barrier(0)
; template <class Epi, class Sched, bool ALIGN_EPI>
; __device__ __forceinline__ void gemm_phase(LAS unsigned char* lds, const Gemm g, const Sched& S, const Epi& E) {
;     ...
;             PG8_BWAIT(2); PG8_BCOMMIT(1); PG8_SCHED; PG8_LDA(At, 1, 1); PG8_BISSUE(t + 4 >= nt ? pbn + (size_t)(t + 4 - nt) * 64 * Sched::LDN : pbc + (size_t)(t + 4) * 64 * Sched::LDN); PG8_STAGE_A(PG8_SA(1, 0), vc00, vc01, kb2 + 128u);
;             PG8_WAIT_V(12); PG8_WAIT_L(0); PG8_BAR; if (half1) { PG8_MMA(1, 0, At, B0); PG8_MMA(1, 1, At, B1); } PG8_BAR; PG8_SCHED;
	s_lshl_b32 s10, s50, 16
	s_lshl_b64 s[28:29], s[10:11], 2
	s_add_u32 s28, s47, s28
	s_addc_u32 s29, s21, s29
	s_add_u32 s30, s28, 0x1000
	s_waitcnt vmcnt(2)
	s_nop 0
	v_cvt_pk_bf16_f32 v194, v2, v6
	v_cvt_pk_bf16_f32 v198, v3, v7
	v_cvt_pk_bf16_f32 v202, v4, v8
	v_cvt_pk_bf16_f32 v206, v5, v9
	global_load_dwordx4 v[2:5], v240, s[28:29] offset:0
	s_addc_u32 s31, s29, 0
	global_load_dwordx4 v[6:9], v240, s[30:31] offset:0
	v_cvt_pk_bf16_f32 v195, v10, v14
	v_cvt_pk_bf16_f32 v199, v11, v15
	v_cvt_pk_bf16_f32 v203, v12, v16
	v_cvt_pk_bf16_f32 v207, v13, v17
	s_add_u32 s30, s28, 0x2000
	s_addc_u32 s31, s29, 0
	global_load_dwordx4 v[10:13], v240, s[30:31] offset:0
	s_add_u32 s30, s28, 0x3000
	s_addc_u32 s31, s29, 0
	global_load_dwordx4 v[14:17], v240, s[30:31] offset:0
	v_cvt_pk_bf16_f32 v196, v18, v22
	v_cvt_pk_bf16_f32 v200, v19, v23
	v_cvt_pk_bf16_f32 v204, v20, v24
	v_cvt_pk_bf16_f32 v208, v21, v25
	s_add_u32 s30, s28, 0x4000
	s_addc_u32 s31, s29, 0
	global_load_dwordx4 v[18:21], v240, s[30:31] offset:0
	s_add_u32 s30, s28, 0x5000
	s_addc_u32 s31, s29, 0
	global_load_dwordx4 v[22:25], v240, s[30:31] offset:0
	v_cvt_pk_bf16_f32 v197, v26, v30
	v_cvt_pk_bf16_f32 v201, v27, v31
	v_cvt_pk_bf16_f32 v205, v28, v32
	v_cvt_pk_bf16_f32 v209, v29, v33
	s_add_u32 s30, s28, 0x6000
	s_addc_u32 s31, s29, 0
	global_load_dwordx4 v[26:29], v240, s[30:31] offset:0
	s_add_u32 s28, s28, 0x7000
	s_mov_b32 m0, s39
	s_addc_u32 s29, s29, 0
	global_load_dwordx4 v[30:33], v240, s[28:29] offset:0
	v_add_u32_e32 v210, 0x18000, v242
	v_xor_b32_e32 v211, 64, v210
	v_xor_b32_e32 v212, 0x80, v210
	v_xor_b32_e32 v213, 0xc0, v210
	ds_write_b128 v210, v[194:197]
	ds_write_b128 v211, v[198:201]
	ds_write_b128 v212, v[202:205]
	ds_write_b128 v213, v[206:209]
	ds_read_b128 v[218:221], v248 offset:49152
	ds_read_b128 v[222:225], v248 offset:50176
	ds_read_b128 v[210:213], v248 offset:51200
	ds_read_b128 v[214:217], v248 offset:52224
	ds_read_b128 v[202:205], v248 offset:53248
	ds_read_b128 v[206:209], v248 offset:54272
	ds_read_b128 v[194:197], v248 offset:55296
	ds_read_b128 v[198:201], v248 offset:56320
	v_lshl_add_u64 v[238:239], v[238:239], 0, s[16:17]
	global_load_lds_dwordx4 v[238:239], off
	v_lshl_add_u64 v[236:237], v[236:237], 0, s[16:17]
	s_mov_b32 m0, s40
	s_and_b64 vcc, exec, s[4:5]
	global_load_lds_dwordx4 v[236:237], off
	s_waitcnt vmcnt(12)
	s_waitcnt lgkmcnt(0)
	s_barrier
	s_cbranch_vccnz .LBB0_2447
	s_waitcnt lgkmcnt(0)
	v_mfma_f32_16x16x32_bf16 v[94:97], v[178:181], v[218:221], v[94:97]
	v_mfma_f32_16x16x32_bf16 v[90:93], v[186:189], v[218:221], v[90:93]
	v_mfma_f32_16x16x32_bf16 v[78:81], v[178:181], v[210:213], v[78:81]
	v_mfma_f32_16x16x32_bf16 v[74:77], v[186:189], v[210:213], v[74:77]
	v_mfma_f32_16x16x32_bf16 v[62:65], v[178:181], v[202:205], v[62:65]
	v_mfma_f32_16x16x32_bf16 v[58:61], v[186:189], v[202:205], v[58:61]
	v_mfma_f32_16x16x32_bf16 v[46:49], v[178:181], v[194:197], v[46:49]
	v_mfma_f32_16x16x32_bf16 v[42:45], v[186:189], v[194:197], v[42:45]
	v_mfma_f32_16x16x32_bf16 v[94:97], v[182:185], v[222:225], v[94:97]
	v_mfma_f32_16x16x32_bf16 v[90:93], v[190:193], v[222:225], v[90:93]
	v_mfma_f32_16x16x32_bf16 v[78:81], v[182:185], v[214:217], v[78:81]
	v_mfma_f32_16x16x32_bf16 v[74:77], v[190:193], v[214:217], v[74:77]
	v_mfma_f32_16x16x32_bf16 v[62:65], v[182:185], v[206:209], v[62:65]
	v_mfma_f32_16x16x32_bf16 v[58:61], v[190:193], v[206:209], v[58:61]
	v_mfma_f32_16x16x32_bf16 v[46:49], v[182:185], v[198:201], v[46:49]
	v_mfma_f32_16x16x32_bf16 v[42:45], v[190:193], v[198:201], v[42:45]
	v_mfma_f32_16x16x32_bf16 v[86:89], v[162:165], v[218:221], v[86:89]
	v_mfma_f32_16x16x32_bf16 v[82:85], v[170:173], v[218:221], v[82:85]
	v_mfma_f32_16x16x32_bf16 v[70:73], v[162:165], v[210:213], v[70:73]
	v_mfma_f32_16x16x32_bf16 v[66:69], v[170:173], v[210:213], v[66:69]
	v_mfma_f32_16x16x32_bf16 v[54:57], v[162:165], v[202:205], v[54:57]
	v_mfma_f32_16x16x32_bf16 v[50:53], v[170:173], v[202:205], v[50:53]
	v_mfma_f32_16x16x32_bf16 v[38:41], v[162:165], v[194:197], v[38:41]
	v_mfma_f32_16x16x32_bf16 v[34:37], v[170:173], v[194:197], v[34:37]
	v_mfma_f32_16x16x32_bf16 v[86:89], v[166:169], v[222:225], v[86:89]
	v_mfma_f32_16x16x32_bf16 v[82:85], v[174:177], v[222:225], v[82:85]
	v_mfma_f32_16x16x32_bf16 v[70:73], v[166:169], v[214:217], v[70:73]
	v_mfma_f32_16x16x32_bf16 v[66:69], v[174:177], v[214:217], v[66:69]
	v_mfma_f32_16x16x32_bf16 v[54:57], v[166:169], v[206:209], v[54:57]
	v_mfma_f32_16x16x32_bf16 v[50:53], v[174:177], v[206:209], v[50:53]
	v_mfma_f32_16x16x32_bf16 v[38:41], v[166:169], v[198:201], v[38:41]
	v_mfma_f32_16x16x32_bf16 v[34:37], v[174:177], v[198:201], v[34:37]
	s_branch .LBB0_2447

; #define PG8_STAGE_B(bufoff, gbase) do { _Pragma("unroll") for (int _i = 0; _i < 2; ++_i) \
;         __builtin_amdgcn_global_load_lds((const unsigned*)((const char*)(gbase) + voffB[_i]), (LAS unsigned*)(lds + (bufoff) + ldsw + _i * 8192), 16, 0, 0); } while (0)
; #define PG8_STAGE_A(bufoff, V0, V1, kb) do { \
;         __builtin_amdgcn_global_load_lds((const unsigned*)((Abase + (kb)) + (V0)), (LAS unsigned*)(lds + (bufoff) + ldsw), 16, 0, 0); \
;         __builtin_amdgcn_global_load_lds((const unsigned*)((Abase + (kb)) + (V1)), (LAS unsigned*)(lds + (bufoff) + ldsw + 8192), 16, 0, 0); } while (0)
; #define PG8_LDA(dst, b, h) do { _Pragma("unroll") for (int m = 0; m < 4; ++m) _Pragma("unroll") for (int k = 0; k < 2; ++k) dst[m][k] = *(const LAS bf16x8*)(lds + PG8_SA(b, h) + aoff + m * 2048 + k * 1024); } while (0)
; #define PG8_LDB(dst, b, h) do { _Pragma("unroll") for (int n = 0; n < 2; ++n) _Pragma("unroll") for (int k = 0; k < 2; ++k) dst[n][k] = *(const LAS bf16x8*)(lds + PG8_SB(b, h) + boff + n * 2048 + k * 1024); } while (0)
; #define PG8_MMA(ai, bj, At, Bt) do { __builtin_amdgcn_s_setprio(1); _Pragma("unroll") for (int m = 0; m < 4; ++m) _Pragma("unroll") for (int n = 0; n < 2; ++n) _Pragma("unroll") for (int k = 0; k < 2; ++k) \
;         acc[ai][bj][m][n] = __builtin_amdgcn_mfma_f32_16x16x32_bf16(Bt[n][k], At[m][k], acc[ai][bj][m][n], 0, 0, 0); __builtin_amdgcn_s_setprio(0); } while (0)
; #define PG8_WAIT_V(n) asm volatile("s_waitcnt vmcnt(" #n ")" ::: "memory")
; #define PG8_WAIT_L(n) asm volatile("s_waitcnt lgkmcnt(" #n ")" ::: "memory")
; #define PG8_BAR __builtin_amdgcn_s_barrier()
; #define PG8_SCHED __builtin_amdgcn_sched_barrier(0)
; template <class Epi, class Sched, bool ALIGN_EPI>
; __device__ __forceinline__ void gemm_phase(LAS unsigned char* lds, const Gemm g, const Sched& S, const Epi& E) {
;     ...
;             PG8_LDB(B0, 0, 0); PG8_LDB(B1, 0, 1); PG8_SCHED; PG8_LDA(At, 0, 0); PG8_STAGE_A(PG8_SA(1, 1), vc10, vc11, kb1);
;             PG8_WAIT_V(8); PG8_WAIT_L(0); PG8_BAR; PG8_MMA(0, 0, At, B0); PG8_MMA(0, 1, At, B1); PG8_BAR; PG8_SCHED;
;             PG8_LDA(At, 0, 1); PG8_STAGE_B(PG8_SB(0, 0), b2); PG8_STAGE_B(PG8_SB(0, 1), b2 + hstepB); PG8_STAGE_A(PG8_SA(0, 0), s00, s01, kb2);
;             PG8_WAIT_V(8); PG8_WAIT_L(0); PG8_BAR; if (half1) { PG8_MMA(1, 0, At, B0); PG8_MMA(1, 1, At, B1); } PG8_BAR; PG8_SCHED;
.LBB0_2617:
	v_add_u32_e32 v5, s50, v223
	ds_read_b128 v[150:153], v5
	ds_read_b128 v[154:157], v5 offset:1024
	ds_read_b128 v[158:161], v5 offset:2048
	ds_read_b128 v[162:165], v5 offset:3072
	v_add_u32_e32 v5, s51, v223
	ds_read_b128 v[134:137], v5
	ds_read_b128 v[138:141], v5 offset:1024
	ds_read_b128 v[142:145], v5 offset:2048
	ds_read_b128 v[146:149], v5 offset:3072
	v_lshl_add_u64 v[214:215], v[212:213], 0, s[4:5]
	s_add_i32 m0, s40, 0xc000
	s_waitcnt lgkmcnt(0)
	ds_read_b128 v[166:169], v231
	ds_read_b128 v[170:173], v231 offset:1024
	ds_read_b128 v[174:177], v231 offset:2048
	ds_read_b128 v[178:181], v231 offset:3072
	ds_read_b128 v[182:185], v231 offset:4096
	ds_read_b128 v[186:189], v231 offset:5120
	ds_read_b128 v[190:193], v231 offset:6144
	ds_read_b128 v[194:197], v231 offset:7168
	global_load_lds_dwordx4 v[214:215], off
	v_lshl_add_u64 v[214:215], v[210:211], 0, s[4:5]
	s_add_i32 m0, s40, 0xe000
	s_nop 0
	global_load_lds_dwordx4 v[214:215], off
	s_waitcnt vmcnt(8)
	s_waitcnt lgkmcnt(0)
	s_barrier
	s_waitcnt lgkmcnt(0)
	v_mfma_f32_16x16x32_bf16 v[130:133], v[150:153], v[166:169], v[130:133]
	v_mfma_f32_16x16x32_bf16 v[126:129], v[158:161], v[166:169], v[126:129]
	v_mfma_f32_16x16x32_bf16 v[114:117], v[150:153], v[174:177], v[114:117]
	v_mfma_f32_16x16x32_bf16 v[110:113], v[158:161], v[174:177], v[110:113]
	v_mfma_f32_16x16x32_bf16 v[98:101], v[150:153], v[182:185], v[98:101]
	v_mfma_f32_16x16x32_bf16 v[94:97], v[158:161], v[182:185], v[94:97]
	v_mfma_f32_16x16x32_bf16 v[82:85], v[150:153], v[190:193], v[82:85]
	v_mfma_f32_16x16x32_bf16 v[78:81], v[158:161], v[190:193], v[78:81]
	v_mfma_f32_16x16x32_bf16 v[130:133], v[154:157], v[170:173], v[130:133]
	v_mfma_f32_16x16x32_bf16 v[126:129], v[162:165], v[170:173], v[126:129]
	v_mfma_f32_16x16x32_bf16 v[114:117], v[154:157], v[178:181], v[114:117]
	v_mfma_f32_16x16x32_bf16 v[110:113], v[162:165], v[178:181], v[110:113]
	v_mfma_f32_16x16x32_bf16 v[98:101], v[154:157], v[186:189], v[98:101]
	v_mfma_f32_16x16x32_bf16 v[94:97], v[162:165], v[186:189], v[94:97]
	v_mfma_f32_16x16x32_bf16 v[82:85], v[154:157], v[194:197], v[82:85]
	v_mfma_f32_16x16x32_bf16 v[78:81], v[162:165], v[194:197], v[78:81]
	v_mfma_f32_16x16x32_bf16 v[122:125], v[134:137], v[166:169], v[122:125]
	v_mfma_f32_16x16x32_bf16 v[118:121], v[142:145], v[166:169], v[118:121]
	v_mfma_f32_16x16x32_bf16 v[106:109], v[134:137], v[174:177], v[106:109]
	v_mfma_f32_16x16x32_bf16 v[102:105], v[142:145], v[174:177], v[102:105]
	v_mfma_f32_16x16x32_bf16 v[90:93], v[134:137], v[182:185], v[90:93]
	v_mfma_f32_16x16x32_bf16 v[86:89], v[142:145], v[182:185], v[86:89]
	v_mfma_f32_16x16x32_bf16 v[74:77], v[134:137], v[190:193], v[74:77]
	v_mfma_f32_16x16x32_bf16 v[70:73], v[142:145], v[190:193], v[70:73]
	v_mfma_f32_16x16x32_bf16 v[122:125], v[138:141], v[170:173], v[122:125]
	v_mfma_f32_16x16x32_bf16 v[118:121], v[146:149], v[170:173], v[118:121]
	v_mfma_f32_16x16x32_bf16 v[106:109], v[138:141], v[178:181], v[106:109]
	v_mfma_f32_16x16x32_bf16 v[102:105], v[146:149], v[178:181], v[102:105]
	v_mfma_f32_16x16x32_bf16 v[90:93], v[138:141], v[186:189], v[90:93]
	v_mfma_f32_16x16x32_bf16 v[86:89], v[146:149], v[186:189], v[86:89]
	v_mfma_f32_16x16x32_bf16 v[74:77], v[138:141], v[194:197], v[74:77]
	v_mfma_f32_16x16x32_bf16 v[70:73], v[146:149], v[194:197], v[70:73]
	s_barrier
	s_add_i32 s4, s50, s39
	v_lshl_add_u64 v[214:215], s[34:35], 0, v[198:199]
	s_mov_b32 m0, s4
	ds_read_b128 v[190:193], v231 offset:16384
	ds_read_b128 v[194:197], v231 offset:17408
	ds_read_b128 v[182:185], v231 offset:18432
	ds_read_b128 v[186:189], v231 offset:19456
	ds_read_b128 v[174:177], v231 offset:20480
	ds_read_b128 v[178:181], v231 offset:21504
	ds_read_b128 v[166:169], v231 offset:22528
	ds_read_b128 v[170:173], v231 offset:23552
	global_load_lds_dwordx4 v[214:215], off
	s_add_i32 m0, s4, 0x2000
	s_add_u32 s4, s34, 0x40000
	v_lshl_add_u64 v[216:217], s[34:35], 0, v[200:201]
	s_addc_u32 s5, s35, 0
	s_add_i32 s37, s51, s39
	global_load_lds_dwordx4 v[216:217], off
	v_lshl_add_u64 v[238:239], s[4:5], 0, v[198:199]
	s_mov_b32 m0, s37
	v_cndmask_b32_e64 v5, 0, 1, s[28:29]
	global_load_lds_dwordx4 v[238:239], off
	v_lshl_add_u64 v[238:239], s[4:5], 0, v[200:201]
	s_add_i32 m0, s37, 0x2000
	v_readlane_b32 s4, v253, 52
	v_readlane_b32 s5, v253, 53
	s_add_u32 s36, s4, s36
	global_load_lds_dwordx4 v[238:239], off
	s_addc_u32 s37, s5, 0
	s_mov_b32 m0, s40
	v_cmp_ne_u32_e64 s[4:5], 1, v5
	global_load_lds_dwordx4 v2, s[36:37]
	s_mov_b32 m0, s41
	s_andn2_b64 vcc, exec, s[28:29]
	global_load_lds_dwordx4 v4, s[36:37]
	s_waitcnt vmcnt(8)
	s_waitcnt lgkmcnt(0)
	s_barrier
	s_cbranch_vccnz .LBB0_2619
	s_waitcnt lgkmcnt(0)
	v_mfma_f32_16x16x32_bf16 v[66:69], v[150:153], v[190:193], v[66:69]
	v_mfma_f32_16x16x32_bf16 v[62:65], v[158:161], v[190:193], v[62:65]
	v_mfma_f32_16x16x32_bf16 v[50:53], v[150:153], v[182:185], v[50:53]
	v_mfma_f32_16x16x32_bf16 v[46:49], v[158:161], v[182:185], v[46:49]
	v_mfma_f32_16x16x32_bf16 v[34:37], v[150:153], v[174:177], v[34:37]
	v_mfma_f32_16x16x32_bf16 v[30:33], v[158:161], v[174:177], v[30:33]
	v_mfma_f32_16x16x32_bf16 v[18:21], v[150:153], v[166:169], v[18:21]
	v_mfma_f32_16x16x32_bf16 v[14:17], v[158:161], v[166:169], v[14:17]
	v_mfma_f32_16x16x32_bf16 v[66:69], v[154:157], v[194:197], v[66:69]
	v_mfma_f32_16x16x32_bf16 v[62:65], v[162:165], v[194:197], v[62:65]
	v_mfma_f32_16x16x32_bf16 v[50:53], v[154:157], v[186:189], v[50:53]
	v_mfma_f32_16x16x32_bf16 v[46:49], v[162:165], v[186:189], v[46:49]
	v_mfma_f32_16x16x32_bf16 v[34:37], v[154:157], v[178:181], v[34:37]
	v_mfma_f32_16x16x32_bf16 v[30:33], v[162:165], v[178:181], v[30:33]
	v_mfma_f32_16x16x32_bf16 v[18:21], v[154:157], v[170:173], v[18:21]
	v_mfma_f32_16x16x32_bf16 v[14:17], v[162:165], v[170:173], v[14:17]
	v_mfma_f32_16x16x32_bf16 v[58:61], v[134:137], v[190:193], v[58:61]
	v_mfma_f32_16x16x32_bf16 v[54:57], v[142:145], v[190:193], v[54:57]
	v_mfma_f32_16x16x32_bf16 v[42:45], v[134:137], v[182:185], v[42:45]
	v_mfma_f32_16x16x32_bf16 v[38:41], v[142:145], v[182:185], v[38:41]
	v_mfma_f32_16x16x32_bf16 v[26:29], v[134:137], v[174:177], v[26:29]
	v_mfma_f32_16x16x32_bf16 v[22:25], v[142:145], v[174:177], v[22:25]
	v_mfma_f32_16x16x32_bf16 v[10:13], v[134:137], v[166:169], v[10:13]
	v_mfma_f32_16x16x32_bf16 v[6:9], v[142:145], v[166:169], v[6:9]
	v_mfma_f32_16x16x32_bf16 v[58:61], v[138:141], v[194:197], v[58:61]
	v_mfma_f32_16x16x32_bf16 v[54:57], v[146:149], v[194:197], v[54:57]
	v_mfma_f32_16x16x32_bf16 v[42:45], v[138:141], v[186:189], v[42:45]
	v_mfma_f32_16x16x32_bf16 v[38:41], v[146:149], v[186:189], v[38:41]
	v_mfma_f32_16x16x32_bf16 v[26:29], v[138:141], v[178:181], v[26:29]
	v_mfma_f32_16x16x32_bf16 v[22:25], v[146:149], v[178:181], v[22:25]
	v_mfma_f32_16x16x32_bf16 v[10:13], v[138:141], v[170:173], v[10:13]
	v_mfma_f32_16x16x32_bf16 v[6:9], v[146:149], v[170:173], v[6:9]
; #define PG8_STAGE_B(bufoff, gbase) do { _Pragma("unroll") for (int _i = 0; _i < 2; ++_i) \
;         __builtin_amdgcn_global_load_lds((const unsigned*)((const char*)(gbase) + voffB[_i]), (LAS unsigned*)(lds + (bufoff) + ldsw + _i * 8192), 16, 0, 0); } while (0)
; #define PG8_STAGE_A(bufoff, V0, V1, kb) do { \
;         __builtin_amdgcn_global_load_lds((const unsigned*)((Abase + (kb)) + (V0)), (LAS unsigned*)(lds + (bufoff) + ldsw), 16, 0, 0); \
;         __builtin_amdgcn_global_load_lds((const unsigned*)((Abase + (kb)) + (V1)), (LAS unsigned*)(lds + (bufoff) + ldsw + 8192), 16, 0, 0); } while (0)
; #define PG8_LDA(dst, b, h) do { _Pragma("unroll") for (int m = 0; m < 4; ++m) _Pragma("unroll") for (int k = 0; k < 2; ++k) dst[m][k] = *(const LAS bf16x8*)(lds + PG8_SA(b, h) + aoff + m * 2048 + k * 1024); } while (0)
; #define PG8_LDB(dst, b, h) do { _Pragma("unroll") for (int n = 0; n < 2; ++n) _Pragma("unroll") for (int k = 0; k < 2; ++k) dst[n][k] = *(const LAS bf16x8*)(lds + PG8_SB(b, h) + boff + n * 2048 + k * 1024); } while (0)
; #define PG8_WAIT_V(n) asm volatile("s_waitcnt vmcnt(" #n ")" ::: "memory")
; #define PG8_BAR __builtin_amdgcn_s_barrier()
; template <class Epi, class Sched, bool ALIGN_EPI>
; __device__ __forceinline__ void gemm_phase(LAS unsigned char* lds, const Gemm g, const Sched& S, const Epi& E) {
;     ...
;             PG8_LDB(B0, 0, 0); PG8_LDB(B1, 0, 1); PG8_SCHED; PG8_LDA(At, 0, 0); PG8_STAGE_A(PG8_SA(1, 1), vc10, vc11, kb1);
;             PG8_WAIT_V(8); PG8_WAIT_L(0); PG8_BAR; PG8_MMA(0, 0, At, B0); PG8_MMA(0, 1, At, B1); PG8_BAR; PG8_SCHED;
;             PG8_LDA(At, 0, 1); PG8_STAGE_B(PG8_SB(0, 0), b2); PG8_STAGE_B(PG8_SB(0, 1), b2 + hstepB); PG8_STAGE_A(PG8_SA(0, 0), s00, s01, kb2);
;             PG8_WAIT_V(8); PG8_WAIT_L(0); PG8_BAR; if (half1) { PG8_MMA(1, 0, At, B0); PG8_MMA(1, 1, At, B1); } PG8_BAR; PG8_SCHED;
;             PG8_LDB(B0, 1, 0); PG8_LDB(B1, 1, 1); PG8_SCHED; PG8_LDA(At, 1, 0); PG8_STAGE_A(PG8_SA(0, 1), s10, s11, kb2);
;             PG8_WAIT_V(8); PG8_WAIT_L(0); PG8_BAR; PG8_MMA(0, 0, At, B0); PG8_MMA(0, 1, At, B1); PG8_BAR; PG8_SCHED;
;             PG8_LDA(At, 1, 1); PG8_STAGE_B(PG8_SB(1, 0), b3); PG8_STAGE_B(PG8_SB(1, 1), b3 + hstepB); PG8_STAGE_A(PG8_SA(1, 0), s00, s01, kb3);
;             PG8_WAIT_V(8); PG8_WAIT_L(0); PG8_BAR; if (half1) { PG8_MMA(1, 0, At, B0); PG8_MMA(1, 1, At, B1); } PG8_BAR; PG8_SCHED;
.LBB0_2619:
	v_mov_b32_e32 v5, v3
	v_lshl_add_u64 v[238:239], s[36:37], 0, v[2:3]
	v_lshl_add_u64 v[4:5], s[36:37], 0, v[4:5]
	s_barrier
	v_add_u32_e32 v2, s52, v223
	ds_read_b128 v[150:153], v2
	ds_read_b128 v[154:157], v2 offset:1024
	ds_read_b128 v[158:161], v2 offset:2048
	ds_read_b128 v[162:165], v2 offset:3072
	v_add_u32_e32 v2, s53, v223
	ds_read_b128 v[134:137], v2
	ds_read_b128 v[138:141], v2 offset:1024
	ds_read_b128 v[142:145], v2 offset:2048
	ds_read_b128 v[146:149], v2 offset:3072
	s_mov_b32 m0, s42
	s_waitcnt lgkmcnt(0)
	ds_read_b128 v[166:169], v231 offset:32768
	ds_read_b128 v[170:173], v231 offset:33792
	ds_read_b128 v[174:177], v231 offset:34816
	ds_read_b128 v[178:181], v231 offset:35840
	ds_read_b128 v[182:185], v231 offset:36864
	ds_read_b128 v[186:189], v231 offset:37888
	ds_read_b128 v[190:193], v231 offset:38912
	ds_read_b128 v[194:197], v231 offset:39936
	global_load_lds_dwordx4 v207, s[36:37]
	s_mov_b32 m0, s43
	s_nop 0
	global_load_lds_dwordx4 v209, s[36:37]
	s_waitcnt vmcnt(8)
	s_waitcnt lgkmcnt(0)
	s_barrier
	s_waitcnt lgkmcnt(0)
	v_mfma_f32_16x16x32_bf16 v[130:133], v[150:153], v[166:169], v[130:133]
	v_mfma_f32_16x16x32_bf16 v[126:129], v[158:161], v[166:169], v[126:129]
	v_mfma_f32_16x16x32_bf16 v[114:117], v[150:153], v[174:177], v[114:117]
	v_mfma_f32_16x16x32_bf16 v[110:113], v[158:161], v[174:177], v[110:113]
	v_mfma_f32_16x16x32_bf16 v[98:101], v[150:153], v[182:185], v[98:101]
	v_mfma_f32_16x16x32_bf16 v[94:97], v[158:161], v[182:185], v[94:97]
	v_mfma_f32_16x16x32_bf16 v[82:85], v[150:153], v[190:193], v[82:85]
	v_mfma_f32_16x16x32_bf16 v[78:81], v[158:161], v[190:193], v[78:81]
	v_mfma_f32_16x16x32_bf16 v[130:133], v[154:157], v[170:173], v[130:133]
	v_mfma_f32_16x16x32_bf16 v[126:129], v[162:165], v[170:173], v[126:129]
	v_mfma_f32_16x16x32_bf16 v[114:117], v[154:157], v[178:181], v[114:117]
	v_mfma_f32_16x16x32_bf16 v[110:113], v[162:165], v[178:181], v[110:113]
	v_mfma_f32_16x16x32_bf16 v[98:101], v[154:157], v[186:189], v[98:101]
	v_mfma_f32_16x16x32_bf16 v[94:97], v[162:165], v[186:189], v[94:97]
	v_mfma_f32_16x16x32_bf16 v[82:85], v[154:157], v[194:197], v[82:85]
	v_mfma_f32_16x16x32_bf16 v[78:81], v[162:165], v[194:197], v[78:81]
	v_mfma_f32_16x16x32_bf16 v[122:125], v[134:137], v[166:169], v[122:125]
	v_mfma_f32_16x16x32_bf16 v[118:121], v[142:145], v[166:169], v[118:121]
	v_mfma_f32_16x16x32_bf16 v[106:109], v[134:137], v[174:177], v[106:109]
	v_mfma_f32_16x16x32_bf16 v[102:105], v[142:145], v[174:177], v[102:105]
	v_mfma_f32_16x16x32_bf16 v[90:93], v[134:137], v[182:185], v[90:93]
	v_mfma_f32_16x16x32_bf16 v[86:89], v[142:145], v[182:185], v[86:89]
	v_mfma_f32_16x16x32_bf16 v[74:77], v[134:137], v[190:193], v[74:77]
	v_mfma_f32_16x16x32_bf16 v[70:73], v[142:145], v[190:193], v[70:73]
	v_mfma_f32_16x16x32_bf16 v[122:125], v[138:141], v[170:173], v[122:125]
	v_mfma_f32_16x16x32_bf16 v[118:121], v[146:149], v[170:173], v[118:121]
	v_mfma_f32_16x16x32_bf16 v[106:109], v[138:141], v[178:181], v[106:109]
	v_mfma_f32_16x16x32_bf16 v[102:105], v[146:149], v[178:181], v[102:105]
	v_mfma_f32_16x16x32_bf16 v[90:93], v[138:141], v[186:189], v[90:93]
	v_mfma_f32_16x16x32_bf16 v[86:89], v[146:149], v[186:189], v[86:89]
	v_mfma_f32_16x16x32_bf16 v[74:77], v[138:141], v[194:197], v[74:77]
	v_mfma_f32_16x16x32_bf16 v[70:73], v[146:149], v[194:197], v[70:73]
	s_barrier
	s_add_i32 s36, s52, s39
	v_lshl_add_u64 v[214:215], v[214:215], 0, s[10:11]
	s_mov_b32 m0, s36
	ds_read_b128 v[190:193], v231 offset:49152
	ds_read_b128 v[194:197], v231 offset:50176
	ds_read_b128 v[182:185], v231 offset:51200
	ds_read_b128 v[186:189], v231 offset:52224
	ds_read_b128 v[174:177], v231 offset:53248
	ds_read_b128 v[178:181], v231 offset:54272
	ds_read_b128 v[166:169], v231 offset:55296
	ds_read_b128 v[170:173], v231 offset:56320
	global_load_lds_dwordx4 v[214:215], off
	s_add_i32 m0, s36, 0x2000
	s_add_u32 s34, s34, 0x40080
	v_lshl_add_u64 v[214:215], v[216:217], 0, s[10:11]
	s_addc_u32 s35, s35, 0
	s_add_i32 s36, s53, s39
	global_load_lds_dwordx4 v[214:215], off
	v_lshl_add_u64 v[214:215], s[34:35], 0, v[198:199]
	s_mov_b32 m0, s36
	v_lshl_add_u64 v[4:5], v[4:5], 0, s[10:11]
	global_load_lds_dwordx4 v[214:215], off
	v_lshl_add_u64 v[214:215], s[34:35], 0, v[200:201]
	s_add_i32 m0, s36, 0x2000
	s_and_b64 vcc, exec, s[4:5]
	global_load_lds_dwordx4 v[214:215], off
	v_lshl_add_u64 v[214:215], v[238:239], 0, s[10:11]
	s_mov_b32 m0, s44
	s_nop 0
	global_load_lds_dwordx4 v[214:215], off
	s_mov_b32 m0, s45
	s_nop 0
	global_load_lds_dwordx4 v[4:5], off
	s_waitcnt vmcnt(8)
	s_waitcnt lgkmcnt(0)
	s_barrier
	s_cbranch_vccnz .LBB0_2621
	s_waitcnt lgkmcnt(0)
	v_mfma_f32_16x16x32_bf16 v[66:69], v[150:153], v[190:193], v[66:69]
	v_mfma_f32_16x16x32_bf16 v[62:65], v[158:161], v[190:193], v[62:65]
	v_mfma_f32_16x16x32_bf16 v[50:53], v[150:153], v[182:185], v[50:53]
	v_mfma_f32_16x16x32_bf16 v[46:49], v[158:161], v[182:185], v[46:49]
	v_mfma_f32_16x16x32_bf16 v[34:37], v[150:153], v[174:177], v[34:37]
	v_mfma_f32_16x16x32_bf16 v[30:33], v[158:161], v[174:177], v[30:33]
	v_mfma_f32_16x16x32_bf16 v[18:21], v[150:153], v[166:169], v[18:21]
	v_mfma_f32_16x16x32_bf16 v[14:17], v[158:161], v[166:169], v[14:17]
	v_mfma_f32_16x16x32_bf16 v[66:69], v[154:157], v[194:197], v[66:69]
	v_mfma_f32_16x16x32_bf16 v[62:65], v[162:165], v[194:197], v[62:65]
	v_mfma_f32_16x16x32_bf16 v[50:53], v[154:157], v[186:189], v[50:53]
	v_mfma_f32_16x16x32_bf16 v[46:49], v[162:165], v[186:189], v[46:49]
	v_mfma_f32_16x16x32_bf16 v[34:37], v[154:157], v[178:181], v[34:37]
	v_mfma_f32_16x16x32_bf16 v[30:33], v[162:165], v[178:181], v[30:33]
	v_mfma_f32_16x16x32_bf16 v[18:21], v[154:157], v[170:173], v[18:21]
	v_mfma_f32_16x16x32_bf16 v[14:17], v[162:165], v[170:173], v[14:17]
	v_mfma_f32_16x16x32_bf16 v[58:61], v[134:137], v[190:193], v[58:61]
	v_mfma_f32_16x16x32_bf16 v[54:57], v[142:145], v[190:193], v[54:57]
	v_mfma_f32_16x16x32_bf16 v[42:45], v[134:137], v[182:185], v[42:45]
	v_mfma_f32_16x16x32_bf16 v[38:41], v[142:145], v[182:185], v[38:41]
	v_mfma_f32_16x16x32_bf16 v[26:29], v[134:137], v[174:177], v[26:29]
	v_mfma_f32_16x16x32_bf16 v[22:25], v[142:145], v[174:177], v[22:25]
	v_mfma_f32_16x16x32_bf16 v[10:13], v[134:137], v[166:169], v[10:13]
	v_mfma_f32_16x16x32_bf16 v[4:7], v[142:145], v[166:169], v[6:9]
	v_mfma_f32_16x16x32_bf16 v[58:61], v[138:141], v[194:197], v[58:61]
	v_mfma_f32_16x16x32_bf16 v[54:57], v[146:149], v[194:197], v[54:57]
	v_mfma_f32_16x16x32_bf16 v[42:45], v[138:141], v[186:189], v[42:45]
	v_mfma_f32_16x16x32_bf16 v[38:41], v[146:149], v[186:189], v[38:41]
	v_mfma_f32_16x16x32_bf16 v[26:29], v[138:141], v[178:181], v[26:29]
	v_mfma_f32_16x16x32_bf16 v[22:25], v[146:149], v[178:181], v[22:25]
	v_mfma_f32_16x16x32_bf16 v[10:13], v[138:141], v[170:173], v[10:13]
	v_mfma_f32_16x16x32_bf16 v[6:9], v[146:149], v[170:173], v[4:7]

; #define PG8_STAGE_B(bufoff, gbase) do { _Pragma("unroll") for (int _i = 0; _i < 2; ++_i) \
;         __builtin_amdgcn_global_load_lds((const unsigned*)((const char*)(gbase) + voffB[_i]), (LAS unsigned*)(lds + (bufoff) + ldsw + _i * 8192), 16, 0, 0); } while (0)
; #define PG8_STAGE_A(bufoff, V0, V1, kb) do { \
;         __builtin_amdgcn_global_load_lds((const unsigned*)((Abase + (kb)) + (V0)), (LAS unsigned*)(lds + (bufoff) + ldsw), 16, 0, 0); \
;         __builtin_amdgcn_global_load_lds((const unsigned*)((Abase + (kb)) + (V1)), (LAS unsigned*)(lds + (bufoff) + ldsw + 8192), 16, 0, 0); } while (0)
; #define PG8_LDA(dst, b, h) do { _Pragma("unroll") for (int m = 0; m < 4; ++m) _Pragma("unroll") for (int k = 0; k < 2; ++k) dst[m][k] = *(const LAS bf16x8*)(lds + PG8_SA(b, h) + aoff + m * 2048 + k * 1024); } while (0)
; #define PG8_LDB(dst, b, h) do { _Pragma("unroll") for (int n = 0; n < 2; ++n) _Pragma("unroll") for (int k = 0; k < 2; ++k) dst[n][k] = *(const LAS bf16x8*)(lds + PG8_SB(b, h) + boff + n * 2048 + k * 1024); } while (0)
; #define PG8_WAIT_V(n) asm volatile("s_waitcnt vmcnt(" #n ")" ::: "memory")
; #define PG8_BAR __builtin_amdgcn_s_barrier()
; template <class Epi, class Sched, bool ALIGN_EPI>
; __device__ __forceinline__ void gemm_phase(LAS unsigned char* lds, const Gemm g, const Sched& S, const Epi& E) {
;     ...
;             PG8_LDB(B0, 0, 0); PG8_LDB(B1, 0, 1); PG8_SCHED; PG8_LDA(At, 0, 0); PG8_STAGE_A(PG8_SA(1, 1), vc10, vc11, kb1);
;             PG8_WAIT_V(8); PG8_WAIT_L(0); PG8_BAR; PG8_MMA(0, 0, At, B0); PG8_MMA(0, 1, At, B1); PG8_BAR; PG8_SCHED;
;             PG8_LDA(At, 0, 1); PG8_STAGE_B(PG8_SB(0, 0), b2); PG8_STAGE_B(PG8_SB(0, 1), b2 + hstepB); PG8_STAGE_A(PG8_SA(0, 0), s00, s01, kb2);
;             PG8_WAIT_V(8); PG8_WAIT_L(0); PG8_BAR; if (half1) { PG8_MMA(1, 0, At, B0); PG8_MMA(1, 1, At, B1); } PG8_BAR; PG8_SCHED;
;             PG8_LDB(B0, 1, 0); PG8_LDB(B1, 1, 1); PG8_SCHED; PG8_LDA(At, 1, 0); PG8_STAGE_A(PG8_SA(0, 1), s10, s11, kb2);
;             PG8_WAIT_V(8); PG8_WAIT_L(0); PG8_BAR; PG8_MMA(0, 0, At, B0); PG8_MMA(0, 1, At, B1); PG8_BAR; PG8_SCHED;
;             PG8_LDA(At, 1, 1); PG8_STAGE_B(PG8_SB(1, 0), b3); PG8_STAGE_B(PG8_SB(1, 1), b3 + hstepB); PG8_STAGE_A(PG8_SA(1, 0), s00, s01, kb3);
;             PG8_WAIT_V(8); PG8_WAIT_L(0); PG8_BAR; if (half1) { PG8_MMA(1, 0, At, B0); PG8_MMA(1, 1, At, B1); } PG8_BAR; PG8_SCHED;
.LBB0_2912:
	v_add_u32_e32 v5, s50, v219
	ds_read_b128 v[150:153], v5
	ds_read_b128 v[154:157], v5 offset:1024
	ds_read_b128 v[158:161], v5 offset:2048
	ds_read_b128 v[162:165], v5 offset:3072
	v_add_u32_e32 v5, s51, v219
	ds_read_b128 v[134:137], v5
	ds_read_b128 v[138:141], v5 offset:1024
	ds_read_b128 v[142:145], v5 offset:2048
	ds_read_b128 v[146:149], v5 offset:3072
	v_readlane_b32 s60, v253, 60
	v_readlane_b32 s61, v253, 61
	s_add_u32 s34, s60, s3
	s_addc_u32 s35, s61, 0
	v_lshl_add_u64 v[212:213], s[34:35], 0, v[208:209]
	v_lshl_add_u64 v[212:213], v[212:213], 0, s[6:7]
	s_add_i32 m0, s41, 0xc000
	s_waitcnt lgkmcnt(0)
	ds_read_b128 v[166:169], v220
	ds_read_b128 v[170:173], v220 offset:1024
	ds_read_b128 v[174:177], v220 offset:2048
	ds_read_b128 v[178:181], v220 offset:3072
	ds_read_b128 v[182:185], v220 offset:4096
	ds_read_b128 v[186:189], v220 offset:5120
	ds_read_b128 v[190:193], v220 offset:6144
	ds_read_b128 v[194:197], v220 offset:7168
	global_load_lds_dwordx4 v[212:213], off
	v_lshl_add_u64 v[212:213], s[34:35], 0, v[210:211]
	v_lshl_add_u64 v[212:213], v[212:213], 0, s[6:7]
	s_add_i32 m0, s41, 0xe000
	s_nop 0
	global_load_lds_dwordx4 v[212:213], off
	s_waitcnt vmcnt(8)
	s_waitcnt lgkmcnt(0)
	s_barrier
	s_waitcnt lgkmcnt(0)
	v_mfma_f32_16x16x32_bf16 v[130:133], v[150:153], v[166:169], v[130:133]
	v_mfma_f32_16x16x32_bf16 v[126:129], v[158:161], v[166:169], v[126:129]
	v_mfma_f32_16x16x32_bf16 v[114:117], v[150:153], v[174:177], v[114:117]
	v_mfma_f32_16x16x32_bf16 v[110:113], v[158:161], v[174:177], v[110:113]
	v_mfma_f32_16x16x32_bf16 v[98:101], v[150:153], v[182:185], v[98:101]
	v_mfma_f32_16x16x32_bf16 v[94:97], v[158:161], v[182:185], v[94:97]
	v_mfma_f32_16x16x32_bf16 v[82:85], v[150:153], v[190:193], v[82:85]
	v_mfma_f32_16x16x32_bf16 v[78:81], v[158:161], v[190:193], v[78:81]
	v_mfma_f32_16x16x32_bf16 v[130:133], v[154:157], v[170:173], v[130:133]
	v_mfma_f32_16x16x32_bf16 v[126:129], v[162:165], v[170:173], v[126:129]
	v_mfma_f32_16x16x32_bf16 v[114:117], v[154:157], v[178:181], v[114:117]
	v_mfma_f32_16x16x32_bf16 v[110:113], v[162:165], v[178:181], v[110:113]
	v_mfma_f32_16x16x32_bf16 v[98:101], v[154:157], v[186:189], v[98:101]
	v_mfma_f32_16x16x32_bf16 v[94:97], v[162:165], v[186:189], v[94:97]
	v_mfma_f32_16x16x32_bf16 v[82:85], v[154:157], v[194:197], v[82:85]
	v_mfma_f32_16x16x32_bf16 v[78:81], v[162:165], v[194:197], v[78:81]
	v_mfma_f32_16x16x32_bf16 v[122:125], v[134:137], v[166:169], v[122:125]
	v_mfma_f32_16x16x32_bf16 v[118:121], v[142:145], v[166:169], v[118:121]
	v_mfma_f32_16x16x32_bf16 v[106:109], v[134:137], v[174:177], v[106:109]
	v_mfma_f32_16x16x32_bf16 v[102:105], v[142:145], v[174:177], v[102:105]
	v_mfma_f32_16x16x32_bf16 v[90:93], v[134:137], v[182:185], v[90:93]
	v_mfma_f32_16x16x32_bf16 v[86:89], v[142:145], v[182:185], v[86:89]
	v_mfma_f32_16x16x32_bf16 v[74:77], v[134:137], v[190:193], v[74:77]
	v_mfma_f32_16x16x32_bf16 v[70:73], v[142:145], v[190:193], v[70:73]
	v_mfma_f32_16x16x32_bf16 v[122:125], v[138:141], v[170:173], v[122:125]
	v_mfma_f32_16x16x32_bf16 v[118:121], v[146:149], v[170:173], v[118:121]
	v_mfma_f32_16x16x32_bf16 v[106:109], v[138:141], v[178:181], v[106:109]
	v_mfma_f32_16x16x32_bf16 v[102:105], v[146:149], v[178:181], v[102:105]
	v_mfma_f32_16x16x32_bf16 v[90:93], v[138:141], v[186:189], v[90:93]
	v_mfma_f32_16x16x32_bf16 v[86:89], v[146:149], v[186:189], v[86:89]
	v_mfma_f32_16x16x32_bf16 v[74:77], v[138:141], v[194:197], v[74:77]
	v_mfma_f32_16x16x32_bf16 v[70:73], v[146:149], v[194:197], v[70:73]
	s_barrier
	s_add_i32 s3, s50, s40
	v_lshl_add_u64 v[212:213], s[30:31], 0, v[198:199]
	s_mov_b32 m0, s3
	ds_read_b128 v[190:193], v220 offset:16384
	ds_read_b128 v[194:197], v220 offset:17408
	ds_read_b128 v[182:185], v220 offset:18432
	ds_read_b128 v[186:189], v220 offset:19456
	ds_read_b128 v[174:177], v220 offset:20480
	ds_read_b128 v[178:181], v220 offset:21504
	ds_read_b128 v[166:169], v220 offset:22528
	ds_read_b128 v[170:173], v220 offset:23552
	global_load_lds_dwordx4 v[212:213], off
	s_add_i32 m0, s3, 0x2000
	s_add_u32 s34, s30, 0x10000
	v_lshl_add_u64 v[214:215], s[30:31], 0, v[200:201]
	s_addc_u32 s35, s31, 0
	s_add_i32 s3, s51, s40
	global_load_lds_dwordx4 v[214:215], off
	v_lshl_add_u64 v[230:231], s[34:35], 0, v[198:199]
	s_mov_b32 m0, s3
	v_cndmask_b32_e64 v5, 0, 1, s[26:27]
	global_load_lds_dwordx4 v[230:231], off
	s_add_i32 m0, s3, 0x2000
	v_lshl_add_u64 v[230:231], s[34:35], 0, v[200:201]
	s_add_u32 s34, s60, s4
	global_load_lds_dwordx4 v[230:231], off
	s_addc_u32 s35, s61, 0
	s_mov_b32 m0, s41
	v_cmp_ne_u32_e64 s[4:5], 1, v5
	global_load_lds_dwordx4 v2, s[34:35]
	s_mov_b32 m0, s42
	s_andn2_b64 vcc, exec, s[26:27]
	global_load_lds_dwordx4 v4, s[34:35]
	s_waitcnt vmcnt(8)
	s_waitcnt lgkmcnt(0)
	s_barrier
	s_cbranch_vccnz .LBB0_2914
	s_waitcnt lgkmcnt(0)
	v_mfma_f32_16x16x32_bf16 v[66:69], v[150:153], v[190:193], v[66:69]
	v_mfma_f32_16x16x32_bf16 v[62:65], v[158:161], v[190:193], v[62:65]
	v_mfma_f32_16x16x32_bf16 v[50:53], v[150:153], v[182:185], v[50:53]
	v_mfma_f32_16x16x32_bf16 v[46:49], v[158:161], v[182:185], v[46:49]
	v_mfma_f32_16x16x32_bf16 v[34:37], v[150:153], v[174:177], v[34:37]
	v_mfma_f32_16x16x32_bf16 v[30:33], v[158:161], v[174:177], v[30:33]
	v_mfma_f32_16x16x32_bf16 v[18:21], v[150:153], v[166:169], v[18:21]
	v_mfma_f32_16x16x32_bf16 v[14:17], v[158:161], v[166:169], v[14:17]
	v_mfma_f32_16x16x32_bf16 v[66:69], v[154:157], v[194:197], v[66:69]
	v_mfma_f32_16x16x32_bf16 v[62:65], v[162:165], v[194:197], v[62:65]
	v_mfma_f32_16x16x32_bf16 v[50:53], v[154:157], v[186:189], v[50:53]
	v_mfma_f32_16x16x32_bf16 v[46:49], v[162:165], v[186:189], v[46:49]
	v_mfma_f32_16x16x32_bf16 v[34:37], v[154:157], v[178:181], v[34:37]
	v_mfma_f32_16x16x32_bf16 v[30:33], v[162:165], v[178:181], v[30:33]
	v_mfma_f32_16x16x32_bf16 v[18:21], v[154:157], v[170:173], v[18:21]
	v_mfma_f32_16x16x32_bf16 v[14:17], v[162:165], v[170:173], v[14:17]
	v_mfma_f32_16x16x32_bf16 v[58:61], v[134:137], v[190:193], v[58:61]
	v_mfma_f32_16x16x32_bf16 v[54:57], v[142:145], v[190:193], v[54:57]
	v_mfma_f32_16x16x32_bf16 v[42:45], v[134:137], v[182:185], v[42:45]
	v_mfma_f32_16x16x32_bf16 v[38:41], v[142:145], v[182:185], v[38:41]
	v_mfma_f32_16x16x32_bf16 v[26:29], v[134:137], v[174:177], v[26:29]
	v_mfma_f32_16x16x32_bf16 v[22:25], v[142:145], v[174:177], v[22:25]
	v_mfma_f32_16x16x32_bf16 v[10:13], v[134:137], v[166:169], v[10:13]
	v_mfma_f32_16x16x32_bf16 v[6:9], v[142:145], v[166:169], v[6:9]
	v_mfma_f32_16x16x32_bf16 v[58:61], v[138:141], v[194:197], v[58:61]
	v_mfma_f32_16x16x32_bf16 v[54:57], v[146:149], v[194:197], v[54:57]
	v_mfma_f32_16x16x32_bf16 v[42:45], v[138:141], v[186:189], v[42:45]
	v_mfma_f32_16x16x32_bf16 v[38:41], v[146:149], v[186:189], v[38:41]
	v_mfma_f32_16x16x32_bf16 v[26:29], v[138:141], v[178:181], v[26:29]
	v_mfma_f32_16x16x32_bf16 v[22:25], v[146:149], v[178:181], v[22:25]
	v_mfma_f32_16x16x32_bf16 v[10:13], v[138:141], v[170:173], v[10:13]
	v_mfma_f32_16x16x32_bf16 v[6:9], v[146:149], v[170:173], v[6:9]
; #define PG8_STAGE_B(bufoff, gbase) do { _Pragma("unroll") for (int _i = 0; _i < 2; ++_i) \
;         __builtin_amdgcn_global_load_lds((const unsigned*)((const char*)(gbase) + voffB[_i]), (LAS unsigned*)(lds + (bufoff) + ldsw + _i * 8192), 16, 0, 0); } while (0)
; #define PG8_STAGE_A(bufoff, V0, V1, kb) do { \
;         __builtin_amdgcn_global_load_lds((const unsigned*)((Abase + (kb)) + (V0)), (LAS unsigned*)(lds + (bufoff) + ldsw), 16, 0, 0); \
;         __builtin_amdgcn_global_load_lds((const unsigned*)((Abase + (kb)) + (V1)), (LAS unsigned*)(lds + (bufoff) + ldsw + 8192), 16, 0, 0); } while (0)
; #define PG8_LDA(dst, b, h) do { _Pragma("unroll") for (int m = 0; m < 4; ++m) _Pragma("unroll") for (int k = 0; k < 2; ++k) dst[m][k] = *(const LAS bf16x8*)(lds + PG8_SA(b, h) + aoff + m * 2048 + k * 1024); } while (0)
; #define PG8_LDB(dst, b, h) do { _Pragma("unroll") for (int n = 0; n < 2; ++n) _Pragma("unroll") for (int k = 0; k < 2; ++k) dst[n][k] = *(const LAS bf16x8*)(lds + PG8_SB(b, h) + boff + n * 2048 + k * 1024); } while (0)
; #define PG8_WAIT_V(n) asm volatile("s_waitcnt vmcnt(" #n ")" ::: "memory")
; #define PG8_BAR __builtin_amdgcn_s_barrier()
; template <class Epi, class Sched, bool ALIGN_EPI>
; __device__ __forceinline__ void gemm_phase(LAS unsigned char* lds, const Gemm g, const Sched& S, const Epi& E) {
;     ...
;             PG8_LDB(B0, 0, 0); PG8_LDB(B1, 0, 1); PG8_SCHED; PG8_LDA(At, 0, 0); PG8_STAGE_A(PG8_SA(1, 1), vc10, vc11, kb1);
;             PG8_WAIT_V(8); PG8_WAIT_L(0); PG8_BAR; PG8_MMA(0, 0, At, B0); PG8_MMA(0, 1, At, B1); PG8_BAR; PG8_SCHED;
;             PG8_LDA(At, 0, 1); PG8_STAGE_B(PG8_SB(0, 0), b2); PG8_STAGE_B(PG8_SB(0, 1), b2 + hstepB); PG8_STAGE_A(PG8_SA(0, 0), s00, s01, kb2);
;             PG8_WAIT_V(8); PG8_WAIT_L(0); PG8_BAR; if (half1) { PG8_MMA(1, 0, At, B0); PG8_MMA(1, 1, At, B1); } PG8_BAR; PG8_SCHED;
;             PG8_LDB(B0, 1, 0); PG8_LDB(B1, 1, 1); PG8_SCHED; PG8_LDA(At, 1, 0); PG8_STAGE_A(PG8_SA(0, 1), s10, s11, kb2);
;             PG8_WAIT_V(8); PG8_WAIT_L(0); PG8_BAR; PG8_MMA(0, 0, At, B0); PG8_MMA(0, 1, At, B1); PG8_BAR; PG8_SCHED;
;             PG8_LDA(At, 1, 1); PG8_STAGE_B(PG8_SB(1, 0), b3); PG8_STAGE_B(PG8_SB(1, 1), b3 + hstepB); PG8_STAGE_A(PG8_SA(1, 0), s00, s01, kb3);
;             PG8_WAIT_V(8); PG8_WAIT_L(0); PG8_BAR; if (half1) { PG8_MMA(1, 0, At, B0); PG8_MMA(1, 1, At, B1); } PG8_BAR; PG8_SCHED;
.LBB0_2914:
	v_mov_b32_e32 v5, v3
	v_lshl_add_u64 v[230:231], s[34:35], 0, v[2:3]
	v_lshl_add_u64 v[4:5], s[34:35], 0, v[4:5]
	s_barrier
	v_add_u32_e32 v2, s52, v219
	ds_read_b128 v[150:153], v2
	ds_read_b128 v[154:157], v2 offset:1024
	ds_read_b128 v[158:161], v2 offset:2048
	ds_read_b128 v[162:165], v2 offset:3072
	v_add_u32_e32 v2, s53, v219
	ds_read_b128 v[134:137], v2
	ds_read_b128 v[138:141], v2 offset:1024
	ds_read_b128 v[142:145], v2 offset:2048
	ds_read_b128 v[146:149], v2 offset:3072
	s_mov_b32 m0, s43
	s_waitcnt lgkmcnt(0)
	ds_read_b128 v[166:169], v220 offset:32768
	ds_read_b128 v[170:173], v220 offset:33792
	ds_read_b128 v[174:177], v220 offset:34816
	ds_read_b128 v[178:181], v220 offset:35840
	ds_read_b128 v[182:185], v220 offset:36864
	ds_read_b128 v[186:189], v220 offset:37888
	ds_read_b128 v[190:193], v220 offset:38912
	ds_read_b128 v[194:197], v220 offset:39936
	global_load_lds_dwordx4 v227, s[34:35]
	s_mov_b32 m0, s44
	s_nop 0
	global_load_lds_dwordx4 v228, s[34:35]
	s_waitcnt vmcnt(8)
	s_waitcnt lgkmcnt(0)
	s_barrier
	s_waitcnt lgkmcnt(0)
	v_mfma_f32_16x16x32_bf16 v[130:133], v[150:153], v[166:169], v[130:133]
	v_mfma_f32_16x16x32_bf16 v[126:129], v[158:161], v[166:169], v[126:129]
	v_mfma_f32_16x16x32_bf16 v[114:117], v[150:153], v[174:177], v[114:117]
	v_mfma_f32_16x16x32_bf16 v[110:113], v[158:161], v[174:177], v[110:113]
	v_mfma_f32_16x16x32_bf16 v[98:101], v[150:153], v[182:185], v[98:101]
	v_mfma_f32_16x16x32_bf16 v[94:97], v[158:161], v[182:185], v[94:97]
	v_mfma_f32_16x16x32_bf16 v[82:85], v[150:153], v[190:193], v[82:85]
	v_mfma_f32_16x16x32_bf16 v[78:81], v[158:161], v[190:193], v[78:81]
	v_mfma_f32_16x16x32_bf16 v[130:133], v[154:157], v[170:173], v[130:133]
	v_mfma_f32_16x16x32_bf16 v[126:129], v[162:165], v[170:173], v[126:129]
	v_mfma_f32_16x16x32_bf16 v[114:117], v[154:157], v[178:181], v[114:117]
	v_mfma_f32_16x16x32_bf16 v[110:113], v[162:165], v[178:181], v[110:113]
	v_mfma_f32_16x16x32_bf16 v[98:101], v[154:157], v[186:189], v[98:101]
	v_mfma_f32_16x16x32_bf16 v[94:97], v[162:165], v[186:189], v[94:97]
	v_mfma_f32_16x16x32_bf16 v[82:85], v[154:157], v[194:197], v[82:85]
	v_mfma_f32_16x16x32_bf16 v[78:81], v[162:165], v[194:197], v[78:81]
	v_mfma_f32_16x16x32_bf16 v[122:125], v[134:137], v[166:169], v[122:125]
	v_mfma_f32_16x16x32_bf16 v[118:121], v[142:145], v[166:169], v[118:121]
	v_mfma_f32_16x16x32_bf16 v[106:109], v[134:137], v[174:177], v[106:109]
	v_mfma_f32_16x16x32_bf16 v[102:105], v[142:145], v[174:177], v[102:105]
	v_mfma_f32_16x16x32_bf16 v[90:93], v[134:137], v[182:185], v[90:93]
	v_mfma_f32_16x16x32_bf16 v[86:89], v[142:145], v[182:185], v[86:89]
	v_mfma_f32_16x16x32_bf16 v[74:77], v[134:137], v[190:193], v[74:77]
	v_mfma_f32_16x16x32_bf16 v[70:73], v[142:145], v[190:193], v[70:73]
	v_mfma_f32_16x16x32_bf16 v[122:125], v[138:141], v[170:173], v[122:125]
	v_mfma_f32_16x16x32_bf16 v[118:121], v[146:149], v[170:173], v[118:121]
	v_mfma_f32_16x16x32_bf16 v[106:109], v[138:141], v[178:181], v[106:109]
	v_mfma_f32_16x16x32_bf16 v[102:105], v[146:149], v[178:181], v[102:105]
	v_mfma_f32_16x16x32_bf16 v[90:93], v[138:141], v[186:189], v[90:93]
	v_mfma_f32_16x16x32_bf16 v[86:89], v[146:149], v[186:189], v[86:89]
	v_mfma_f32_16x16x32_bf16 v[74:77], v[138:141], v[194:197], v[74:77]
	v_mfma_f32_16x16x32_bf16 v[70:73], v[146:149], v[194:197], v[70:73]
	s_barrier
	s_add_i32 s3, s52, s40
	v_lshl_add_u64 v[212:213], v[212:213], 0, s[6:7]
	s_mov_b32 m0, s3
	ds_read_b128 v[190:193], v220 offset:49152
	ds_read_b128 v[194:197], v220 offset:50176
	ds_read_b128 v[182:185], v220 offset:51200
	ds_read_b128 v[186:189], v220 offset:52224
	ds_read_b128 v[174:177], v220 offset:53248
	ds_read_b128 v[178:181], v220 offset:54272
	ds_read_b128 v[166:169], v220 offset:55296
	ds_read_b128 v[170:173], v220 offset:56320
	global_load_lds_dwordx4 v[212:213], off
	s_add_i32 m0, s3, 0x2000
	s_add_u32 s30, s30, 0x10080
	v_lshl_add_u64 v[212:213], v[214:215], 0, s[6:7]
	s_addc_u32 s31, s31, 0
	s_add_i32 s3, s53, s40
	global_load_lds_dwordx4 v[212:213], off
	v_lshl_add_u64 v[212:213], s[30:31], 0, v[198:199]
	s_mov_b32 m0, s3
	v_lshl_add_u64 v[4:5], v[4:5], 0, s[6:7]
	global_load_lds_dwordx4 v[212:213], off
	v_lshl_add_u64 v[212:213], s[30:31], 0, v[200:201]
	s_add_i32 m0, s3, 0x2000
	s_and_b64 vcc, exec, s[4:5]
	global_load_lds_dwordx4 v[212:213], off
	v_lshl_add_u64 v[212:213], v[230:231], 0, s[6:7]
	s_mov_b32 m0, s45
	s_nop 0
	global_load_lds_dwordx4 v[212:213], off
	s_mov_b32 m0, s46
	s_nop 0
	global_load_lds_dwordx4 v[4:5], off
	s_waitcnt vmcnt(8)
	s_waitcnt lgkmcnt(0)
	s_barrier
	s_cbranch_vccnz .LBB0_2908
	s_waitcnt lgkmcnt(0)
	v_mfma_f32_16x16x32_bf16 v[66:69], v[150:153], v[190:193], v[66:69]
	v_mfma_f32_16x16x32_bf16 v[62:65], v[158:161], v[190:193], v[62:65]
	v_mfma_f32_16x16x32_bf16 v[50:53], v[150:153], v[182:185], v[50:53]
	v_mfma_f32_16x16x32_bf16 v[46:49], v[158:161], v[182:185], v[46:49]
	v_mfma_f32_16x16x32_bf16 v[34:37], v[150:153], v[174:177], v[34:37]
	v_mfma_f32_16x16x32_bf16 v[30:33], v[158:161], v[174:177], v[30:33]
	v_mfma_f32_16x16x32_bf16 v[18:21], v[150:153], v[166:169], v[18:21]
	v_mfma_f32_16x16x32_bf16 v[14:17], v[158:161], v[166:169], v[14:17]
	v_mfma_f32_16x16x32_bf16 v[66:69], v[154:157], v[194:197], v[66:69]
	v_mfma_f32_16x16x32_bf16 v[62:65], v[162:165], v[194:197], v[62:65]
	v_mfma_f32_16x16x32_bf16 v[50:53], v[154:157], v[186:189], v[50:53]
	v_mfma_f32_16x16x32_bf16 v[46:49], v[162:165], v[186:189], v[46:49]
	v_mfma_f32_16x16x32_bf16 v[34:37], v[154:157], v[178:181], v[34:37]
	v_mfma_f32_16x16x32_bf16 v[30:33], v[162:165], v[178:181], v[30:33]
	v_mfma_f32_16x16x32_bf16 v[18:21], v[154:157], v[170:173], v[18:21]
	v_mfma_f32_16x16x32_bf16 v[14:17], v[162:165], v[170:173], v[14:17]
	v_mfma_f32_16x16x32_bf16 v[58:61], v[134:137], v[190:193], v[58:61]
	v_mfma_f32_16x16x32_bf16 v[54:57], v[142:145], v[190:193], v[54:57]
	v_mfma_f32_16x16x32_bf16 v[42:45], v[134:137], v[182:185], v[42:45]
	v_mfma_f32_16x16x32_bf16 v[38:41], v[142:145], v[182:185], v[38:41]
	v_mfma_f32_16x16x32_bf16 v[26:29], v[134:137], v[174:177], v[26:29]
	v_mfma_f32_16x16x32_bf16 v[22:25], v[142:145], v[174:177], v[22:25]
	v_mfma_f32_16x16x32_bf16 v[10:13], v[134:137], v[166:169], v[10:13]
	v_mfma_f32_16x16x32_bf16 v[4:7], v[142:145], v[166:169], v[6:9]
	v_mfma_f32_16x16x32_bf16 v[58:61], v[138:141], v[194:197], v[58:61]
	v_mfma_f32_16x16x32_bf16 v[54:57], v[146:149], v[194:197], v[54:57]
	v_mfma_f32_16x16x32_bf16 v[42:45], v[138:141], v[186:189], v[42:45]
	v_mfma_f32_16x16x32_bf16 v[38:41], v[146:149], v[186:189], v[38:41]
	v_mfma_f32_16x16x32_bf16 v[26:29], v[138:141], v[178:181], v[26:29]
	v_mfma_f32_16x16x32_bf16 v[22:25], v[146:149], v[178:181], v[22:25]
	v_mfma_f32_16x16x32_bf16 v[10:13], v[138:141], v[170:173], v[10:13]
	v_mfma_f32_16x16x32_bf16 v[6:9], v[146:149], v[170:173], v[4:7]
	s_branch .LBB0_2908

; #define PG8_STAGE_B(bufoff, gbase) do { _Pragma("unroll") for (int _i = 0; _i < 2; ++_i) \
;         __builtin_amdgcn_global_load_lds((const unsigned*)((const char*)(gbase) + voffB[_i]), (LAS unsigned*)(lds + (bufoff) + ldsw + _i * 8192), 16, 0, 0); } while (0)
; #define PG8_STAGE_A(bufoff, V0, V1, kb) do { \
;         __builtin_amdgcn_global_load_lds((const unsigned*)((Abase + (kb)) + (V0)), (LAS unsigned*)(lds + (bufoff) + ldsw), 16, 0, 0); \
;         __builtin_amdgcn_global_load_lds((const unsigned*)((Abase + (kb)) + (V1)), (LAS unsigned*)(lds + (bufoff) + ldsw + 8192), 16, 0, 0); } while (0)
; #define PG8_LDA(dst, b, h) do { _Pragma("unroll") for (int m = 0; m < 4; ++m) _Pragma("unroll") for (int k = 0; k < 2; ++k) dst[m][k] = *(const LAS bf16x8*)(lds + PG8_SA(b, h) + aoff + m * 2048 + k * 1024); } while (0)
; #define PG8_LDB(dst, b, h) do { _Pragma("unroll") for (int n = 0; n < 2; ++n) _Pragma("unroll") for (int k = 0; k < 2; ++k) dst[n][k] = *(const LAS bf16x8*)(lds + PG8_SB(b, h) + boff + n * 2048 + k * 1024); } while (0)
; #define PG8_WAIT_V(n) asm volatile("s_waitcnt vmcnt(" #n ")" ::: "memory")
; #define PG8_BAR __builtin_amdgcn_s_barrier()
; template <class Epi, class Sched, bool ALIGN_EPI>
; __device__ __forceinline__ void gemm_phase(LAS unsigned char* lds, const Gemm g, const Sched& S, const Epi& E) {
;     ...
;             PG8_LDB(B0, 0, 0); PG8_LDB(B1, 0, 1); PG8_SCHED; PG8_LDA(At, 0, 0); PG8_STAGE_A(PG8_SA(1, 1), vc10, vc11, kb1);
;             PG8_WAIT_V(8); PG8_WAIT_L(0); PG8_BAR; PG8_MMA(0, 0, At, B0); PG8_MMA(0, 1, At, B1); PG8_BAR; PG8_SCHED;
;             PG8_LDA(At, 0, 1); PG8_STAGE_B(PG8_SB(0, 0), b2); PG8_STAGE_B(PG8_SB(0, 1), b2 + hstepB); PG8_STAGE_A(PG8_SA(0, 0), s00, s01, kb2);
;             PG8_WAIT_V(8); PG8_WAIT_L(0); PG8_BAR; if (half1) { PG8_MMA(1, 0, At, B0); PG8_MMA(1, 1, At, B1); } PG8_BAR; PG8_SCHED;
;             PG8_LDB(B0, 1, 0); PG8_LDB(B1, 1, 1); PG8_SCHED; PG8_LDA(At, 1, 0); PG8_STAGE_A(PG8_SA(0, 1), s10, s11, kb2);
;             PG8_WAIT_V(8); PG8_WAIT_L(0); PG8_BAR; PG8_MMA(0, 0, At, B0); PG8_MMA(0, 1, At, B1); PG8_BAR; PG8_SCHED;
;             PG8_LDA(At, 1, 1); PG8_STAGE_B(PG8_SB(1, 0), b3); PG8_STAGE_B(PG8_SB(1, 1), b3 + hstepB); PG8_STAGE_A(PG8_SA(1, 0), s00, s01, kb3);
;             PG8_WAIT_V(8); PG8_WAIT_L(0); PG8_BAR; if (half1) { PG8_MMA(1, 0, At, B0); PG8_MMA(1, 1, At, B1); } PG8_BAR; PG8_SCHED;
.LBB0_3003:
	v_add_u32_e32 v5, s41, v221
	ds_read_b128 v[150:153], v5
	ds_read_b128 v[154:157], v5 offset:1024
	ds_read_b128 v[158:161], v5 offset:2048
	ds_read_b128 v[162:165], v5 offset:3072
	v_add_u32_e32 v5, s42, v221
	ds_read_b128 v[134:137], v5
	ds_read_b128 v[138:141], v5 offset:1024
	ds_read_b128 v[142:145], v5 offset:2048
	ds_read_b128 v[146:149], v5 offset:3072
	v_lshl_add_u64 v[230:231], v[228:229], 0, s[4:5]
	s_add_i32 m0, s28, 0xc000
	s_waitcnt lgkmcnt(0)
	ds_read_b128 v[166:169], v234
	ds_read_b128 v[170:173], v234 offset:1024
	ds_read_b128 v[174:177], v234 offset:2048
	ds_read_b128 v[178:181], v234 offset:3072
	ds_read_b128 v[182:185], v234 offset:4096
	ds_read_b128 v[186:189], v234 offset:5120
	ds_read_b128 v[190:193], v234 offset:6144
	ds_read_b128 v[194:197], v234 offset:7168
	global_load_lds_dwordx4 v[230:231], off
	v_lshl_add_u64 v[230:231], v[226:227], 0, s[4:5]
	s_add_i32 m0, s28, 0xe000
	s_nop 0
	global_load_lds_dwordx4 v[230:231], off
	s_waitcnt vmcnt(8)
	s_waitcnt lgkmcnt(0)
	s_barrier
	s_waitcnt lgkmcnt(0)
	v_mfma_f32_16x16x32_bf16 v[130:133], v[150:153], v[166:169], v[130:133]
	v_mfma_f32_16x16x32_bf16 v[126:129], v[158:161], v[166:169], v[126:129]
	v_mfma_f32_16x16x32_bf16 v[114:117], v[150:153], v[174:177], v[114:117]
	v_mfma_f32_16x16x32_bf16 v[110:113], v[158:161], v[174:177], v[110:113]
	v_mfma_f32_16x16x32_bf16 v[98:101], v[150:153], v[182:185], v[98:101]
	v_mfma_f32_16x16x32_bf16 v[94:97], v[158:161], v[182:185], v[94:97]
	v_mfma_f32_16x16x32_bf16 v[82:85], v[150:153], v[190:193], v[82:85]
	v_mfma_f32_16x16x32_bf16 v[78:81], v[158:161], v[190:193], v[78:81]
	v_mfma_f32_16x16x32_bf16 v[130:133], v[154:157], v[170:173], v[130:133]
	v_mfma_f32_16x16x32_bf16 v[126:129], v[162:165], v[170:173], v[126:129]
	v_mfma_f32_16x16x32_bf16 v[114:117], v[154:157], v[178:181], v[114:117]
	v_mfma_f32_16x16x32_bf16 v[110:113], v[162:165], v[178:181], v[110:113]
	v_mfma_f32_16x16x32_bf16 v[98:101], v[154:157], v[186:189], v[98:101]
	v_mfma_f32_16x16x32_bf16 v[94:97], v[162:165], v[186:189], v[94:97]
	v_mfma_f32_16x16x32_bf16 v[82:85], v[154:157], v[194:197], v[82:85]
	v_mfma_f32_16x16x32_bf16 v[78:81], v[162:165], v[194:197], v[78:81]
	v_mfma_f32_16x16x32_bf16 v[122:125], v[134:137], v[166:169], v[122:125]
	v_mfma_f32_16x16x32_bf16 v[118:121], v[142:145], v[166:169], v[118:121]
	v_mfma_f32_16x16x32_bf16 v[106:109], v[134:137], v[174:177], v[106:109]
	v_mfma_f32_16x16x32_bf16 v[102:105], v[142:145], v[174:177], v[102:105]
	v_mfma_f32_16x16x32_bf16 v[90:93], v[134:137], v[182:185], v[90:93]
	v_mfma_f32_16x16x32_bf16 v[86:89], v[142:145], v[182:185], v[86:89]
	v_mfma_f32_16x16x32_bf16 v[74:77], v[134:137], v[190:193], v[74:77]
	v_mfma_f32_16x16x32_bf16 v[70:73], v[142:145], v[190:193], v[70:73]
	v_mfma_f32_16x16x32_bf16 v[122:125], v[138:141], v[170:173], v[122:125]
	v_mfma_f32_16x16x32_bf16 v[118:121], v[146:149], v[170:173], v[118:121]
	v_mfma_f32_16x16x32_bf16 v[106:109], v[138:141], v[178:181], v[106:109]
	v_mfma_f32_16x16x32_bf16 v[102:105], v[146:149], v[178:181], v[102:105]
	v_mfma_f32_16x16x32_bf16 v[90:93], v[138:141], v[186:189], v[90:93]
	v_mfma_f32_16x16x32_bf16 v[86:89], v[146:149], v[186:189], v[86:89]
	v_mfma_f32_16x16x32_bf16 v[74:77], v[138:141], v[194:197], v[74:77]
	v_mfma_f32_16x16x32_bf16 v[70:73], v[146:149], v[194:197], v[70:73]
	s_barrier
	s_add_i32 s4, s41, s27
	v_lshl_add_u64 v[230:231], s[22:23], 0, v[200:201]
	s_mov_b32 m0, s4
	ds_read_b128 v[190:193], v234 offset:16384
	ds_read_b128 v[194:197], v234 offset:17408
	ds_read_b128 v[182:185], v234 offset:18432
	ds_read_b128 v[186:189], v234 offset:19456
	ds_read_b128 v[174:177], v234 offset:20480
	ds_read_b128 v[178:181], v234 offset:21504
	ds_read_b128 v[166:169], v234 offset:22528
	ds_read_b128 v[170:173], v234 offset:23552
	global_load_lds_dwordx4 v[230:231], off
	s_add_i32 m0, s4, 0x2000
	s_add_u32 s4, s22, 0x18000
	v_lshl_add_u64 v[232:233], s[22:23], 0, v[204:205]
	s_addc_u32 s5, s23, 0
	s_add_i32 s25, s42, s27
	global_load_lds_dwordx4 v[232:233], off
	v_lshl_add_u64 v[236:237], s[4:5], 0, v[200:201]
	s_mov_b32 m0, s25
	v_cndmask_b32_e64 v5, 0, 1, s[18:19]
	global_load_lds_dwordx4 v[236:237], off
	v_lshl_add_u64 v[236:237], s[4:5], 0, v[204:205]
	s_add_i32 m0, s25, 0x2000
	v_readlane_b32 s4, v253, 58
	v_readlane_b32 s5, v253, 59
	s_add_u32 s24, s4, s24
	global_load_lds_dwordx4 v[236:237], off
	s_addc_u32 s25, s5, 0
	s_mov_b32 m0, s28
	v_cmp_ne_u32_e64 s[4:5], 1, v5
	global_load_lds_dwordx4 v2, s[24:25]
	s_mov_b32 m0, s30
	s_andn2_b64 vcc, exec, s[18:19]
	global_load_lds_dwordx4 v4, s[24:25]
	s_waitcnt vmcnt(8)
	s_waitcnt lgkmcnt(0)
	s_barrier
	s_cbranch_vccnz .LBB0_3005
	s_waitcnt lgkmcnt(0)
	v_mfma_f32_16x16x32_bf16 v[66:69], v[150:153], v[190:193], v[66:69]
	v_mfma_f32_16x16x32_bf16 v[62:65], v[158:161], v[190:193], v[62:65]
	v_mfma_f32_16x16x32_bf16 v[50:53], v[150:153], v[182:185], v[50:53]
	v_mfma_f32_16x16x32_bf16 v[46:49], v[158:161], v[182:185], v[46:49]
	v_mfma_f32_16x16x32_bf16 v[34:37], v[150:153], v[174:177], v[34:37]
	v_mfma_f32_16x16x32_bf16 v[30:33], v[158:161], v[174:177], v[30:33]
	v_mfma_f32_16x16x32_bf16 v[18:21], v[150:153], v[166:169], v[18:21]
	v_mfma_f32_16x16x32_bf16 v[14:17], v[158:161], v[166:169], v[14:17]
	v_mfma_f32_16x16x32_bf16 v[66:69], v[154:157], v[194:197], v[66:69]
	v_mfma_f32_16x16x32_bf16 v[62:65], v[162:165], v[194:197], v[62:65]
	v_mfma_f32_16x16x32_bf16 v[50:53], v[154:157], v[186:189], v[50:53]
	v_mfma_f32_16x16x32_bf16 v[46:49], v[162:165], v[186:189], v[46:49]
	v_mfma_f32_16x16x32_bf16 v[34:37], v[154:157], v[178:181], v[34:37]
	v_mfma_f32_16x16x32_bf16 v[30:33], v[162:165], v[178:181], v[30:33]
	v_mfma_f32_16x16x32_bf16 v[18:21], v[154:157], v[170:173], v[18:21]
	v_mfma_f32_16x16x32_bf16 v[14:17], v[162:165], v[170:173], v[14:17]
	v_mfma_f32_16x16x32_bf16 v[58:61], v[134:137], v[190:193], v[58:61]
	v_mfma_f32_16x16x32_bf16 v[54:57], v[142:145], v[190:193], v[54:57]
	v_mfma_f32_16x16x32_bf16 v[42:45], v[134:137], v[182:185], v[42:45]
	v_mfma_f32_16x16x32_bf16 v[38:41], v[142:145], v[182:185], v[38:41]
	v_mfma_f32_16x16x32_bf16 v[26:29], v[134:137], v[174:177], v[26:29]
	v_mfma_f32_16x16x32_bf16 v[22:25], v[142:145], v[174:177], v[22:25]
	v_mfma_f32_16x16x32_bf16 v[10:13], v[134:137], v[166:169], v[10:13]
	v_mfma_f32_16x16x32_bf16 v[6:9], v[142:145], v[166:169], v[6:9]
	v_mfma_f32_16x16x32_bf16 v[58:61], v[138:141], v[194:197], v[58:61]
	v_mfma_f32_16x16x32_bf16 v[54:57], v[146:149], v[194:197], v[54:57]
	v_mfma_f32_16x16x32_bf16 v[42:45], v[138:141], v[186:189], v[42:45]
	v_mfma_f32_16x16x32_bf16 v[38:41], v[146:149], v[186:189], v[38:41]
	v_mfma_f32_16x16x32_bf16 v[26:29], v[138:141], v[178:181], v[26:29]
	v_mfma_f32_16x16x32_bf16 v[22:25], v[146:149], v[178:181], v[22:25]
	v_mfma_f32_16x16x32_bf16 v[10:13], v[138:141], v[170:173], v[10:13]
	v_mfma_f32_16x16x32_bf16 v[6:9], v[146:149], v[170:173], v[6:9]
; #define PG8_STAGE_B(bufoff, gbase) do { _Pragma("unroll") for (int _i = 0; _i < 2; ++_i) \
;         __builtin_amdgcn_global_load_lds((const unsigned*)((const char*)(gbase) + voffB[_i]), (LAS unsigned*)(lds + (bufoff) + ldsw + _i * 8192), 16, 0, 0); } while (0)
; #define PG8_STAGE_A(bufoff, V0, V1, kb) do { \
;         __builtin_amdgcn_global_load_lds((const unsigned*)((Abase + (kb)) + (V0)), (LAS unsigned*)(lds + (bufoff) + ldsw), 16, 0, 0); \
;         __builtin_amdgcn_global_load_lds((const unsigned*)((Abase + (kb)) + (V1)), (LAS unsigned*)(lds + (bufoff) + ldsw + 8192), 16, 0, 0); } while (0)
; #define PG8_LDA(dst, b, h) do { _Pragma("unroll") for (int m = 0; m < 4; ++m) _Pragma("unroll") for (int k = 0; k < 2; ++k) dst[m][k] = *(const LAS bf16x8*)(lds + PG8_SA(b, h) + aoff + m * 2048 + k * 1024); } while (0)
; #define PG8_LDB(dst, b, h) do { _Pragma("unroll") for (int n = 0; n < 2; ++n) _Pragma("unroll") for (int k = 0; k < 2; ++k) dst[n][k] = *(const LAS bf16x8*)(lds + PG8_SB(b, h) + boff + n * 2048 + k * 1024); } while (0)
; #define PG8_WAIT_V(n) asm volatile("s_waitcnt vmcnt(" #n ")" ::: "memory")
; #define PG8_BAR __builtin_amdgcn_s_barrier()
; template <class Epi, class Sched, bool ALIGN_EPI>
; __device__ __forceinline__ void gemm_phase(LAS unsigned char* lds, const Gemm g, const Sched& S, const Epi& E) {
;     ...
;             PG8_LDB(B0, 0, 0); PG8_LDB(B1, 0, 1); PG8_SCHED; PG8_LDA(At, 0, 0); PG8_STAGE_A(PG8_SA(1, 1), vc10, vc11, kb1);
;             PG8_WAIT_V(8); PG8_WAIT_L(0); PG8_BAR; PG8_MMA(0, 0, At, B0); PG8_MMA(0, 1, At, B1); PG8_BAR; PG8_SCHED;
;             PG8_LDA(At, 0, 1); PG8_STAGE_B(PG8_SB(0, 0), b2); PG8_STAGE_B(PG8_SB(0, 1), b2 + hstepB); PG8_STAGE_A(PG8_SA(0, 0), s00, s01, kb2);
;             PG8_WAIT_V(8); PG8_WAIT_L(0); PG8_BAR; if (half1) { PG8_MMA(1, 0, At, B0); PG8_MMA(1, 1, At, B1); } PG8_BAR; PG8_SCHED;
;             PG8_LDB(B0, 1, 0); PG8_LDB(B1, 1, 1); PG8_SCHED; PG8_LDA(At, 1, 0); PG8_STAGE_A(PG8_SA(0, 1), s10, s11, kb2);
;             PG8_WAIT_V(8); PG8_WAIT_L(0); PG8_BAR; PG8_MMA(0, 0, At, B0); PG8_MMA(0, 1, At, B1); PG8_BAR; PG8_SCHED;
;             PG8_LDA(At, 1, 1); PG8_STAGE_B(PG8_SB(1, 0), b3); PG8_STAGE_B(PG8_SB(1, 1), b3 + hstepB); PG8_STAGE_A(PG8_SA(1, 0), s00, s01, kb3);
;             PG8_WAIT_V(8); PG8_WAIT_L(0); PG8_BAR; if (half1) { PG8_MMA(1, 0, At, B0); PG8_MMA(1, 1, At, B1); } PG8_BAR; PG8_SCHED;
.LBB0_3005:
	v_mov_b32_e32 v5, v3
	v_lshl_add_u64 v[236:237], s[24:25], 0, v[2:3]
	v_lshl_add_u64 v[4:5], s[24:25], 0, v[4:5]
	s_barrier
	v_add_u32_e32 v2, s43, v221
	ds_read_b128 v[150:153], v2
	ds_read_b128 v[154:157], v2 offset:1024
	ds_read_b128 v[158:161], v2 offset:2048
	ds_read_b128 v[162:165], v2 offset:3072
	v_add_u32_e32 v2, s44, v221
	ds_read_b128 v[134:137], v2
	ds_read_b128 v[138:141], v2 offset:1024
	ds_read_b128 v[142:145], v2 offset:2048
	ds_read_b128 v[146:149], v2 offset:3072
	s_mov_b32 m0, s31
	s_waitcnt lgkmcnt(0)
	ds_read_b128 v[166:169], v234 offset:32768
	ds_read_b128 v[170:173], v234 offset:33792
	ds_read_b128 v[174:177], v234 offset:34816
	ds_read_b128 v[178:181], v234 offset:35840
	ds_read_b128 v[182:185], v234 offset:36864
	ds_read_b128 v[186:189], v234 offset:37888
	ds_read_b128 v[190:193], v234 offset:38912
	ds_read_b128 v[194:197], v234 offset:39936
	global_load_lds_dwordx4 v211, s[24:25]
	s_mov_b32 m0, s33
	s_nop 0
	global_load_lds_dwordx4 v213, s[24:25]
	s_waitcnt vmcnt(8)
	s_waitcnt lgkmcnt(0)
	s_barrier
	s_waitcnt lgkmcnt(0)
	v_mfma_f32_16x16x32_bf16 v[130:133], v[150:153], v[166:169], v[130:133]
	v_mfma_f32_16x16x32_bf16 v[126:129], v[158:161], v[166:169], v[126:129]
	v_mfma_f32_16x16x32_bf16 v[114:117], v[150:153], v[174:177], v[114:117]
	v_mfma_f32_16x16x32_bf16 v[110:113], v[158:161], v[174:177], v[110:113]
	v_mfma_f32_16x16x32_bf16 v[98:101], v[150:153], v[182:185], v[98:101]
	v_mfma_f32_16x16x32_bf16 v[94:97], v[158:161], v[182:185], v[94:97]
	v_mfma_f32_16x16x32_bf16 v[82:85], v[150:153], v[190:193], v[82:85]
	v_mfma_f32_16x16x32_bf16 v[78:81], v[158:161], v[190:193], v[78:81]
	v_mfma_f32_16x16x32_bf16 v[130:133], v[154:157], v[170:173], v[130:133]
	v_mfma_f32_16x16x32_bf16 v[126:129], v[162:165], v[170:173], v[126:129]
	v_mfma_f32_16x16x32_bf16 v[114:117], v[154:157], v[178:181], v[114:117]
	v_mfma_f32_16x16x32_bf16 v[110:113], v[162:165], v[178:181], v[110:113]
	v_mfma_f32_16x16x32_bf16 v[98:101], v[154:157], v[186:189], v[98:101]
	v_mfma_f32_16x16x32_bf16 v[94:97], v[162:165], v[186:189], v[94:97]
	v_mfma_f32_16x16x32_bf16 v[82:85], v[154:157], v[194:197], v[82:85]
	v_mfma_f32_16x16x32_bf16 v[78:81], v[162:165], v[194:197], v[78:81]
	v_mfma_f32_16x16x32_bf16 v[122:125], v[134:137], v[166:169], v[122:125]
	v_mfma_f32_16x16x32_bf16 v[118:121], v[142:145], v[166:169], v[118:121]
	v_mfma_f32_16x16x32_bf16 v[106:109], v[134:137], v[174:177], v[106:109]
	v_mfma_f32_16x16x32_bf16 v[102:105], v[142:145], v[174:177], v[102:105]
	v_mfma_f32_16x16x32_bf16 v[90:93], v[134:137], v[182:185], v[90:93]
	v_mfma_f32_16x16x32_bf16 v[86:89], v[142:145], v[182:185], v[86:89]
	v_mfma_f32_16x16x32_bf16 v[74:77], v[134:137], v[190:193], v[74:77]
	v_mfma_f32_16x16x32_bf16 v[70:73], v[142:145], v[190:193], v[70:73]
	v_mfma_f32_16x16x32_bf16 v[122:125], v[138:141], v[170:173], v[122:125]
	v_mfma_f32_16x16x32_bf16 v[118:121], v[146:149], v[170:173], v[118:121]
	v_mfma_f32_16x16x32_bf16 v[106:109], v[138:141], v[178:181], v[106:109]
	v_mfma_f32_16x16x32_bf16 v[102:105], v[146:149], v[178:181], v[102:105]
	v_mfma_f32_16x16x32_bf16 v[90:93], v[138:141], v[186:189], v[90:93]
	v_mfma_f32_16x16x32_bf16 v[86:89], v[146:149], v[186:189], v[86:89]
	v_mfma_f32_16x16x32_bf16 v[74:77], v[138:141], v[194:197], v[74:77]
	v_mfma_f32_16x16x32_bf16 v[70:73], v[146:149], v[194:197], v[70:73]
	s_barrier
	s_add_i32 s24, s43, s27
	v_lshl_add_u64 v[230:231], v[230:231], 0, s[2:3]
	s_mov_b32 m0, s24
	ds_read_b128 v[190:193], v234 offset:49152
	ds_read_b128 v[194:197], v234 offset:50176
	ds_read_b128 v[182:185], v234 offset:51200
	ds_read_b128 v[186:189], v234 offset:52224
	ds_read_b128 v[174:177], v234 offset:53248
	ds_read_b128 v[178:181], v234 offset:54272
	ds_read_b128 v[166:169], v234 offset:55296
	ds_read_b128 v[170:173], v234 offset:56320
	global_load_lds_dwordx4 v[230:231], off
	s_add_i32 m0, s24, 0x2000
	s_add_u32 s22, s22, 0x18080
	v_lshl_add_u64 v[230:231], v[232:233], 0, s[2:3]
	s_addc_u32 s23, s23, 0
	s_add_i32 s24, s44, s27
	global_load_lds_dwordx4 v[230:231], off
	v_lshl_add_u64 v[230:231], s[22:23], 0, v[200:201]
	s_mov_b32 m0, s24
	v_lshl_add_u64 v[4:5], v[4:5], 0, s[2:3]
	global_load_lds_dwordx4 v[230:231], off
	v_lshl_add_u64 v[230:231], s[22:23], 0, v[204:205]
	s_add_i32 m0, s24, 0x2000
	s_and_b64 vcc, exec, s[4:5]
	global_load_lds_dwordx4 v[230:231], off
	v_lshl_add_u64 v[230:231], v[236:237], 0, s[2:3]
	s_mov_b32 m0, s34
	s_nop 0
	global_load_lds_dwordx4 v[230:231], off
	s_mov_b32 m0, s35
	s_nop 0
	global_load_lds_dwordx4 v[4:5], off
	s_waitcnt vmcnt(8)
	s_waitcnt lgkmcnt(0)
	s_barrier
	s_cbranch_vccnz .LBB0_3007
	s_waitcnt lgkmcnt(0)
	v_mfma_f32_16x16x32_bf16 v[66:69], v[150:153], v[190:193], v[66:69]
	v_mfma_f32_16x16x32_bf16 v[62:65], v[158:161], v[190:193], v[62:65]
	v_mfma_f32_16x16x32_bf16 v[50:53], v[150:153], v[182:185], v[50:53]
	v_mfma_f32_16x16x32_bf16 v[46:49], v[158:161], v[182:185], v[46:49]
	v_mfma_f32_16x16x32_bf16 v[34:37], v[150:153], v[174:177], v[34:37]
	v_mfma_f32_16x16x32_bf16 v[30:33], v[158:161], v[174:177], v[30:33]
	v_mfma_f32_16x16x32_bf16 v[18:21], v[150:153], v[166:169], v[18:21]
	v_mfma_f32_16x16x32_bf16 v[14:17], v[158:161], v[166:169], v[14:17]
	v_mfma_f32_16x16x32_bf16 v[66:69], v[154:157], v[194:197], v[66:69]
	v_mfma_f32_16x16x32_bf16 v[62:65], v[162:165], v[194:197], v[62:65]
	v_mfma_f32_16x16x32_bf16 v[50:53], v[154:157], v[186:189], v[50:53]
	v_mfma_f32_16x16x32_bf16 v[46:49], v[162:165], v[186:189], v[46:49]
	v_mfma_f32_16x16x32_bf16 v[34:37], v[154:157], v[178:181], v[34:37]
	v_mfma_f32_16x16x32_bf16 v[30:33], v[162:165], v[178:181], v[30:33]
	v_mfma_f32_16x16x32_bf16 v[18:21], v[154:157], v[170:173], v[18:21]
	v_mfma_f32_16x16x32_bf16 v[14:17], v[162:165], v[170:173], v[14:17]
	v_mfma_f32_16x16x32_bf16 v[58:61], v[134:137], v[190:193], v[58:61]
	v_mfma_f32_16x16x32_bf16 v[54:57], v[142:145], v[190:193], v[54:57]
	v_mfma_f32_16x16x32_bf16 v[42:45], v[134:137], v[182:185], v[42:45]
	v_mfma_f32_16x16x32_bf16 v[38:41], v[142:145], v[182:185], v[38:41]
	v_mfma_f32_16x16x32_bf16 v[26:29], v[134:137], v[174:177], v[26:29]
	v_mfma_f32_16x16x32_bf16 v[22:25], v[142:145], v[174:177], v[22:25]
	v_mfma_f32_16x16x32_bf16 v[10:13], v[134:137], v[166:169], v[10:13]
	v_mfma_f32_16x16x32_bf16 v[4:7], v[142:145], v[166:169], v[6:9]
	v_mfma_f32_16x16x32_bf16 v[58:61], v[138:141], v[194:197], v[58:61]
	v_mfma_f32_16x16x32_bf16 v[54:57], v[146:149], v[194:197], v[54:57]
	v_mfma_f32_16x16x32_bf16 v[42:45], v[138:141], v[186:189], v[42:45]
	v_mfma_f32_16x16x32_bf16 v[38:41], v[146:149], v[186:189], v[38:41]
	v_mfma_f32_16x16x32_bf16 v[26:29], v[138:141], v[178:181], v[26:29]
	v_mfma_f32_16x16x32_bf16 v[22:25], v[146:149], v[178:181], v[22:25]
	v_mfma_f32_16x16x32_bf16 v[10:13], v[138:141], v[170:173], v[10:13]
	v_mfma_f32_16x16x32_bf16 v[6:9], v[146:149], v[170:173], v[4:7]

; #define PG8_STAGE_B(bufoff, gbase) do { _Pragma("unroll") for (int _i = 0; _i < 2; ++_i) \
;         __builtin_amdgcn_global_load_lds((const unsigned*)((const char*)(gbase) + voffB[_i]), (LAS unsigned*)(lds + (bufoff) + ldsw + _i * 8192), 16, 0, 0); } while (0)
; #define PG8_STAGE_A(bufoff, V0, V1, kb) do { \
;         __builtin_amdgcn_global_load_lds((const unsigned*)((Abase + (kb)) + (V0)), (LAS unsigned*)(lds + (bufoff) + ldsw), 16, 0, 0); \
;         __builtin_amdgcn_global_load_lds((const unsigned*)((Abase + (kb)) + (V1)), (LAS unsigned*)(lds + (bufoff) + ldsw + 8192), 16, 0, 0); } while (0)
; #define PG8_LDA(dst, b, h) do { _Pragma("unroll") for (int m = 0; m < 4; ++m) _Pragma("unroll") for (int k = 0; k < 2; ++k) dst[m][k] = *(const LAS bf16x8*)(lds + PG8_SA(b, h) + aoff + m * 2048 + k * 1024); } while (0)
; #define PG8_LDB(dst, b, h) do { _Pragma("unroll") for (int n = 0; n < 2; ++n) _Pragma("unroll") for (int k = 0; k < 2; ++k) dst[n][k] = *(const LAS bf16x8*)(lds + PG8_SB(b, h) + boff + n * 2048 + k * 1024); } while (0)
; #define PG8_WAIT_V(n) asm volatile("s_waitcnt vmcnt(" #n ")" ::: "memory")
; #define PG8_BAR __builtin_amdgcn_s_barrier()
; template <class Epi, class Sched, bool ALIGN_EPI>
; __device__ __forceinline__ void gemm_phase(LAS unsigned char* lds, const Gemm g, const Sched& S, const Epi& E) {
;     ...
;             PG8_LDB(B0, 0, 0); PG8_LDB(B1, 0, 1); PG8_SCHED; PG8_LDA(At, 0, 0); PG8_STAGE_A(PG8_SA(1, 1), vc10, vc11, kb1);
;             PG8_WAIT_V(8); PG8_WAIT_L(0); PG8_BAR; PG8_MMA(0, 0, At, B0); PG8_MMA(0, 1, At, B1); PG8_BAR; PG8_SCHED;
;             PG8_LDA(At, 0, 1); PG8_STAGE_B(PG8_SB(0, 0), b2); PG8_STAGE_B(PG8_SB(0, 1), b2 + hstepB); PG8_STAGE_A(PG8_SA(0, 0), s00, s01, kb2);
;             PG8_WAIT_V(8); PG8_WAIT_L(0); PG8_BAR; if (half1) { PG8_MMA(1, 0, At, B0); PG8_MMA(1, 1, At, B1); } PG8_BAR; PG8_SCHED;
;             PG8_LDB(B0, 1, 0); PG8_LDB(B1, 1, 1); PG8_SCHED; PG8_LDA(At, 1, 0); PG8_STAGE_A(PG8_SA(0, 1), s10, s11, kb2);
;             PG8_WAIT_V(8); PG8_WAIT_L(0); PG8_BAR; PG8_MMA(0, 0, At, B0); PG8_MMA(0, 1, At, B1); PG8_BAR; PG8_SCHED;
;             PG8_LDA(At, 1, 1); PG8_STAGE_B(PG8_SB(1, 0), b3); PG8_STAGE_B(PG8_SB(1, 1), b3 + hstepB); PG8_STAGE_A(PG8_SA(1, 0), s00, s01, kb3);
;             PG8_WAIT_V(8); PG8_WAIT_L(0); PG8_BAR; if (half1) { PG8_MMA(1, 0, At, B0); PG8_MMA(1, 1, At, B1); } PG8_BAR; PG8_SCHED;
.LBB0_3070:
	v_add_u32_e32 v5, s49, v219
	ds_read_b128 v[150:153], v5
	ds_read_b128 v[154:157], v5 offset:1024
	ds_read_b128 v[158:161], v5 offset:2048
	ds_read_b128 v[162:165], v5 offset:3072
	v_add_u32_e32 v5, s50, v219
	ds_read_b128 v[134:137], v5
	ds_read_b128 v[138:141], v5 offset:1024
	ds_read_b128 v[142:145], v5 offset:2048
	ds_read_b128 v[146:149], v5 offset:3072
	v_lshl_add_u64 v[210:211], v[208:209], 0, s[4:5]
	s_add_i32 m0, s39, 0xc000
	s_waitcnt lgkmcnt(0)
	ds_read_b128 v[166:169], v227
	ds_read_b128 v[170:173], v227 offset:1024
	ds_read_b128 v[174:177], v227 offset:2048
	ds_read_b128 v[178:181], v227 offset:3072
	ds_read_b128 v[182:185], v227 offset:4096
	ds_read_b128 v[186:189], v227 offset:5120
	ds_read_b128 v[190:193], v227 offset:6144
	ds_read_b128 v[194:197], v227 offset:7168
	global_load_lds_dwordx4 v[210:211], off
	v_lshl_add_u64 v[210:211], v[206:207], 0, s[4:5]
	s_add_i32 m0, s39, 0xe000
	s_nop 0
	global_load_lds_dwordx4 v[210:211], off
	s_waitcnt vmcnt(8)
	s_waitcnt lgkmcnt(0)
	s_barrier
	s_waitcnt lgkmcnt(0)
	v_mfma_f32_16x16x32_bf16 v[130:133], v[150:153], v[166:169], v[130:133]
	v_mfma_f32_16x16x32_bf16 v[126:129], v[158:161], v[166:169], v[126:129]
	v_mfma_f32_16x16x32_bf16 v[114:117], v[150:153], v[174:177], v[114:117]
	v_mfma_f32_16x16x32_bf16 v[110:113], v[158:161], v[174:177], v[110:113]
	v_mfma_f32_16x16x32_bf16 v[98:101], v[150:153], v[182:185], v[98:101]
	v_mfma_f32_16x16x32_bf16 v[94:97], v[158:161], v[182:185], v[94:97]
	v_mfma_f32_16x16x32_bf16 v[82:85], v[150:153], v[190:193], v[82:85]
	v_mfma_f32_16x16x32_bf16 v[78:81], v[158:161], v[190:193], v[78:81]
	v_mfma_f32_16x16x32_bf16 v[130:133], v[154:157], v[170:173], v[130:133]
	v_mfma_f32_16x16x32_bf16 v[126:129], v[162:165], v[170:173], v[126:129]
	v_mfma_f32_16x16x32_bf16 v[114:117], v[154:157], v[178:181], v[114:117]
	v_mfma_f32_16x16x32_bf16 v[110:113], v[162:165], v[178:181], v[110:113]
	v_mfma_f32_16x16x32_bf16 v[98:101], v[154:157], v[186:189], v[98:101]
	v_mfma_f32_16x16x32_bf16 v[94:97], v[162:165], v[186:189], v[94:97]
	v_mfma_f32_16x16x32_bf16 v[82:85], v[154:157], v[194:197], v[82:85]
	v_mfma_f32_16x16x32_bf16 v[78:81], v[162:165], v[194:197], v[78:81]
	v_mfma_f32_16x16x32_bf16 v[122:125], v[134:137], v[166:169], v[122:125]
	v_mfma_f32_16x16x32_bf16 v[118:121], v[142:145], v[166:169], v[118:121]
	v_mfma_f32_16x16x32_bf16 v[106:109], v[134:137], v[174:177], v[106:109]
	v_mfma_f32_16x16x32_bf16 v[102:105], v[142:145], v[174:177], v[102:105]
	v_mfma_f32_16x16x32_bf16 v[90:93], v[134:137], v[182:185], v[90:93]
	v_mfma_f32_16x16x32_bf16 v[86:89], v[142:145], v[182:185], v[86:89]
	v_mfma_f32_16x16x32_bf16 v[74:77], v[134:137], v[190:193], v[74:77]
	v_mfma_f32_16x16x32_bf16 v[70:73], v[142:145], v[190:193], v[70:73]
	v_mfma_f32_16x16x32_bf16 v[122:125], v[138:141], v[170:173], v[122:125]
	v_mfma_f32_16x16x32_bf16 v[118:121], v[146:149], v[170:173], v[118:121]
	v_mfma_f32_16x16x32_bf16 v[106:109], v[138:141], v[178:181], v[106:109]
	v_mfma_f32_16x16x32_bf16 v[102:105], v[146:149], v[178:181], v[102:105]
	v_mfma_f32_16x16x32_bf16 v[90:93], v[138:141], v[186:189], v[90:93]
	v_mfma_f32_16x16x32_bf16 v[86:89], v[146:149], v[186:189], v[86:89]
	v_mfma_f32_16x16x32_bf16 v[74:77], v[138:141], v[194:197], v[74:77]
	v_mfma_f32_16x16x32_bf16 v[70:73], v[146:149], v[194:197], v[70:73]
	s_barrier
	s_add_i32 s4, s49, s37
	v_lshl_add_u64 v[210:211], s[30:31], 0, v[198:199]
	s_mov_b32 m0, s4
	ds_read_b128 v[190:193], v227 offset:16384
	ds_read_b128 v[194:197], v227 offset:17408
	ds_read_b128 v[182:185], v227 offset:18432
	ds_read_b128 v[186:189], v227 offset:19456
	ds_read_b128 v[174:177], v227 offset:20480
	ds_read_b128 v[178:181], v227 offset:21504
	ds_read_b128 v[166:169], v227 offset:22528
	ds_read_b128 v[170:173], v227 offset:23552
	global_load_lds_dwordx4 v[210:211], off
	s_add_i32 m0, s4, 0x2000
	s_add_u32 s4, s30, 0x40000
	v_lshl_add_u64 v[212:213], s[30:31], 0, v[200:201]
	s_addc_u32 s5, s31, 0
	s_add_i32 s35, s50, s37
	global_load_lds_dwordx4 v[212:213], off
	v_lshl_add_u64 v[234:235], s[4:5], 0, v[198:199]
	s_mov_b32 m0, s35
	v_cndmask_b32_e64 v5, 0, 1, s[26:27]
	global_load_lds_dwordx4 v[234:235], off
	v_lshl_add_u64 v[234:235], s[4:5], 0, v[200:201]
	s_add_i32 m0, s35, 0x2000
	v_readlane_b32 s4, v253, 52
	v_readlane_b32 s5, v253, 53
	s_add_u32 s34, s4, s34
	global_load_lds_dwordx4 v[234:235], off
	s_addc_u32 s35, s5, 0
	s_mov_b32 m0, s39
	v_cmp_ne_u32_e64 s[4:5], 1, v5
	global_load_lds_dwordx4 v2, s[34:35]
	s_mov_b32 m0, s40
	s_andn2_b64 vcc, exec, s[26:27]
	global_load_lds_dwordx4 v4, s[34:35]
	s_waitcnt vmcnt(8)
	s_waitcnt lgkmcnt(0)
	s_barrier
	s_cbranch_vccnz .LBB0_3072
	s_waitcnt lgkmcnt(0)
	v_mfma_f32_16x16x32_bf16 v[66:69], v[150:153], v[190:193], v[66:69]
	v_mfma_f32_16x16x32_bf16 v[62:65], v[158:161], v[190:193], v[62:65]
	v_mfma_f32_16x16x32_bf16 v[50:53], v[150:153], v[182:185], v[50:53]
	v_mfma_f32_16x16x32_bf16 v[46:49], v[158:161], v[182:185], v[46:49]
	v_mfma_f32_16x16x32_bf16 v[34:37], v[150:153], v[174:177], v[34:37]
	v_mfma_f32_16x16x32_bf16 v[30:33], v[158:161], v[174:177], v[30:33]
	v_mfma_f32_16x16x32_bf16 v[18:21], v[150:153], v[166:169], v[18:21]
	v_mfma_f32_16x16x32_bf16 v[14:17], v[158:161], v[166:169], v[14:17]
	v_mfma_f32_16x16x32_bf16 v[66:69], v[154:157], v[194:197], v[66:69]
	v_mfma_f32_16x16x32_bf16 v[62:65], v[162:165], v[194:197], v[62:65]
	v_mfma_f32_16x16x32_bf16 v[50:53], v[154:157], v[186:189], v[50:53]
	v_mfma_f32_16x16x32_bf16 v[46:49], v[162:165], v[186:189], v[46:49]
	v_mfma_f32_16x16x32_bf16 v[34:37], v[154:157], v[178:181], v[34:37]
	v_mfma_f32_16x16x32_bf16 v[30:33], v[162:165], v[178:181], v[30:33]
	v_mfma_f32_16x16x32_bf16 v[18:21], v[154:157], v[170:173], v[18:21]
	v_mfma_f32_16x16x32_bf16 v[14:17], v[162:165], v[170:173], v[14:17]
	v_mfma_f32_16x16x32_bf16 v[58:61], v[134:137], v[190:193], v[58:61]
	v_mfma_f32_16x16x32_bf16 v[54:57], v[142:145], v[190:193], v[54:57]
	v_mfma_f32_16x16x32_bf16 v[42:45], v[134:137], v[182:185], v[42:45]
	v_mfma_f32_16x16x32_bf16 v[38:41], v[142:145], v[182:185], v[38:41]
	v_mfma_f32_16x16x32_bf16 v[26:29], v[134:137], v[174:177], v[26:29]
	v_mfma_f32_16x16x32_bf16 v[22:25], v[142:145], v[174:177], v[22:25]
	v_mfma_f32_16x16x32_bf16 v[10:13], v[134:137], v[166:169], v[10:13]
	v_mfma_f32_16x16x32_bf16 v[6:9], v[142:145], v[166:169], v[6:9]
	v_mfma_f32_16x16x32_bf16 v[58:61], v[138:141], v[194:197], v[58:61]
	v_mfma_f32_16x16x32_bf16 v[54:57], v[146:149], v[194:197], v[54:57]
	v_mfma_f32_16x16x32_bf16 v[42:45], v[138:141], v[186:189], v[42:45]
	v_mfma_f32_16x16x32_bf16 v[38:41], v[146:149], v[186:189], v[38:41]
	v_mfma_f32_16x16x32_bf16 v[26:29], v[138:141], v[178:181], v[26:29]
	v_mfma_f32_16x16x32_bf16 v[22:25], v[146:149], v[178:181], v[22:25]
	v_mfma_f32_16x16x32_bf16 v[10:13], v[138:141], v[170:173], v[10:13]
	v_mfma_f32_16x16x32_bf16 v[6:9], v[146:149], v[170:173], v[6:9]
; #define PG8_STAGE_B(bufoff, gbase) do { _Pragma("unroll") for (int _i = 0; _i < 2; ++_i) \
;         __builtin_amdgcn_global_load_lds((const unsigned*)((const char*)(gbase) + voffB[_i]), (LAS unsigned*)(lds + (bufoff) + ldsw + _i * 8192), 16, 0, 0); } while (0)
; #define PG8_STAGE_A(bufoff, V0, V1, kb) do { \
;         __builtin_amdgcn_global_load_lds((const unsigned*)((Abase + (kb)) + (V0)), (LAS unsigned*)(lds + (bufoff) + ldsw), 16, 0, 0); \
;         __builtin_amdgcn_global_load_lds((const unsigned*)((Abase + (kb)) + (V1)), (LAS unsigned*)(lds + (bufoff) + ldsw + 8192), 16, 0, 0); } while (0)
; #define PG8_LDA(dst, b, h) do { _Pragma("unroll") for (int m = 0; m < 4; ++m) _Pragma("unroll") for (int k = 0; k < 2; ++k) dst[m][k] = *(const LAS bf16x8*)(lds + PG8_SA(b, h) + aoff + m * 2048 + k * 1024); } while (0)
; #define PG8_LDB(dst, b, h) do { _Pragma("unroll") for (int n = 0; n < 2; ++n) _Pragma("unroll") for (int k = 0; k < 2; ++k) dst[n][k] = *(const LAS bf16x8*)(lds + PG8_SB(b, h) + boff + n * 2048 + k * 1024); } while (0)
; #define PG8_WAIT_V(n) asm volatile("s_waitcnt vmcnt(" #n ")" ::: "memory")
; #define PG8_BAR __builtin_amdgcn_s_barrier()
; template <class Epi, class Sched, bool ALIGN_EPI>
; __device__ __forceinline__ void gemm_phase(LAS unsigned char* lds, const Gemm g, const Sched& S, const Epi& E) {
;     ...
;             PG8_LDB(B0, 0, 0); PG8_LDB(B1, 0, 1); PG8_SCHED; PG8_LDA(At, 0, 0); PG8_STAGE_A(PG8_SA(1, 1), vc10, vc11, kb1);
;             PG8_WAIT_V(8); PG8_WAIT_L(0); PG8_BAR; PG8_MMA(0, 0, At, B0); PG8_MMA(0, 1, At, B1); PG8_BAR; PG8_SCHED;
;             PG8_LDA(At, 0, 1); PG8_STAGE_B(PG8_SB(0, 0), b2); PG8_STAGE_B(PG8_SB(0, 1), b2 + hstepB); PG8_STAGE_A(PG8_SA(0, 0), s00, s01, kb2);
;             PG8_WAIT_V(8); PG8_WAIT_L(0); PG8_BAR; if (half1) { PG8_MMA(1, 0, At, B0); PG8_MMA(1, 1, At, B1); } PG8_BAR; PG8_SCHED;
;             PG8_LDB(B0, 1, 0); PG8_LDB(B1, 1, 1); PG8_SCHED; PG8_LDA(At, 1, 0); PG8_STAGE_A(PG8_SA(0, 1), s10, s11, kb2);
;             PG8_WAIT_V(8); PG8_WAIT_L(0); PG8_BAR; PG8_MMA(0, 0, At, B0); PG8_MMA(0, 1, At, B1); PG8_BAR; PG8_SCHED;
;             PG8_LDA(At, 1, 1); PG8_STAGE_B(PG8_SB(1, 0), b3); PG8_STAGE_B(PG8_SB(1, 1), b3 + hstepB); PG8_STAGE_A(PG8_SA(1, 0), s00, s01, kb3);
;             PG8_WAIT_V(8); PG8_WAIT_L(0); PG8_BAR; if (half1) { PG8_MMA(1, 0, At, B0); PG8_MMA(1, 1, At, B1); } PG8_BAR; PG8_SCHED;
.LBB0_3072:
	v_mov_b32_e32 v5, v3
	v_lshl_add_u64 v[234:235], s[34:35], 0, v[2:3]
	v_lshl_add_u64 v[4:5], s[34:35], 0, v[4:5]
	s_barrier
	v_add_u32_e32 v2, s51, v219
	ds_read_b128 v[150:153], v2
	ds_read_b128 v[154:157], v2 offset:1024
	ds_read_b128 v[158:161], v2 offset:2048
	ds_read_b128 v[162:165], v2 offset:3072
	v_add_u32_e32 v2, s52, v219
	ds_read_b128 v[134:137], v2
	ds_read_b128 v[138:141], v2 offset:1024
	ds_read_b128 v[142:145], v2 offset:2048
	ds_read_b128 v[146:149], v2 offset:3072
	s_mov_b32 m0, s41
	s_waitcnt lgkmcnt(0)
	ds_read_b128 v[166:169], v227 offset:32768
	ds_read_b128 v[170:173], v227 offset:33792
	ds_read_b128 v[174:177], v227 offset:34816
	ds_read_b128 v[178:181], v227 offset:35840
	ds_read_b128 v[182:185], v227 offset:36864
	ds_read_b128 v[186:189], v227 offset:37888
	ds_read_b128 v[190:193], v227 offset:38912
	ds_read_b128 v[194:197], v227 offset:39936
	global_load_lds_dwordx4 v203, s[34:35]
	s_mov_b32 m0, s42
	s_nop 0
	global_load_lds_dwordx4 v205, s[34:35]
	s_waitcnt vmcnt(8)
	s_waitcnt lgkmcnt(0)
	s_barrier
	s_waitcnt lgkmcnt(0)
	v_mfma_f32_16x16x32_bf16 v[130:133], v[150:153], v[166:169], v[130:133]
	v_mfma_f32_16x16x32_bf16 v[126:129], v[158:161], v[166:169], v[126:129]
	v_mfma_f32_16x16x32_bf16 v[114:117], v[150:153], v[174:177], v[114:117]
	v_mfma_f32_16x16x32_bf16 v[110:113], v[158:161], v[174:177], v[110:113]
	v_mfma_f32_16x16x32_bf16 v[98:101], v[150:153], v[182:185], v[98:101]
	v_mfma_f32_16x16x32_bf16 v[94:97], v[158:161], v[182:185], v[94:97]
	v_mfma_f32_16x16x32_bf16 v[82:85], v[150:153], v[190:193], v[82:85]
	v_mfma_f32_16x16x32_bf16 v[78:81], v[158:161], v[190:193], v[78:81]
	v_mfma_f32_16x16x32_bf16 v[130:133], v[154:157], v[170:173], v[130:133]
	v_mfma_f32_16x16x32_bf16 v[126:129], v[162:165], v[170:173], v[126:129]
	v_mfma_f32_16x16x32_bf16 v[114:117], v[154:157], v[178:181], v[114:117]
	v_mfma_f32_16x16x32_bf16 v[110:113], v[162:165], v[178:181], v[110:113]
	v_mfma_f32_16x16x32_bf16 v[98:101], v[154:157], v[186:189], v[98:101]
	v_mfma_f32_16x16x32_bf16 v[94:97], v[162:165], v[186:189], v[94:97]
	v_mfma_f32_16x16x32_bf16 v[82:85], v[154:157], v[194:197], v[82:85]
	v_mfma_f32_16x16x32_bf16 v[78:81], v[162:165], v[194:197], v[78:81]
	v_mfma_f32_16x16x32_bf16 v[122:125], v[134:137], v[166:169], v[122:125]
	v_mfma_f32_16x16x32_bf16 v[118:121], v[142:145], v[166:169], v[118:121]
	v_mfma_f32_16x16x32_bf16 v[106:109], v[134:137], v[174:177], v[106:109]
	v_mfma_f32_16x16x32_bf16 v[102:105], v[142:145], v[174:177], v[102:105]
	v_mfma_f32_16x16x32_bf16 v[90:93], v[134:137], v[182:185], v[90:93]
	v_mfma_f32_16x16x32_bf16 v[86:89], v[142:145], v[182:185], v[86:89]
	v_mfma_f32_16x16x32_bf16 v[74:77], v[134:137], v[190:193], v[74:77]
	v_mfma_f32_16x16x32_bf16 v[70:73], v[142:145], v[190:193], v[70:73]
	v_mfma_f32_16x16x32_bf16 v[122:125], v[138:141], v[170:173], v[122:125]
	v_mfma_f32_16x16x32_bf16 v[118:121], v[146:149], v[170:173], v[118:121]
	v_mfma_f32_16x16x32_bf16 v[106:109], v[138:141], v[178:181], v[106:109]
	v_mfma_f32_16x16x32_bf16 v[102:105], v[146:149], v[178:181], v[102:105]
	v_mfma_f32_16x16x32_bf16 v[90:93], v[138:141], v[186:189], v[90:93]
	v_mfma_f32_16x16x32_bf16 v[86:89], v[146:149], v[186:189], v[86:89]
	v_mfma_f32_16x16x32_bf16 v[74:77], v[138:141], v[194:197], v[74:77]
	v_mfma_f32_16x16x32_bf16 v[70:73], v[146:149], v[194:197], v[70:73]
	s_barrier
	s_add_i32 s34, s51, s37
	v_lshl_add_u64 v[210:211], v[210:211], 0, s[16:17]
	s_mov_b32 m0, s34
	ds_read_b128 v[190:193], v227 offset:49152
	ds_read_b128 v[194:197], v227 offset:50176
	ds_read_b128 v[182:185], v227 offset:51200
	ds_read_b128 v[186:189], v227 offset:52224
	ds_read_b128 v[174:177], v227 offset:53248
	ds_read_b128 v[178:181], v227 offset:54272
	ds_read_b128 v[166:169], v227 offset:55296
	ds_read_b128 v[170:173], v227 offset:56320
	global_load_lds_dwordx4 v[210:211], off
	s_add_i32 m0, s34, 0x2000
	s_add_u32 s30, s30, 0x40080
	v_lshl_add_u64 v[210:211], v[212:213], 0, s[16:17]
	s_addc_u32 s31, s31, 0
	s_add_i32 s34, s52, s37
	global_load_lds_dwordx4 v[210:211], off
	v_lshl_add_u64 v[210:211], s[30:31], 0, v[198:199]
	s_mov_b32 m0, s34
	v_lshl_add_u64 v[4:5], v[4:5], 0, s[16:17]
	global_load_lds_dwordx4 v[210:211], off
	v_lshl_add_u64 v[210:211], s[30:31], 0, v[200:201]
	s_add_i32 m0, s34, 0x2000
	s_and_b64 vcc, exec, s[4:5]
	global_load_lds_dwordx4 v[210:211], off
	v_lshl_add_u64 v[210:211], v[234:235], 0, s[16:17]
	s_mov_b32 m0, s43
	s_nop 0
	global_load_lds_dwordx4 v[210:211], off
	s_mov_b32 m0, s44
	s_nop 0
	global_load_lds_dwordx4 v[4:5], off
	s_waitcnt vmcnt(8)
	s_waitcnt lgkmcnt(0)
	s_barrier
	s_cbranch_vccnz .LBB0_3074
	s_waitcnt lgkmcnt(0)
	v_mfma_f32_16x16x32_bf16 v[66:69], v[150:153], v[190:193], v[66:69]
	v_mfma_f32_16x16x32_bf16 v[62:65], v[158:161], v[190:193], v[62:65]
	v_mfma_f32_16x16x32_bf16 v[50:53], v[150:153], v[182:185], v[50:53]
	v_mfma_f32_16x16x32_bf16 v[46:49], v[158:161], v[182:185], v[46:49]
	v_mfma_f32_16x16x32_bf16 v[34:37], v[150:153], v[174:177], v[34:37]
	v_mfma_f32_16x16x32_bf16 v[30:33], v[158:161], v[174:177], v[30:33]
	v_mfma_f32_16x16x32_bf16 v[18:21], v[150:153], v[166:169], v[18:21]
	v_mfma_f32_16x16x32_bf16 v[14:17], v[158:161], v[166:169], v[14:17]
	v_mfma_f32_16x16x32_bf16 v[66:69], v[154:157], v[194:197], v[66:69]
	v_mfma_f32_16x16x32_bf16 v[62:65], v[162:165], v[194:197], v[62:65]
	v_mfma_f32_16x16x32_bf16 v[50:53], v[154:157], v[186:189], v[50:53]
	v_mfma_f32_16x16x32_bf16 v[46:49], v[162:165], v[186:189], v[46:49]
	v_mfma_f32_16x16x32_bf16 v[34:37], v[154:157], v[178:181], v[34:37]
	v_mfma_f32_16x16x32_bf16 v[30:33], v[162:165], v[178:181], v[30:33]
	v_mfma_f32_16x16x32_bf16 v[18:21], v[154:157], v[170:173], v[18:21]
	v_mfma_f32_16x16x32_bf16 v[14:17], v[162:165], v[170:173], v[14:17]
	v_mfma_f32_16x16x32_bf16 v[58:61], v[134:137], v[190:193], v[58:61]
	v_mfma_f32_16x16x32_bf16 v[54:57], v[142:145], v[190:193], v[54:57]
	v_mfma_f32_16x16x32_bf16 v[42:45], v[134:137], v[182:185], v[42:45]
	v_mfma_f32_16x16x32_bf16 v[38:41], v[142:145], v[182:185], v[38:41]
	v_mfma_f32_16x16x32_bf16 v[26:29], v[134:137], v[174:177], v[26:29]
	v_mfma_f32_16x16x32_bf16 v[22:25], v[142:145], v[174:177], v[22:25]
	v_mfma_f32_16x16x32_bf16 v[10:13], v[134:137], v[166:169], v[10:13]
	v_mfma_f32_16x16x32_bf16 v[4:7], v[142:145], v[166:169], v[6:9]
	v_mfma_f32_16x16x32_bf16 v[58:61], v[138:141], v[194:197], v[58:61]
	v_mfma_f32_16x16x32_bf16 v[54:57], v[146:149], v[194:197], v[54:57]
	v_mfma_f32_16x16x32_bf16 v[42:45], v[138:141], v[186:189], v[42:45]
	v_mfma_f32_16x16x32_bf16 v[38:41], v[146:149], v[186:189], v[38:41]
	v_mfma_f32_16x16x32_bf16 v[26:29], v[138:141], v[178:181], v[26:29]
	v_mfma_f32_16x16x32_bf16 v[22:25], v[146:149], v[178:181], v[22:25]
	v_mfma_f32_16x16x32_bf16 v[10:13], v[138:141], v[170:173], v[10:13]
	v_mfma_f32_16x16x32_bf16 v[6:9], v[146:149], v[170:173], v[4:7]

; #define PG8_STAGE_B(bufoff, gbase) do { _Pragma("unroll") for (int _i = 0; _i < 2; ++_i) \
;         __builtin_amdgcn_global_load_lds((const unsigned*)((const char*)(gbase) + voffB[_i]), (LAS unsigned*)(lds + (bufoff) + ldsw + _i * 8192), 16, 0, 0); } while (0)
; #define PG8_STAGE_A(bufoff, V0, V1, kb) do { \
;         __builtin_amdgcn_global_load_lds((const unsigned*)((Abase + (kb)) + (V0)), (LAS unsigned*)(lds + (bufoff) + ldsw), 16, 0, 0); \
;         __builtin_amdgcn_global_load_lds((const unsigned*)((Abase + (kb)) + (V1)), (LAS unsigned*)(lds + (bufoff) + ldsw + 8192), 16, 0, 0); } while (0)
; #define PG8_LDA(dst, b, h) do { _Pragma("unroll") for (int m = 0; m < 4; ++m) _Pragma("unroll") for (int k = 0; k < 2; ++k) dst[m][k] = *(const LAS bf16x8*)(lds + PG8_SA(b, h) + aoff + m * 2048 + k * 1024); } while (0)
; #define PG8_LDB(dst, b, h) do { _Pragma("unroll") for (int n = 0; n < 2; ++n) _Pragma("unroll") for (int k = 0; k < 2; ++k) dst[n][k] = *(const LAS bf16x8*)(lds + PG8_SB(b, h) + boff + n * 2048 + k * 1024); } while (0)
; #define PG8_WAIT_V(n) asm volatile("s_waitcnt vmcnt(" #n ")" ::: "memory")
; #define PG8_BAR __builtin_amdgcn_s_barrier()
; template <class Epi, class Sched, bool ALIGN_EPI>
; __device__ __forceinline__ void gemm_phase(LAS unsigned char* lds, const Gemm g, const Sched& S, const Epi& E) {
;     ...
;             PG8_LDB(B0, 0, 0); PG8_LDB(B1, 0, 1); PG8_SCHED; PG8_LDA(At, 0, 0); PG8_STAGE_A(PG8_SA(1, 1), vc10, vc11, kb1);
;             PG8_WAIT_V(8); PG8_WAIT_L(0); PG8_BAR; PG8_MMA(0, 0, At, B0); PG8_MMA(0, 1, At, B1); PG8_BAR; PG8_SCHED;
;             PG8_LDA(At, 0, 1); PG8_STAGE_B(PG8_SB(0, 0), b2); PG8_STAGE_B(PG8_SB(0, 1), b2 + hstepB); PG8_STAGE_A(PG8_SA(0, 0), s00, s01, kb2);
;             PG8_WAIT_V(8); PG8_WAIT_L(0); PG8_BAR; if (half1) { PG8_MMA(1, 0, At, B0); PG8_MMA(1, 1, At, B1); } PG8_BAR; PG8_SCHED;
;             PG8_LDB(B0, 1, 0); PG8_LDB(B1, 1, 1); PG8_SCHED; PG8_LDA(At, 1, 0); PG8_STAGE_A(PG8_SA(0, 1), s10, s11, kb2);
;             PG8_WAIT_V(8); PG8_WAIT_L(0); PG8_BAR; PG8_MMA(0, 0, At, B0); PG8_MMA(0, 1, At, B1); PG8_BAR; PG8_SCHED;
;             PG8_LDA(At, 1, 1); PG8_STAGE_B(PG8_SB(1, 0), b3); PG8_STAGE_B(PG8_SB(1, 1), b3 + hstepB); PG8_STAGE_A(PG8_SA(1, 0), s00, s01, kb3);
;             PG8_WAIT_V(8); PG8_WAIT_L(0); PG8_BAR; if (half1) { PG8_MMA(1, 0, At, B0); PG8_MMA(1, 1, At, B1); } PG8_BAR; PG8_SCHED;
.LBB0_3601:
	v_add_u32_e32 v5, s50, v227
	ds_read_b128 v[150:153], v5
	ds_read_b128 v[154:157], v5 offset:1024
	ds_read_b128 v[158:161], v5 offset:2048
	ds_read_b128 v[162:165], v5 offset:3072
	v_add_u32_e32 v5, s51, v227
	ds_read_b128 v[134:137], v5
	ds_read_b128 v[138:141], v5 offset:1024
	ds_read_b128 v[142:145], v5 offset:2048
	ds_read_b128 v[146:149], v5 offset:3072
	v_lshl_add_u64 v[218:219], v[216:217], 0, s[4:5]
	s_add_i32 m0, s37, 0xc000
	s_waitcnt lgkmcnt(0)
	ds_read_b128 v[166:169], v229
	ds_read_b128 v[170:173], v229 offset:1024
	ds_read_b128 v[174:177], v229 offset:2048
	ds_read_b128 v[178:181], v229 offset:3072
	ds_read_b128 v[182:185], v229 offset:4096
	ds_read_b128 v[186:189], v229 offset:5120
	ds_read_b128 v[190:193], v229 offset:6144
	ds_read_b128 v[194:197], v229 offset:7168
	global_load_lds_dwordx4 v[218:219], off
	v_lshl_add_u64 v[218:219], v[214:215], 0, s[4:5]
	s_add_i32 m0, s37, 0xe000
	s_nop 0
	global_load_lds_dwordx4 v[218:219], off
	s_waitcnt vmcnt(8)
	s_waitcnt lgkmcnt(0)
	s_barrier
	s_waitcnt lgkmcnt(0)
	v_mfma_f32_16x16x32_bf16 v[130:133], v[150:153], v[166:169], v[130:133]
	v_mfma_f32_16x16x32_bf16 v[126:129], v[158:161], v[166:169], v[126:129]
	v_mfma_f32_16x16x32_bf16 v[114:117], v[150:153], v[174:177], v[114:117]
	v_mfma_f32_16x16x32_bf16 v[110:113], v[158:161], v[174:177], v[110:113]
	v_mfma_f32_16x16x32_bf16 v[98:101], v[150:153], v[182:185], v[98:101]
	v_mfma_f32_16x16x32_bf16 v[94:97], v[158:161], v[182:185], v[94:97]
	v_mfma_f32_16x16x32_bf16 v[82:85], v[150:153], v[190:193], v[82:85]
	v_mfma_f32_16x16x32_bf16 v[78:81], v[158:161], v[190:193], v[78:81]
	v_mfma_f32_16x16x32_bf16 v[130:133], v[154:157], v[170:173], v[130:133]
	v_mfma_f32_16x16x32_bf16 v[126:129], v[162:165], v[170:173], v[126:129]
	v_mfma_f32_16x16x32_bf16 v[114:117], v[154:157], v[178:181], v[114:117]
	v_mfma_f32_16x16x32_bf16 v[110:113], v[162:165], v[178:181], v[110:113]
	v_mfma_f32_16x16x32_bf16 v[98:101], v[154:157], v[186:189], v[98:101]
	v_mfma_f32_16x16x32_bf16 v[94:97], v[162:165], v[186:189], v[94:97]
	v_mfma_f32_16x16x32_bf16 v[82:85], v[154:157], v[194:197], v[82:85]
	v_mfma_f32_16x16x32_bf16 v[78:81], v[162:165], v[194:197], v[78:81]
	v_mfma_f32_16x16x32_bf16 v[122:125], v[134:137], v[166:169], v[122:125]
	v_mfma_f32_16x16x32_bf16 v[118:121], v[142:145], v[166:169], v[118:121]
	v_mfma_f32_16x16x32_bf16 v[106:109], v[134:137], v[174:177], v[106:109]
	v_mfma_f32_16x16x32_bf16 v[102:105], v[142:145], v[174:177], v[102:105]
	v_mfma_f32_16x16x32_bf16 v[90:93], v[134:137], v[182:185], v[90:93]
	v_mfma_f32_16x16x32_bf16 v[86:89], v[142:145], v[182:185], v[86:89]
	v_mfma_f32_16x16x32_bf16 v[74:77], v[134:137], v[190:193], v[74:77]
	v_mfma_f32_16x16x32_bf16 v[70:73], v[142:145], v[190:193], v[70:73]
	v_mfma_f32_16x16x32_bf16 v[122:125], v[138:141], v[170:173], v[122:125]
	v_mfma_f32_16x16x32_bf16 v[118:121], v[146:149], v[170:173], v[118:121]
	v_mfma_f32_16x16x32_bf16 v[106:109], v[138:141], v[178:181], v[106:109]
	v_mfma_f32_16x16x32_bf16 v[102:105], v[146:149], v[178:181], v[102:105]
	v_mfma_f32_16x16x32_bf16 v[90:93], v[138:141], v[186:189], v[90:93]
	v_mfma_f32_16x16x32_bf16 v[86:89], v[146:149], v[186:189], v[86:89]
	v_mfma_f32_16x16x32_bf16 v[74:77], v[138:141], v[194:197], v[74:77]
	v_mfma_f32_16x16x32_bf16 v[70:73], v[146:149], v[194:197], v[70:73]
	s_barrier
	s_add_i32 s4, s50, s36
	v_lshl_add_u64 v[218:219], s[28:29], 0, v[198:199]
	s_mov_b32 m0, s4
	ds_read_b128 v[190:193], v229 offset:16384
	ds_read_b128 v[194:197], v229 offset:17408
	ds_read_b128 v[182:185], v229 offset:18432
	ds_read_b128 v[186:189], v229 offset:19456
	ds_read_b128 v[174:177], v229 offset:20480
	ds_read_b128 v[178:181], v229 offset:21504
	ds_read_b128 v[166:169], v229 offset:22528
	ds_read_b128 v[170:173], v229 offset:23552
	global_load_lds_dwordx4 v[218:219], off
	s_add_i32 m0, s4, 0x2000
	s_add_u32 s4, s28, 0x40000
	v_lshl_add_u64 v[220:221], s[28:29], 0, v[200:201]
	s_addc_u32 s5, s29, 0
	s_add_i32 s31, s51, s36
	global_load_lds_dwordx4 v[220:221], off
	v_lshl_add_u64 v[236:237], s[4:5], 0, v[198:199]
	s_mov_b32 m0, s31
	v_cndmask_b32_e64 v5, 0, 1, s[24:25]
	global_load_lds_dwordx4 v[236:237], off
	v_lshl_add_u64 v[236:237], s[4:5], 0, v[200:201]
	s_add_i32 m0, s31, 0x2000
	v_readlane_b32 s4, v255, 11
	v_readlane_b32 s5, v255, 12
	s_add_u32 s30, s4, s30
	global_load_lds_dwordx4 v[236:237], off
	s_addc_u32 s31, s5, 0
	s_mov_b32 m0, s37
	v_cmp_ne_u32_e64 s[4:5], 1, v5
	global_load_lds_dwordx4 v2, s[30:31]
	s_mov_b32 m0, s38
	s_andn2_b64 vcc, exec, s[24:25]
	global_load_lds_dwordx4 v4, s[30:31]
	s_waitcnt vmcnt(8)
	s_waitcnt lgkmcnt(0)
	s_barrier
	s_cbranch_vccnz .LBB0_3603
	s_waitcnt lgkmcnt(0)
	v_mfma_f32_16x16x32_bf16 v[66:69], v[150:153], v[190:193], v[66:69]
	v_mfma_f32_16x16x32_bf16 v[62:65], v[158:161], v[190:193], v[62:65]
	v_mfma_f32_16x16x32_bf16 v[50:53], v[150:153], v[182:185], v[50:53]
	v_mfma_f32_16x16x32_bf16 v[46:49], v[158:161], v[182:185], v[46:49]
	v_mfma_f32_16x16x32_bf16 v[34:37], v[150:153], v[174:177], v[34:37]
	v_mfma_f32_16x16x32_bf16 v[30:33], v[158:161], v[174:177], v[30:33]
	v_mfma_f32_16x16x32_bf16 v[18:21], v[150:153], v[166:169], v[18:21]
	v_mfma_f32_16x16x32_bf16 v[14:17], v[158:161], v[166:169], v[14:17]
	v_mfma_f32_16x16x32_bf16 v[66:69], v[154:157], v[194:197], v[66:69]
	v_mfma_f32_16x16x32_bf16 v[62:65], v[162:165], v[194:197], v[62:65]
	v_mfma_f32_16x16x32_bf16 v[50:53], v[154:157], v[186:189], v[50:53]
	v_mfma_f32_16x16x32_bf16 v[46:49], v[162:165], v[186:189], v[46:49]
	v_mfma_f32_16x16x32_bf16 v[34:37], v[154:157], v[178:181], v[34:37]
	v_mfma_f32_16x16x32_bf16 v[30:33], v[162:165], v[178:181], v[30:33]
	v_mfma_f32_16x16x32_bf16 v[18:21], v[154:157], v[170:173], v[18:21]
	v_mfma_f32_16x16x32_bf16 v[14:17], v[162:165], v[170:173], v[14:17]
	v_mfma_f32_16x16x32_bf16 v[58:61], v[134:137], v[190:193], v[58:61]
	v_mfma_f32_16x16x32_bf16 v[54:57], v[142:145], v[190:193], v[54:57]
	v_mfma_f32_16x16x32_bf16 v[42:45], v[134:137], v[182:185], v[42:45]
	v_mfma_f32_16x16x32_bf16 v[38:41], v[142:145], v[182:185], v[38:41]
	v_mfma_f32_16x16x32_bf16 v[26:29], v[134:137], v[174:177], v[26:29]
	v_mfma_f32_16x16x32_bf16 v[22:25], v[142:145], v[174:177], v[22:25]
	v_mfma_f32_16x16x32_bf16 v[10:13], v[134:137], v[166:169], v[10:13]
	v_mfma_f32_16x16x32_bf16 v[6:9], v[142:145], v[166:169], v[6:9]
	v_mfma_f32_16x16x32_bf16 v[58:61], v[138:141], v[194:197], v[58:61]
	v_mfma_f32_16x16x32_bf16 v[54:57], v[146:149], v[194:197], v[54:57]
	v_mfma_f32_16x16x32_bf16 v[42:45], v[138:141], v[186:189], v[42:45]
	v_mfma_f32_16x16x32_bf16 v[38:41], v[146:149], v[186:189], v[38:41]
	v_mfma_f32_16x16x32_bf16 v[26:29], v[138:141], v[178:181], v[26:29]
	v_mfma_f32_16x16x32_bf16 v[22:25], v[146:149], v[178:181], v[22:25]
	v_mfma_f32_16x16x32_bf16 v[10:13], v[138:141], v[170:173], v[10:13]
	v_mfma_f32_16x16x32_bf16 v[6:9], v[146:149], v[170:173], v[6:9]
; #define PG8_STAGE_B(bufoff, gbase) do { _Pragma("unroll") for (int _i = 0; _i < 2; ++_i) \
;         __builtin_amdgcn_global_load_lds((const unsigned*)((const char*)(gbase) + voffB[_i]), (LAS unsigned*)(lds + (bufoff) + ldsw + _i * 8192), 16, 0, 0); } while (0)
; #define PG8_STAGE_A(bufoff, V0, V1, kb) do { \
;         __builtin_amdgcn_global_load_lds((const unsigned*)((Abase + (kb)) + (V0)), (LAS unsigned*)(lds + (bufoff) + ldsw), 16, 0, 0); \
;         __builtin_amdgcn_global_load_lds((const unsigned*)((Abase + (kb)) + (V1)), (LAS unsigned*)(lds + (bufoff) + ldsw + 8192), 16, 0, 0); } while (0)
; #define PG8_LDA(dst, b, h) do { _Pragma("unroll") for (int m = 0; m < 4; ++m) _Pragma("unroll") for (int k = 0; k < 2; ++k) dst[m][k] = *(const LAS bf16x8*)(lds + PG8_SA(b, h) + aoff + m * 2048 + k * 1024); } while (0)
; #define PG8_LDB(dst, b, h) do { _Pragma("unroll") for (int n = 0; n < 2; ++n) _Pragma("unroll") for (int k = 0; k < 2; ++k) dst[n][k] = *(const LAS bf16x8*)(lds + PG8_SB(b, h) + boff + n * 2048 + k * 1024); } while (0)
; #define PG8_WAIT_V(n) asm volatile("s_waitcnt vmcnt(" #n ")" ::: "memory")
; #define PG8_BAR __builtin_amdgcn_s_barrier()
; template <class Epi, class Sched, bool ALIGN_EPI>
; __device__ __forceinline__ void gemm_phase(LAS unsigned char* lds, const Gemm g, const Sched& S, const Epi& E) {
;     ...
;             PG8_LDB(B0, 0, 0); PG8_LDB(B1, 0, 1); PG8_SCHED; PG8_LDA(At, 0, 0); PG8_STAGE_A(PG8_SA(1, 1), vc10, vc11, kb1);
;             PG8_WAIT_V(8); PG8_WAIT_L(0); PG8_BAR; PG8_MMA(0, 0, At, B0); PG8_MMA(0, 1, At, B1); PG8_BAR; PG8_SCHED;
;             PG8_LDA(At, 0, 1); PG8_STAGE_B(PG8_SB(0, 0), b2); PG8_STAGE_B(PG8_SB(0, 1), b2 + hstepB); PG8_STAGE_A(PG8_SA(0, 0), s00, s01, kb2);
;             PG8_WAIT_V(8); PG8_WAIT_L(0); PG8_BAR; if (half1) { PG8_MMA(1, 0, At, B0); PG8_MMA(1, 1, At, B1); } PG8_BAR; PG8_SCHED;
;             PG8_LDB(B0, 1, 0); PG8_LDB(B1, 1, 1); PG8_SCHED; PG8_LDA(At, 1, 0); PG8_STAGE_A(PG8_SA(0, 1), s10, s11, kb2);
;             PG8_WAIT_V(8); PG8_WAIT_L(0); PG8_BAR; PG8_MMA(0, 0, At, B0); PG8_MMA(0, 1, At, B1); PG8_BAR; PG8_SCHED;
;             PG8_LDA(At, 1, 1); PG8_STAGE_B(PG8_SB(1, 0), b3); PG8_STAGE_B(PG8_SB(1, 1), b3 + hstepB); PG8_STAGE_A(PG8_SA(1, 0), s00, s01, kb3);
;             PG8_WAIT_V(8); PG8_WAIT_L(0); PG8_BAR; if (half1) { PG8_MMA(1, 0, At, B0); PG8_MMA(1, 1, At, B1); } PG8_BAR; PG8_SCHED;
.LBB0_3603:
	v_mov_b32_e32 v5, v3
	v_lshl_add_u64 v[236:237], s[30:31], 0, v[2:3]
	v_lshl_add_u64 v[4:5], s[30:31], 0, v[4:5]
	s_barrier
	v_add_u32_e32 v2, s52, v227
	ds_read_b128 v[150:153], v2
	ds_read_b128 v[154:157], v2 offset:1024
	ds_read_b128 v[158:161], v2 offset:2048
	ds_read_b128 v[162:165], v2 offset:3072
	v_add_u32_e32 v2, s53, v227
	ds_read_b128 v[134:137], v2
	ds_read_b128 v[138:141], v2 offset:1024
	ds_read_b128 v[142:145], v2 offset:2048
	ds_read_b128 v[146:149], v2 offset:3072
	s_mov_b32 m0, s39
	s_waitcnt lgkmcnt(0)
	ds_read_b128 v[166:169], v229 offset:32768
	ds_read_b128 v[170:173], v229 offset:33792
	ds_read_b128 v[174:177], v229 offset:34816
	ds_read_b128 v[178:181], v229 offset:35840
	ds_read_b128 v[182:185], v229 offset:36864
	ds_read_b128 v[186:189], v229 offset:37888
	ds_read_b128 v[190:193], v229 offset:38912
	ds_read_b128 v[194:197], v229 offset:39936
	global_load_lds_dwordx4 v209, s[30:31]
	s_mov_b32 m0, s40
	s_nop 0
	global_load_lds_dwordx4 v211, s[30:31]
	s_waitcnt vmcnt(8)
	s_waitcnt lgkmcnt(0)
	s_barrier
	s_waitcnt lgkmcnt(0)
	v_mfma_f32_16x16x32_bf16 v[130:133], v[150:153], v[166:169], v[130:133]
	v_mfma_f32_16x16x32_bf16 v[126:129], v[158:161], v[166:169], v[126:129]
	v_mfma_f32_16x16x32_bf16 v[114:117], v[150:153], v[174:177], v[114:117]
	v_mfma_f32_16x16x32_bf16 v[110:113], v[158:161], v[174:177], v[110:113]
	v_mfma_f32_16x16x32_bf16 v[98:101], v[150:153], v[182:185], v[98:101]
	v_mfma_f32_16x16x32_bf16 v[94:97], v[158:161], v[182:185], v[94:97]
	v_mfma_f32_16x16x32_bf16 v[82:85], v[150:153], v[190:193], v[82:85]
	v_mfma_f32_16x16x32_bf16 v[78:81], v[158:161], v[190:193], v[78:81]
	v_mfma_f32_16x16x32_bf16 v[130:133], v[154:157], v[170:173], v[130:133]
	v_mfma_f32_16x16x32_bf16 v[126:129], v[162:165], v[170:173], v[126:129]
	v_mfma_f32_16x16x32_bf16 v[114:117], v[154:157], v[178:181], v[114:117]
	v_mfma_f32_16x16x32_bf16 v[110:113], v[162:165], v[178:181], v[110:113]
	v_mfma_f32_16x16x32_bf16 v[98:101], v[154:157], v[186:189], v[98:101]
	v_mfma_f32_16x16x32_bf16 v[94:97], v[162:165], v[186:189], v[94:97]
	v_mfma_f32_16x16x32_bf16 v[82:85], v[154:157], v[194:197], v[82:85]
	v_mfma_f32_16x16x32_bf16 v[78:81], v[162:165], v[194:197], v[78:81]
	v_mfma_f32_16x16x32_bf16 v[122:125], v[134:137], v[166:169], v[122:125]
	v_mfma_f32_16x16x32_bf16 v[118:121], v[142:145], v[166:169], v[118:121]
	v_mfma_f32_16x16x32_bf16 v[106:109], v[134:137], v[174:177], v[106:109]
	v_mfma_f32_16x16x32_bf16 v[102:105], v[142:145], v[174:177], v[102:105]
	v_mfma_f32_16x16x32_bf16 v[90:93], v[134:137], v[182:185], v[90:93]
	v_mfma_f32_16x16x32_bf16 v[86:89], v[142:145], v[182:185], v[86:89]
	v_mfma_f32_16x16x32_bf16 v[74:77], v[134:137], v[190:193], v[74:77]
	v_mfma_f32_16x16x32_bf16 v[70:73], v[142:145], v[190:193], v[70:73]
	v_mfma_f32_16x16x32_bf16 v[122:125], v[138:141], v[170:173], v[122:125]
	v_mfma_f32_16x16x32_bf16 v[118:121], v[146:149], v[170:173], v[118:121]
	v_mfma_f32_16x16x32_bf16 v[106:109], v[138:141], v[178:181], v[106:109]
	v_mfma_f32_16x16x32_bf16 v[102:105], v[146:149], v[178:181], v[102:105]
	v_mfma_f32_16x16x32_bf16 v[90:93], v[138:141], v[186:189], v[90:93]
	v_mfma_f32_16x16x32_bf16 v[86:89], v[146:149], v[186:189], v[86:89]
	v_mfma_f32_16x16x32_bf16 v[74:77], v[138:141], v[194:197], v[74:77]
	v_mfma_f32_16x16x32_bf16 v[70:73], v[146:149], v[194:197], v[70:73]
	s_barrier
	s_add_i32 s30, s52, s36
	v_lshl_add_u64 v[218:219], v[218:219], 0, s[6:7]
	s_mov_b32 m0, s30
	ds_read_b128 v[190:193], v229 offset:49152
	ds_read_b128 v[194:197], v229 offset:50176
	ds_read_b128 v[182:185], v229 offset:51200
	ds_read_b128 v[186:189], v229 offset:52224
	ds_read_b128 v[174:177], v229 offset:53248
	ds_read_b128 v[178:181], v229 offset:54272
	ds_read_b128 v[166:169], v229 offset:55296
	ds_read_b128 v[170:173], v229 offset:56320
	global_load_lds_dwordx4 v[218:219], off
	s_add_i32 m0, s30, 0x2000
	s_add_u32 s28, s28, 0x40080
	v_lshl_add_u64 v[218:219], v[220:221], 0, s[6:7]
	s_addc_u32 s29, s29, 0
	s_add_i32 s30, s53, s36
	global_load_lds_dwordx4 v[218:219], off
	v_lshl_add_u64 v[218:219], s[28:29], 0, v[198:199]
	s_mov_b32 m0, s30
	v_lshl_add_u64 v[4:5], v[4:5], 0, s[6:7]
	global_load_lds_dwordx4 v[218:219], off
	v_lshl_add_u64 v[218:219], s[28:29], 0, v[200:201]
	s_add_i32 m0, s30, 0x2000
	s_and_b64 vcc, exec, s[4:5]
	global_load_lds_dwordx4 v[218:219], off
	v_lshl_add_u64 v[218:219], v[236:237], 0, s[6:7]
	s_mov_b32 m0, s41
	s_nop 0
	global_load_lds_dwordx4 v[218:219], off
	s_mov_b32 m0, s42
	s_nop 0
	global_load_lds_dwordx4 v[4:5], off
	s_waitcnt vmcnt(8)
	s_waitcnt lgkmcnt(0)
	s_barrier
	s_cbranch_vccnz .LBB0_3605
	s_waitcnt lgkmcnt(0)
	v_mfma_f32_16x16x32_bf16 v[66:69], v[150:153], v[190:193], v[66:69]
	v_mfma_f32_16x16x32_bf16 v[62:65], v[158:161], v[190:193], v[62:65]
	v_mfma_f32_16x16x32_bf16 v[50:53], v[150:153], v[182:185], v[50:53]
	v_mfma_f32_16x16x32_bf16 v[46:49], v[158:161], v[182:185], v[46:49]
	v_mfma_f32_16x16x32_bf16 v[34:37], v[150:153], v[174:177], v[34:37]
	v_mfma_f32_16x16x32_bf16 v[30:33], v[158:161], v[174:177], v[30:33]
	v_mfma_f32_16x16x32_bf16 v[18:21], v[150:153], v[166:169], v[18:21]
	v_mfma_f32_16x16x32_bf16 v[14:17], v[158:161], v[166:169], v[14:17]
	v_mfma_f32_16x16x32_bf16 v[66:69], v[154:157], v[194:197], v[66:69]
	v_mfma_f32_16x16x32_bf16 v[62:65], v[162:165], v[194:197], v[62:65]
	v_mfma_f32_16x16x32_bf16 v[50:53], v[154:157], v[186:189], v[50:53]
	v_mfma_f32_16x16x32_bf16 v[46:49], v[162:165], v[186:189], v[46:49]
	v_mfma_f32_16x16x32_bf16 v[34:37], v[154:157], v[178:181], v[34:37]
	v_mfma_f32_16x16x32_bf16 v[30:33], v[162:165], v[178:181], v[30:33]
	v_mfma_f32_16x16x32_bf16 v[18:21], v[154:157], v[170:173], v[18:21]
	v_mfma_f32_16x16x32_bf16 v[14:17], v[162:165], v[170:173], v[14:17]
	v_mfma_f32_16x16x32_bf16 v[58:61], v[134:137], v[190:193], v[58:61]
	v_mfma_f32_16x16x32_bf16 v[54:57], v[142:145], v[190:193], v[54:57]
	v_mfma_f32_16x16x32_bf16 v[42:45], v[134:137], v[182:185], v[42:45]
	v_mfma_f32_16x16x32_bf16 v[38:41], v[142:145], v[182:185], v[38:41]
	v_mfma_f32_16x16x32_bf16 v[26:29], v[134:137], v[174:177], v[26:29]
	v_mfma_f32_16x16x32_bf16 v[22:25], v[142:145], v[174:177], v[22:25]
	v_mfma_f32_16x16x32_bf16 v[10:13], v[134:137], v[166:169], v[10:13]
	v_mfma_f32_16x16x32_bf16 v[4:7], v[142:145], v[166:169], v[6:9]
	v_mfma_f32_16x16x32_bf16 v[58:61], v[138:141], v[194:197], v[58:61]
	v_mfma_f32_16x16x32_bf16 v[54:57], v[146:149], v[194:197], v[54:57]
	v_mfma_f32_16x16x32_bf16 v[42:45], v[138:141], v[186:189], v[42:45]
	v_mfma_f32_16x16x32_bf16 v[38:41], v[146:149], v[186:189], v[38:41]
	v_mfma_f32_16x16x32_bf16 v[26:29], v[138:141], v[178:181], v[26:29]
	v_mfma_f32_16x16x32_bf16 v[22:25], v[146:149], v[178:181], v[22:25]
	v_mfma_f32_16x16x32_bf16 v[10:13], v[138:141], v[170:173], v[10:13]
	v_mfma_f32_16x16x32_bf16 v[6:9], v[146:149], v[170:173], v[4:7]

; #define PG8_STAGE_B(bufoff, gbase) do { _Pragma("unroll") for (int _i = 0; _i < 2; ++_i) \
;         __builtin_amdgcn_global_load_lds((const unsigned*)((const char*)(gbase) + voffB[_i]), (LAS unsigned*)(lds + (bufoff) + ldsw + _i * 8192), 16, 0, 0); } while (0)
; #define PG8_STAGE_A(bufoff, V0, V1, kb) do { \
;         __builtin_amdgcn_global_load_lds((const unsigned*)((Abase + (kb)) + (V0)), (LAS unsigned*)(lds + (bufoff) + ldsw), 16, 0, 0); \
;         __builtin_amdgcn_global_load_lds((const unsigned*)((Abase + (kb)) + (V1)), (LAS unsigned*)(lds + (bufoff) + ldsw + 8192), 16, 0, 0); } while (0)
; #define PG8_LDA(dst, b, h) do { _Pragma("unroll") for (int m = 0; m < 4; ++m) _Pragma("unroll") for (int k = 0; k < 2; ++k) dst[m][k] = *(const LAS bf16x8*)(lds + PG8_SA(b, h) + aoff + m * 2048 + k * 1024); } while (0)
; #define PG8_LDB(dst, b, h) do { _Pragma("unroll") for (int n = 0; n < 2; ++n) _Pragma("unroll") for (int k = 0; k < 2; ++k) dst[n][k] = *(const LAS bf16x8*)(lds + PG8_SB(b, h) + boff + n * 2048 + k * 1024); } while (0)
; #define PG8_WAIT_V(n) asm volatile("s_waitcnt vmcnt(" #n ")" ::: "memory")
; #define PG8_BAR __builtin_amdgcn_s_barrier()
; template <class Epi, class Sched, bool ALIGN_EPI>
; __device__ __forceinline__ void gemm_phase(LAS unsigned char* lds, const Gemm g, const Sched& S, const Epi& E) {
;     ...
;             PG8_LDB(B0, 0, 0); PG8_LDB(B1, 0, 1); PG8_SCHED; PG8_LDA(At, 0, 0); PG8_STAGE_A(PG8_SA(1, 1), vc10, vc11, kb1);
;             PG8_WAIT_V(8); PG8_WAIT_L(0); PG8_BAR; PG8_MMA(0, 0, At, B0); PG8_MMA(0, 1, At, B1); PG8_BAR; PG8_SCHED;
;             PG8_LDA(At, 0, 1); PG8_STAGE_B(PG8_SB(0, 0), b2); PG8_STAGE_B(PG8_SB(0, 1), b2 + hstepB); PG8_STAGE_A(PG8_SA(0, 0), s00, s01, kb2);
;             PG8_WAIT_V(8); PG8_WAIT_L(0); PG8_BAR; if (half1) { PG8_MMA(1, 0, At, B0); PG8_MMA(1, 1, At, B1); } PG8_BAR; PG8_SCHED;
;             PG8_LDB(B0, 1, 0); PG8_LDB(B1, 1, 1); PG8_SCHED; PG8_LDA(At, 1, 0); PG8_STAGE_A(PG8_SA(0, 1), s10, s11, kb2);
;             PG8_WAIT_V(8); PG8_WAIT_L(0); PG8_BAR; PG8_MMA(0, 0, At, B0); PG8_MMA(0, 1, At, B1); PG8_BAR; PG8_SCHED;
;             PG8_LDA(At, 1, 1); PG8_STAGE_B(PG8_SB(1, 0), b3); PG8_STAGE_B(PG8_SB(1, 1), b3 + hstepB); PG8_STAGE_A(PG8_SA(1, 0), s00, s01, kb3);
;             PG8_WAIT_V(8); PG8_WAIT_L(0); PG8_BAR; if (half1) { PG8_MMA(1, 0, At, B0); PG8_MMA(1, 1, At, B1); } PG8_BAR; PG8_SCHED;
.LBB0_3686:
	v_add_u32_e32 v100, s49, v228
	ds_read_b128 v[150:153], v100
	ds_read_b128 v[154:157], v100 offset:1024
	ds_read_b128 v[158:161], v100 offset:2048
	ds_read_b128 v[162:165], v100 offset:3072
	v_add_u32_e32 v100, s50, v228
	ds_read_b128 v[134:137], v100
	ds_read_b128 v[138:141], v100 offset:1024
	ds_read_b128 v[142:145], v100 offset:2048
	ds_read_b128 v[146:149], v100 offset:3072
	v_lshl_add_u64 v[100:101], v[212:213], 0, s[6:7]
	s_add_i32 m0, s41, 0xc000
	s_waitcnt lgkmcnt(0)
	ds_read_b128 v[166:169], v229
	ds_read_b128 v[170:173], v229 offset:1024
	ds_read_b128 v[174:177], v229 offset:2048
	ds_read_b128 v[178:181], v229 offset:3072
	ds_read_b128 v[182:185], v229 offset:4096
	ds_read_b128 v[186:189], v229 offset:5120
	ds_read_b128 v[190:193], v229 offset:6144
	ds_read_b128 v[194:197], v229 offset:7168
	global_load_lds_dwordx4 v[100:101], off
	v_lshl_add_u64 v[100:101], v[210:211], 0, s[6:7]
	s_add_i32 m0, s41, 0xe000
	s_nop 0
	global_load_lds_dwordx4 v[100:101], off
	s_waitcnt vmcnt(8)
	s_waitcnt lgkmcnt(0)
	s_barrier
	s_waitcnt lgkmcnt(0)
	v_mfma_f32_16x16x32_bf16 v[130:133], v[150:153], v[166:169], v[130:133]
	v_mfma_f32_16x16x32_bf16 v[126:129], v[158:161], v[166:169], v[126:129]
	v_mfma_f32_16x16x32_bf16 v[114:117], v[150:153], v[174:177], v[114:117]
	v_mfma_f32_16x16x32_bf16 v[110:113], v[158:161], v[174:177], v[110:113]
	v_mfma_f32_16x16x32_bf16 v[94:97], v[150:153], v[182:185], v[94:97]
	v_mfma_f32_16x16x32_bf16 v[90:93], v[158:161], v[182:185], v[90:93]
	v_mfma_f32_16x16x32_bf16 v[78:81], v[150:153], v[190:193], v[78:81]
	v_mfma_f32_16x16x32_bf16 v[74:77], v[158:161], v[190:193], v[74:77]
	v_mfma_f32_16x16x32_bf16 v[130:133], v[154:157], v[170:173], v[130:133]
	v_mfma_f32_16x16x32_bf16 v[126:129], v[162:165], v[170:173], v[126:129]
	v_mfma_f32_16x16x32_bf16 v[114:117], v[154:157], v[178:181], v[114:117]
	v_mfma_f32_16x16x32_bf16 v[110:113], v[162:165], v[178:181], v[110:113]
	v_mfma_f32_16x16x32_bf16 v[94:97], v[154:157], v[186:189], v[94:97]
	v_mfma_f32_16x16x32_bf16 v[90:93], v[162:165], v[186:189], v[90:93]
	v_mfma_f32_16x16x32_bf16 v[78:81], v[154:157], v[194:197], v[78:81]
	v_mfma_f32_16x16x32_bf16 v[74:77], v[162:165], v[194:197], v[74:77]
	v_mfma_f32_16x16x32_bf16 v[122:125], v[134:137], v[166:169], v[122:125]
	v_mfma_f32_16x16x32_bf16 v[118:121], v[142:145], v[166:169], v[118:121]
	v_mfma_f32_16x16x32_bf16 v[106:109], v[134:137], v[174:177], v[106:109]
	v_mfma_f32_16x16x32_bf16 v[100:103], v[142:145], v[174:177], v[102:105]
	v_mfma_f32_16x16x32_bf16 v[86:89], v[134:137], v[182:185], v[86:89]
	v_mfma_f32_16x16x32_bf16 v[82:85], v[142:145], v[182:185], v[82:85]
	v_mfma_f32_16x16x32_bf16 v[70:73], v[134:137], v[190:193], v[70:73]
	v_mfma_f32_16x16x32_bf16 v[66:69], v[142:145], v[190:193], v[66:69]
	v_mfma_f32_16x16x32_bf16 v[122:125], v[138:141], v[170:173], v[122:125]
	v_mfma_f32_16x16x32_bf16 v[118:121], v[146:149], v[170:173], v[118:121]
	v_mfma_f32_16x16x32_bf16 v[106:109], v[138:141], v[178:181], v[106:109]
	v_mfma_f32_16x16x32_bf16 v[100:103], v[146:149], v[178:181], v[100:103]
	v_mfma_f32_16x16x32_bf16 v[86:89], v[138:141], v[186:189], v[86:89]
	v_mfma_f32_16x16x32_bf16 v[82:85], v[146:149], v[186:189], v[82:85]
	v_mfma_f32_16x16x32_bf16 v[70:73], v[138:141], v[194:197], v[70:73]
	v_mfma_f32_16x16x32_bf16 v[66:69], v[146:149], v[194:197], v[66:69]
	s_barrier
	s_add_i32 s6, s49, s40
	v_lshl_add_u64 v[216:217], s[28:29], 0, v[198:199]
	s_mov_b32 m0, s6
	ds_read_b128 v[190:193], v229 offset:16384
	ds_read_b128 v[194:197], v229 offset:17408
	ds_read_b128 v[182:185], v229 offset:18432
	ds_read_b128 v[186:189], v229 offset:19456
	ds_read_b128 v[174:177], v229 offset:20480
	ds_read_b128 v[178:181], v229 offset:21504
	ds_read_b128 v[166:169], v229 offset:22528
	ds_read_b128 v[170:173], v229 offset:23552
	global_load_lds_dwordx4 v[216:217], off
	s_add_i32 m0, s6, 0x2000
	s_add_u32 s6, s28, 0x40000
	v_lshl_add_u64 v[218:219], s[28:29], 0, v[200:201]
	s_addc_u32 s7, s29, 0
	s_add_i32 s31, s50, s40
	global_load_lds_dwordx4 v[218:219], off
	v_lshl_add_u64 v[104:105], s[6:7], 0, v[198:199]
	s_mov_b32 m0, s31
	s_nop 0
	global_load_lds_dwordx4 v[104:105], off
	v_lshl_add_u64 v[104:105], s[6:7], 0, v[200:201]
	s_add_i32 m0, s31, 0x2000
	v_readlane_b32 s6, v254, 59
	v_readlane_b32 s7, v254, 60
	s_add_u32 s30, s6, s30
	global_load_lds_dwordx4 v[104:105], off
	s_addc_u32 s31, s7, 0
	s_mov_b32 m0, s41
	v_cndmask_b32_e64 v104, 0, 1, s[24:25]
	global_load_lds_dwordx4 v98, s[30:31]
	s_mov_b32 m0, s43
	v_cmp_ne_u32_e64 s[6:7], 1, v104
	global_load_lds_dwordx4 v214, s[30:31]
	s_waitcnt vmcnt(8)
	s_waitcnt lgkmcnt(0)
	s_andn2_b64 vcc, exec, s[24:25]
	s_barrier
	s_cbranch_vccnz .LBB0_3688
	s_waitcnt lgkmcnt(0)
	v_mfma_f32_16x16x32_bf16 v[62:65], v[150:153], v[190:193], v[62:65]
	v_mfma_f32_16x16x32_bf16 v[58:61], v[158:161], v[190:193], v[58:61]
	v_mfma_f32_16x16x32_bf16 v[46:49], v[150:153], v[182:185], v[46:49]
	v_mfma_f32_16x16x32_bf16 v[42:45], v[158:161], v[182:185], v[42:45]
	v_mfma_f32_16x16x32_bf16 v[30:33], v[150:153], v[174:177], v[30:33]
	v_mfma_f32_16x16x32_bf16 v[26:29], v[158:161], v[174:177], v[26:29]
	v_mfma_f32_16x16x32_bf16 v[14:17], v[150:153], v[166:169], v[14:17]
	v_mfma_f32_16x16x32_bf16 v[10:13], v[158:161], v[166:169], v[10:13]
	v_mfma_f32_16x16x32_bf16 v[62:65], v[154:157], v[194:197], v[62:65]
	v_mfma_f32_16x16x32_bf16 v[58:61], v[162:165], v[194:197], v[58:61]
	v_mfma_f32_16x16x32_bf16 v[46:49], v[154:157], v[186:189], v[46:49]
	v_mfma_f32_16x16x32_bf16 v[42:45], v[162:165], v[186:189], v[42:45]
	v_mfma_f32_16x16x32_bf16 v[30:33], v[154:157], v[178:181], v[30:33]
	v_mfma_f32_16x16x32_bf16 v[26:29], v[162:165], v[178:181], v[26:29]
	v_mfma_f32_16x16x32_bf16 v[14:17], v[154:157], v[170:173], v[14:17]
	v_mfma_f32_16x16x32_bf16 v[10:13], v[162:165], v[170:173], v[10:13]
	v_mfma_f32_16x16x32_bf16 v[54:57], v[134:137], v[190:193], v[54:57]
	v_mfma_f32_16x16x32_bf16 v[50:53], v[142:145], v[190:193], v[50:53]
	v_mfma_f32_16x16x32_bf16 v[38:41], v[134:137], v[182:185], v[38:41]
	v_mfma_f32_16x16x32_bf16 v[34:37], v[142:145], v[182:185], v[34:37]
	v_mfma_f32_16x16x32_bf16 v[22:25], v[134:137], v[174:177], v[22:25]
	v_mfma_f32_16x16x32_bf16 v[18:21], v[142:145], v[174:177], v[18:21]
	v_mfma_f32_16x16x32_bf16 v[6:9], v[134:137], v[166:169], v[6:9]
	v_mfma_f32_16x16x32_bf16 v[2:5], v[142:145], v[166:169], v[2:5]
	v_mfma_f32_16x16x32_bf16 v[54:57], v[138:141], v[194:197], v[54:57]
	v_mfma_f32_16x16x32_bf16 v[50:53], v[146:149], v[194:197], v[50:53]
	v_mfma_f32_16x16x32_bf16 v[38:41], v[138:141], v[186:189], v[38:41]
	v_mfma_f32_16x16x32_bf16 v[34:37], v[146:149], v[186:189], v[34:37]
	v_mfma_f32_16x16x32_bf16 v[22:25], v[138:141], v[178:181], v[22:25]
	v_mfma_f32_16x16x32_bf16 v[18:21], v[146:149], v[178:181], v[18:21]
	v_mfma_f32_16x16x32_bf16 v[6:9], v[138:141], v[170:173], v[6:9]
	v_mfma_f32_16x16x32_bf16 v[2:5], v[146:149], v[170:173], v[2:5]
; #define PG8_STAGE_B(bufoff, gbase) do { _Pragma("unroll") for (int _i = 0; _i < 2; ++_i) \
;         __builtin_amdgcn_global_load_lds((const unsigned*)((const char*)(gbase) + voffB[_i]), (LAS unsigned*)(lds + (bufoff) + ldsw + _i * 8192), 16, 0, 0); } while (0)
; #define PG8_STAGE_A(bufoff, V0, V1, kb) do { \
;         __builtin_amdgcn_global_load_lds((const unsigned*)((Abase + (kb)) + (V0)), (LAS unsigned*)(lds + (bufoff) + ldsw), 16, 0, 0); \
;         __builtin_amdgcn_global_load_lds((const unsigned*)((Abase + (kb)) + (V1)), (LAS unsigned*)(lds + (bufoff) + ldsw + 8192), 16, 0, 0); } while (0)
; #define PG8_LDA(dst, b, h) do { _Pragma("unroll") for (int m = 0; m < 4; ++m) _Pragma("unroll") for (int k = 0; k < 2; ++k) dst[m][k] = *(const LAS bf16x8*)(lds + PG8_SA(b, h) + aoff + m * 2048 + k * 1024); } while (0)
; #define PG8_LDB(dst, b, h) do { _Pragma("unroll") for (int n = 0; n < 2; ++n) _Pragma("unroll") for (int k = 0; k < 2; ++k) dst[n][k] = *(const LAS bf16x8*)(lds + PG8_SB(b, h) + boff + n * 2048 + k * 1024); } while (0)
; #define PG8_WAIT_V(n) asm volatile("s_waitcnt vmcnt(" #n ")" ::: "memory")
; #define PG8_BAR __builtin_amdgcn_s_barrier()
; template <class Epi, class Sched, bool ALIGN_EPI>
; __device__ __forceinline__ void gemm_phase(LAS unsigned char* lds, const Gemm g, const Sched& S, const Epi& E) {
;     ...
;             PG8_LDB(B0, 0, 0); PG8_LDB(B1, 0, 1); PG8_SCHED; PG8_LDA(At, 0, 0); PG8_STAGE_A(PG8_SA(1, 1), vc10, vc11, kb1);
;             PG8_WAIT_V(8); PG8_WAIT_L(0); PG8_BAR; PG8_MMA(0, 0, At, B0); PG8_MMA(0, 1, At, B1); PG8_BAR; PG8_SCHED;
;             PG8_LDA(At, 0, 1); PG8_STAGE_B(PG8_SB(0, 0), b2); PG8_STAGE_B(PG8_SB(0, 1), b2 + hstepB); PG8_STAGE_A(PG8_SA(0, 0), s00, s01, kb2);
;             PG8_WAIT_V(8); PG8_WAIT_L(0); PG8_BAR; if (half1) { PG8_MMA(1, 0, At, B0); PG8_MMA(1, 1, At, B1); } PG8_BAR; PG8_SCHED;
;             PG8_LDB(B0, 1, 0); PG8_LDB(B1, 1, 1); PG8_SCHED; PG8_LDA(At, 1, 0); PG8_STAGE_A(PG8_SA(0, 1), s10, s11, kb2);
;             PG8_WAIT_V(8); PG8_WAIT_L(0); PG8_BAR; PG8_MMA(0, 0, At, B0); PG8_MMA(0, 1, At, B1); PG8_BAR; PG8_SCHED;
;             PG8_LDA(At, 1, 1); PG8_STAGE_B(PG8_SB(1, 0), b3); PG8_STAGE_B(PG8_SB(1, 1), b3 + hstepB); PG8_STAGE_A(PG8_SA(1, 0), s00, s01, kb3);
;             PG8_WAIT_V(8); PG8_WAIT_L(0); PG8_BAR; if (half1) { PG8_MMA(1, 0, At, B0); PG8_MMA(1, 1, At, B1); } PG8_BAR; PG8_SCHED;
.LBB0_3688:
	v_mov_b32_e32 v215, v99
	v_lshl_add_u64 v[236:237], s[30:31], 0, v[98:99]
	v_lshl_add_u64 v[214:215], s[30:31], 0, v[214:215]
	s_barrier
	v_add_u32_e32 v98, s51, v228
	ds_read_b128 v[150:153], v98
	ds_read_b128 v[154:157], v98 offset:1024
	ds_read_b128 v[158:161], v98 offset:2048
	ds_read_b128 v[162:165], v98 offset:3072
	v_add_u32_e32 v98, s52, v228
	ds_read_b128 v[134:137], v98
	ds_read_b128 v[138:141], v98 offset:1024
	ds_read_b128 v[142:145], v98 offset:2048
	ds_read_b128 v[146:149], v98 offset:3072
	s_mov_b32 m0, s44
	s_waitcnt lgkmcnt(0)
	ds_read_b128 v[166:169], v229 offset:32768
	ds_read_b128 v[170:173], v229 offset:33792
	ds_read_b128 v[174:177], v229 offset:34816
	ds_read_b128 v[178:181], v229 offset:35840
	ds_read_b128 v[182:185], v229 offset:36864
	ds_read_b128 v[186:189], v229 offset:37888
	ds_read_b128 v[190:193], v229 offset:38912
	ds_read_b128 v[194:197], v229 offset:39936
	global_load_lds_dwordx4 v207, s[30:31]
	s_mov_b32 m0, s45
	s_nop 0
	global_load_lds_dwordx4 v209, s[30:31]
	s_waitcnt vmcnt(8)
	s_waitcnt lgkmcnt(0)
	s_barrier
	s_waitcnt lgkmcnt(0)
	v_mfma_f32_16x16x32_bf16 v[130:133], v[150:153], v[166:169], v[130:133]
	v_mfma_f32_16x16x32_bf16 v[126:129], v[158:161], v[166:169], v[126:129]
	v_mfma_f32_16x16x32_bf16 v[114:117], v[150:153], v[174:177], v[114:117]
	v_mfma_f32_16x16x32_bf16 v[110:113], v[158:161], v[174:177], v[110:113]
	v_mfma_f32_16x16x32_bf16 v[94:97], v[150:153], v[182:185], v[94:97]
	v_mfma_f32_16x16x32_bf16 v[90:93], v[158:161], v[182:185], v[90:93]
	v_mfma_f32_16x16x32_bf16 v[78:81], v[150:153], v[190:193], v[78:81]
	v_mfma_f32_16x16x32_bf16 v[74:77], v[158:161], v[190:193], v[74:77]
	v_mfma_f32_16x16x32_bf16 v[130:133], v[154:157], v[170:173], v[130:133]
	v_mfma_f32_16x16x32_bf16 v[126:129], v[162:165], v[170:173], v[126:129]
	v_mfma_f32_16x16x32_bf16 v[114:117], v[154:157], v[178:181], v[114:117]
	v_mfma_f32_16x16x32_bf16 v[110:113], v[162:165], v[178:181], v[110:113]
	v_mfma_f32_16x16x32_bf16 v[94:97], v[154:157], v[186:189], v[94:97]
	v_mfma_f32_16x16x32_bf16 v[90:93], v[162:165], v[186:189], v[90:93]
	v_mfma_f32_16x16x32_bf16 v[78:81], v[154:157], v[194:197], v[78:81]
	v_mfma_f32_16x16x32_bf16 v[74:77], v[162:165], v[194:197], v[74:77]
	v_mfma_f32_16x16x32_bf16 v[122:125], v[134:137], v[166:169], v[122:125]
	v_mfma_f32_16x16x32_bf16 v[118:121], v[142:145], v[166:169], v[118:121]
	v_mfma_f32_16x16x32_bf16 v[104:107], v[134:137], v[174:177], v[106:109]
	v_mfma_f32_16x16x32_bf16 v[100:103], v[142:145], v[174:177], v[100:103]
	v_mfma_f32_16x16x32_bf16 v[86:89], v[134:137], v[182:185], v[86:89]
	v_mfma_f32_16x16x32_bf16 v[82:85], v[142:145], v[182:185], v[82:85]
	v_mfma_f32_16x16x32_bf16 v[70:73], v[134:137], v[190:193], v[70:73]
	v_mfma_f32_16x16x32_bf16 v[66:69], v[142:145], v[190:193], v[66:69]
	v_mfma_f32_16x16x32_bf16 v[122:125], v[138:141], v[170:173], v[122:125]
	v_mfma_f32_16x16x32_bf16 v[118:121], v[146:149], v[170:173], v[118:121]
	v_mfma_f32_16x16x32_bf16 v[106:109], v[138:141], v[178:181], v[104:107]
	v_mfma_f32_16x16x32_bf16 v[102:105], v[146:149], v[178:181], v[100:103]
	v_mfma_f32_16x16x32_bf16 v[86:89], v[138:141], v[186:189], v[86:89]
	v_mfma_f32_16x16x32_bf16 v[82:85], v[146:149], v[186:189], v[82:85]
	v_mfma_f32_16x16x32_bf16 v[70:73], v[138:141], v[194:197], v[70:73]
	v_mfma_f32_16x16x32_bf16 v[66:69], v[146:149], v[194:197], v[66:69]
	s_barrier
	s_add_i32 s30, s51, s40
	v_lshl_add_u64 v[100:101], v[216:217], 0, s[10:11]
	s_mov_b32 m0, s30
	ds_read_b128 v[190:193], v229 offset:49152
	ds_read_b128 v[194:197], v229 offset:50176
	ds_read_b128 v[182:185], v229 offset:51200
	ds_read_b128 v[186:189], v229 offset:52224
	ds_read_b128 v[174:177], v229 offset:53248
	ds_read_b128 v[178:181], v229 offset:54272
	ds_read_b128 v[166:169], v229 offset:55296
	ds_read_b128 v[170:173], v229 offset:56320
	global_load_lds_dwordx4 v[100:101], off
	s_add_i32 m0, s30, 0x2000
	s_add_u32 s28, s28, 0x40080
	v_lshl_add_u64 v[100:101], v[218:219], 0, s[10:11]
	s_addc_u32 s29, s29, 0
	s_add_i32 s30, s52, s40
	global_load_lds_dwordx4 v[100:101], off
	v_lshl_add_u64 v[100:101], s[28:29], 0, v[198:199]
	s_mov_b32 m0, s30
	s_and_b64 vcc, exec, s[6:7]
	global_load_lds_dwordx4 v[100:101], off
	v_lshl_add_u64 v[100:101], s[28:29], 0, v[200:201]
	s_add_i32 m0, s30, 0x2000
	s_nop 0
	global_load_lds_dwordx4 v[100:101], off
	v_lshl_add_u64 v[100:101], v[236:237], 0, s[10:11]
	s_mov_b32 m0, s46
	s_nop 0
	global_load_lds_dwordx4 v[100:101], off
	v_lshl_add_u64 v[100:101], v[214:215], 0, s[10:11]
	s_mov_b32 m0, s47
	s_nop 0
	global_load_lds_dwordx4 v[100:101], off
	s_waitcnt vmcnt(8)
	s_waitcnt lgkmcnt(0)
	s_barrier
	s_cbranch_vccnz .LBB0_3690
	s_waitcnt lgkmcnt(0)
	v_mfma_f32_16x16x32_bf16 v[62:65], v[150:153], v[190:193], v[62:65]
	v_mfma_f32_16x16x32_bf16 v[58:61], v[158:161], v[190:193], v[58:61]
	v_mfma_f32_16x16x32_bf16 v[46:49], v[150:153], v[182:185], v[46:49]
	v_mfma_f32_16x16x32_bf16 v[42:45], v[158:161], v[182:185], v[42:45]
	v_mfma_f32_16x16x32_bf16 v[30:33], v[150:153], v[174:177], v[30:33]
	v_mfma_f32_16x16x32_bf16 v[26:29], v[158:161], v[174:177], v[26:29]
	v_mfma_f32_16x16x32_bf16 v[14:17], v[150:153], v[166:169], v[14:17]
	v_mfma_f32_16x16x32_bf16 v[10:13], v[158:161], v[166:169], v[10:13]
	v_mfma_f32_16x16x32_bf16 v[62:65], v[154:157], v[194:197], v[62:65]
	v_mfma_f32_16x16x32_bf16 v[58:61], v[162:165], v[194:197], v[58:61]
	v_mfma_f32_16x16x32_bf16 v[46:49], v[154:157], v[186:189], v[46:49]
	v_mfma_f32_16x16x32_bf16 v[42:45], v[162:165], v[186:189], v[42:45]
	v_mfma_f32_16x16x32_bf16 v[30:33], v[154:157], v[178:181], v[30:33]
	v_mfma_f32_16x16x32_bf16 v[26:29], v[162:165], v[178:181], v[26:29]
	v_mfma_f32_16x16x32_bf16 v[14:17], v[154:157], v[170:173], v[14:17]
	v_mfma_f32_16x16x32_bf16 v[10:13], v[162:165], v[170:173], v[10:13]
	v_mfma_f32_16x16x32_bf16 v[54:57], v[134:137], v[190:193], v[54:57]
	v_mfma_f32_16x16x32_bf16 v[50:53], v[142:145], v[190:193], v[50:53]
	v_mfma_f32_16x16x32_bf16 v[38:41], v[134:137], v[182:185], v[38:41]
	v_mfma_f32_16x16x32_bf16 v[34:37], v[142:145], v[182:185], v[34:37]
	v_mfma_f32_16x16x32_bf16 v[22:25], v[134:137], v[174:177], v[22:25]
	v_mfma_f32_16x16x32_bf16 v[18:21], v[142:145], v[174:177], v[18:21]
	v_mfma_f32_16x16x32_bf16 v[6:9], v[134:137], v[166:169], v[6:9]
	v_mfma_f32_16x16x32_bf16 v[2:5], v[142:145], v[166:169], v[2:5]
	v_mfma_f32_16x16x32_bf16 v[54:57], v[138:141], v[194:197], v[54:57]
	v_mfma_f32_16x16x32_bf16 v[50:53], v[146:149], v[194:197], v[50:53]
	v_mfma_f32_16x16x32_bf16 v[38:41], v[138:141], v[186:189], v[38:41]
	v_mfma_f32_16x16x32_bf16 v[34:37], v[146:149], v[186:189], v[34:37]
	v_mfma_f32_16x16x32_bf16 v[22:25], v[138:141], v[178:181], v[22:25]
	v_mfma_f32_16x16x32_bf16 v[18:21], v[146:149], v[178:181], v[18:21]
	v_mfma_f32_16x16x32_bf16 v[6:9], v[138:141], v[170:173], v[6:9]
	v_mfma_f32_16x16x32_bf16 v[2:5], v[146:149], v[170:173], v[2:5]

; #define PG8_STAGE_B(bufoff, gbase) do { _Pragma("unroll") for (int _i = 0; _i < 2; ++_i) \
;         __builtin_amdgcn_global_load_lds((const unsigned*)((const char*)(gbase) + voffB[_i]), (LAS unsigned*)(lds + (bufoff) + ldsw + _i * 8192), 16, 0, 0); } while (0)
; #define PG8_STAGE_A(bufoff, V0, V1, kb) do { \
;         __builtin_amdgcn_global_load_lds((const unsigned*)((Abase + (kb)) + (V0)), (LAS unsigned*)(lds + (bufoff) + ldsw), 16, 0, 0); \
;         __builtin_amdgcn_global_load_lds((const unsigned*)((Abase + (kb)) + (V1)), (LAS unsigned*)(lds + (bufoff) + ldsw + 8192), 16, 0, 0); } while (0)
; #define PG8_LDA(dst, b, h) do { _Pragma("unroll") for (int m = 0; m < 4; ++m) _Pragma("unroll") for (int k = 0; k < 2; ++k) dst[m][k] = *(const LAS bf16x8*)(lds + PG8_SA(b, h) + aoff + m * 2048 + k * 1024); } while (0)
; #define PG8_LDB(dst, b, h) do { _Pragma("unroll") for (int n = 0; n < 2; ++n) _Pragma("unroll") for (int k = 0; k < 2; ++k) dst[n][k] = *(const LAS bf16x8*)(lds + PG8_SB(b, h) + boff + n * 2048 + k * 1024); } while (0)
; #define PG8_WAIT_V(n) asm volatile("s_waitcnt vmcnt(" #n ")" ::: "memory")
; #define PG8_BAR __builtin_amdgcn_s_barrier()
; template <class Epi, class Sched, bool ALIGN_EPI>
; __device__ __forceinline__ void gemm_phase(LAS unsigned char* lds, const Gemm g, const Sched& S, const Epi& E) {
;     ...
;             PG8_LDB(B0, 0, 0); PG8_LDB(B1, 0, 1); PG8_SCHED; PG8_LDA(At, 0, 0); PG8_STAGE_A(PG8_SA(1, 1), vc10, vc11, kb1);
;             PG8_WAIT_V(8); PG8_WAIT_L(0); PG8_BAR; PG8_MMA(0, 0, At, B0); PG8_MMA(0, 1, At, B1); PG8_BAR; PG8_SCHED;
;             PG8_LDA(At, 0, 1); PG8_STAGE_B(PG8_SB(0, 0), b2); PG8_STAGE_B(PG8_SB(0, 1), b2 + hstepB); PG8_STAGE_A(PG8_SA(0, 0), s00, s01, kb2);
;             PG8_WAIT_V(8); PG8_WAIT_L(0); PG8_BAR; if (half1) { PG8_MMA(1, 0, At, B0); PG8_MMA(1, 1, At, B1); } PG8_BAR; PG8_SCHED;
;             PG8_LDB(B0, 1, 0); PG8_LDB(B1, 1, 1); PG8_SCHED; PG8_LDA(At, 1, 0); PG8_STAGE_A(PG8_SA(0, 1), s10, s11, kb2);
;             PG8_WAIT_V(8); PG8_WAIT_L(0); PG8_BAR; PG8_MMA(0, 0, At, B0); PG8_MMA(0, 1, At, B1); PG8_BAR; PG8_SCHED;
;             PG8_LDA(At, 1, 1); PG8_STAGE_B(PG8_SB(1, 0), b3); PG8_STAGE_B(PG8_SB(1, 1), b3 + hstepB); PG8_STAGE_A(PG8_SA(1, 0), s00, s01, kb3);
;             PG8_WAIT_V(8); PG8_WAIT_L(0); PG8_BAR; if (half1) { PG8_MMA(1, 0, At, B0); PG8_MMA(1, 1, At, B1); } PG8_BAR; PG8_SCHED;
.LBB0_3814:
	v_add_u32_e32 v5, s40, v220
	ds_read_b128 v[150:153], v5
	ds_read_b128 v[154:157], v5 offset:1024
	ds_read_b128 v[158:161], v5 offset:2048
	ds_read_b128 v[162:165], v5 offset:3072
	v_add_u32_e32 v5, s41, v220
	ds_read_b128 v[134:137], v5
	ds_read_b128 v[138:141], v5 offset:1024
	ds_read_b128 v[142:145], v5 offset:2048
	ds_read_b128 v[146:149], v5 offset:3072
	v_lshl_add_u64 v[212:213], v[210:211], 0, s[4:5]
	s_add_i32 m0, s33, 0xc000
	s_waitcnt lgkmcnt(0)
	ds_read_b128 v[166:169], v221
	ds_read_b128 v[170:173], v221 offset:1024
	ds_read_b128 v[174:177], v221 offset:2048
	ds_read_b128 v[178:181], v221 offset:3072
	ds_read_b128 v[182:185], v221 offset:4096
	ds_read_b128 v[186:189], v221 offset:5120
	ds_read_b128 v[190:193], v221 offset:6144
	ds_read_b128 v[194:197], v221 offset:7168
	global_load_lds_dwordx4 v[212:213], off
	v_lshl_add_u64 v[212:213], v[208:209], 0, s[4:5]
	s_add_i32 m0, s33, 0xe000
	s_nop 0
	global_load_lds_dwordx4 v[212:213], off
	s_waitcnt vmcnt(8)
	s_waitcnt lgkmcnt(0)
	s_barrier
	s_waitcnt lgkmcnt(0)
	v_mfma_f32_16x16x32_bf16 v[130:133], v[150:153], v[166:169], v[130:133]
	v_mfma_f32_16x16x32_bf16 v[126:129], v[158:161], v[166:169], v[126:129]
	v_mfma_f32_16x16x32_bf16 v[122:125], v[150:153], v[174:177], v[122:125]
	v_mfma_f32_16x16x32_bf16 v[118:121], v[158:161], v[174:177], v[118:121]
	v_mfma_f32_16x16x32_bf16 v[106:109], v[150:153], v[182:185], v[106:109]
	v_mfma_f32_16x16x32_bf16 v[102:105], v[158:161], v[182:185], v[102:105]
	v_mfma_f32_16x16x32_bf16 v[90:93], v[150:153], v[190:193], v[90:93]
	v_mfma_f32_16x16x32_bf16 v[86:89], v[158:161], v[190:193], v[86:89]
	v_mfma_f32_16x16x32_bf16 v[130:133], v[154:157], v[170:173], v[130:133]
	v_mfma_f32_16x16x32_bf16 v[126:129], v[162:165], v[170:173], v[126:129]
	v_mfma_f32_16x16x32_bf16 v[122:125], v[154:157], v[178:181], v[122:125]
	v_mfma_f32_16x16x32_bf16 v[118:121], v[162:165], v[178:181], v[118:121]
	v_mfma_f32_16x16x32_bf16 v[106:109], v[154:157], v[186:189], v[106:109]
	v_mfma_f32_16x16x32_bf16 v[102:105], v[162:165], v[186:189], v[102:105]
	v_mfma_f32_16x16x32_bf16 v[90:93], v[154:157], v[194:197], v[90:93]
	v_mfma_f32_16x16x32_bf16 v[86:89], v[162:165], v[194:197], v[86:89]
	v_mfma_f32_16x16x32_bf16 v[114:117], v[134:137], v[166:169], v[114:117]
	v_mfma_f32_16x16x32_bf16 v[110:113], v[142:145], v[166:169], v[110:113]
	v_mfma_f32_16x16x32_bf16 v[98:101], v[134:137], v[174:177], v[98:101]
	v_mfma_f32_16x16x32_bf16 v[94:97], v[142:145], v[174:177], v[94:97]
	v_mfma_f32_16x16x32_bf16 v[82:85], v[134:137], v[182:185], v[82:85]
	v_mfma_f32_16x16x32_bf16 v[78:81], v[142:145], v[182:185], v[78:81]
	v_mfma_f32_16x16x32_bf16 v[74:77], v[134:137], v[190:193], v[74:77]
	v_mfma_f32_16x16x32_bf16 v[70:73], v[142:145], v[190:193], v[70:73]
	v_mfma_f32_16x16x32_bf16 v[114:117], v[138:141], v[170:173], v[114:117]
	v_mfma_f32_16x16x32_bf16 v[110:113], v[146:149], v[170:173], v[110:113]
	v_mfma_f32_16x16x32_bf16 v[98:101], v[138:141], v[178:181], v[98:101]
	v_mfma_f32_16x16x32_bf16 v[94:97], v[146:149], v[178:181], v[94:97]
	v_mfma_f32_16x16x32_bf16 v[82:85], v[138:141], v[186:189], v[82:85]
	v_mfma_f32_16x16x32_bf16 v[78:81], v[146:149], v[186:189], v[78:81]
	v_mfma_f32_16x16x32_bf16 v[74:77], v[138:141], v[194:197], v[74:77]
	v_mfma_f32_16x16x32_bf16 v[70:73], v[146:149], v[194:197], v[70:73]
	s_barrier
	s_add_i32 s4, s40, s31
	v_lshl_add_u64 v[212:213], s[26:27], 0, v[198:199]
	s_mov_b32 m0, s4
	ds_read_b128 v[190:193], v221 offset:16384
	ds_read_b128 v[194:197], v221 offset:17408
	ds_read_b128 v[182:185], v221 offset:18432
	ds_read_b128 v[186:189], v221 offset:19456
	ds_read_b128 v[174:177], v221 offset:20480
	ds_read_b128 v[178:181], v221 offset:21504
	ds_read_b128 v[166:169], v221 offset:22528
	ds_read_b128 v[170:173], v221 offset:23552
	global_load_lds_dwordx4 v[212:213], off
	s_add_i32 m0, s4, 0x2000
	s_add_u32 s4, s26, 0x40000
	v_lshl_add_u64 v[214:215], s[26:27], 0, v[200:201]
	s_addc_u32 s5, s27, 0
	s_add_i32 s29, s41, s31
	global_load_lds_dwordx4 v[214:215], off
	v_lshl_add_u64 v[228:229], s[4:5], 0, v[198:199]
	s_mov_b32 m0, s29
	v_cndmask_b32_e64 v5, 0, 1, s[22:23]
	global_load_lds_dwordx4 v[228:229], off
	v_lshl_add_u64 v[228:229], s[4:5], 0, v[200:201]
	s_add_i32 m0, s29, 0x2000
	v_readlane_b32 s4, v255, 13
	v_readlane_b32 s5, v255, 14
	s_add_u32 s28, s4, s28
	global_load_lds_dwordx4 v[228:229], off
	s_addc_u32 s29, s5, 0
	s_mov_b32 m0, s33
	v_cmp_ne_u32_e64 s[4:5], 1, v5
	global_load_lds_dwordx4 v2, s[28:29]
	s_mov_b32 m0, s34
	s_andn2_b64 vcc, exec, s[22:23]
	global_load_lds_dwordx4 v4, s[28:29]
	s_waitcnt vmcnt(8)
	s_waitcnt lgkmcnt(0)
	s_barrier
	s_cbranch_vccnz .LBB0_3816
	s_waitcnt lgkmcnt(0)
	v_mfma_f32_16x16x32_bf16 v[66:69], v[150:153], v[190:193], v[66:69]
	v_mfma_f32_16x16x32_bf16 v[62:65], v[158:161], v[190:193], v[62:65]
	v_mfma_f32_16x16x32_bf16 v[50:53], v[150:153], v[182:185], v[50:53]
	v_mfma_f32_16x16x32_bf16 v[46:49], v[158:161], v[182:185], v[46:49]
	v_mfma_f32_16x16x32_bf16 v[34:37], v[150:153], v[174:177], v[34:37]
	v_mfma_f32_16x16x32_bf16 v[30:33], v[158:161], v[174:177], v[30:33]
	v_mfma_f32_16x16x32_bf16 v[18:21], v[150:153], v[166:169], v[18:21]
	v_mfma_f32_16x16x32_bf16 v[14:17], v[158:161], v[166:169], v[14:17]
	v_mfma_f32_16x16x32_bf16 v[66:69], v[154:157], v[194:197], v[66:69]
	v_mfma_f32_16x16x32_bf16 v[62:65], v[162:165], v[194:197], v[62:65]
	v_mfma_f32_16x16x32_bf16 v[50:53], v[154:157], v[186:189], v[50:53]
	v_mfma_f32_16x16x32_bf16 v[46:49], v[162:165], v[186:189], v[46:49]
	v_mfma_f32_16x16x32_bf16 v[34:37], v[154:157], v[178:181], v[34:37]
	v_mfma_f32_16x16x32_bf16 v[30:33], v[162:165], v[178:181], v[30:33]
	v_mfma_f32_16x16x32_bf16 v[18:21], v[154:157], v[170:173], v[18:21]
	v_mfma_f32_16x16x32_bf16 v[14:17], v[162:165], v[170:173], v[14:17]
	v_mfma_f32_16x16x32_bf16 v[58:61], v[134:137], v[190:193], v[58:61]
	v_mfma_f32_16x16x32_bf16 v[54:57], v[142:145], v[190:193], v[54:57]
	v_mfma_f32_16x16x32_bf16 v[42:45], v[134:137], v[182:185], v[42:45]
	v_mfma_f32_16x16x32_bf16 v[38:41], v[142:145], v[182:185], v[38:41]
	v_mfma_f32_16x16x32_bf16 v[26:29], v[134:137], v[174:177], v[26:29]
	v_mfma_f32_16x16x32_bf16 v[22:25], v[142:145], v[174:177], v[22:25]
	v_mfma_f32_16x16x32_bf16 v[10:13], v[134:137], v[166:169], v[10:13]
	v_mfma_f32_16x16x32_bf16 v[6:9], v[142:145], v[166:169], v[6:9]
	v_mfma_f32_16x16x32_bf16 v[58:61], v[138:141], v[194:197], v[58:61]
	v_mfma_f32_16x16x32_bf16 v[54:57], v[146:149], v[194:197], v[54:57]
	v_mfma_f32_16x16x32_bf16 v[42:45], v[138:141], v[186:189], v[42:45]
	v_mfma_f32_16x16x32_bf16 v[38:41], v[146:149], v[186:189], v[38:41]
	v_mfma_f32_16x16x32_bf16 v[26:29], v[138:141], v[178:181], v[26:29]
	v_mfma_f32_16x16x32_bf16 v[22:25], v[146:149], v[178:181], v[22:25]
	v_mfma_f32_16x16x32_bf16 v[10:13], v[138:141], v[170:173], v[10:13]
	v_mfma_f32_16x16x32_bf16 v[6:9], v[146:149], v[170:173], v[6:9]
; #define PG8_STAGE_B(bufoff, gbase) do { _Pragma("unroll") for (int _i = 0; _i < 2; ++_i) \
;         __builtin_amdgcn_global_load_lds((const unsigned*)((const char*)(gbase) + voffB[_i]), (LAS unsigned*)(lds + (bufoff) + ldsw + _i * 8192), 16, 0, 0); } while (0)
; #define PG8_STAGE_A(bufoff, V0, V1, kb) do { \
;         __builtin_amdgcn_global_load_lds((const unsigned*)((Abase + (kb)) + (V0)), (LAS unsigned*)(lds + (bufoff) + ldsw), 16, 0, 0); \
;         __builtin_amdgcn_global_load_lds((const unsigned*)((Abase + (kb)) + (V1)), (LAS unsigned*)(lds + (bufoff) + ldsw + 8192), 16, 0, 0); } while (0)
; #define PG8_LDA(dst, b, h) do { _Pragma("unroll") for (int m = 0; m < 4; ++m) _Pragma("unroll") for (int k = 0; k < 2; ++k) dst[m][k] = *(const LAS bf16x8*)(lds + PG8_SA(b, h) + aoff + m * 2048 + k * 1024); } while (0)
; #define PG8_LDB(dst, b, h) do { _Pragma("unroll") for (int n = 0; n < 2; ++n) _Pragma("unroll") for (int k = 0; k < 2; ++k) dst[n][k] = *(const LAS bf16x8*)(lds + PG8_SB(b, h) + boff + n * 2048 + k * 1024); } while (0)
; #define PG8_WAIT_V(n) asm volatile("s_waitcnt vmcnt(" #n ")" ::: "memory")
; #define PG8_BAR __builtin_amdgcn_s_barrier()
; template <class Epi, class Sched, bool ALIGN_EPI>
; __device__ __forceinline__ void gemm_phase(LAS unsigned char* lds, const Gemm g, const Sched& S, const Epi& E) {
;     ...
;             PG8_LDB(B0, 0, 0); PG8_LDB(B1, 0, 1); PG8_SCHED; PG8_LDA(At, 0, 0); PG8_STAGE_A(PG8_SA(1, 1), vc10, vc11, kb1);
;             PG8_WAIT_V(8); PG8_WAIT_L(0); PG8_BAR; PG8_MMA(0, 0, At, B0); PG8_MMA(0, 1, At, B1); PG8_BAR; PG8_SCHED;
;             PG8_LDA(At, 0, 1); PG8_STAGE_B(PG8_SB(0, 0), b2); PG8_STAGE_B(PG8_SB(0, 1), b2 + hstepB); PG8_STAGE_A(PG8_SA(0, 0), s00, s01, kb2);
;             PG8_WAIT_V(8); PG8_WAIT_L(0); PG8_BAR; if (half1) { PG8_MMA(1, 0, At, B0); PG8_MMA(1, 1, At, B1); } PG8_BAR; PG8_SCHED;
;             PG8_LDB(B0, 1, 0); PG8_LDB(B1, 1, 1); PG8_SCHED; PG8_LDA(At, 1, 0); PG8_STAGE_A(PG8_SA(0, 1), s10, s11, kb2);
;             PG8_WAIT_V(8); PG8_WAIT_L(0); PG8_BAR; PG8_MMA(0, 0, At, B0); PG8_MMA(0, 1, At, B1); PG8_BAR; PG8_SCHED;
;             PG8_LDA(At, 1, 1); PG8_STAGE_B(PG8_SB(1, 0), b3); PG8_STAGE_B(PG8_SB(1, 1), b3 + hstepB); PG8_STAGE_A(PG8_SA(1, 0), s00, s01, kb3);
;             PG8_WAIT_V(8); PG8_WAIT_L(0); PG8_BAR; if (half1) { PG8_MMA(1, 0, At, B0); PG8_MMA(1, 1, At, B1); } PG8_BAR; PG8_SCHED;
.LBB0_3816:
	v_mov_b32_e32 v5, v3
	v_lshl_add_u64 v[228:229], s[28:29], 0, v[2:3]
	v_lshl_add_u64 v[4:5], s[28:29], 0, v[4:5]
	s_barrier
	v_add_u32_e32 v2, s42, v220
	ds_read_b128 v[150:153], v2
	ds_read_b128 v[154:157], v2 offset:1024
	ds_read_b128 v[158:161], v2 offset:2048
	ds_read_b128 v[162:165], v2 offset:3072
	v_add_u32_e32 v2, s43, v220
	ds_read_b128 v[134:137], v2
	ds_read_b128 v[138:141], v2 offset:1024
	ds_read_b128 v[142:145], v2 offset:2048
	ds_read_b128 v[146:149], v2 offset:3072
	s_mov_b32 m0, s35
	s_waitcnt lgkmcnt(0)
	ds_read_b128 v[166:169], v221 offset:32768
	ds_read_b128 v[170:173], v221 offset:33792
	ds_read_b128 v[174:177], v221 offset:34816
	ds_read_b128 v[178:181], v221 offset:35840
	ds_read_b128 v[182:185], v221 offset:36864
	ds_read_b128 v[186:189], v221 offset:37888
	ds_read_b128 v[190:193], v221 offset:38912
	ds_read_b128 v[194:197], v221 offset:39936
	global_load_lds_dwordx4 v205, s[28:29]
	s_mov_b32 m0, s36
	s_nop 0
	global_load_lds_dwordx4 v207, s[28:29]
	s_waitcnt vmcnt(8)
	s_waitcnt lgkmcnt(0)
	s_barrier
	s_waitcnt lgkmcnt(0)
	v_mfma_f32_16x16x32_bf16 v[130:133], v[150:153], v[166:169], v[130:133]
	v_mfma_f32_16x16x32_bf16 v[126:129], v[158:161], v[166:169], v[126:129]
	v_mfma_f32_16x16x32_bf16 v[122:125], v[150:153], v[174:177], v[122:125]
	v_mfma_f32_16x16x32_bf16 v[118:121], v[158:161], v[174:177], v[118:121]
	v_mfma_f32_16x16x32_bf16 v[106:109], v[150:153], v[182:185], v[106:109]
	v_mfma_f32_16x16x32_bf16 v[102:105], v[158:161], v[182:185], v[102:105]
	v_mfma_f32_16x16x32_bf16 v[90:93], v[150:153], v[190:193], v[90:93]
	v_mfma_f32_16x16x32_bf16 v[86:89], v[158:161], v[190:193], v[86:89]
	v_mfma_f32_16x16x32_bf16 v[130:133], v[154:157], v[170:173], v[130:133]
	v_mfma_f32_16x16x32_bf16 v[126:129], v[162:165], v[170:173], v[126:129]
	v_mfma_f32_16x16x32_bf16 v[122:125], v[154:157], v[178:181], v[122:125]
	v_mfma_f32_16x16x32_bf16 v[118:121], v[162:165], v[178:181], v[118:121]
	v_mfma_f32_16x16x32_bf16 v[106:109], v[154:157], v[186:189], v[106:109]
	v_mfma_f32_16x16x32_bf16 v[102:105], v[162:165], v[186:189], v[102:105]
	v_mfma_f32_16x16x32_bf16 v[90:93], v[154:157], v[194:197], v[90:93]
	v_mfma_f32_16x16x32_bf16 v[86:89], v[162:165], v[194:197], v[86:89]
	v_mfma_f32_16x16x32_bf16 v[114:117], v[134:137], v[166:169], v[114:117]
	v_mfma_f32_16x16x32_bf16 v[110:113], v[142:145], v[166:169], v[110:113]
	v_mfma_f32_16x16x32_bf16 v[98:101], v[134:137], v[174:177], v[98:101]
	v_mfma_f32_16x16x32_bf16 v[94:97], v[142:145], v[174:177], v[94:97]
	v_mfma_f32_16x16x32_bf16 v[82:85], v[134:137], v[182:185], v[82:85]
	v_mfma_f32_16x16x32_bf16 v[78:81], v[142:145], v[182:185], v[78:81]
	v_mfma_f32_16x16x32_bf16 v[74:77], v[134:137], v[190:193], v[74:77]
	v_mfma_f32_16x16x32_bf16 v[70:73], v[142:145], v[190:193], v[70:73]
	v_mfma_f32_16x16x32_bf16 v[114:117], v[138:141], v[170:173], v[114:117]
	v_mfma_f32_16x16x32_bf16 v[110:113], v[146:149], v[170:173], v[110:113]
	v_mfma_f32_16x16x32_bf16 v[98:101], v[138:141], v[178:181], v[98:101]
	v_mfma_f32_16x16x32_bf16 v[94:97], v[146:149], v[178:181], v[94:97]
	v_mfma_f32_16x16x32_bf16 v[82:85], v[138:141], v[186:189], v[82:85]
	v_mfma_f32_16x16x32_bf16 v[78:81], v[146:149], v[186:189], v[78:81]
	v_mfma_f32_16x16x32_bf16 v[74:77], v[138:141], v[194:197], v[74:77]
	v_mfma_f32_16x16x32_bf16 v[70:73], v[146:149], v[194:197], v[70:73]
	s_barrier
	s_add_i32 s28, s42, s31
	v_lshl_add_u64 v[212:213], v[212:213], 0, s[14:15]
	s_mov_b32 m0, s28
	ds_read_b128 v[190:193], v221 offset:49152
	ds_read_b128 v[194:197], v221 offset:50176
	ds_read_b128 v[182:185], v221 offset:51200
	ds_read_b128 v[186:189], v221 offset:52224
	ds_read_b128 v[174:177], v221 offset:53248
	ds_read_b128 v[178:181], v221 offset:54272
	ds_read_b128 v[166:169], v221 offset:55296
	ds_read_b128 v[170:173], v221 offset:56320
	global_load_lds_dwordx4 v[212:213], off
	s_add_i32 m0, s28, 0x2000
	s_add_u32 s26, s26, 0x40080
	v_lshl_add_u64 v[212:213], v[214:215], 0, s[14:15]
	s_addc_u32 s27, s27, 0
	s_add_i32 s28, s43, s31
	global_load_lds_dwordx4 v[212:213], off
	v_lshl_add_u64 v[212:213], s[26:27], 0, v[198:199]
	s_mov_b32 m0, s28
	v_lshl_add_u64 v[4:5], v[4:5], 0, s[14:15]
	global_load_lds_dwordx4 v[212:213], off
	v_lshl_add_u64 v[212:213], s[26:27], 0, v[200:201]
	s_add_i32 m0, s28, 0x2000
	s_and_b64 vcc, exec, s[4:5]
	global_load_lds_dwordx4 v[212:213], off
	v_lshl_add_u64 v[212:213], v[228:229], 0, s[14:15]
	s_mov_b32 m0, s37
	s_nop 0
	global_load_lds_dwordx4 v[212:213], off
	s_mov_b32 m0, s38
	s_nop 0
	global_load_lds_dwordx4 v[4:5], off
	s_waitcnt vmcnt(8)
	s_waitcnt lgkmcnt(0)
	s_barrier
	s_cbranch_vccnz .LBB0_3818
	s_waitcnt lgkmcnt(0)
	v_mfma_f32_16x16x32_bf16 v[66:69], v[150:153], v[190:193], v[66:69]
	v_mfma_f32_16x16x32_bf16 v[62:65], v[158:161], v[190:193], v[62:65]
	v_mfma_f32_16x16x32_bf16 v[50:53], v[150:153], v[182:185], v[50:53]
	v_mfma_f32_16x16x32_bf16 v[46:49], v[158:161], v[182:185], v[46:49]
	v_mfma_f32_16x16x32_bf16 v[34:37], v[150:153], v[174:177], v[34:37]
	v_mfma_f32_16x16x32_bf16 v[30:33], v[158:161], v[174:177], v[30:33]
	v_mfma_f32_16x16x32_bf16 v[18:21], v[150:153], v[166:169], v[18:21]
	v_mfma_f32_16x16x32_bf16 v[14:17], v[158:161], v[166:169], v[14:17]
	v_mfma_f32_16x16x32_bf16 v[66:69], v[154:157], v[194:197], v[66:69]
	v_mfma_f32_16x16x32_bf16 v[62:65], v[162:165], v[194:197], v[62:65]
	v_mfma_f32_16x16x32_bf16 v[50:53], v[154:157], v[186:189], v[50:53]
	v_mfma_f32_16x16x32_bf16 v[46:49], v[162:165], v[186:189], v[46:49]
	v_mfma_f32_16x16x32_bf16 v[34:37], v[154:157], v[178:181], v[34:37]
	v_mfma_f32_16x16x32_bf16 v[30:33], v[162:165], v[178:181], v[30:33]
	v_mfma_f32_16x16x32_bf16 v[18:21], v[154:157], v[170:173], v[18:21]
	v_mfma_f32_16x16x32_bf16 v[14:17], v[162:165], v[170:173], v[14:17]
	v_mfma_f32_16x16x32_bf16 v[58:61], v[134:137], v[190:193], v[58:61]
	v_mfma_f32_16x16x32_bf16 v[54:57], v[142:145], v[190:193], v[54:57]
	v_mfma_f32_16x16x32_bf16 v[42:45], v[134:137], v[182:185], v[42:45]
	v_mfma_f32_16x16x32_bf16 v[38:41], v[142:145], v[182:185], v[38:41]
	v_mfma_f32_16x16x32_bf16 v[26:29], v[134:137], v[174:177], v[26:29]
	v_mfma_f32_16x16x32_bf16 v[22:25], v[142:145], v[174:177], v[22:25]
	v_mfma_f32_16x16x32_bf16 v[10:13], v[134:137], v[166:169], v[10:13]
	v_mfma_f32_16x16x32_bf16 v[4:7], v[142:145], v[166:169], v[6:9]
	v_mfma_f32_16x16x32_bf16 v[58:61], v[138:141], v[194:197], v[58:61]
	v_mfma_f32_16x16x32_bf16 v[54:57], v[146:149], v[194:197], v[54:57]
	v_mfma_f32_16x16x32_bf16 v[42:45], v[138:141], v[186:189], v[42:45]
	v_mfma_f32_16x16x32_bf16 v[38:41], v[146:149], v[186:189], v[38:41]
	v_mfma_f32_16x16x32_bf16 v[26:29], v[138:141], v[178:181], v[26:29]
	v_mfma_f32_16x16x32_bf16 v[22:25], v[146:149], v[178:181], v[22:25]
	v_mfma_f32_16x16x32_bf16 v[10:13], v[138:141], v[170:173], v[10:13]
	v_mfma_f32_16x16x32_bf16 v[6:9], v[146:149], v[170:173], v[4:7]

; #define PG8_STAGE_B(bufoff, gbase) do { _Pragma("unroll") for (int _i = 0; _i < 2; ++_i) \
;         __builtin_amdgcn_global_load_lds((const unsigned*)((const char*)(gbase) + voffB[_i]), (LAS unsigned*)(lds + (bufoff) + ldsw + _i * 8192), 16, 0, 0); } while (0)
; #define PG8_STAGE_A(bufoff, V0, V1, kb) do { \
;         __builtin_amdgcn_global_load_lds((const unsigned*)((Abase + (kb)) + (V0)), (LAS unsigned*)(lds + (bufoff) + ldsw), 16, 0, 0); \
;         __builtin_amdgcn_global_load_lds((const unsigned*)((Abase + (kb)) + (V1)), (LAS unsigned*)(lds + (bufoff) + ldsw + 8192), 16, 0, 0); } while (0)
; #define PG8_LDA(dst, b, h) do { _Pragma("unroll") for (int m = 0; m < 4; ++m) _Pragma("unroll") for (int k = 0; k < 2; ++k) dst[m][k] = *(const LAS bf16x8*)(lds + PG8_SA(b, h) + aoff + m * 2048 + k * 1024); } while (0)
; #define PG8_LDB(dst, b, h) do { _Pragma("unroll") for (int n = 0; n < 2; ++n) _Pragma("unroll") for (int k = 0; k < 2; ++k) dst[n][k] = *(const LAS bf16x8*)(lds + PG8_SB(b, h) + boff + n * 2048 + k * 1024); } while (0)
; #define PG8_WAIT_V(n) asm volatile("s_waitcnt vmcnt(" #n ")" ::: "memory")
; #define PG8_BAR __builtin_amdgcn_s_barrier()
; template <class Epi, class Sched, bool ALIGN_EPI>
; __device__ __forceinline__ void gemm_phase(LAS unsigned char* lds, const Gemm g, const Sched& S, const Epi& E) {
;     ...
;             PG8_LDB(B0, 0, 0); PG8_LDB(B1, 0, 1); PG8_SCHED; PG8_LDA(At, 0, 0); PG8_STAGE_A(PG8_SA(1, 1), vc10, vc11, kb1);
;             PG8_WAIT_V(8); PG8_WAIT_L(0); PG8_BAR; PG8_MMA(0, 0, At, B0); PG8_MMA(0, 1, At, B1); PG8_BAR; PG8_SCHED;
;             PG8_LDA(At, 0, 1); PG8_STAGE_B(PG8_SB(0, 0), b2); PG8_STAGE_B(PG8_SB(0, 1), b2 + hstepB); PG8_STAGE_A(PG8_SA(0, 0), s00, s01, kb2);
;             PG8_WAIT_V(8); PG8_WAIT_L(0); PG8_BAR; if (half1) { PG8_MMA(1, 0, At, B0); PG8_MMA(1, 1, At, B1); } PG8_BAR; PG8_SCHED;
;             PG8_LDB(B0, 1, 0); PG8_LDB(B1, 1, 1); PG8_SCHED; PG8_LDA(At, 1, 0); PG8_STAGE_A(PG8_SA(0, 1), s10, s11, kb2);
;             PG8_WAIT_V(8); PG8_WAIT_L(0); PG8_BAR; PG8_MMA(0, 0, At, B0); PG8_MMA(0, 1, At, B1); PG8_BAR; PG8_SCHED;
;             PG8_LDA(At, 1, 1); PG8_STAGE_B(PG8_SB(1, 0), b3); PG8_STAGE_B(PG8_SB(1, 1), b3 + hstepB); PG8_STAGE_A(PG8_SA(1, 0), s00, s01, kb3);
;             PG8_WAIT_V(8); PG8_WAIT_L(0); PG8_BAR; if (half1) { PG8_MMA(1, 0, At, B0); PG8_MMA(1, 1, At, B1); } PG8_BAR; PG8_SCHED;
.LBB0_3849:
	v_add_u32_e32 v5, s46, v223
	ds_read_b128 v[150:153], v5
	ds_read_b128 v[154:157], v5 offset:1024
	ds_read_b128 v[158:161], v5 offset:2048
	ds_read_b128 v[162:165], v5 offset:3072
	v_add_u32_e32 v5, s47, v223
	ds_read_b128 v[134:137], v5
	ds_read_b128 v[138:141], v5 offset:1024
	ds_read_b128 v[142:145], v5 offset:2048
	ds_read_b128 v[146:149], v5 offset:3072
	v_lshl_add_u64 v[216:217], v[214:215], 0, s[4:5]
	s_add_i32 m0, s7, 0xc000
	s_waitcnt lgkmcnt(0)
	ds_read_b128 v[166:169], v227
	ds_read_b128 v[170:173], v227 offset:1024
	ds_read_b128 v[174:177], v227 offset:2048
	ds_read_b128 v[178:181], v227 offset:3072
	ds_read_b128 v[182:185], v227 offset:4096
	ds_read_b128 v[186:189], v227 offset:5120
	ds_read_b128 v[190:193], v227 offset:6144
	ds_read_b128 v[194:197], v227 offset:7168
	global_load_lds_dwordx4 v[216:217], off
	v_lshl_add_u64 v[216:217], v[212:213], 0, s[4:5]
	s_add_i32 m0, s7, 0xe000
	s_nop 0
	global_load_lds_dwordx4 v[216:217], off
	s_waitcnt vmcnt(8)
	s_waitcnt lgkmcnt(0)
	s_barrier
	s_waitcnt lgkmcnt(0)
	v_mfma_f32_16x16x32_bf16 v[130:133], v[150:153], v[166:169], v[130:133]
	v_mfma_f32_16x16x32_bf16 v[126:129], v[158:161], v[166:169], v[126:129]
	v_mfma_f32_16x16x32_bf16 v[114:117], v[150:153], v[174:177], v[114:117]
	v_mfma_f32_16x16x32_bf16 v[110:113], v[158:161], v[174:177], v[110:113]
	v_mfma_f32_16x16x32_bf16 v[98:101], v[150:153], v[182:185], v[98:101]
	v_mfma_f32_16x16x32_bf16 v[94:97], v[158:161], v[182:185], v[94:97]
	v_mfma_f32_16x16x32_bf16 v[82:85], v[150:153], v[190:193], v[82:85]
	v_mfma_f32_16x16x32_bf16 v[78:81], v[158:161], v[190:193], v[78:81]
	v_mfma_f32_16x16x32_bf16 v[130:133], v[154:157], v[170:173], v[130:133]
	v_mfma_f32_16x16x32_bf16 v[126:129], v[162:165], v[170:173], v[126:129]
	v_mfma_f32_16x16x32_bf16 v[114:117], v[154:157], v[178:181], v[114:117]
	v_mfma_f32_16x16x32_bf16 v[110:113], v[162:165], v[178:181], v[110:113]
	v_mfma_f32_16x16x32_bf16 v[98:101], v[154:157], v[186:189], v[98:101]
	v_mfma_f32_16x16x32_bf16 v[94:97], v[162:165], v[186:189], v[94:97]
	v_mfma_f32_16x16x32_bf16 v[82:85], v[154:157], v[194:197], v[82:85]
	v_mfma_f32_16x16x32_bf16 v[78:81], v[162:165], v[194:197], v[78:81]
	v_mfma_f32_16x16x32_bf16 v[122:125], v[134:137], v[166:169], v[122:125]
	v_mfma_f32_16x16x32_bf16 v[118:121], v[142:145], v[166:169], v[118:121]
	v_mfma_f32_16x16x32_bf16 v[106:109], v[134:137], v[174:177], v[106:109]
	v_mfma_f32_16x16x32_bf16 v[102:105], v[142:145], v[174:177], v[102:105]
	v_mfma_f32_16x16x32_bf16 v[90:93], v[134:137], v[182:185], v[90:93]
	v_mfma_f32_16x16x32_bf16 v[86:89], v[142:145], v[182:185], v[86:89]
	v_mfma_f32_16x16x32_bf16 v[74:77], v[134:137], v[190:193], v[74:77]
	v_mfma_f32_16x16x32_bf16 v[70:73], v[142:145], v[190:193], v[70:73]
	v_mfma_f32_16x16x32_bf16 v[122:125], v[138:141], v[170:173], v[122:125]
	v_mfma_f32_16x16x32_bf16 v[118:121], v[146:149], v[170:173], v[118:121]
	v_mfma_f32_16x16x32_bf16 v[106:109], v[138:141], v[178:181], v[106:109]
	v_mfma_f32_16x16x32_bf16 v[102:105], v[146:149], v[178:181], v[102:105]
	v_mfma_f32_16x16x32_bf16 v[90:93], v[138:141], v[186:189], v[90:93]
	v_mfma_f32_16x16x32_bf16 v[86:89], v[146:149], v[186:189], v[86:89]
	v_mfma_f32_16x16x32_bf16 v[74:77], v[138:141], v[194:197], v[74:77]
	v_mfma_f32_16x16x32_bf16 v[70:73], v[146:149], v[194:197], v[70:73]
	s_barrier
	s_add_i32 s4, s46, s36
	v_lshl_add_u64 v[216:217], s[28:29], 0, v[198:199]
	s_mov_b32 m0, s4
	ds_read_b128 v[190:193], v227 offset:16384
	ds_read_b128 v[194:197], v227 offset:17408
	ds_read_b128 v[182:185], v227 offset:18432
	ds_read_b128 v[186:189], v227 offset:19456
	ds_read_b128 v[174:177], v227 offset:20480
	ds_read_b128 v[178:181], v227 offset:21504
	ds_read_b128 v[166:169], v227 offset:22528
	ds_read_b128 v[170:173], v227 offset:23552
	global_load_lds_dwordx4 v[216:217], off
	s_add_i32 m0, s4, 0x2000
	s_add_u32 s4, s28, 0x40000
	v_lshl_add_u64 v[218:219], s[28:29], 0, v[200:201]
	s_addc_u32 s5, s29, 0
	s_add_i32 s31, s47, s36
	global_load_lds_dwordx4 v[218:219], off
	v_lshl_add_u64 v[234:235], s[4:5], 0, v[198:199]
	s_mov_b32 m0, s31
	v_cndmask_b32_e64 v5, 0, 1, s[24:25]
	global_load_lds_dwordx4 v[234:235], off
	v_lshl_add_u64 v[234:235], s[4:5], 0, v[200:201]
	s_add_i32 m0, s31, 0x2000
	v_readlane_b32 s4, v255, 13
	v_readlane_b32 s5, v255, 14
	s_add_u32 s30, s4, s30
	global_load_lds_dwordx4 v[234:235], off
	s_addc_u32 s31, s5, 0
	s_mov_b32 m0, s7
	v_cmp_ne_u32_e64 s[4:5], 1, v5
	global_load_lds_dwordx4 v2, s[30:31]
	s_mov_b32 m0, s38
	s_andn2_b64 vcc, exec, s[24:25]
	global_load_lds_dwordx4 v4, s[30:31]
	s_waitcnt vmcnt(8)
	s_waitcnt lgkmcnt(0)
	s_barrier
	s_cbranch_vccnz .LBB0_3851
	s_waitcnt lgkmcnt(0)
	v_mfma_f32_16x16x32_bf16 v[66:69], v[150:153], v[190:193], v[66:69]
	v_mfma_f32_16x16x32_bf16 v[62:65], v[158:161], v[190:193], v[62:65]
	v_mfma_f32_16x16x32_bf16 v[50:53], v[150:153], v[182:185], v[50:53]
	v_mfma_f32_16x16x32_bf16 v[46:49], v[158:161], v[182:185], v[46:49]
	v_mfma_f32_16x16x32_bf16 v[34:37], v[150:153], v[174:177], v[34:37]
	v_mfma_f32_16x16x32_bf16 v[30:33], v[158:161], v[174:177], v[30:33]
	v_mfma_f32_16x16x32_bf16 v[18:21], v[150:153], v[166:169], v[18:21]
	v_mfma_f32_16x16x32_bf16 v[14:17], v[158:161], v[166:169], v[14:17]
	v_mfma_f32_16x16x32_bf16 v[66:69], v[154:157], v[194:197], v[66:69]
	v_mfma_f32_16x16x32_bf16 v[62:65], v[162:165], v[194:197], v[62:65]
	v_mfma_f32_16x16x32_bf16 v[50:53], v[154:157], v[186:189], v[50:53]
	v_mfma_f32_16x16x32_bf16 v[46:49], v[162:165], v[186:189], v[46:49]
	v_mfma_f32_16x16x32_bf16 v[34:37], v[154:157], v[178:181], v[34:37]
	v_mfma_f32_16x16x32_bf16 v[30:33], v[162:165], v[178:181], v[30:33]
	v_mfma_f32_16x16x32_bf16 v[18:21], v[154:157], v[170:173], v[18:21]
	v_mfma_f32_16x16x32_bf16 v[14:17], v[162:165], v[170:173], v[14:17]
	v_mfma_f32_16x16x32_bf16 v[58:61], v[134:137], v[190:193], v[58:61]
	v_mfma_f32_16x16x32_bf16 v[54:57], v[142:145], v[190:193], v[54:57]
	v_mfma_f32_16x16x32_bf16 v[42:45], v[134:137], v[182:185], v[42:45]
	v_mfma_f32_16x16x32_bf16 v[38:41], v[142:145], v[182:185], v[38:41]
	v_mfma_f32_16x16x32_bf16 v[26:29], v[134:137], v[174:177], v[26:29]
	v_mfma_f32_16x16x32_bf16 v[22:25], v[142:145], v[174:177], v[22:25]
	v_mfma_f32_16x16x32_bf16 v[10:13], v[134:137], v[166:169], v[10:13]
	v_mfma_f32_16x16x32_bf16 v[6:9], v[142:145], v[166:169], v[6:9]
	v_mfma_f32_16x16x32_bf16 v[58:61], v[138:141], v[194:197], v[58:61]
	v_mfma_f32_16x16x32_bf16 v[54:57], v[146:149], v[194:197], v[54:57]
	v_mfma_f32_16x16x32_bf16 v[42:45], v[138:141], v[186:189], v[42:45]
	v_mfma_f32_16x16x32_bf16 v[38:41], v[146:149], v[186:189], v[38:41]
	v_mfma_f32_16x16x32_bf16 v[26:29], v[138:141], v[178:181], v[26:29]
	v_mfma_f32_16x16x32_bf16 v[22:25], v[146:149], v[178:181], v[22:25]
	v_mfma_f32_16x16x32_bf16 v[10:13], v[138:141], v[170:173], v[10:13]
	v_mfma_f32_16x16x32_bf16 v[6:9], v[146:149], v[170:173], v[6:9]
; #define PG8_STAGE_B(bufoff, gbase) do { _Pragma("unroll") for (int _i = 0; _i < 2; ++_i) \
;         __builtin_amdgcn_global_load_lds((const unsigned*)((const char*)(gbase) + voffB[_i]), (LAS unsigned*)(lds + (bufoff) + ldsw + _i * 8192), 16, 0, 0); } while (0)
; #define PG8_STAGE_A(bufoff, V0, V1, kb) do { \
;         __builtin_amdgcn_global_load_lds((const unsigned*)((Abase + (kb)) + (V0)), (LAS unsigned*)(lds + (bufoff) + ldsw), 16, 0, 0); \
;         __builtin_amdgcn_global_load_lds((const unsigned*)((Abase + (kb)) + (V1)), (LAS unsigned*)(lds + (bufoff) + ldsw + 8192), 16, 0, 0); } while (0)
; #define PG8_LDA(dst, b, h) do { _Pragma("unroll") for (int m = 0; m < 4; ++m) _Pragma("unroll") for (int k = 0; k < 2; ++k) dst[m][k] = *(const LAS bf16x8*)(lds + PG8_SA(b, h) + aoff + m * 2048 + k * 1024); } while (0)
; #define PG8_LDB(dst, b, h) do { _Pragma("unroll") for (int n = 0; n < 2; ++n) _Pragma("unroll") for (int k = 0; k < 2; ++k) dst[n][k] = *(const LAS bf16x8*)(lds + PG8_SB(b, h) + boff + n * 2048 + k * 1024); } while (0)
; #define PG8_WAIT_V(n) asm volatile("s_waitcnt vmcnt(" #n ")" ::: "memory")
; #define PG8_BAR __builtin_amdgcn_s_barrier()
; template <class Epi, class Sched, bool ALIGN_EPI>
; __device__ __forceinline__ void gemm_phase(LAS unsigned char* lds, const Gemm g, const Sched& S, const Epi& E) {
;     ...
;             PG8_LDB(B0, 0, 0); PG8_LDB(B1, 0, 1); PG8_SCHED; PG8_LDA(At, 0, 0); PG8_STAGE_A(PG8_SA(1, 1), vc10, vc11, kb1);
;             PG8_WAIT_V(8); PG8_WAIT_L(0); PG8_BAR; PG8_MMA(0, 0, At, B0); PG8_MMA(0, 1, At, B1); PG8_BAR; PG8_SCHED;
;             PG8_LDA(At, 0, 1); PG8_STAGE_B(PG8_SB(0, 0), b2); PG8_STAGE_B(PG8_SB(0, 1), b2 + hstepB); PG8_STAGE_A(PG8_SA(0, 0), s00, s01, kb2);
;             PG8_WAIT_V(8); PG8_WAIT_L(0); PG8_BAR; if (half1) { PG8_MMA(1, 0, At, B0); PG8_MMA(1, 1, At, B1); } PG8_BAR; PG8_SCHED;
;             PG8_LDB(B0, 1, 0); PG8_LDB(B1, 1, 1); PG8_SCHED; PG8_LDA(At, 1, 0); PG8_STAGE_A(PG8_SA(0, 1), s10, s11, kb2);
;             PG8_WAIT_V(8); PG8_WAIT_L(0); PG8_BAR; PG8_MMA(0, 0, At, B0); PG8_MMA(0, 1, At, B1); PG8_BAR; PG8_SCHED;
;             PG8_LDA(At, 1, 1); PG8_STAGE_B(PG8_SB(1, 0), b3); PG8_STAGE_B(PG8_SB(1, 1), b3 + hstepB); PG8_STAGE_A(PG8_SA(1, 0), s00, s01, kb3);
;             PG8_WAIT_V(8); PG8_WAIT_L(0); PG8_BAR; if (half1) { PG8_MMA(1, 0, At, B0); PG8_MMA(1, 1, At, B1); } PG8_BAR; PG8_SCHED;
.LBB0_3851:
	v_mov_b32_e32 v5, v3
	v_lshl_add_u64 v[234:235], s[30:31], 0, v[2:3]
	v_lshl_add_u64 v[4:5], s[30:31], 0, v[4:5]
	s_barrier
	v_add_u32_e32 v2, s48, v223
	ds_read_b128 v[150:153], v2
	ds_read_b128 v[154:157], v2 offset:1024
	ds_read_b128 v[158:161], v2 offset:2048
	ds_read_b128 v[162:165], v2 offset:3072
	v_add_u32_e32 v2, s49, v223
	ds_read_b128 v[134:137], v2
	ds_read_b128 v[138:141], v2 offset:1024
	ds_read_b128 v[142:145], v2 offset:2048
	ds_read_b128 v[146:149], v2 offset:3072
	s_mov_b32 m0, s39
	s_waitcnt lgkmcnt(0)
	ds_read_b128 v[166:169], v227 offset:32768
	ds_read_b128 v[170:173], v227 offset:33792
	ds_read_b128 v[174:177], v227 offset:34816
	ds_read_b128 v[178:181], v227 offset:35840
	ds_read_b128 v[182:185], v227 offset:36864
	ds_read_b128 v[186:189], v227 offset:37888
	ds_read_b128 v[190:193], v227 offset:38912
	ds_read_b128 v[194:197], v227 offset:39936
	global_load_lds_dwordx4 v209, s[30:31]
	s_mov_b32 m0, s40
	s_nop 0
	global_load_lds_dwordx4 v211, s[30:31]
	s_waitcnt vmcnt(8)
	s_waitcnt lgkmcnt(0)
	s_barrier
	s_waitcnt lgkmcnt(0)
	v_mfma_f32_16x16x32_bf16 v[130:133], v[150:153], v[166:169], v[130:133]
	v_mfma_f32_16x16x32_bf16 v[126:129], v[158:161], v[166:169], v[126:129]
	v_mfma_f32_16x16x32_bf16 v[114:117], v[150:153], v[174:177], v[114:117]
	v_mfma_f32_16x16x32_bf16 v[110:113], v[158:161], v[174:177], v[110:113]
	v_mfma_f32_16x16x32_bf16 v[98:101], v[150:153], v[182:185], v[98:101]
	v_mfma_f32_16x16x32_bf16 v[94:97], v[158:161], v[182:185], v[94:97]
	v_mfma_f32_16x16x32_bf16 v[82:85], v[150:153], v[190:193], v[82:85]
	v_mfma_f32_16x16x32_bf16 v[78:81], v[158:161], v[190:193], v[78:81]
	v_mfma_f32_16x16x32_bf16 v[130:133], v[154:157], v[170:173], v[130:133]
	v_mfma_f32_16x16x32_bf16 v[126:129], v[162:165], v[170:173], v[126:129]
	v_mfma_f32_16x16x32_bf16 v[114:117], v[154:157], v[178:181], v[114:117]
	v_mfma_f32_16x16x32_bf16 v[110:113], v[162:165], v[178:181], v[110:113]
	v_mfma_f32_16x16x32_bf16 v[98:101], v[154:157], v[186:189], v[98:101]
	v_mfma_f32_16x16x32_bf16 v[94:97], v[162:165], v[186:189], v[94:97]
	v_mfma_f32_16x16x32_bf16 v[82:85], v[154:157], v[194:197], v[82:85]
	v_mfma_f32_16x16x32_bf16 v[78:81], v[162:165], v[194:197], v[78:81]
	v_mfma_f32_16x16x32_bf16 v[122:125], v[134:137], v[166:169], v[122:125]
	v_mfma_f32_16x16x32_bf16 v[118:121], v[142:145], v[166:169], v[118:121]
	v_mfma_f32_16x16x32_bf16 v[106:109], v[134:137], v[174:177], v[106:109]
	v_mfma_f32_16x16x32_bf16 v[102:105], v[142:145], v[174:177], v[102:105]
	v_mfma_f32_16x16x32_bf16 v[90:93], v[134:137], v[182:185], v[90:93]
	v_mfma_f32_16x16x32_bf16 v[86:89], v[142:145], v[182:185], v[86:89]
	v_mfma_f32_16x16x32_bf16 v[74:77], v[134:137], v[190:193], v[74:77]
	v_mfma_f32_16x16x32_bf16 v[70:73], v[142:145], v[190:193], v[70:73]
	v_mfma_f32_16x16x32_bf16 v[122:125], v[138:141], v[170:173], v[122:125]
	v_mfma_f32_16x16x32_bf16 v[118:121], v[146:149], v[170:173], v[118:121]
	v_mfma_f32_16x16x32_bf16 v[106:109], v[138:141], v[178:181], v[106:109]
	v_mfma_f32_16x16x32_bf16 v[102:105], v[146:149], v[178:181], v[102:105]
	v_mfma_f32_16x16x32_bf16 v[90:93], v[138:141], v[186:189], v[90:93]
	v_mfma_f32_16x16x32_bf16 v[86:89], v[146:149], v[186:189], v[86:89]
	v_mfma_f32_16x16x32_bf16 v[74:77], v[138:141], v[194:197], v[74:77]
	v_mfma_f32_16x16x32_bf16 v[70:73], v[146:149], v[194:197], v[70:73]
	s_barrier
	s_add_i32 s30, s48, s36
	v_lshl_add_u64 v[216:217], v[216:217], 0, s[8:9]
	s_mov_b32 m0, s30
	ds_read_b128 v[190:193], v227 offset:49152
	ds_read_b128 v[194:197], v227 offset:50176
	ds_read_b128 v[182:185], v227 offset:51200
	ds_read_b128 v[186:189], v227 offset:52224
	ds_read_b128 v[174:177], v227 offset:53248
	ds_read_b128 v[178:181], v227 offset:54272
	ds_read_b128 v[166:169], v227 offset:55296
	ds_read_b128 v[170:173], v227 offset:56320
	global_load_lds_dwordx4 v[216:217], off
	s_add_i32 m0, s30, 0x2000
	s_add_u32 s28, s28, 0x40080
	v_lshl_add_u64 v[216:217], v[218:219], 0, s[8:9]
	s_addc_u32 s29, s29, 0
	s_add_i32 s30, s49, s36
	global_load_lds_dwordx4 v[216:217], off
	v_lshl_add_u64 v[216:217], s[28:29], 0, v[198:199]
	s_mov_b32 m0, s30
	v_lshl_add_u64 v[4:5], v[4:5], 0, s[8:9]
	global_load_lds_dwordx4 v[216:217], off
	v_lshl_add_u64 v[216:217], s[28:29], 0, v[200:201]
	s_add_i32 m0, s30, 0x2000
	s_and_b64 vcc, exec, s[4:5]
	global_load_lds_dwordx4 v[216:217], off
	v_lshl_add_u64 v[216:217], v[234:235], 0, s[8:9]
	s_mov_b32 m0, s41
	s_nop 0
	global_load_lds_dwordx4 v[216:217], off
	s_mov_b32 m0, s42
	s_nop 0
	global_load_lds_dwordx4 v[4:5], off
	s_waitcnt vmcnt(8)
	s_waitcnt lgkmcnt(0)
	s_barrier
	s_cbranch_vccnz .LBB0_3853
	s_waitcnt lgkmcnt(0)
	v_mfma_f32_16x16x32_bf16 v[66:69], v[150:153], v[190:193], v[66:69]
	v_mfma_f32_16x16x32_bf16 v[62:65], v[158:161], v[190:193], v[62:65]
	v_mfma_f32_16x16x32_bf16 v[50:53], v[150:153], v[182:185], v[50:53]
	v_mfma_f32_16x16x32_bf16 v[46:49], v[158:161], v[182:185], v[46:49]
	v_mfma_f32_16x16x32_bf16 v[34:37], v[150:153], v[174:177], v[34:37]
	v_mfma_f32_16x16x32_bf16 v[30:33], v[158:161], v[174:177], v[30:33]
	v_mfma_f32_16x16x32_bf16 v[18:21], v[150:153], v[166:169], v[18:21]
	v_mfma_f32_16x16x32_bf16 v[14:17], v[158:161], v[166:169], v[14:17]
	v_mfma_f32_16x16x32_bf16 v[66:69], v[154:157], v[194:197], v[66:69]
	v_mfma_f32_16x16x32_bf16 v[62:65], v[162:165], v[194:197], v[62:65]
	v_mfma_f32_16x16x32_bf16 v[50:53], v[154:157], v[186:189], v[50:53]
	v_mfma_f32_16x16x32_bf16 v[46:49], v[162:165], v[186:189], v[46:49]
	v_mfma_f32_16x16x32_bf16 v[34:37], v[154:157], v[178:181], v[34:37]
	v_mfma_f32_16x16x32_bf16 v[30:33], v[162:165], v[178:181], v[30:33]
	v_mfma_f32_16x16x32_bf16 v[18:21], v[154:157], v[170:173], v[18:21]
	v_mfma_f32_16x16x32_bf16 v[14:17], v[162:165], v[170:173], v[14:17]
	v_mfma_f32_16x16x32_bf16 v[58:61], v[134:137], v[190:193], v[58:61]
	v_mfma_f32_16x16x32_bf16 v[54:57], v[142:145], v[190:193], v[54:57]
	v_mfma_f32_16x16x32_bf16 v[42:45], v[134:137], v[182:185], v[42:45]
	v_mfma_f32_16x16x32_bf16 v[38:41], v[142:145], v[182:185], v[38:41]
	v_mfma_f32_16x16x32_bf16 v[26:29], v[134:137], v[174:177], v[26:29]
	v_mfma_f32_16x16x32_bf16 v[22:25], v[142:145], v[174:177], v[22:25]
	v_mfma_f32_16x16x32_bf16 v[10:13], v[134:137], v[166:169], v[10:13]
	v_mfma_f32_16x16x32_bf16 v[4:7], v[142:145], v[166:169], v[6:9]
	v_mfma_f32_16x16x32_bf16 v[58:61], v[138:141], v[194:197], v[58:61]
	v_mfma_f32_16x16x32_bf16 v[54:57], v[146:149], v[194:197], v[54:57]
	v_mfma_f32_16x16x32_bf16 v[42:45], v[138:141], v[186:189], v[42:45]
	v_mfma_f32_16x16x32_bf16 v[38:41], v[146:149], v[186:189], v[38:41]
	v_mfma_f32_16x16x32_bf16 v[26:29], v[138:141], v[178:181], v[26:29]
	v_mfma_f32_16x16x32_bf16 v[22:25], v[146:149], v[178:181], v[22:25]
	v_mfma_f32_16x16x32_bf16 v[10:13], v[138:141], v[170:173], v[10:13]
	v_mfma_f32_16x16x32_bf16 v[6:9], v[146:149], v[170:173], v[4:7]

; #define PG8_BWAIT(n) asm volatile("s_waitcnt vmcnt(" #n ")" : "+v"(bv[0]), "+v"(bv[1]), "+v"(bv[2]), "+v"(bv[3]), "+v"(bv[4]), "+v"(bv[5]), "+v"(bv[6]), "+v"(bv[7]) :: "memory")
; #define PG8_STAGE_A(bufoff, V0, V1, kb) do { \
;         __builtin_amdgcn_global_load_lds((const unsigned*)((Abase + (kb)) + (V0)), (LAS unsigned*)(lds + (bufoff) + ldsw), 16, 0, 0); \
;         __builtin_amdgcn_global_load_lds((const unsigned*)((Abase + (kb)) + (V1)), (LAS unsigned*)(lds + (bufoff) + ldsw + 8192), 16, 0, 0); } while (0)
; #define PG8_LDA(dst, b, h) do { _Pragma("unroll") for (int m = 0; m < 4; ++m) _Pragma("unroll") for (int k = 0; k < 2; ++k) dst[m][k] = *(const LAS bf16x8*)(lds + PG8_SA(b, h) + aoff + m * 2048 + k * 1024); } while (0)
; #define PG8_LDB(dst, b, h) do { _Pragma("unroll") for (int n = 0; n < 2; ++n) _Pragma("unroll") for (int k = 0; k < 2; ++k) dst[n][k] = *(const LAS bf16x8*)(lds + PG8_SB(b, h) + boff + n * 2048 + k * 1024); } while (0)
; #define PG8_MMA(ai, bj, At, Bt) do { __builtin_amdgcn_s_setprio(1); _Pragma("unroll") for (int m = 0; m < 4; ++m) _Pragma("unroll") for (int n = 0; n < 2; ++n) _Pragma("unroll") for (int k = 0; k < 2; ++k) \
;         acc[ai][bj][m][n] = __builtin_amdgcn_mfma_f32_16x16x32_bf16(Bt[n][k], At[m][k], acc[ai][bj][m][n], 0, 0, 0); __builtin_amdgcn_s_setprio(0); } while (0)
; #define PG8_WAIT_V(n) asm volatile("s_waitcnt vmcnt(" #n ")" ::: "memory")
; #define PG8_WAIT_L(n) asm volatile("s_waitcnt lgkmcnt(" #n ")" ::: "memory")
; #define PG8_BAR __builtin_amdgcn_s_barrier()
; template <class Epi, class Sched, bool ALIGN_EPI>
; __device__ __forceinline__ void gemm_phase(LAS unsigned char* lds, const Gemm g, const Sched& S, const Epi& E) {
;     ...
;             PG8_LDB(B0, 0, 0); PG8_LDB(B1, 0, 1); PG8_SCHED; PG8_LDA(At, 0, 0); PG8_STAGE_A(PG8_SA(1, 1), vc10, vc11, kb1);
;             PG8_WAIT_V(12); PG8_WAIT_L(0); PG8_BAR; PG8_MMA(0, 0, At, B0); PG8_MMA(0, 1, At, B1); PG8_BAR; PG8_SCHED;
;             if (last) { vc10 = vn10; vc11 = vn11; }
;             PG8_BWAIT(2); PG8_BCOMMIT(0); PG8_SCHED; PG8_LDA(At, 0, 1); PG8_BISSUE(t + 3 >= nt ? pbn + (size_t)(t + 3 - nt) * 64 * Sched::LDN : pbc + (size_t)(t + 3) * 64 * Sched::LDN); PG8_STAGE_A(PG8_SA(0, 0), vc00, vc01, kb2);
;             PG8_WAIT_V(12); PG8_WAIT_L(0); PG8_BAR; if (half1) { PG8_MMA(1, 0, At, B0); PG8_MMA(1, 1, At, B1); } PG8_BAR; PG8_SCHED;
.LBB0_4711:
	v_add_u32_e32 v162, 0x10000, v240
	v_add_u32_e32 v174, 0x14000, v240
	ds_read_b128 v[178:181], v162
	ds_read_b128 v[182:185], v162 offset:1024
	ds_read_b128 v[186:189], v162 offset:2048
	ds_read_b128 v[190:193], v162 offset:3072
	ds_read_b128 v[162:165], v174
	ds_read_b128 v[166:169], v174 offset:1024
	ds_read_b128 v[170:173], v174 offset:2048
	ds_read_b128 v[174:177], v174 offset:3072
	s_add_i32 s54, s53, 2
	s_add_i32 m0, s40, 0xc000
	s_add_u32 s2, s90, s22
	s_addc_u32 s3, s91, s23
	s_waitcnt lgkmcnt(0)
	ds_read_b128 v[194:197], v241
	ds_read_b128 v[198:201], v241 offset:1024
	ds_read_b128 v[202:205], v241 offset:2048
	ds_read_b128 v[206:209], v241 offset:3072
	ds_read_b128 v[210:213], v241 offset:4096
	ds_read_b128 v[214:217], v241 offset:5120
	ds_read_b128 v[218:221], v241 offset:6144
	ds_read_b128 v[222:225], v241 offset:7168
	global_load_lds_dwordx4 v233, s[2:3]
	s_add_i32 m0, s40, 0xe000
	s_nop 0
	global_load_lds_dwordx4 v234, s[2:3]
	s_waitcnt vmcnt(12)
	s_waitcnt lgkmcnt(0)
	s_barrier
	s_waitcnt lgkmcnt(0)
	v_mfma_f32_16x16x32_bf16 v[158:161], v[178:181], v[194:197], v[158:161]
	v_mfma_f32_16x16x32_bf16 v[154:157], v[186:189], v[194:197], v[154:157]
	v_mfma_f32_16x16x32_bf16 v[142:145], v[178:181], v[202:205], v[142:145]
	v_mfma_f32_16x16x32_bf16 v[138:141], v[186:189], v[202:205], v[138:141]
	v_mfma_f32_16x16x32_bf16 v[126:129], v[178:181], v[210:213], v[126:129]
	v_mfma_f32_16x16x32_bf16 v[122:125], v[186:189], v[210:213], v[122:125]
	v_mfma_f32_16x16x32_bf16 v[110:113], v[178:181], v[218:221], v[110:113]
	v_mfma_f32_16x16x32_bf16 v[106:109], v[186:189], v[218:221], v[106:109]
	v_mfma_f32_16x16x32_bf16 v[158:161], v[182:185], v[198:201], v[158:161]
	v_mfma_f32_16x16x32_bf16 v[154:157], v[190:193], v[198:201], v[154:157]
	v_mfma_f32_16x16x32_bf16 v[142:145], v[182:185], v[206:209], v[142:145]
	v_mfma_f32_16x16x32_bf16 v[138:141], v[190:193], v[206:209], v[138:141]
	v_mfma_f32_16x16x32_bf16 v[126:129], v[182:185], v[214:217], v[126:129]
	v_mfma_f32_16x16x32_bf16 v[122:125], v[190:193], v[214:217], v[122:125]
	v_mfma_f32_16x16x32_bf16 v[110:113], v[182:185], v[222:225], v[110:113]
	v_mfma_f32_16x16x32_bf16 v[106:109], v[190:193], v[222:225], v[106:109]
	v_mfma_f32_16x16x32_bf16 v[150:153], v[162:165], v[194:197], v[150:153]
	v_mfma_f32_16x16x32_bf16 v[146:149], v[170:173], v[194:197], v[146:149]
	v_mfma_f32_16x16x32_bf16 v[134:137], v[162:165], v[202:205], v[134:137]
	v_mfma_f32_16x16x32_bf16 v[130:133], v[170:173], v[202:205], v[130:133]
	v_mfma_f32_16x16x32_bf16 v[118:121], v[162:165], v[210:213], v[118:121]
	v_mfma_f32_16x16x32_bf16 v[114:117], v[170:173], v[210:213], v[114:117]
	v_mfma_f32_16x16x32_bf16 v[102:105], v[162:165], v[218:221], v[102:105]
	v_mfma_f32_16x16x32_bf16 v[98:101], v[170:173], v[218:221], v[98:101]
	v_mfma_f32_16x16x32_bf16 v[150:153], v[166:169], v[198:201], v[150:153]
	v_mfma_f32_16x16x32_bf16 v[146:149], v[174:177], v[198:201], v[146:149]
	v_mfma_f32_16x16x32_bf16 v[134:137], v[166:169], v[206:209], v[134:137]
	v_mfma_f32_16x16x32_bf16 v[130:133], v[174:177], v[206:209], v[130:133]
	v_mfma_f32_16x16x32_bf16 v[118:121], v[166:169], v[214:217], v[118:121]
	v_mfma_f32_16x16x32_bf16 v[114:117], v[174:177], v[214:217], v[114:117]
	v_mfma_f32_16x16x32_bf16 v[102:105], v[166:169], v[222:225], v[102:105]
	v_mfma_f32_16x16x32_bf16 v[98:101], v[174:177], v[222:225], v[98:101]
	s_barrier
	s_cmp_lt_u32 s54, 13
	s_mov_b64 s[4:5], -1
	s_cbranch_scc0 .LBB0_4713
	s_add_u32 s2, s20, 0x30000
	s_addc_u32 s3, s21, 0
	s_mov_b64 s[4:5], 0

; #define PG8_BWAIT(n) asm volatile("s_waitcnt vmcnt(" #n ")" : "+v"(bv[0]), "+v"(bv[1]), "+v"(bv[2]), "+v"(bv[3]), "+v"(bv[4]), "+v"(bv[5]), "+v"(bv[6]), "+v"(bv[7]) :: "memory")
; #define PG8_STAGE_A(bufoff, V0, V1, kb) do { \
;         __builtin_amdgcn_global_load_lds((const unsigned*)((Abase + (kb)) + (V0)), (LAS unsigned*)(lds + (bufoff) + ldsw), 16, 0, 0); \
;         __builtin_amdgcn_global_load_lds((const unsigned*)((Abase + (kb)) + (V1)), (LAS unsigned*)(lds + (bufoff) + ldsw + 8192), 16, 0, 0); } while (0)
; #define PG8_LDA(dst, b, h) do { _Pragma("unroll") for (int m = 0; m < 4; ++m) _Pragma("unroll") for (int k = 0; k < 2; ++k) dst[m][k] = *(const LAS bf16x8*)(lds + PG8_SA(b, h) + aoff + m * 2048 + k * 1024); } while (0)
; #define PG8_LDB(dst, b, h) do { _Pragma("unroll") for (int n = 0; n < 2; ++n) _Pragma("unroll") for (int k = 0; k < 2; ++k) dst[n][k] = *(const LAS bf16x8*)(lds + PG8_SB(b, h) + boff + n * 2048 + k * 1024); } while (0)
; #define PG8_MMA(ai, bj, At, Bt) do { __builtin_amdgcn_s_setprio(1); _Pragma("unroll") for (int m = 0; m < 4; ++m) _Pragma("unroll") for (int n = 0; n < 2; ++n) _Pragma("unroll") for (int k = 0; k < 2; ++k) \
;         acc[ai][bj][m][n] = __builtin_amdgcn_mfma_f32_16x16x32_bf16(Bt[n][k], At[m][k], acc[ai][bj][m][n], 0, 0, 0); __builtin_amdgcn_s_setprio(0); } while (0)
; #define PG8_WAIT_V(n) asm volatile("s_waitcnt vmcnt(" #n ")" ::: "memory")
; #define PG8_WAIT_L(n) asm volatile("s_waitcnt lgkmcnt(" #n ")" ::: "memory")
; #define PG8_BAR __builtin_amdgcn_s_barrier()
; #define PG8_SCHED __builtin_amdgcn_sched_barrier(0)
; template <class Epi, class Sched, bool ALIGN_EPI>
; __device__ __forceinline__ void gemm_phase(LAS unsigned char* lds, const Gemm g, const Sched& S, const Epi& E) {
;     ...
;             PG8_BWAIT(2); PG8_BCOMMIT(0); PG8_SCHED; PG8_LDA(At, 0, 1); PG8_BISSUE(t + 3 >= nt ? pbn + (size_t)(t + 3 - nt) * 64 * Sched::LDN : pbc + (size_t)(t + 3) * 64 * Sched::LDN); PG8_STAGE_A(PG8_SA(0, 0), vc00, vc01, kb2);
;             PG8_WAIT_V(12); PG8_WAIT_L(0); PG8_BAR; if (half1) { PG8_MMA(1, 0, At, B0); PG8_MMA(1, 1, At, B1); } PG8_BAR; PG8_SCHED;
;             PG8_LDB(B0, 1, 0); PG8_LDB(B1, 1, 1); PG8_SCHED; PG8_LDA(At, 1, 0); PG8_STAGE_A(PG8_SA(0, 1), vc10, vc11, kb2);
.LBB0_4715:
	s_add_i32 s8, s22, 0xe8940080
	s_cmp_eq_u32 s53, 12
	s_waitcnt vmcnt(2)
	s_nop 0
	v_cvt_pk_bf16_f32 v194, v2, v6
	v_cvt_pk_bf16_f32 v198, v3, v7
	v_cvt_pk_bf16_f32 v202, v4, v8
	v_cvt_pk_bf16_f32 v206, v5, v9
	global_load_dwordx4 v[2:5], v232, s[2:3] offset:0
	s_cselect_b64 s[4:5], -1, 0
	global_load_dwordx4 v[6:9], v232, s[2:3] offset:0x400
	v_cvt_pk_bf16_f32 v195, v10, v14
	v_cvt_pk_bf16_f32 v199, v11, v15
	v_cvt_pk_bf16_f32 v203, v12, v16
	v_cvt_pk_bf16_f32 v207, v13, v17
	s_and_b64 s[26:27], s[4:5], exec
	global_load_dwordx4 v[10:13], v232, s[2:3] offset:0x800
	s_cselect_b32 s8, 0, s8
	global_load_dwordx4 v[14:17], v232, s[2:3] offset:0xc00
	v_cvt_pk_bf16_f32 v196, v18, v22
	v_cvt_pk_bf16_f32 v200, v19, v23
	v_cvt_pk_bf16_f32 v204, v20, v24
	v_cvt_pk_bf16_f32 v208, v21, v25
	s_add_u32 s2, s2, 0x1000
	s_addc_u32 s3, s3, 0
	global_load_dwordx4 v[18:21], v232, s[2:3] offset:0
	global_load_dwordx4 v[22:25], v232, s[2:3] offset:0x400
	v_cvt_pk_bf16_f32 v197, v26, v30
	v_cvt_pk_bf16_f32 v201, v27, v31
	v_cvt_pk_bf16_f32 v205, v28, v32
	v_cvt_pk_bf16_f32 v209, v29, v33
	global_load_dwordx4 v[26:29], v232, s[2:3] offset:0x800
	global_load_dwordx4 v[30:33], v232, s[2:3] offset:0xc00
	v_add_u32_e32 v210, 0x10000, v235
	v_xor_b32_e32 v211, 64, v210
	v_xor_b32_e32 v212, 0x80, v210
	v_xor_b32_e32 v213, 0xc0, v210
	ds_write_b128 v210, v[194:197]
	ds_write_b128 v211, v[198:201]
	ds_write_b128 v212, v[202:205]
	ds_write_b128 v213, v[206:209]
	ds_read_b128 v[218:221], v241 offset:16384
	ds_read_b128 v[222:225], v241 offset:17408
	ds_read_b128 v[210:213], v241 offset:18432
	ds_read_b128 v[214:217], v241 offset:19456
	ds_read_b128 v[202:205], v241 offset:20480
	ds_read_b128 v[206:209], v241 offset:21504
	ds_read_b128 v[194:197], v241 offset:22528
	ds_read_b128 v[198:201], v241 offset:23552
	v_readlane_b32 s2, v255, 13
	v_readlane_b32 s3, v255, 14
	s_add_u32 s26, s2, s8
	s_mov_b32 m0, s40
	v_cndmask_b32_e64 v226, v226, v242, s[4:5]
	s_addc_u32 s27, s3, 0
	v_cndmask_b32_e64 v228, v228, v243, s[4:5]
	global_load_lds_dwordx4 v226, s[26:27]
	s_mov_b32 m0, s41
	v_cndmask_b32_e64 v229, 0, 1, s[24:25]
	global_load_lds_dwordx4 v228, s[26:27]
	s_waitcnt vmcnt(12)
	s_waitcnt lgkmcnt(0)
	v_cmp_ne_u32_e64 s[2:3], 1, v229
	s_andn2_b64 vcc, exec, s[24:25]
	s_barrier
	s_cbranch_vccnz .LBB0_4717
	s_waitcnt lgkmcnt(0)
	v_mfma_f32_16x16x32_bf16 v[94:97], v[178:181], v[218:221], v[94:97]
	v_mfma_f32_16x16x32_bf16 v[90:93], v[186:189], v[218:221], v[90:93]
	v_mfma_f32_16x16x32_bf16 v[78:81], v[178:181], v[210:213], v[78:81]
	v_mfma_f32_16x16x32_bf16 v[74:77], v[186:189], v[210:213], v[74:77]
	v_mfma_f32_16x16x32_bf16 v[62:65], v[178:181], v[202:205], v[62:65]
	v_mfma_f32_16x16x32_bf16 v[58:61], v[186:189], v[202:205], v[58:61]
	v_mfma_f32_16x16x32_bf16 v[46:49], v[178:181], v[194:197], v[46:49]
	v_mfma_f32_16x16x32_bf16 v[42:45], v[186:189], v[194:197], v[42:45]
	v_mfma_f32_16x16x32_bf16 v[94:97], v[182:185], v[222:225], v[94:97]
	v_mfma_f32_16x16x32_bf16 v[90:93], v[190:193], v[222:225], v[90:93]
	v_mfma_f32_16x16x32_bf16 v[78:81], v[182:185], v[214:217], v[78:81]
	v_mfma_f32_16x16x32_bf16 v[74:77], v[190:193], v[214:217], v[74:77]
	v_mfma_f32_16x16x32_bf16 v[62:65], v[182:185], v[206:209], v[62:65]
	v_mfma_f32_16x16x32_bf16 v[58:61], v[190:193], v[206:209], v[58:61]
	v_mfma_f32_16x16x32_bf16 v[46:49], v[182:185], v[198:201], v[46:49]
	v_mfma_f32_16x16x32_bf16 v[42:45], v[190:193], v[198:201], v[42:45]
	v_mfma_f32_16x16x32_bf16 v[86:89], v[162:165], v[218:221], v[86:89]
	v_mfma_f32_16x16x32_bf16 v[82:85], v[170:173], v[218:221], v[82:85]
	v_mfma_f32_16x16x32_bf16 v[70:73], v[162:165], v[210:213], v[70:73]
	v_mfma_f32_16x16x32_bf16 v[66:69], v[170:173], v[210:213], v[66:69]
	v_mfma_f32_16x16x32_bf16 v[54:57], v[162:165], v[202:205], v[54:57]
	v_mfma_f32_16x16x32_bf16 v[50:53], v[170:173], v[202:205], v[50:53]
	v_mfma_f32_16x16x32_bf16 v[38:41], v[162:165], v[194:197], v[38:41]
	v_mfma_f32_16x16x32_bf16 v[34:37], v[170:173], v[194:197], v[34:37]
	v_mfma_f32_16x16x32_bf16 v[86:89], v[166:169], v[222:225], v[86:89]
	v_mfma_f32_16x16x32_bf16 v[82:85], v[174:177], v[222:225], v[82:85]
	v_mfma_f32_16x16x32_bf16 v[70:73], v[166:169], v[214:217], v[70:73]
	v_mfma_f32_16x16x32_bf16 v[66:69], v[174:177], v[214:217], v[66:69]
	v_mfma_f32_16x16x32_bf16 v[54:57], v[166:169], v[206:209], v[54:57]
	v_mfma_f32_16x16x32_bf16 v[50:53], v[174:177], v[206:209], v[50:53]
	v_mfma_f32_16x16x32_bf16 v[38:41], v[166:169], v[198:201], v[38:41]
	v_mfma_f32_16x16x32_bf16 v[34:37], v[174:177], v[198:201], v[34:37]
; #define PG8_BWAIT(n) asm volatile("s_waitcnt vmcnt(" #n ")" : "+v"(bv[0]), "+v"(bv[1]), "+v"(bv[2]), "+v"(bv[3]), "+v"(bv[4]), "+v"(bv[5]), "+v"(bv[6]), "+v"(bv[7]) :: "memory")
; #define PG8_STAGE_A(bufoff, V0, V1, kb) do { \
;         __builtin_amdgcn_global_load_lds((const unsigned*)((Abase + (kb)) + (V0)), (LAS unsigned*)(lds + (bufoff) + ldsw), 16, 0, 0); \
;         __builtin_amdgcn_global_load_lds((const unsigned*)((Abase + (kb)) + (V1)), (LAS unsigned*)(lds + (bufoff) + ldsw + 8192), 16, 0, 0); } while (0)
; #define PG8_LDA(dst, b, h) do { _Pragma("unroll") for (int m = 0; m < 4; ++m) _Pragma("unroll") for (int k = 0; k < 2; ++k) dst[m][k] = *(const LAS bf16x8*)(lds + PG8_SA(b, h) + aoff + m * 2048 + k * 1024); } while (0)
; #define PG8_LDB(dst, b, h) do { _Pragma("unroll") for (int n = 0; n < 2; ++n) _Pragma("unroll") for (int k = 0; k < 2; ++k) dst[n][k] = *(const LAS bf16x8*)(lds + PG8_SB(b, h) + boff + n * 2048 + k * 1024); } while (0)
; #define PG8_MMA(ai, bj, At, Bt) do { __builtin_amdgcn_s_setprio(1); _Pragma("unroll") for (int m = 0; m < 4; ++m) _Pragma("unroll") for (int n = 0; n < 2; ++n) _Pragma("unroll") for (int k = 0; k < 2; ++k) \
;         acc[ai][bj][m][n] = __builtin_amdgcn_mfma_f32_16x16x32_bf16(Bt[n][k], At[m][k], acc[ai][bj][m][n], 0, 0, 0); __builtin_amdgcn_s_setprio(0); } while (0)
; #define PG8_WAIT_V(n) asm volatile("s_waitcnt vmcnt(" #n ")" ::: "memory")
; #define PG8_WAIT_L(n) asm volatile("s_waitcnt lgkmcnt(" #n ")" ::: "memory")
; #define PG8_BAR __builtin_amdgcn_s_barrier()
; #define PG8_SCHED __builtin_amdgcn_sched_barrier(0)
; template <class Epi, class Sched, bool ALIGN_EPI>
; __device__ __forceinline__ void gemm_phase(LAS unsigned char* lds, const Gemm g, const Sched& S, const Epi& E) {
;     ...
;             PG8_LDB(B0, 1, 0); PG8_LDB(B1, 1, 1); PG8_SCHED; PG8_LDA(At, 1, 0); PG8_STAGE_A(PG8_SA(0, 1), vc10, vc11, kb2);
;             PG8_WAIT_V(12); PG8_WAIT_L(0); PG8_BAR; PG8_MMA(0, 0, At, B0); PG8_MMA(0, 1, At, B1); PG8_BAR; PG8_SCHED;
;             PG8_BWAIT(2); PG8_BCOMMIT(1); PG8_SCHED; PG8_LDA(At, 1, 1); PG8_BISSUE(t + 4 >= nt ? pbn + (size_t)(t + 4 - nt) * 64 * Sched::LDN : pbc + (size_t)(t + 4) * 64 * Sched::LDN); PG8_STAGE_A(PG8_SA(1, 0), vc00, vc01, kb2 + 128u);
;             PG8_WAIT_V(12); PG8_WAIT_L(0); PG8_BAR; if (half1) { PG8_MMA(1, 0, At, B0); PG8_MMA(1, 1, At, B1); } PG8_BAR; PG8_SCHED;
.LBB0_4717:
	v_cndmask_b32_e64 v234, v234, v245, s[4:5]
	v_cndmask_b32_e64 v233, v233, v244, s[4:5]
	s_barrier
	v_add_u32_e32 v162, 0x18000, v240
	v_add_u32_e32 v174, 0x1c000, v240
	ds_read_b128 v[178:181], v162
	ds_read_b128 v[182:185], v162 offset:1024
	ds_read_b128 v[186:189], v162 offset:2048
	ds_read_b128 v[190:193], v162 offset:3072
	ds_read_b128 v[162:165], v174
	ds_read_b128 v[166:169], v174 offset:1024
	ds_read_b128 v[170:173], v174 offset:2048
	ds_read_b128 v[174:177], v174 offset:3072
	s_mov_b32 m0, s42
	s_waitcnt lgkmcnt(0)
	ds_read_b128 v[194:197], v241 offset:32768
	ds_read_b128 v[198:201], v241 offset:33792
	ds_read_b128 v[202:205], v241 offset:34816
	ds_read_b128 v[206:209], v241 offset:35840
	ds_read_b128 v[210:213], v241 offset:36864
	ds_read_b128 v[214:217], v241 offset:37888
	ds_read_b128 v[218:221], v241 offset:38912
	ds_read_b128 v[222:225], v241 offset:39936
	global_load_lds_dwordx4 v233, s[26:27]
	s_mov_b32 m0, s43
	s_nop 0
	global_load_lds_dwordx4 v234, s[26:27]
	s_waitcnt vmcnt(12)
	s_waitcnt lgkmcnt(0)
	s_barrier
	s_waitcnt lgkmcnt(0)
	v_mfma_f32_16x16x32_bf16 v[158:161], v[178:181], v[194:197], v[158:161]
	v_mfma_f32_16x16x32_bf16 v[154:157], v[186:189], v[194:197], v[154:157]
	v_mfma_f32_16x16x32_bf16 v[142:145], v[178:181], v[202:205], v[142:145]
	v_mfma_f32_16x16x32_bf16 v[138:141], v[186:189], v[202:205], v[138:141]
	v_mfma_f32_16x16x32_bf16 v[126:129], v[178:181], v[210:213], v[126:129]
	v_mfma_f32_16x16x32_bf16 v[122:125], v[186:189], v[210:213], v[122:125]
	v_mfma_f32_16x16x32_bf16 v[110:113], v[178:181], v[218:221], v[110:113]
	v_mfma_f32_16x16x32_bf16 v[106:109], v[186:189], v[218:221], v[106:109]
	v_mfma_f32_16x16x32_bf16 v[158:161], v[182:185], v[198:201], v[158:161]
	v_mfma_f32_16x16x32_bf16 v[154:157], v[190:193], v[198:201], v[154:157]
	v_mfma_f32_16x16x32_bf16 v[142:145], v[182:185], v[206:209], v[142:145]
	v_mfma_f32_16x16x32_bf16 v[138:141], v[190:193], v[206:209], v[138:141]
	v_mfma_f32_16x16x32_bf16 v[126:129], v[182:185], v[214:217], v[126:129]
	v_mfma_f32_16x16x32_bf16 v[122:125], v[190:193], v[214:217], v[122:125]
	v_mfma_f32_16x16x32_bf16 v[110:113], v[182:185], v[222:225], v[110:113]
	v_mfma_f32_16x16x32_bf16 v[106:109], v[190:193], v[222:225], v[106:109]
	v_mfma_f32_16x16x32_bf16 v[150:153], v[162:165], v[194:197], v[150:153]
	v_mfma_f32_16x16x32_bf16 v[146:149], v[170:173], v[194:197], v[146:149]
	v_mfma_f32_16x16x32_bf16 v[134:137], v[162:165], v[202:205], v[134:137]
	v_mfma_f32_16x16x32_bf16 v[130:133], v[170:173], v[202:205], v[130:133]
	v_mfma_f32_16x16x32_bf16 v[118:121], v[162:165], v[210:213], v[118:121]
	v_mfma_f32_16x16x32_bf16 v[114:117], v[170:173], v[210:213], v[114:117]
	v_mfma_f32_16x16x32_bf16 v[102:105], v[162:165], v[218:221], v[102:105]
	v_mfma_f32_16x16x32_bf16 v[98:101], v[170:173], v[218:221], v[98:101]
	v_mfma_f32_16x16x32_bf16 v[150:153], v[166:169], v[198:201], v[150:153]
	v_mfma_f32_16x16x32_bf16 v[146:149], v[174:177], v[198:201], v[146:149]
	v_mfma_f32_16x16x32_bf16 v[134:137], v[166:169], v[206:209], v[134:137]
	v_mfma_f32_16x16x32_bf16 v[130:133], v[174:177], v[206:209], v[130:133]
	v_mfma_f32_16x16x32_bf16 v[118:121], v[166:169], v[214:217], v[118:121]
	v_mfma_f32_16x16x32_bf16 v[114:117], v[174:177], v[214:217], v[114:117]
	v_mfma_f32_16x16x32_bf16 v[102:105], v[166:169], v[222:225], v[102:105]
	v_mfma_f32_16x16x32_bf16 v[98:101], v[174:177], v[222:225], v[98:101]
	s_barrier
	s_cmp_lt_u32 s54, 12
	s_mov_b64 s[28:29], -1
	s_cbranch_scc0 .LBB0_4719
	s_add_u32 s4, s20, 0x40000
	s_addc_u32 s5, s21, 0
	s_mov_b64 s[28:29], 0

; #define PG8_BWAIT(n) asm volatile("s_waitcnt vmcnt(" #n ")" : "+v"(bv[0]), "+v"(bv[1]), "+v"(bv[2]), "+v"(bv[3]), "+v"(bv[4]), "+v"(bv[5]), "+v"(bv[6]), "+v"(bv[7]) :: "memory")
; #define PG8_STAGE_A(bufoff, V0, V1, kb) do { \
;         __builtin_amdgcn_global_load_lds((const unsigned*)((Abase + (kb)) + (V0)), (LAS unsigned*)(lds + (bufoff) + ldsw), 16, 0, 0); \
;         __builtin_amdgcn_global_load_lds((const unsigned*)((Abase + (kb)) + (V1)), (LAS unsigned*)(lds + (bufoff) + ldsw + 8192), 16, 0, 0); } while (0)
; #define PG8_LDA(dst, b, h) do { _Pragma("unroll") for (int m = 0; m < 4; ++m) _Pragma("unroll") for (int k = 0; k < 2; ++k) dst[m][k] = *(const LAS bf16x8*)(lds + PG8_SA(b, h) + aoff + m * 2048 + k * 1024); } while (0)
; #define PG8_MMA(ai, bj, At, Bt) do { __builtin_amdgcn_s_setprio(1); _Pragma("unroll") for (int m = 0; m < 4; ++m) _Pragma("unroll") for (int n = 0; n < 2; ++n) _Pragma("unroll") for (int k = 0; k < 2; ++k) \
;         acc[ai][bj][m][n] = __builtin_amdgcn_mfma_f32_16x16x32_bf16(Bt[n][k], At[m][k], acc[ai][bj][m][n], 0, 0, 0); __builtin_amdgcn_s_setprio(0); } while (0)
; #define PG8_WAIT_V(n) asm volatile("s_waitcnt vmcnt(" #n ")" ::: "memory")
; #define PG8_WAIT_L(n) asm volatile("s_waitcnt lgkmcnt(" #n ")" ::: "memory")
; #define PG8_BAR __builtin_amdgcn_s_barrier()
; #define PG8_SCHED __builtin_amdgcn_sched_barrier(0)
; template <class Epi, class Sched, bool ALIGN_EPI>
; __device__ __forceinline__ void gemm_phase(LAS unsigned char* lds, const Gemm g, const Sched& S, const Epi& E) {
;     ...
;             PG8_BWAIT(2); PG8_BCOMMIT(1); PG8_SCHED; PG8_LDA(At, 1, 1); PG8_BISSUE(t + 4 >= nt ? pbn + (size_t)(t + 4 - nt) * 64 * Sched::LDN : pbc + (size_t)(t + 4) * 64 * Sched::LDN); PG8_STAGE_A(PG8_SA(1, 0), vc00, vc01, kb2 + 128u);
;             PG8_WAIT_V(12); PG8_WAIT_L(0); PG8_BAR; if (half1) { PG8_MMA(1, 0, At, B0); PG8_MMA(1, 1, At, B1); } PG8_BAR; PG8_SCHED;
.LBB0_4721:
	s_waitcnt vmcnt(2)
	s_nop 0
	v_cvt_pk_bf16_f32 v194, v2, v6
	v_cvt_pk_bf16_f32 v198, v3, v7
	v_cvt_pk_bf16_f32 v202, v4, v8
	v_cvt_pk_bf16_f32 v206, v5, v9
	global_load_dwordx4 v[2:5], v232, s[4:5] offset:0
	global_load_dwordx4 v[6:9], v232, s[4:5] offset:0x400
	v_cvt_pk_bf16_f32 v195, v10, v14
	v_cvt_pk_bf16_f32 v199, v11, v15
	v_cvt_pk_bf16_f32 v203, v12, v16
	v_cvt_pk_bf16_f32 v207, v13, v17
	global_load_dwordx4 v[10:13], v232, s[4:5] offset:0x800
	global_load_dwordx4 v[14:17], v232, s[4:5] offset:0xc00
	v_cvt_pk_bf16_f32 v196, v18, v22
	v_cvt_pk_bf16_f32 v200, v19, v23
	v_cvt_pk_bf16_f32 v204, v20, v24
	v_cvt_pk_bf16_f32 v208, v21, v25
	s_add_u32 s4, s4, 0x1000
	s_addc_u32 s5, s5, 0
	global_load_dwordx4 v[18:21], v232, s[4:5] offset:0
	global_load_dwordx4 v[22:25], v232, s[4:5] offset:0x400
	v_cvt_pk_bf16_f32 v197, v26, v30
	v_cvt_pk_bf16_f32 v201, v27, v31
	v_cvt_pk_bf16_f32 v205, v28, v32
	v_cvt_pk_bf16_f32 v209, v29, v33
	v_lshl_add_u64 v[246:247], s[26:27], 0, v[226:227]
	v_mov_b32_e32 v229, v227
	global_load_dwordx4 v[26:29], v232, s[4:5] offset:0x800
	s_mov_b32 m0, s44
	v_lshl_add_u64 v[248:249], s[26:27], 0, v[228:229]
	global_load_dwordx4 v[30:33], v232, s[4:5] offset:0xc00
	v_add_u32_e32 v210, 0x18000, v235
	v_xor_b32_e32 v211, 64, v210
	v_xor_b32_e32 v212, 0x80, v210
	v_xor_b32_e32 v213, 0xc0, v210
	ds_write_b128 v210, v[194:197]
	ds_write_b128 v211, v[198:201]
	ds_write_b128 v212, v[202:205]
	ds_write_b128 v213, v[206:209]
	ds_read_b128 v[218:221], v241 offset:49152
	ds_read_b128 v[222:225], v241 offset:50176
	ds_read_b128 v[210:213], v241 offset:51200
	ds_read_b128 v[214:217], v241 offset:52224
	ds_read_b128 v[202:205], v241 offset:53248
	ds_read_b128 v[206:209], v241 offset:54272
	ds_read_b128 v[194:197], v241 offset:55296
	ds_read_b128 v[198:201], v241 offset:56320
	v_lshl_add_u64 v[246:247], v[246:247], 0, s[12:13]
	global_load_lds_dwordx4 v[246:247], off
	v_lshl_add_u64 v[246:247], v[248:249], 0, s[12:13]
	s_mov_b32 m0, s45
	s_and_b64 vcc, exec, s[2:3]
	global_load_lds_dwordx4 v[246:247], off
	s_waitcnt vmcnt(12)
	s_waitcnt lgkmcnt(0)
	s_barrier
	s_cbranch_vccnz .LBB0_4723
	s_waitcnt lgkmcnt(0)
	v_mfma_f32_16x16x32_bf16 v[94:97], v[178:181], v[218:221], v[94:97]
	v_mfma_f32_16x16x32_bf16 v[90:93], v[186:189], v[218:221], v[90:93]
	v_mfma_f32_16x16x32_bf16 v[78:81], v[178:181], v[210:213], v[78:81]
	v_mfma_f32_16x16x32_bf16 v[74:77], v[186:189], v[210:213], v[74:77]
	v_mfma_f32_16x16x32_bf16 v[62:65], v[178:181], v[202:205], v[62:65]
	v_mfma_f32_16x16x32_bf16 v[58:61], v[186:189], v[202:205], v[58:61]
	v_mfma_f32_16x16x32_bf16 v[46:49], v[178:181], v[194:197], v[46:49]
	v_mfma_f32_16x16x32_bf16 v[42:45], v[186:189], v[194:197], v[42:45]
	v_mfma_f32_16x16x32_bf16 v[94:97], v[182:185], v[222:225], v[94:97]
	v_mfma_f32_16x16x32_bf16 v[90:93], v[190:193], v[222:225], v[90:93]
	v_mfma_f32_16x16x32_bf16 v[78:81], v[182:185], v[214:217], v[78:81]
	v_mfma_f32_16x16x32_bf16 v[74:77], v[190:193], v[214:217], v[74:77]
	v_mfma_f32_16x16x32_bf16 v[62:65], v[182:185], v[206:209], v[62:65]
	v_mfma_f32_16x16x32_bf16 v[58:61], v[190:193], v[206:209], v[58:61]
	v_mfma_f32_16x16x32_bf16 v[46:49], v[182:185], v[198:201], v[46:49]
	v_mfma_f32_16x16x32_bf16 v[42:45], v[190:193], v[198:201], v[42:45]
	v_mfma_f32_16x16x32_bf16 v[86:89], v[162:165], v[218:221], v[86:89]
	v_mfma_f32_16x16x32_bf16 v[82:85], v[170:173], v[218:221], v[82:85]
	v_mfma_f32_16x16x32_bf16 v[70:73], v[162:165], v[210:213], v[70:73]
	v_mfma_f32_16x16x32_bf16 v[66:69], v[170:173], v[210:213], v[66:69]
	v_mfma_f32_16x16x32_bf16 v[54:57], v[162:165], v[202:205], v[54:57]
	v_mfma_f32_16x16x32_bf16 v[50:53], v[170:173], v[202:205], v[50:53]
	v_mfma_f32_16x16x32_bf16 v[38:41], v[162:165], v[194:197], v[38:41]
	v_mfma_f32_16x16x32_bf16 v[34:37], v[170:173], v[194:197], v[34:37]
	v_mfma_f32_16x16x32_bf16 v[86:89], v[166:169], v[222:225], v[86:89]
	v_mfma_f32_16x16x32_bf16 v[82:85], v[174:177], v[222:225], v[82:85]
	v_mfma_f32_16x16x32_bf16 v[70:73], v[166:169], v[214:217], v[70:73]
	v_mfma_f32_16x16x32_bf16 v[66:69], v[174:177], v[214:217], v[66:69]
	v_mfma_f32_16x16x32_bf16 v[54:57], v[166:169], v[206:209], v[54:57]
	v_mfma_f32_16x16x32_bf16 v[50:53], v[174:177], v[206:209], v[50:53]
	v_mfma_f32_16x16x32_bf16 v[38:41], v[166:169], v[198:201], v[38:41]
	v_mfma_f32_16x16x32_bf16 v[34:37], v[174:177], v[198:201], v[34:37]

; #define PG8_STAGE_B(bufoff, gbase) do { _Pragma("unroll") for (int _i = 0; _i < 2; ++_i) \
;         __builtin_amdgcn_global_load_lds((const unsigned*)((const char*)(gbase) + voffB[_i]), (LAS unsigned*)(lds + (bufoff) + ldsw + _i * 8192), 16, 0, 0); } while (0)
; #define PG8_STAGE_A(bufoff, V0, V1, kb) do { \
;         __builtin_amdgcn_global_load_lds((const unsigned*)((Abase + (kb)) + (V0)), (LAS unsigned*)(lds + (bufoff) + ldsw), 16, 0, 0); \
;         __builtin_amdgcn_global_load_lds((const unsigned*)((Abase + (kb)) + (V1)), (LAS unsigned*)(lds + (bufoff) + ldsw + 8192), 16, 0, 0); } while (0)
; #define PG8_LDA(dst, b, h) do { _Pragma("unroll") for (int m = 0; m < 4; ++m) _Pragma("unroll") for (int k = 0; k < 2; ++k) dst[m][k] = *(const LAS bf16x8*)(lds + PG8_SA(b, h) + aoff + m * 2048 + k * 1024); } while (0)
; #define PG8_LDB(dst, b, h) do { _Pragma("unroll") for (int n = 0; n < 2; ++n) _Pragma("unroll") for (int k = 0; k < 2; ++k) dst[n][k] = *(const LAS bf16x8*)(lds + PG8_SB(b, h) + boff + n * 2048 + k * 1024); } while (0)
; #define PG8_MMA(ai, bj, At, Bt) do { __builtin_amdgcn_s_setprio(1); _Pragma("unroll") for (int m = 0; m < 4; ++m) _Pragma("unroll") for (int n = 0; n < 2; ++n) _Pragma("unroll") for (int k = 0; k < 2; ++k) \
;         acc[ai][bj][m][n] = __builtin_amdgcn_mfma_f32_16x16x32_bf16(Bt[n][k], At[m][k], acc[ai][bj][m][n], 0, 0, 0); __builtin_amdgcn_s_setprio(0); } while (0)
; #define PG8_WAIT_V(n) asm volatile("s_waitcnt vmcnt(" #n ")" ::: "memory")
; #define PG8_WAIT_L(n) asm volatile("s_waitcnt lgkmcnt(" #n ")" ::: "memory")
; #define PG8_BAR __builtin_amdgcn_s_barrier()
; #define PG8_SCHED __builtin_amdgcn_sched_barrier(0)
; template <class Epi, class Sched, bool ALIGN_EPI>
; __device__ __forceinline__ void gemm_phase(LAS unsigned char* lds, const Gemm g, const Sched& S, const Epi& E) {
;     ...
;             PG8_LDB(B0, 0, 0); PG8_LDB(B1, 0, 1); PG8_SCHED; PG8_LDA(At, 0, 0); PG8_STAGE_A(PG8_SA(1, 1), vc10, vc11, kb1);
;             PG8_WAIT_V(8); PG8_WAIT_L(0); PG8_BAR; PG8_MMA(0, 0, At, B0); PG8_MMA(0, 1, At, B1); PG8_BAR; PG8_SCHED;
;             PG8_LDA(At, 0, 1); PG8_STAGE_B(PG8_SB(0, 0), b2); PG8_STAGE_B(PG8_SB(0, 1), b2 + hstepB); PG8_STAGE_A(PG8_SA(0, 0), s00, s01, kb2);
;             PG8_WAIT_V(8); PG8_WAIT_L(0); PG8_BAR; if (half1) { PG8_MMA(1, 0, At, B0); PG8_MMA(1, 1, At, B1); } PG8_BAR; PG8_SCHED;
.LBB0_4787:
	v_add_u32_e32 v5, s49, v216
	ds_read_b128 v[150:153], v5
	ds_read_b128 v[154:157], v5 offset:1024
	ds_read_b128 v[158:161], v5 offset:2048
	ds_read_b128 v[162:165], v5 offset:3072
	v_add_u32_e32 v5, s50, v216
	ds_read_b128 v[134:137], v5
	ds_read_b128 v[138:141], v5 offset:1024
	ds_read_b128 v[142:145], v5 offset:2048
	ds_read_b128 v[146:149], v5 offset:3072
	v_readlane_b32 s60, v254, 55
	v_readlane_b32 s61, v254, 56
	s_add_u32 s36, s60, s13
	s_addc_u32 s37, s61, 0
	v_lshl_add_u64 v[210:211], s[36:37], 0, v[206:207]
	v_lshl_add_u64 v[210:211], v[210:211], 0, s[4:5]
	s_add_i32 m0, s19, 0xc000
	s_waitcnt lgkmcnt(0)
	ds_read_b128 v[166:169], v217
	ds_read_b128 v[170:173], v217 offset:1024
	ds_read_b128 v[174:177], v217 offset:2048
	ds_read_b128 v[178:181], v217 offset:3072
	ds_read_b128 v[182:185], v217 offset:4096
	ds_read_b128 v[186:189], v217 offset:5120
	ds_read_b128 v[190:193], v217 offset:6144
	ds_read_b128 v[194:197], v217 offset:7168
	global_load_lds_dwordx4 v[210:211], off
	v_lshl_add_u64 v[210:211], s[36:37], 0, v[208:209]
	v_lshl_add_u64 v[210:211], v[210:211], 0, s[4:5]
	s_add_i32 m0, s19, 0xe000
	s_nop 0
	global_load_lds_dwordx4 v[210:211], off
	s_waitcnt vmcnt(8)
	s_waitcnt lgkmcnt(0)
	s_barrier
	s_waitcnt lgkmcnt(0)
	v_mfma_f32_16x16x32_bf16 v[130:133], v[150:153], v[166:169], v[130:133]
	v_mfma_f32_16x16x32_bf16 v[126:129], v[158:161], v[166:169], v[126:129]
	v_mfma_f32_16x16x32_bf16 v[114:117], v[150:153], v[174:177], v[114:117]
	v_mfma_f32_16x16x32_bf16 v[110:113], v[158:161], v[174:177], v[110:113]
	v_mfma_f32_16x16x32_bf16 v[98:101], v[150:153], v[182:185], v[98:101]
	v_mfma_f32_16x16x32_bf16 v[94:97], v[158:161], v[182:185], v[94:97]
	v_mfma_f32_16x16x32_bf16 v[82:85], v[150:153], v[190:193], v[82:85]
	v_mfma_f32_16x16x32_bf16 v[78:81], v[158:161], v[190:193], v[78:81]
	v_mfma_f32_16x16x32_bf16 v[130:133], v[154:157], v[170:173], v[130:133]
	v_mfma_f32_16x16x32_bf16 v[126:129], v[162:165], v[170:173], v[126:129]
	v_mfma_f32_16x16x32_bf16 v[114:117], v[154:157], v[178:181], v[114:117]
	v_mfma_f32_16x16x32_bf16 v[110:113], v[162:165], v[178:181], v[110:113]
	v_mfma_f32_16x16x32_bf16 v[98:101], v[154:157], v[186:189], v[98:101]
	v_mfma_f32_16x16x32_bf16 v[94:97], v[162:165], v[186:189], v[94:97]
	v_mfma_f32_16x16x32_bf16 v[82:85], v[154:157], v[194:197], v[82:85]
	v_mfma_f32_16x16x32_bf16 v[78:81], v[162:165], v[194:197], v[78:81]
	v_mfma_f32_16x16x32_bf16 v[122:125], v[134:137], v[166:169], v[122:125]
	v_mfma_f32_16x16x32_bf16 v[118:121], v[142:145], v[166:169], v[118:121]
	v_mfma_f32_16x16x32_bf16 v[106:109], v[134:137], v[174:177], v[106:109]
	v_mfma_f32_16x16x32_bf16 v[102:105], v[142:145], v[174:177], v[102:105]
	v_mfma_f32_16x16x32_bf16 v[90:93], v[134:137], v[182:185], v[90:93]
	v_mfma_f32_16x16x32_bf16 v[86:89], v[142:145], v[182:185], v[86:89]
	v_mfma_f32_16x16x32_bf16 v[74:77], v[134:137], v[190:193], v[74:77]
	v_mfma_f32_16x16x32_bf16 v[70:73], v[142:145], v[190:193], v[70:73]
	v_mfma_f32_16x16x32_bf16 v[122:125], v[138:141], v[170:173], v[122:125]
	v_mfma_f32_16x16x32_bf16 v[118:121], v[146:149], v[170:173], v[118:121]
	v_mfma_f32_16x16x32_bf16 v[106:109], v[138:141], v[178:181], v[106:109]
	v_mfma_f32_16x16x32_bf16 v[102:105], v[146:149], v[178:181], v[102:105]
	v_mfma_f32_16x16x32_bf16 v[90:93], v[138:141], v[186:189], v[90:93]
	v_mfma_f32_16x16x32_bf16 v[86:89], v[146:149], v[186:189], v[86:89]
	v_mfma_f32_16x16x32_bf16 v[74:77], v[138:141], v[194:197], v[74:77]
	v_mfma_f32_16x16x32_bf16 v[70:73], v[146:149], v[194:197], v[70:73]
	s_barrier
	s_add_i32 s3, s49, s40
	v_lshl_add_u64 v[210:211], s[28:29], 0, v[198:199]
	s_mov_b32 m0, s3
	ds_read_b128 v[190:193], v217 offset:16384
	ds_read_b128 v[194:197], v217 offset:17408
	ds_read_b128 v[182:185], v217 offset:18432
	ds_read_b128 v[186:189], v217 offset:19456
	ds_read_b128 v[174:177], v217 offset:20480
	ds_read_b128 v[178:181], v217 offset:21504
	ds_read_b128 v[166:169], v217 offset:22528
	ds_read_b128 v[170:173], v217 offset:23552
	global_load_lds_dwordx4 v[210:211], off
	s_add_i32 m0, s3, 0x2000
	s_add_u32 s36, s28, 0x10000
	v_lshl_add_u64 v[212:213], s[28:29], 0, v[200:201]
	s_addc_u32 s37, s29, 0
	s_add_i32 s3, s50, s40
	global_load_lds_dwordx4 v[212:213], off
	v_lshl_add_u64 v[226:227], s[36:37], 0, v[198:199]
	s_mov_b32 m0, s3
	v_cndmask_b32_e64 v5, 0, 1, s[24:25]
	global_load_lds_dwordx4 v[226:227], off
	s_add_i32 m0, s3, 0x2000
	v_lshl_add_u64 v[226:227], s[36:37], 0, v[200:201]
	s_add_u32 s36, s60, s2
	global_load_lds_dwordx4 v[226:227], off
	s_addc_u32 s37, s61, 0
	s_mov_b32 m0, s19
	v_cmp_ne_u32_e64 s[2:3], 1, v5
	global_load_lds_dwordx4 v2, s[36:37]
	s_mov_b32 m0, s41
	s_andn2_b64 vcc, exec, s[24:25]
	global_load_lds_dwordx4 v4, s[36:37]
	s_waitcnt vmcnt(8)
	s_waitcnt lgkmcnt(0)
	s_barrier
	s_cbranch_vccnz .LBB0_4789
	s_waitcnt lgkmcnt(0)
	v_mfma_f32_16x16x32_bf16 v[66:69], v[150:153], v[190:193], v[66:69]
	v_mfma_f32_16x16x32_bf16 v[62:65], v[158:161], v[190:193], v[62:65]
	v_mfma_f32_16x16x32_bf16 v[50:53], v[150:153], v[182:185], v[50:53]
	v_mfma_f32_16x16x32_bf16 v[46:49], v[158:161], v[182:185], v[46:49]
	v_mfma_f32_16x16x32_bf16 v[34:37], v[150:153], v[174:177], v[34:37]
	v_mfma_f32_16x16x32_bf16 v[30:33], v[158:161], v[174:177], v[30:33]
	v_mfma_f32_16x16x32_bf16 v[18:21], v[150:153], v[166:169], v[18:21]
	v_mfma_f32_16x16x32_bf16 v[14:17], v[158:161], v[166:169], v[14:17]
	v_mfma_f32_16x16x32_bf16 v[66:69], v[154:157], v[194:197], v[66:69]
	v_mfma_f32_16x16x32_bf16 v[62:65], v[162:165], v[194:197], v[62:65]
	v_mfma_f32_16x16x32_bf16 v[50:53], v[154:157], v[186:189], v[50:53]
	v_mfma_f32_16x16x32_bf16 v[46:49], v[162:165], v[186:189], v[46:49]
	v_mfma_f32_16x16x32_bf16 v[34:37], v[154:157], v[178:181], v[34:37]
	v_mfma_f32_16x16x32_bf16 v[30:33], v[162:165], v[178:181], v[30:33]
	v_mfma_f32_16x16x32_bf16 v[18:21], v[154:157], v[170:173], v[18:21]
	v_mfma_f32_16x16x32_bf16 v[14:17], v[162:165], v[170:173], v[14:17]
	v_mfma_f32_16x16x32_bf16 v[58:61], v[134:137], v[190:193], v[58:61]
	v_mfma_f32_16x16x32_bf16 v[54:57], v[142:145], v[190:193], v[54:57]
	v_mfma_f32_16x16x32_bf16 v[42:45], v[134:137], v[182:185], v[42:45]
	v_mfma_f32_16x16x32_bf16 v[38:41], v[142:145], v[182:185], v[38:41]
	v_mfma_f32_16x16x32_bf16 v[26:29], v[134:137], v[174:177], v[26:29]
	v_mfma_f32_16x16x32_bf16 v[22:25], v[142:145], v[174:177], v[22:25]
	v_mfma_f32_16x16x32_bf16 v[10:13], v[134:137], v[166:169], v[10:13]
	v_mfma_f32_16x16x32_bf16 v[6:9], v[142:145], v[166:169], v[6:9]
	v_mfma_f32_16x16x32_bf16 v[58:61], v[138:141], v[194:197], v[58:61]
	v_mfma_f32_16x16x32_bf16 v[54:57], v[146:149], v[194:197], v[54:57]
	v_mfma_f32_16x16x32_bf16 v[42:45], v[138:141], v[186:189], v[42:45]
	v_mfma_f32_16x16x32_bf16 v[38:41], v[146:149], v[186:189], v[38:41]
	v_mfma_f32_16x16x32_bf16 v[26:29], v[138:141], v[178:181], v[26:29]
	v_mfma_f32_16x16x32_bf16 v[22:25], v[146:149], v[178:181], v[22:25]
	v_mfma_f32_16x16x32_bf16 v[10:13], v[138:141], v[170:173], v[10:13]
	v_mfma_f32_16x16x32_bf16 v[6:9], v[146:149], v[170:173], v[6:9]
; #define PG8_STAGE_B(bufoff, gbase) do { _Pragma("unroll") for (int _i = 0; _i < 2; ++_i) \
;         __builtin_amdgcn_global_load_lds((const unsigned*)((const char*)(gbase) + voffB[_i]), (LAS unsigned*)(lds + (bufoff) + ldsw + _i * 8192), 16, 0, 0); } while (0)
; #define PG8_STAGE_A(bufoff, V0, V1, kb) do { \
;         __builtin_amdgcn_global_load_lds((const unsigned*)((Abase + (kb)) + (V0)), (LAS unsigned*)(lds + (bufoff) + ldsw), 16, 0, 0); \
;         __builtin_amdgcn_global_load_lds((const unsigned*)((Abase + (kb)) + (V1)), (LAS unsigned*)(lds + (bufoff) + ldsw + 8192), 16, 0, 0); } while (0)
; #define PG8_LDA(dst, b, h) do { _Pragma("unroll") for (int m = 0; m < 4; ++m) _Pragma("unroll") for (int k = 0; k < 2; ++k) dst[m][k] = *(const LAS bf16x8*)(lds + PG8_SA(b, h) + aoff + m * 2048 + k * 1024); } while (0)
; #define PG8_LDB(dst, b, h) do { _Pragma("unroll") for (int n = 0; n < 2; ++n) _Pragma("unroll") for (int k = 0; k < 2; ++k) dst[n][k] = *(const LAS bf16x8*)(lds + PG8_SB(b, h) + boff + n * 2048 + k * 1024); } while (0)
; #define PG8_MMA(ai, bj, At, Bt) do { __builtin_amdgcn_s_setprio(1); _Pragma("unroll") for (int m = 0; m < 4; ++m) _Pragma("unroll") for (int n = 0; n < 2; ++n) _Pragma("unroll") for (int k = 0; k < 2; ++k) \
;         acc[ai][bj][m][n] = __builtin_amdgcn_mfma_f32_16x16x32_bf16(Bt[n][k], At[m][k], acc[ai][bj][m][n], 0, 0, 0); __builtin_amdgcn_s_setprio(0); } while (0)
; #define PG8_WAIT_V(n) asm volatile("s_waitcnt vmcnt(" #n ")" ::: "memory")
; #define PG8_WAIT_L(n) asm volatile("s_waitcnt lgkmcnt(" #n ")" ::: "memory")
; #define PG8_BAR __builtin_amdgcn_s_barrier()
; #define PG8_SCHED __builtin_amdgcn_sched_barrier(0)
; template <class Epi, class Sched, bool ALIGN_EPI>
; __device__ __forceinline__ void gemm_phase(LAS unsigned char* lds, const Gemm g, const Sched& S, const Epi& E) {
;     ...
;             PG8_LDB(B0, 1, 0); PG8_LDB(B1, 1, 1); PG8_SCHED; PG8_LDA(At, 1, 0); PG8_STAGE_A(PG8_SA(0, 1), s10, s11, kb2);
;             PG8_WAIT_V(8); PG8_WAIT_L(0); PG8_BAR; PG8_MMA(0, 0, At, B0); PG8_MMA(0, 1, At, B1); PG8_BAR; PG8_SCHED;
;             PG8_LDA(At, 1, 1); PG8_STAGE_B(PG8_SB(1, 0), b3); PG8_STAGE_B(PG8_SB(1, 1), b3 + hstepB); PG8_STAGE_A(PG8_SA(1, 0), s00, s01, kb3);
;             PG8_WAIT_V(8); PG8_WAIT_L(0); PG8_BAR; if (half1) { PG8_MMA(1, 0, At, B0); PG8_MMA(1, 1, At, B1); } PG8_BAR; PG8_SCHED;
.LBB0_4789:
	v_mov_b32_e32 v5, v3
	v_lshl_add_u64 v[226:227], s[36:37], 0, v[2:3]
	v_lshl_add_u64 v[4:5], s[36:37], 0, v[4:5]
	s_barrier
	v_add_u32_e32 v2, s51, v216
	ds_read_b128 v[150:153], v2
	ds_read_b128 v[154:157], v2 offset:1024
	ds_read_b128 v[158:161], v2 offset:2048
	ds_read_b128 v[162:165], v2 offset:3072
	v_add_u32_e32 v2, s52, v216
	ds_read_b128 v[134:137], v2
	ds_read_b128 v[138:141], v2 offset:1024
	ds_read_b128 v[142:145], v2 offset:2048
	ds_read_b128 v[146:149], v2 offset:3072
	s_mov_b32 m0, s42
	s_waitcnt lgkmcnt(0)
	ds_read_b128 v[166:169], v217 offset:32768
	ds_read_b128 v[170:173], v217 offset:33792
	ds_read_b128 v[174:177], v217 offset:34816
	ds_read_b128 v[178:181], v217 offset:35840
	ds_read_b128 v[182:185], v217 offset:36864
	ds_read_b128 v[186:189], v217 offset:37888
	ds_read_b128 v[190:193], v217 offset:38912
	ds_read_b128 v[194:197], v217 offset:39936
	global_load_lds_dwordx4 v224, s[36:37]
	s_mov_b32 m0, s43
	s_nop 0
	global_load_lds_dwordx4 v225, s[36:37]
	s_waitcnt vmcnt(8)
	s_waitcnt lgkmcnt(0)
	s_barrier
	s_waitcnt lgkmcnt(0)
	v_mfma_f32_16x16x32_bf16 v[130:133], v[150:153], v[166:169], v[130:133]
	v_mfma_f32_16x16x32_bf16 v[126:129], v[158:161], v[166:169], v[126:129]
	v_mfma_f32_16x16x32_bf16 v[114:117], v[150:153], v[174:177], v[114:117]
	v_mfma_f32_16x16x32_bf16 v[110:113], v[158:161], v[174:177], v[110:113]
	v_mfma_f32_16x16x32_bf16 v[98:101], v[150:153], v[182:185], v[98:101]
	v_mfma_f32_16x16x32_bf16 v[94:97], v[158:161], v[182:185], v[94:97]
	v_mfma_f32_16x16x32_bf16 v[82:85], v[150:153], v[190:193], v[82:85]
	v_mfma_f32_16x16x32_bf16 v[78:81], v[158:161], v[190:193], v[78:81]
	v_mfma_f32_16x16x32_bf16 v[130:133], v[154:157], v[170:173], v[130:133]
	v_mfma_f32_16x16x32_bf16 v[126:129], v[162:165], v[170:173], v[126:129]
	v_mfma_f32_16x16x32_bf16 v[114:117], v[154:157], v[178:181], v[114:117]
	v_mfma_f32_16x16x32_bf16 v[110:113], v[162:165], v[178:181], v[110:113]
	v_mfma_f32_16x16x32_bf16 v[98:101], v[154:157], v[186:189], v[98:101]
	v_mfma_f32_16x16x32_bf16 v[94:97], v[162:165], v[186:189], v[94:97]
	v_mfma_f32_16x16x32_bf16 v[82:85], v[154:157], v[194:197], v[82:85]
	v_mfma_f32_16x16x32_bf16 v[78:81], v[162:165], v[194:197], v[78:81]
	v_mfma_f32_16x16x32_bf16 v[122:125], v[134:137], v[166:169], v[122:125]
	v_mfma_f32_16x16x32_bf16 v[118:121], v[142:145], v[166:169], v[118:121]
	v_mfma_f32_16x16x32_bf16 v[106:109], v[134:137], v[174:177], v[106:109]
	v_mfma_f32_16x16x32_bf16 v[102:105], v[142:145], v[174:177], v[102:105]
	v_mfma_f32_16x16x32_bf16 v[90:93], v[134:137], v[182:185], v[90:93]
	v_mfma_f32_16x16x32_bf16 v[86:89], v[142:145], v[182:185], v[86:89]
	v_mfma_f32_16x16x32_bf16 v[74:77], v[134:137], v[190:193], v[74:77]
	v_mfma_f32_16x16x32_bf16 v[70:73], v[142:145], v[190:193], v[70:73]
	v_mfma_f32_16x16x32_bf16 v[122:125], v[138:141], v[170:173], v[122:125]
	v_mfma_f32_16x16x32_bf16 v[118:121], v[146:149], v[170:173], v[118:121]
	v_mfma_f32_16x16x32_bf16 v[106:109], v[138:141], v[178:181], v[106:109]
	v_mfma_f32_16x16x32_bf16 v[102:105], v[146:149], v[178:181], v[102:105]
	v_mfma_f32_16x16x32_bf16 v[90:93], v[138:141], v[186:189], v[90:93]
	v_mfma_f32_16x16x32_bf16 v[86:89], v[146:149], v[186:189], v[86:89]
	v_mfma_f32_16x16x32_bf16 v[74:77], v[138:141], v[194:197], v[74:77]
	v_mfma_f32_16x16x32_bf16 v[70:73], v[146:149], v[194:197], v[70:73]
	s_barrier
	s_add_i32 s13, s51, s40
	v_lshl_add_u64 v[210:211], v[210:211], 0, s[4:5]
	s_mov_b32 m0, s13
	ds_read_b128 v[190:193], v217 offset:49152
	ds_read_b128 v[194:197], v217 offset:50176
	ds_read_b128 v[182:185], v217 offset:51200
	ds_read_b128 v[186:189], v217 offset:52224
	ds_read_b128 v[174:177], v217 offset:53248
	ds_read_b128 v[178:181], v217 offset:54272
	ds_read_b128 v[166:169], v217 offset:55296
	ds_read_b128 v[170:173], v217 offset:56320
	global_load_lds_dwordx4 v[210:211], off
	s_add_i32 m0, s13, 0x2000
	s_add_u32 s28, s28, 0x10080
	v_lshl_add_u64 v[210:211], v[212:213], 0, s[4:5]
	s_addc_u32 s29, s29, 0
	s_add_i32 s13, s52, s40
	global_load_lds_dwordx4 v[210:211], off
	v_lshl_add_u64 v[210:211], s[28:29], 0, v[198:199]
	s_mov_b32 m0, s13
	v_lshl_add_u64 v[4:5], v[4:5], 0, s[4:5]
	global_load_lds_dwordx4 v[210:211], off
	v_lshl_add_u64 v[210:211], s[28:29], 0, v[200:201]
	s_add_i32 m0, s13, 0x2000
	s_and_b64 vcc, exec, s[2:3]
	global_load_lds_dwordx4 v[210:211], off
	v_lshl_add_u64 v[210:211], v[226:227], 0, s[4:5]
	s_mov_b32 m0, s44
	s_nop 0
	global_load_lds_dwordx4 v[210:211], off
	s_mov_b32 m0, s45
	s_nop 0
	global_load_lds_dwordx4 v[4:5], off
	s_waitcnt vmcnt(8)
	s_waitcnt lgkmcnt(0)
	s_barrier
	s_cbranch_vccnz .LBB0_4783
	s_waitcnt lgkmcnt(0)
	v_mfma_f32_16x16x32_bf16 v[66:69], v[150:153], v[190:193], v[66:69]
	v_mfma_f32_16x16x32_bf16 v[62:65], v[158:161], v[190:193], v[62:65]
	v_mfma_f32_16x16x32_bf16 v[50:53], v[150:153], v[182:185], v[50:53]
	v_mfma_f32_16x16x32_bf16 v[46:49], v[158:161], v[182:185], v[46:49]
	v_mfma_f32_16x16x32_bf16 v[34:37], v[150:153], v[174:177], v[34:37]
	v_mfma_f32_16x16x32_bf16 v[30:33], v[158:161], v[174:177], v[30:33]
	v_mfma_f32_16x16x32_bf16 v[18:21], v[150:153], v[166:169], v[18:21]
	v_mfma_f32_16x16x32_bf16 v[14:17], v[158:161], v[166:169], v[14:17]
	v_mfma_f32_16x16x32_bf16 v[66:69], v[154:157], v[194:197], v[66:69]
	v_mfma_f32_16x16x32_bf16 v[62:65], v[162:165], v[194:197], v[62:65]
	v_mfma_f32_16x16x32_bf16 v[50:53], v[154:157], v[186:189], v[50:53]
	v_mfma_f32_16x16x32_bf16 v[46:49], v[162:165], v[186:189], v[46:49]
	v_mfma_f32_16x16x32_bf16 v[34:37], v[154:157], v[178:181], v[34:37]
	v_mfma_f32_16x16x32_bf16 v[30:33], v[162:165], v[178:181], v[30:33]
	v_mfma_f32_16x16x32_bf16 v[18:21], v[154:157], v[170:173], v[18:21]
	v_mfma_f32_16x16x32_bf16 v[14:17], v[162:165], v[170:173], v[14:17]
	v_mfma_f32_16x16x32_bf16 v[58:61], v[134:137], v[190:193], v[58:61]
	v_mfma_f32_16x16x32_bf16 v[54:57], v[142:145], v[190:193], v[54:57]
	v_mfma_f32_16x16x32_bf16 v[42:45], v[134:137], v[182:185], v[42:45]
	v_mfma_f32_16x16x32_bf16 v[38:41], v[142:145], v[182:185], v[38:41]
	v_mfma_f32_16x16x32_bf16 v[26:29], v[134:137], v[174:177], v[26:29]
	v_mfma_f32_16x16x32_bf16 v[22:25], v[142:145], v[174:177], v[22:25]
	v_mfma_f32_16x16x32_bf16 v[10:13], v[134:137], v[166:169], v[10:13]
	v_mfma_f32_16x16x32_bf16 v[4:7], v[142:145], v[166:169], v[6:9]
	v_mfma_f32_16x16x32_bf16 v[58:61], v[138:141], v[194:197], v[58:61]
	v_mfma_f32_16x16x32_bf16 v[54:57], v[146:149], v[194:197], v[54:57]
	v_mfma_f32_16x16x32_bf16 v[42:45], v[138:141], v[186:189], v[42:45]
	v_mfma_f32_16x16x32_bf16 v[38:41], v[146:149], v[186:189], v[38:41]
	v_mfma_f32_16x16x32_bf16 v[26:29], v[138:141], v[178:181], v[26:29]
	v_mfma_f32_16x16x32_bf16 v[22:25], v[146:149], v[178:181], v[22:25]
	v_mfma_f32_16x16x32_bf16 v[10:13], v[138:141], v[170:173], v[10:13]
	v_mfma_f32_16x16x32_bf16 v[6:9], v[146:149], v[170:173], v[4:7]
	s_branch .LBB0_4783

; #define PG8_BWAIT(n) asm volatile("s_waitcnt vmcnt(" #n ")" : "+v"(bv[0]), "+v"(bv[1]), "+v"(bv[2]), "+v"(bv[3]), "+v"(bv[4]), "+v"(bv[5]), "+v"(bv[6]), "+v"(bv[7]) :: "memory")
; #define PG8_STAGE_A(bufoff, V0, V1, kb) do { \
;         __builtin_amdgcn_global_load_lds((const unsigned*)((Abase + (kb)) + (V0)), (LAS unsigned*)(lds + (bufoff) + ldsw), 16, 0, 0); \
;         __builtin_amdgcn_global_load_lds((const unsigned*)((Abase + (kb)) + (V1)), (LAS unsigned*)(lds + (bufoff) + ldsw + 8192), 16, 0, 0); } while (0)
; #define PG8_LDA(dst, b, h) do { _Pragma("unroll") for (int m = 0; m < 4; ++m) _Pragma("unroll") for (int k = 0; k < 2; ++k) dst[m][k] = *(const LAS bf16x8*)(lds + PG8_SA(b, h) + aoff + m * 2048 + k * 1024); } while (0)
; #define PG8_LDB(dst, b, h) do { _Pragma("unroll") for (int n = 0; n < 2; ++n) _Pragma("unroll") for (int k = 0; k < 2; ++k) dst[n][k] = *(const LAS bf16x8*)(lds + PG8_SB(b, h) + boff + n * 2048 + k * 1024); } while (0)
; #define PG8_WAIT_V(n) asm volatile("s_waitcnt vmcnt(" #n ")" ::: "memory")
; #define PG8_WAIT_L(n) asm volatile("s_waitcnt lgkmcnt(" #n ")" ::: "memory")
; #define PG8_BAR __builtin_amdgcn_s_barrier()
; #define PG8_SCHED __builtin_amdgcn_sched_barrier(0)
; template <class Epi, class Sched, bool ALIGN_EPI>
; __device__ __forceinline__ void gemm_phase(LAS unsigned char* lds, const Gemm g, const Sched& S, const Epi& E) {
;     ...
;         for (int t = 0; t < nt; t += 2) {
;             const bool last = (t == nt - 2);
;             const unsigned kb1 = (unsigned)(t + 1) * 128u, kb2 = last ? 0u : (unsigned)(t + 2) * 128u;
;             if (last) { vc00 = vn00; vc01 = vn01; }
;             PG8_LDB(B0, 0, 0); PG8_LDB(B1, 0, 1); PG8_SCHED; PG8_LDA(At, 0, 0); PG8_STAGE_A(PG8_SA(1, 1), vc10, vc11, kb1);
;             PG8_WAIT_V(12); PG8_WAIT_L(0); PG8_BAR; PG8_MMA(0, 0, At, B0); PG8_MMA(0, 1, At, B1); PG8_BAR; PG8_SCHED;
;             if (last) { vc10 = vn10; vc11 = vn11; }
;             PG8_BWAIT(2); PG8_BCOMMIT(0); PG8_SCHED; PG8_LDA(At, 0, 1); PG8_BISSUE(t + 3 >= nt ? pbn + (size_t)(t + 3 - nt) * 64 * Sched::LDN : pbc + (size_t)(t + 3) * 64 * Sched::LDN); PG8_STAGE_A(PG8_SA(0, 0), vc00, vc01, kb2);
;             PG8_WAIT_V(12); PG8_WAIT_L(0); PG8_BAR; if (half1) { PG8_MMA(1, 0, At, B0); PG8_MMA(1, 1, At, B1); } PG8_BAR; PG8_SCHED;
.LBB0_4908:
	v_add_u32_e32 v162, 0x10000, v247
	v_add_u32_e32 v174, 0x14000, v247
	ds_read_b128 v[178:181], v162
	ds_read_b128 v[182:185], v162 offset:1024
	ds_read_b128 v[186:189], v162 offset:2048
	ds_read_b128 v[190:193], v162 offset:3072
	ds_read_b128 v[162:165], v174
	ds_read_b128 v[166:169], v174 offset:1024
	ds_read_b128 v[170:173], v174 offset:2048
	ds_read_b128 v[174:177], v174 offset:3072
	s_lshl_b32 s3, s52, 7
	s_add_i32 s2, s3, 0x100
	v_cndmask_b32_e64 v228, v228, v250, s[28:29]
	v_readlane_b32 s56, v254, 53
	v_readlane_b32 s57, v254, 54
	s_add_u32 s30, s56, s3
	s_addc_u32 s31, s57, 0
	v_lshl_add_u64 v[236:237], s[30:31], 0, v[230:231]
	v_lshl_add_u64 v[236:237], v[236:237], 0, s[14:15]
	s_add_i32 m0, s37, 0xc000
	v_mov_b32_e32 v233, v231
	s_waitcnt lgkmcnt(0)
	ds_read_b128 v[194:197], v248
	ds_read_b128 v[198:201], v248 offset:1024
	ds_read_b128 v[202:205], v248 offset:2048
	ds_read_b128 v[206:209], v248 offset:3072
	ds_read_b128 v[210:213], v248 offset:4096
	ds_read_b128 v[214:217], v248 offset:5120
	ds_read_b128 v[218:221], v248 offset:6144
	ds_read_b128 v[222:225], v248 offset:7168
	global_load_lds_dwordx4 v[236:237], off
	v_lshl_add_u64 v[236:237], s[30:31], 0, v[232:233]
	v_lshl_add_u64 v[236:237], v[236:237], 0, s[14:15]
	s_add_i32 m0, s37, 0xe000
	s_nop 0
	global_load_lds_dwordx4 v[236:237], off
	s_waitcnt vmcnt(12)
	s_waitcnt lgkmcnt(0)
	s_barrier
	s_waitcnt lgkmcnt(0)
	v_mfma_f32_16x16x32_bf16 v[158:161], v[178:181], v[194:197], v[158:161]
	v_mfma_f32_16x16x32_bf16 v[154:157], v[186:189], v[194:197], v[154:157]
	v_mfma_f32_16x16x32_bf16 v[142:145], v[178:181], v[202:205], v[142:145]
	v_mfma_f32_16x16x32_bf16 v[138:141], v[186:189], v[202:205], v[138:141]
	v_mfma_f32_16x16x32_bf16 v[126:129], v[178:181], v[210:213], v[126:129]
	v_mfma_f32_16x16x32_bf16 v[122:125], v[186:189], v[210:213], v[122:125]
	v_mfma_f32_16x16x32_bf16 v[110:113], v[178:181], v[218:221], v[110:113]
	v_mfma_f32_16x16x32_bf16 v[106:109], v[186:189], v[218:221], v[106:109]
	v_mfma_f32_16x16x32_bf16 v[158:161], v[182:185], v[198:201], v[158:161]
	v_mfma_f32_16x16x32_bf16 v[154:157], v[190:193], v[198:201], v[154:157]
	v_mfma_f32_16x16x32_bf16 v[142:145], v[182:185], v[206:209], v[142:145]
	v_mfma_f32_16x16x32_bf16 v[138:141], v[190:193], v[206:209], v[138:141]
	v_mfma_f32_16x16x32_bf16 v[126:129], v[182:185], v[214:217], v[126:129]
	v_mfma_f32_16x16x32_bf16 v[122:125], v[190:193], v[214:217], v[122:125]
	v_mfma_f32_16x16x32_bf16 v[110:113], v[182:185], v[222:225], v[110:113]
	v_mfma_f32_16x16x32_bf16 v[106:109], v[190:193], v[222:225], v[106:109]
	v_mfma_f32_16x16x32_bf16 v[150:153], v[162:165], v[194:197], v[150:153]
	v_mfma_f32_16x16x32_bf16 v[146:149], v[170:173], v[194:197], v[146:149]
	v_mfma_f32_16x16x32_bf16 v[134:137], v[162:165], v[202:205], v[134:137]
	v_mfma_f32_16x16x32_bf16 v[130:133], v[170:173], v[202:205], v[130:133]
	v_mfma_f32_16x16x32_bf16 v[118:121], v[162:165], v[210:213], v[118:121]
	v_mfma_f32_16x16x32_bf16 v[114:117], v[170:173], v[210:213], v[114:117]
	v_mfma_f32_16x16x32_bf16 v[102:105], v[162:165], v[218:221], v[102:105]
	v_mfma_f32_16x16x32_bf16 v[98:101], v[170:173], v[218:221], v[98:101]
	v_mfma_f32_16x16x32_bf16 v[150:153], v[166:169], v[198:201], v[150:153]
	v_mfma_f32_16x16x32_bf16 v[146:149], v[174:177], v[198:201], v[146:149]
	v_mfma_f32_16x16x32_bf16 v[134:137], v[166:169], v[206:209], v[134:137]
	v_mfma_f32_16x16x32_bf16 v[130:133], v[174:177], v[206:209], v[130:133]
	v_mfma_f32_16x16x32_bf16 v[118:121], v[166:169], v[214:217], v[118:121]
	v_mfma_f32_16x16x32_bf16 v[114:117], v[174:177], v[214:217], v[114:117]
	v_mfma_f32_16x16x32_bf16 v[102:105], v[166:169], v[222:225], v[102:105]
	v_mfma_f32_16x16x32_bf16 v[98:101], v[174:177], v[222:225], v[98:101]
	s_barrier
	s_add_i32 s8, s52, -1
	s_lshl_b64 s[30:31], s[8:9], 18
	s_add_u32 s3, s49, s30
	s_addc_u32 s8, s21, s31
	s_and_b64 s[30:31], s[26:27], exec
	s_cselect_b32 s30, s50, s3
	s_cselect_b32 s31, s51, s8
	s_add_u32 s54, s30, 0x1000
	s_waitcnt vmcnt(2)
	v_cndmask_b32_e64 v226, v226, v249, s[28:29]
	v_cvt_pk_bf16_f32 v194, v2, v6
	v_cvt_pk_bf16_f32 v198, v3, v7
	v_cvt_pk_bf16_f32 v202, v4, v8
	v_cvt_pk_bf16_f32 v206, v5, v9
	global_load_dwordx4 v[2:5], v240, s[30:31] offset:0
	s_addc_u32 s55, s31, 0
	global_load_dwordx4 v[6:9], v240, s[54:55] offset:0
	v_cvt_pk_bf16_f32 v195, v10, v14
	v_cvt_pk_bf16_f32 v199, v11, v15
	v_cvt_pk_bf16_f32 v203, v12, v16
	v_cvt_pk_bf16_f32 v207, v13, v17
	s_add_u32 s54, s30, 0x2000
	s_addc_u32 s55, s31, 0
	global_load_dwordx4 v[10:13], v240, s[54:55] offset:0
	s_add_u32 s54, s30, 0x3000
	s_addc_u32 s55, s31, 0
	global_load_dwordx4 v[14:17], v240, s[54:55] offset:0
	v_cvt_pk_bf16_f32 v196, v18, v22
	v_cvt_pk_bf16_f32 v200, v19, v23
	v_cvt_pk_bf16_f32 v204, v20, v24
	v_cvt_pk_bf16_f32 v208, v21, v25
	s_add_u32 s54, s30, 0x4000
	s_addc_u32 s55, s31, 0
	global_load_dwordx4 v[18:21], v240, s[54:55] offset:0
	s_add_u32 s54, s30, 0x5000
	s_addc_u32 s55, s31, 0
	global_load_dwordx4 v[22:25], v240, s[54:55] offset:0
	v_cvt_pk_bf16_f32 v197, v26, v30
	v_cvt_pk_bf16_f32 v201, v27, v31
	v_cvt_pk_bf16_f32 v205, v28, v32
	v_cvt_pk_bf16_f32 v209, v29, v33
	s_add_u32 s54, s30, 0x6000
	s_addc_u32 s55, s31, 0
	s_add_u32 s30, s30, 0x7000
	global_load_dwordx4 v[26:29], v240, s[54:55] offset:0
	s_addc_u32 s31, s31, 0
	global_load_dwordx4 v[30:33], v240, s[30:31] offset:0
	v_add_u32_e32 v210, 0x10000, v242
	v_xor_b32_e32 v211, 64, v210
	v_xor_b32_e32 v212, 0x80, v210
	v_xor_b32_e32 v213, 0xc0, v210
	ds_write_b128 v210, v[194:197]
	ds_write_b128 v211, v[198:201]
	ds_write_b128 v212, v[202:205]
	ds_write_b128 v213, v[206:209]
	ds_read_b128 v[218:221], v248 offset:16384
	ds_read_b128 v[222:225], v248 offset:17408
	ds_read_b128 v[210:213], v248 offset:18432
	ds_read_b128 v[214:217], v248 offset:19456
	ds_read_b128 v[202:205], v248 offset:20480
	ds_read_b128 v[206:209], v248 offset:21504
	ds_read_b128 v[194:197], v248 offset:22528
	ds_read_b128 v[198:201], v248 offset:23552
	s_and_b64 s[30:31], s[28:29], exec
	s_cselect_b32 s2, 0, s2
	s_cselect_b32 s3, 0, 0
	s_add_u32 s30, s56, s2
	s_mov_b32 m0, s37
	s_addc_u32 s31, s57, s3
	global_load_lds_dwordx4 v226, s[30:31]
	s_mov_b32 m0, s38
	v_mov_b32_e32 v227, v231
	global_load_lds_dwordx4 v228, s[30:31]
	s_waitcnt vmcnt(12)
	s_waitcnt lgkmcnt(0)
	v_lshl_add_u64 v[238:239], s[30:31], 0, v[226:227]
	v_mov_b32_e32 v229, v231
	v_cndmask_b32_e64 v227, 0, 1, s[24:25]
	v_lshl_add_u64 v[236:237], s[30:31], 0, v[228:229]
	v_cmp_ne_u32_e64 s[2:3], 1, v227
	s_andn2_b64 vcc, exec, s[24:25]
	s_barrier
; #define PG8_STAGE_A(bufoff, V0, V1, kb) do { \
;         __builtin_amdgcn_global_load_lds((const unsigned*)((Abase + (kb)) + (V0)), (LAS unsigned*)(lds + (bufoff) + ldsw), 16, 0, 0); \
;         __builtin_amdgcn_global_load_lds((const unsigned*)((Abase + (kb)) + (V1)), (LAS unsigned*)(lds + (bufoff) + ldsw + 8192), 16, 0, 0); } while (0)
; #define PG8_LDA(dst, b, h) do { _Pragma("unroll") for (int m = 0; m < 4; ++m) _Pragma("unroll") for (int k = 0; k < 2; ++k) dst[m][k] = *(const LAS bf16x8*)(lds + PG8_SA(b, h) + aoff + m * 2048 + k * 1024); } while (0)
; #define PG8_LDB(dst, b, h) do { _Pragma("unroll") for (int n = 0; n < 2; ++n) _Pragma("unroll") for (int k = 0; k < 2; ++k) dst[n][k] = *(const LAS bf16x8*)(lds + PG8_SB(b, h) + boff + n * 2048 + k * 1024); } while (0)
; #define PG8_MMA(ai, bj, At, Bt) do { __builtin_amdgcn_s_setprio(1); _Pragma("unroll") for (int m = 0; m < 4; ++m) _Pragma("unroll") for (int n = 0; n < 2; ++n) _Pragma("unroll") for (int k = 0; k < 2; ++k) \
;         acc[ai][bj][m][n] = __builtin_amdgcn_mfma_f32_16x16x32_bf16(Bt[n][k], At[m][k], acc[ai][bj][m][n], 0, 0, 0); __builtin_amdgcn_s_setprio(0); } while (0)
; #define PG8_WAIT_V(n) asm volatile("s_waitcnt vmcnt(" #n ")" ::: "memory")
; #define PG8_WAIT_L(n) asm volatile("s_waitcnt lgkmcnt(" #n ")" ::: "memory")
; #define PG8_BAR __builtin_amdgcn_s_barrier()
; #define PG8_SCHED __builtin_amdgcn_sched_barrier(0)
; template <class Epi, class Sched, bool ALIGN_EPI>
; __device__ __forceinline__ void gemm_phase(LAS unsigned char* lds, const Gemm g, const Sched& S, const Epi& E) {
;     ...
;             PG8_WAIT_V(12); PG8_WAIT_L(0); PG8_BAR; if (half1) { PG8_MMA(1, 0, At, B0); PG8_MMA(1, 1, At, B1); } PG8_BAR; PG8_SCHED;
;             PG8_LDB(B0, 1, 0); PG8_LDB(B1, 1, 1); PG8_SCHED; PG8_LDA(At, 1, 0); PG8_STAGE_A(PG8_SA(0, 1), vc10, vc11, kb2);
;             PG8_WAIT_V(12); PG8_WAIT_L(0); PG8_BAR; PG8_MMA(0, 0, At, B0); PG8_MMA(0, 1, At, B1); PG8_BAR; PG8_SCHED;
	s_cbranch_vccnz .LBB0_4910
	s_waitcnt lgkmcnt(0)
	v_mfma_f32_16x16x32_bf16 v[94:97], v[178:181], v[218:221], v[94:97]
	v_mfma_f32_16x16x32_bf16 v[90:93], v[186:189], v[218:221], v[90:93]
	v_mfma_f32_16x16x32_bf16 v[78:81], v[178:181], v[210:213], v[78:81]
	v_mfma_f32_16x16x32_bf16 v[74:77], v[186:189], v[210:213], v[74:77]
	v_mfma_f32_16x16x32_bf16 v[62:65], v[178:181], v[202:205], v[62:65]
	v_mfma_f32_16x16x32_bf16 v[58:61], v[186:189], v[202:205], v[58:61]
	v_mfma_f32_16x16x32_bf16 v[46:49], v[178:181], v[194:197], v[46:49]
	v_mfma_f32_16x16x32_bf16 v[42:45], v[186:189], v[194:197], v[42:45]
	v_mfma_f32_16x16x32_bf16 v[94:97], v[182:185], v[222:225], v[94:97]
	v_mfma_f32_16x16x32_bf16 v[90:93], v[190:193], v[222:225], v[90:93]
	v_mfma_f32_16x16x32_bf16 v[78:81], v[182:185], v[214:217], v[78:81]
	v_mfma_f32_16x16x32_bf16 v[74:77], v[190:193], v[214:217], v[74:77]
	v_mfma_f32_16x16x32_bf16 v[62:65], v[182:185], v[206:209], v[62:65]
	v_mfma_f32_16x16x32_bf16 v[58:61], v[190:193], v[206:209], v[58:61]
	v_mfma_f32_16x16x32_bf16 v[46:49], v[182:185], v[198:201], v[46:49]
	v_mfma_f32_16x16x32_bf16 v[42:45], v[190:193], v[198:201], v[42:45]
	v_mfma_f32_16x16x32_bf16 v[86:89], v[162:165], v[218:221], v[86:89]
	v_mfma_f32_16x16x32_bf16 v[82:85], v[170:173], v[218:221], v[82:85]
	v_mfma_f32_16x16x32_bf16 v[70:73], v[162:165], v[210:213], v[70:73]
	v_mfma_f32_16x16x32_bf16 v[66:69], v[170:173], v[210:213], v[66:69]
	v_mfma_f32_16x16x32_bf16 v[54:57], v[162:165], v[202:205], v[54:57]
	v_mfma_f32_16x16x32_bf16 v[50:53], v[170:173], v[202:205], v[50:53]
	v_mfma_f32_16x16x32_bf16 v[38:41], v[162:165], v[194:197], v[38:41]
	v_mfma_f32_16x16x32_bf16 v[34:37], v[170:173], v[194:197], v[34:37]
	v_mfma_f32_16x16x32_bf16 v[86:89], v[166:169], v[222:225], v[86:89]
	v_mfma_f32_16x16x32_bf16 v[82:85], v[174:177], v[222:225], v[82:85]
	v_mfma_f32_16x16x32_bf16 v[70:73], v[166:169], v[214:217], v[70:73]
	v_mfma_f32_16x16x32_bf16 v[66:69], v[174:177], v[214:217], v[66:69]
	v_mfma_f32_16x16x32_bf16 v[54:57], v[166:169], v[206:209], v[54:57]
	v_mfma_f32_16x16x32_bf16 v[50:53], v[174:177], v[206:209], v[50:53]
	v_mfma_f32_16x16x32_bf16 v[38:41], v[166:169], v[198:201], v[38:41]
	v_mfma_f32_16x16x32_bf16 v[34:37], v[174:177], v[198:201], v[34:37]
.LBB0_4910:
	v_cndmask_b32_e64 v232, v232, v252, s[28:29]
	v_cndmask_b32_e64 v230, v230, v251, s[28:29]
	s_barrier
	v_add_u32_e32 v162, 0x18000, v247
	v_add_u32_e32 v174, 0x1c000, v247
	ds_read_b128 v[178:181], v162
	ds_read_b128 v[182:185], v162 offset:1024
	ds_read_b128 v[186:189], v162 offset:2048
	ds_read_b128 v[190:193], v162 offset:3072
	ds_read_b128 v[162:165], v174
	ds_read_b128 v[166:169], v174 offset:1024
	ds_read_b128 v[170:173], v174 offset:2048
	ds_read_b128 v[174:177], v174 offset:3072
	s_mov_b32 m0, s39
	s_waitcnt lgkmcnt(0)
	ds_read_b128 v[194:197], v248 offset:32768
	ds_read_b128 v[198:201], v248 offset:33792
	ds_read_b128 v[202:205], v248 offset:34816
	ds_read_b128 v[206:209], v248 offset:35840
	ds_read_b128 v[210:213], v248 offset:36864
	ds_read_b128 v[214:217], v248 offset:37888
	ds_read_b128 v[218:221], v248 offset:38912
	ds_read_b128 v[222:225], v248 offset:39936
	global_load_lds_dwordx4 v230, s[30:31]
	s_mov_b32 m0, s40
	s_nop 0
	global_load_lds_dwordx4 v232, s[30:31]
	s_waitcnt vmcnt(12)
	s_waitcnt lgkmcnt(0)
	s_barrier
	s_waitcnt lgkmcnt(0)
	v_mfma_f32_16x16x32_bf16 v[158:161], v[178:181], v[194:197], v[158:161]
	v_mfma_f32_16x16x32_bf16 v[154:157], v[186:189], v[194:197], v[154:157]
	v_mfma_f32_16x16x32_bf16 v[142:145], v[178:181], v[202:205], v[142:145]
	v_mfma_f32_16x16x32_bf16 v[138:141], v[186:189], v[202:205], v[138:141]
	v_mfma_f32_16x16x32_bf16 v[126:129], v[178:181], v[210:213], v[126:129]
	v_mfma_f32_16x16x32_bf16 v[122:125], v[186:189], v[210:213], v[122:125]
	v_mfma_f32_16x16x32_bf16 v[110:113], v[178:181], v[218:221], v[110:113]
	v_mfma_f32_16x16x32_bf16 v[106:109], v[186:189], v[218:221], v[106:109]
	v_mfma_f32_16x16x32_bf16 v[158:161], v[182:185], v[198:201], v[158:161]
	v_mfma_f32_16x16x32_bf16 v[154:157], v[190:193], v[198:201], v[154:157]
	v_mfma_f32_16x16x32_bf16 v[142:145], v[182:185], v[206:209], v[142:145]
	v_mfma_f32_16x16x32_bf16 v[138:141], v[190:193], v[206:209], v[138:141]
	v_mfma_f32_16x16x32_bf16 v[126:129], v[182:185], v[214:217], v[126:129]
	v_mfma_f32_16x16x32_bf16 v[122:125], v[190:193], v[214:217], v[122:125]
	v_mfma_f32_16x16x32_bf16 v[110:113], v[182:185], v[222:225], v[110:113]
	v_mfma_f32_16x16x32_bf16 v[106:109], v[190:193], v[222:225], v[106:109]
	v_mfma_f32_16x16x32_bf16 v[150:153], v[162:165], v[194:197], v[150:153]
	v_mfma_f32_16x16x32_bf16 v[146:149], v[170:173], v[194:197], v[146:149]
	v_mfma_f32_16x16x32_bf16 v[134:137], v[162:165], v[202:205], v[134:137]
	v_mfma_f32_16x16x32_bf16 v[130:133], v[170:173], v[202:205], v[130:133]
	v_mfma_f32_16x16x32_bf16 v[118:121], v[162:165], v[210:213], v[118:121]
	v_mfma_f32_16x16x32_bf16 v[114:117], v[170:173], v[210:213], v[114:117]
	v_mfma_f32_16x16x32_bf16 v[102:105], v[162:165], v[218:221], v[102:105]
	v_mfma_f32_16x16x32_bf16 v[98:101], v[170:173], v[218:221], v[98:101]
	v_mfma_f32_16x16x32_bf16 v[150:153], v[166:169], v[198:201], v[150:153]
	v_mfma_f32_16x16x32_bf16 v[146:149], v[174:177], v[198:201], v[146:149]
	v_mfma_f32_16x16x32_bf16 v[134:137], v[166:169], v[206:209], v[134:137]
	v_mfma_f32_16x16x32_bf16 v[130:133], v[174:177], v[206:209], v[130:133]
	v_mfma_f32_16x16x32_bf16 v[118:121], v[166:169], v[214:217], v[118:121]
	v_mfma_f32_16x16x32_bf16 v[114:117], v[174:177], v[214:217], v[114:117]
	v_mfma_f32_16x16x32_bf16 v[102:105], v[166:169], v[222:225], v[102:105]
	v_mfma_f32_16x16x32_bf16 v[98:101], v[174:177], v[222:225], v[98:101]
	s_barrier
; #define PG8_BWAIT(n) asm volatile("s_waitcnt vmcnt(" #n ")" : "+v"(bv[0]), "+v"(bv[1]), "+v"(bv[2]), "+v"(bv[3]), "+v"(bv[4]), "+v"(bv[5]), "+v"(bv[6]), "+v"(bv[7]) :: "memory")
; #define PG8_STAGE_A(bufoff, V0, V1, kb) do { \
;         __builtin_amdgcn_global_load_lds((const unsigned*)((Abase + (kb)) + (V0)), (LAS unsigned*)(lds + (bufoff) + ldsw), 16, 0, 0); \
;         __builtin_amdgcn_global_load_lds((const unsigned*)((Abase + (kb)) + (V1)), (LAS unsigned*)(lds + (bufoff) + ldsw + 8192), 16, 0, 0); } while (0)
; #define PG8_LDA(dst, b, h) do { _Pragma("unroll") for (int m = 0; m < 4; ++m) _Pragma("unroll") for (int k = 0; k < 2; ++k) dst[m][k] = *(const LAS bf16x8*)(lds + PG8_SA(b, h) + aoff + m * 2048 + k * 1024); } while (0)
; #define PG8_MMA(ai, bj, At, Bt) do { __builtin_amdgcn_s_setprio(1); _Pragma("unroll") for (int m = 0; m < 4; ++m) _Pragma("unroll") for (int n = 0; n < 2; ++n) _Pragma("unroll") for (int k = 0; k < 2; ++k) \
;         acc[ai][bj][m][n] = __builtin_amdgcn_mfma_f32_16x16x32_bf16(Bt[n][k], At[m][k], acc[ai][bj][m][n], 0, 0, 0); __builtin_amdgcn_s_setprio(0); } while (0)
; #define PG8_WAIT_V(n) asm volatile("s_waitcnt vmcnt(" #n ")" ::: "memory")
; #define PG8_WAIT_L(n) asm volatile("s_waitcnt lgkmcnt(" #n ")" ::: "memory")
; #define PG8_BAR __builtin_amdgcn_s_barrier()
; #define PG8_SCHED __builtin_amdgcn_sched_barrier(0)
; template <class Epi, class Sched, bool ALIGN_EPI>
; __device__ __forceinline__ void gemm_phase(LAS unsigned char* lds, const Gemm g, const Sched& S, const Epi& E) {
;     ...
;             PG8_BWAIT(2); PG8_BCOMMIT(1); PG8_SCHED; PG8_LDA(At, 1, 1); PG8_BISSUE(t + 4 >= nt ? pbn + (size_t)(t + 4 - nt) * 64 * Sched::LDN : pbc + (size_t)(t + 4) * 64 * Sched::LDN); PG8_STAGE_A(PG8_SA(1, 0), vc00, vc01, kb2 + 128u);
;             PG8_WAIT_V(12); PG8_WAIT_L(0); PG8_BAR; if (half1) { PG8_MMA(1, 0, At, B0); PG8_MMA(1, 1, At, B1); } PG8_BAR; PG8_SCHED;
	s_lshl_b32 s8, s52, 16
	s_lshl_b64 s[28:29], s[8:9], 2
	s_add_u32 s28, s49, s28
	s_addc_u32 s29, s21, s29
	s_add_u32 s30, s28, 0x1000
	s_waitcnt vmcnt(2)
	s_nop 0
	v_cvt_pk_bf16_f32 v194, v2, v6
	v_cvt_pk_bf16_f32 v198, v3, v7
	v_cvt_pk_bf16_f32 v202, v4, v8
	v_cvt_pk_bf16_f32 v206, v5, v9
	global_load_dwordx4 v[2:5], v240, s[28:29] offset:0
	s_addc_u32 s31, s29, 0
	global_load_dwordx4 v[6:9], v240, s[30:31] offset:0
	v_cvt_pk_bf16_f32 v195, v10, v14
	v_cvt_pk_bf16_f32 v199, v11, v15
	v_cvt_pk_bf16_f32 v203, v12, v16
	v_cvt_pk_bf16_f32 v207, v13, v17
	s_add_u32 s30, s28, 0x2000
	s_addc_u32 s31, s29, 0
	global_load_dwordx4 v[10:13], v240, s[30:31] offset:0
	s_add_u32 s30, s28, 0x3000
	s_addc_u32 s31, s29, 0
	global_load_dwordx4 v[14:17], v240, s[30:31] offset:0
	v_cvt_pk_bf16_f32 v196, v18, v22
	v_cvt_pk_bf16_f32 v200, v19, v23
	v_cvt_pk_bf16_f32 v204, v20, v24
	v_cvt_pk_bf16_f32 v208, v21, v25
	s_add_u32 s30, s28, 0x4000
	s_addc_u32 s31, s29, 0
	global_load_dwordx4 v[18:21], v240, s[30:31] offset:0
	s_add_u32 s30, s28, 0x5000
	s_addc_u32 s31, s29, 0
	global_load_dwordx4 v[22:25], v240, s[30:31] offset:0
	v_cvt_pk_bf16_f32 v197, v26, v30
	v_cvt_pk_bf16_f32 v201, v27, v31
	v_cvt_pk_bf16_f32 v205, v28, v32
	v_cvt_pk_bf16_f32 v209, v29, v33
	s_add_u32 s30, s28, 0x6000
	s_addc_u32 s31, s29, 0
	global_load_dwordx4 v[26:29], v240, s[30:31] offset:0
	s_add_u32 s28, s28, 0x7000
	s_mov_b32 m0, s41
	s_addc_u32 s29, s29, 0
	global_load_dwordx4 v[30:33], v240, s[28:29] offset:0
	v_add_u32_e32 v210, 0x18000, v242
	v_xor_b32_e32 v211, 64, v210
	v_xor_b32_e32 v212, 0x80, v210
	v_xor_b32_e32 v213, 0xc0, v210
	ds_write_b128 v210, v[194:197]
	ds_write_b128 v211, v[198:201]
	ds_write_b128 v212, v[202:205]
	ds_write_b128 v213, v[206:209]
	ds_read_b128 v[218:221], v248 offset:49152
	ds_read_b128 v[222:225], v248 offset:50176
	ds_read_b128 v[210:213], v248 offset:51200
	ds_read_b128 v[214:217], v248 offset:52224
	ds_read_b128 v[202:205], v248 offset:53248
	ds_read_b128 v[206:209], v248 offset:54272
	ds_read_b128 v[194:197], v248 offset:55296
	ds_read_b128 v[198:201], v248 offset:56320
	v_lshl_add_u64 v[238:239], v[238:239], 0, s[14:15]
	global_load_lds_dwordx4 v[238:239], off
	v_lshl_add_u64 v[236:237], v[236:237], 0, s[14:15]
	s_mov_b32 m0, s42
	s_and_b64 vcc, exec, s[2:3]
	global_load_lds_dwordx4 v[236:237], off
	s_waitcnt vmcnt(12)
	s_waitcnt lgkmcnt(0)
	s_barrier
	s_cbranch_vccnz .LBB0_4907
	s_waitcnt lgkmcnt(0)
	v_mfma_f32_16x16x32_bf16 v[94:97], v[178:181], v[218:221], v[94:97]
	v_mfma_f32_16x16x32_bf16 v[90:93], v[186:189], v[218:221], v[90:93]
	v_mfma_f32_16x16x32_bf16 v[78:81], v[178:181], v[210:213], v[78:81]
	v_mfma_f32_16x16x32_bf16 v[74:77], v[186:189], v[210:213], v[74:77]
	v_mfma_f32_16x16x32_bf16 v[62:65], v[178:181], v[202:205], v[62:65]
	v_mfma_f32_16x16x32_bf16 v[58:61], v[186:189], v[202:205], v[58:61]
	v_mfma_f32_16x16x32_bf16 v[46:49], v[178:181], v[194:197], v[46:49]
	v_mfma_f32_16x16x32_bf16 v[42:45], v[186:189], v[194:197], v[42:45]
	v_mfma_f32_16x16x32_bf16 v[94:97], v[182:185], v[222:225], v[94:97]
	v_mfma_f32_16x16x32_bf16 v[90:93], v[190:193], v[222:225], v[90:93]
	v_mfma_f32_16x16x32_bf16 v[78:81], v[182:185], v[214:217], v[78:81]
	v_mfma_f32_16x16x32_bf16 v[74:77], v[190:193], v[214:217], v[74:77]
	v_mfma_f32_16x16x32_bf16 v[62:65], v[182:185], v[206:209], v[62:65]
	v_mfma_f32_16x16x32_bf16 v[58:61], v[190:193], v[206:209], v[58:61]
	v_mfma_f32_16x16x32_bf16 v[46:49], v[182:185], v[198:201], v[46:49]
	v_mfma_f32_16x16x32_bf16 v[42:45], v[190:193], v[198:201], v[42:45]
	v_mfma_f32_16x16x32_bf16 v[86:89], v[162:165], v[218:221], v[86:89]
	v_mfma_f32_16x16x32_bf16 v[82:85], v[170:173], v[218:221], v[82:85]
	v_mfma_f32_16x16x32_bf16 v[70:73], v[162:165], v[210:213], v[70:73]
	v_mfma_f32_16x16x32_bf16 v[66:69], v[170:173], v[210:213], v[66:69]
	v_mfma_f32_16x16x32_bf16 v[54:57], v[162:165], v[202:205], v[54:57]
	v_mfma_f32_16x16x32_bf16 v[50:53], v[170:173], v[202:205], v[50:53]
	v_mfma_f32_16x16x32_bf16 v[38:41], v[162:165], v[194:197], v[38:41]
	v_mfma_f32_16x16x32_bf16 v[34:37], v[170:173], v[194:197], v[34:37]
	v_mfma_f32_16x16x32_bf16 v[86:89], v[166:169], v[222:225], v[86:89]
	v_mfma_f32_16x16x32_bf16 v[82:85], v[174:177], v[222:225], v[82:85]
	v_mfma_f32_16x16x32_bf16 v[70:73], v[166:169], v[214:217], v[70:73]
	v_mfma_f32_16x16x32_bf16 v[66:69], v[174:177], v[214:217], v[66:69]
	v_mfma_f32_16x16x32_bf16 v[54:57], v[166:169], v[206:209], v[54:57]
	v_mfma_f32_16x16x32_bf16 v[50:53], v[174:177], v[206:209], v[50:53]
	v_mfma_f32_16x16x32_bf16 v[38:41], v[166:169], v[198:201], v[38:41]
	v_mfma_f32_16x16x32_bf16 v[34:37], v[174:177], v[198:201], v[34:37]
	s_branch .LBB0_4907
